# P5 both layers: LN1 gamma/beta + adaLN scale2/shift2 chunks read from LDS (filled once per phase, static LDS +16KB) instead of a global round trip per 4-column chunk; stacked on previous
# speedup vs baseline: 1.0112x; 1.0112x over previous
; #define GAS __attribute__((address_space(1)))
; #define LAS __attribute__((address_space(3)))
; __device__ __forceinline__ unsigned pk2(float lo, float hi) { return f2bf(lo) | (f2bf(hi) << 16); }
; __device__ __forceinline__ int affine_item(int item_, int G) { if (G != 256) return item_; const int c = item_ & 255, i = item_ >> 8; return 64 * (c & 7) + (c >> 3) + 32 * i; }
; template <int l>
; __device__ __forceinline__ void layer_phases(Frame& F, const XcdBarrier& bar, const int lo, const int hi) {
;     ...
;             const bf16* mixb = (const bf16*)(ws + WS_Y1); const float* xin = inptr<const float>(F, I_X); const bf16* xinb = (const bf16*)(ws + WS_X2B); bf16* x1 = (bf16*)(ws + WS_X1); unsigned char* h2q = ws + WS_H2;
;             const float* g1 = inptr<const float>(F, I_LN1G) + (size_t)l * D; const float* b1 = inptr<const float>(F, I_LN1B) + (size_t)l * D;
;             int* tinfo = (int*)(ws + WS_TINFO); float* gates = (float*)(ws + WS_GATE); int* list = (int*)(ws + WS_LIST); int* list2 = (int*)(ws + WS_LIST2);
;             LAS unsigned char* h2s = F.lds + RING_OFF;
;             LAS float* part = (LAS float*)(F.lds + RING_OFF);
;             const unsigned char* wrf = ws + WS_WR + (size_t)l * 524288;
;             const float rb = inptr<const float>(F, I_RBIAS)[l * NE + F.lane];
;             for (int item_ = blockIdx.x; item_ < T / 32; item_ += F.G) {
;                 const int item = affine_item(item_, F.G);
;                 const int m0 = item * 32 + 4 * F.wave;
;                 int lq = F.lane; asm volatile("" : "+v"(lq));
;                 const int r32 = lq & 31, hi5 = lq >> 5;
;                 const float* mrow = (const float*)(ws + WS_MOD) + ((size_t)l * 8 + (m0 >> 11)) * 12288;
;     ...
;                     for (int j = 0; j < 8; ++j) { const int k = 4 * lq + 256 * j;
;                         const f32x4 xv = v[j] * rstd * *(const GAS f32x4*)(g1 + k) + *(const GAS f32x4*)(b1 + k);
;                         { v2u xo; xo.x = pk2(xv.x, xv.y); xo.y = pk2(xv.z, xv.w); *(GAS v2u*)(x1 + (size_t)m * D + k) = xo; }
;                         const f32x4 hv = xv * (*(const GAS f32x4*)(mrow + 8192 + k) + 1.0f) + *(const GAS f32x4*)(mrow + 6144 + k);
.LBB0_605:
	s_cmp_gt_i32 s92, 5
	s_cselect_b64 s[0:1], -1, 0
	s_cmp_lt_i32 s93, 6
	s_cselect_b64 s[4:5], -1, 0
	s_or_b64 s[0:1], s[0:1], s[4:5]
	s_and_b64 vcc, exec, s[0:1]
	v_writelane_b32 v248, s80, 12
	s_cbranch_vccnz .LBB0_675
	s_add_i32 s0, 0, 0x21400
	v_mov_b32_e32 v72, v216
	v_mov_b32_e32 v0, s0
	ds_read_b64 v[4:5], v0
	s_add_i32 s3, 0, 0x21448
	v_mov_b32_e32 v0, s3
	s_add_i32 s0, 0, 0x21460
	ds_read2_b64 v[0:3], v0 offset1:1
	s_waitcnt lgkmcnt(1)
	v_readfirstlane_b32 s20, v4
	v_mov_b32_e32 v4, s0
	v_readfirstlane_b32 s21, v5
	ds_read_b64 v[4:5], v4
	s_waitcnt lgkmcnt(1)
	v_readfirstlane_b32 s5, v1
	v_readfirstlane_b32 s4, v0
	s_mov_b32 s1, 0
	s_cmpk_gt_i32 s2, 0x1ff
	v_writelane_b32 v248, s4, 13
	v_readfirstlane_b32 s25, v3
	v_readfirstlane_b32 s24, v2
	v_writelane_b32 v248, s5, 14
	s_waitcnt lgkmcnt(0)
	v_readfirstlane_b32 s5, v5
	v_readfirstlane_b32 s4, v4
	v_lshlrev_b32_e32 v252, 3, v216
	v_add_u32_e32 v252, 0x21400, v252
	ds_read_b64 v[254:255], v252
	s_waitcnt lgkmcnt(0)
	s_cbranch_scc1 .LBB0_621
	v_ashrrev_i32_e32 v73, 31, v72
	v_lshlrev_b64 v[0:1], 2, v[72:73]
	v_lshl_add_u64 v[2:3], s[4:5], 0, v[0:1]
	flat_load_dword v74, v[2:3]
	s_add_u32 s26, s56, 0x55c00000
	s_addc_u32 s27, s57, 0
	s_add_u32 s3, s56, 0x39c00000
	s_addc_u32 s41, s57, 0
	s_add_u32 s50, s56, 0x41c00000
	s_addc_u32 s51, s57, 0
	s_add_u32 s4, s56, 0xa00000
	s_addc_u32 s5, s57, 0
	v_writelane_b32 v248, s4, 15
	v_and_b32_e32 v2, 64, v216
	v_add_u32_e32 v2, 64, v2
	v_writelane_b32 v248, s5, 16
	s_add_u32 s4, s56, 0x6f600000
	s_addc_u32 s5, s57, 0
	v_writelane_b32 v248, s4, 17
	s_add_u32 s0, s56, 0x100000
	v_xor_b32_e32 v3, 1, v216
	v_writelane_b32 v248, s5, 18
	v_writelane_b32 v248, s0, 19
	s_addc_u32 s0, s57, 0
	s_cmpk_eq_i32 s76, 0x100
	v_writelane_b32 v248, s0, 20
	s_cselect_b64 s[4:5], -1, 0
	v_writelane_b32 v248, s4, 22
	v_cmp_lt_i32_e32 vcc, v3, v2
	s_lshl_b32 s54, s80, 2
	v_writelane_b32 v248, s5, 23
	v_lshl_add_u64 v[0:1], s[56:57], 0, v[0:1]
	s_mov_b64 s[4:5], 0x800000
	s_lshl_b32 s0, s80, 14
	v_cndmask_b32_e32 v3, v216, v3, vcc
	v_lshl_add_u64 v[76:77], v[0:1], 0, s[4:5]
	s_mov_b64 s[4:5], 0x900000
	v_writelane_b32 v248, s0, 24
	s_or_b32 s0, s54, 1
	v_lshlrev_b32_e32 v73, 2, v3
	v_xor_b32_e32 v3, 2, v216
	v_lshl_add_u64 v[78:79], v[0:1], 0, s[4:5]
	s_lshl_b32 s4, s0, 12
	s_and_b32 s66, s0, 13
	s_or_b32 s0, s54, 2
	v_cmp_lt_i32_e32 vcc, v3, v2
	v_writelane_b32 v248, s4, 25
	s_lshl_b32 s4, s0, 12
	s_and_b32 s68, s0, 14
	s_or_b32 s0, s54, 3
	v_cndmask_b32_e32 v3, v216, v3, vcc
	v_writelane_b32 v248, s4, 26
	s_lshl_b32 s4, s0, 12
	s_and_b32 s70, s0, 15
	s_lshl_b32 s0, s80, 4
	v_lshlrev_b32_e32 v217, 2, v3
	v_xor_b32_e32 v3, 4, v216
	s_and_b32 s64, s54, 12
	s_lshl_b64 s[0:1], s[0:1], 12
	v_cmp_lt_i32_e32 vcc, v3, v2
	s_add_u32 s0, s56, s0
	s_addc_u32 s1, s57, s1
	v_cndmask_b32_e32 v3, v216, v3, vcc
	v_lshlrev_b32_e32 v218, 2, v3
	v_xor_b32_e32 v3, 8, v216
	s_add_u32 s36, s0, 0xe00000
	v_cmp_lt_i32_e32 vcc, v3, v2
	s_addc_u32 s37, s1, 0
	s_lshl_b32 s0, s80, 5
	v_cndmask_b32_e32 v3, v216, v3, vcc
	v_writelane_b32 v248, s4, 27
	s_or_b32 s1, s0, 8
	v_lshlrev_b32_e32 v219, 2, v3
	v_xor_b32_e32 v3, 16, v216
	v_writelane_b32 v248, s1, 28
	s_or_b32 s1, s0, 16
	v_cmp_lt_i32_e32 vcc, v3, v2
	v_writelane_b32 v248, s1, 29
	v_writelane_b32 v248, s0, 30
	v_cndmask_b32_e32 v3, v216, v3, vcc
	s_or_b32 s0, s0, 24
	v_lshlrev_b32_e32 v220, 2, v3
	v_xor_b32_e32 v3, 32, v216
	v_writelane_b32 v248, s0, 31
	s_lshl_b32 s0, s80, 13
	v_cmp_lt_i32_e32 vcc, v3, v2
	s_add_i32 s0, s0, 0
	v_writelane_b32 v248, s0, 32
	v_cndmask_b32_e32 v2, v216, v3, vcc
	s_lshl_b32 s0, s80, 10
	v_cmp_gt_i32_e64 s[4:5], 6, v72
	v_lshlrev_b32_e32 v221, 2, v2
	v_lshl_add_u32 v2, v72, 2, 0
	v_writelane_b32 v248, s4, 34
	s_add_u32 s38, s56, 0x8000
	v_sub_u32_e32 v222, 63, v72
	v_writelane_b32 v248, s5, 35
	v_cmp_eq_u32_e64 s[4:5], 1, v72
	v_cmp_eq_u32_e64 s[6:7], 2, v72
	v_cmp_eq_u32_e64 s[8:9], 3, v72
	v_cmp_eq_u32_e64 s[10:11], 4, v72
	v_cmp_eq_u32_e64 s[12:13], 5, v72
	s_addc_u32 s39, s57, 0
	s_waitcnt vmcnt(0) lgkmcnt(0)
	v_mov_b32_e32 v75, v74
	s_lshl_b32 s83, s2, 6
	s_lshl_b32 s1, s76, 6
	s_movk_i32 s85, 0x4000
	s_mov_b32 s86, 0xffff0000
	s_mov_b32 s40, 0x3fb504f3
	s_movk_i32 s87, 0x1000
	v_mov_b32_e32 v223, 0x3727c5ac
	s_mov_b32 s89, 0xf800000
	v_mov_b32_e32 v224, 0x260
	s_movk_i32 s90, 0x7fff
	v_mov_b32_e32 v81, 0
	v_add_u32_e32 v225, s0, v2
	s_movk_i32 s93, 0xffc0
	v_mov_b32_e32 v226, 1
	s_mov_b32 s94, s2
	v_writelane_b32 v248, s1, 36
	s_barrier
	s_lshl_b32 s98, s80, 10
	v_lshl_add_u32 v253, v216, 4, s98
	v_readlane_b32 s98, v248, 13
	v_readlane_b32 s99, v248, 14
	s_nop 4
	global_load_dwordx4 v[100:103], v253, s[98:99]
	s_mov_b32 s98, s24
	s_mov_b32 s99, s25
	global_load_dwordx4 v[104:107], v253, s[98:99]
	s_and_b32 s100, s2, 7
	s_add_u32 s100, s100, 0
	s_mul_i32 s100, s100, 0xc000
	v_readlane_b32 s101, v248, 19
	s_nop 0
	s_add_u32 s100, s101, s100
	v_readlane_b32 s101, v248, 20
	s_nop 0
	s_addc_u32 s101, s101, 0
	s_add_u32 s98, s100, 0x8000
	s_addc_u32 s99, s101, 0
	global_load_dwordx4 v[108:111], v253, s[98:99]
	s_add_u32 s98, s100, 0x6000
	s_addc_u32 s99, s101, 0
	global_load_dwordx4 v[112:115], v253, s[98:99]
	v_add_u32_e32 v253, 0x20000, v253
	s_waitcnt vmcnt(3)
	ds_write_b128 v253, v[100:103]
	s_waitcnt vmcnt(2)
	ds_write_b128 v253, v[104:107] offset:8192
	s_waitcnt vmcnt(1)
	ds_write_b128 v253, v[108:111] offset:16384
	s_waitcnt vmcnt(0)
	ds_write_b128 v253, v[112:115] offset:24576
	v_lshlrev_b32_e32 v252, 4, v216
	v_add_u32_e32 v252, 0x20000, v252
	s_waitcnt lgkmcnt(0)
	s_barrier
	s_branch .LBB0_610

; #define GAS __attribute__((address_space(1)))
; __device__ __forceinline__ f32x4 bf4(unsigned a, unsigned b) { return (f32x4){bflo(a), bfhi(a), bflo(b), bfhi(b)}; }
; template <int l>
; __device__ __forceinline__ void layer_phases(Frame& F, const XcdBarrier& bar, const int lo, const int hi) {
;     ...
; #pragma unroll
;                 for (int rp = 0; rp < 2; ++rp) {
;                 f32x4 vv[2][8];
; #pragma unroll
;                 for (int rr = 0; rr < 2; ++rr)
; #pragma unroll
;                     for (int j = 0; j < 8; ++j) { const size_t off = (size_t)(m0 + 2 * rp + rr) * D + 4 * lq + 256 * j;
;                         f32x4 xv; if (l == 0) xv = __builtin_nontemporal_load((const GAS f32x4*)(xin + off)); else { const v2u xw_ = __builtin_nontemporal_load((const GAS v2u*)(xinb + off)); xv = bf4(xw_.x, xw_.y); } const v2u mw = __builtin_nontemporal_load((const GAS v2u*)(mixb + off)); const f32x4 gv = *(const GAS f32x4*)(mrow + 4096 + 4 * lq + 256 * j);
;                         vv[rr][j] = xv * ALPHA + gv * (f32x4){bflo(mw.x), bfhi(mw.x), bflo(mw.y), bfhi(mw.y)}; }
.LBB0_612:
	s_lshl_b32 s0, s0, 5
	s_add_i32 s42, s0, s54
	s_ashr_i32 s0, s42, 11
	v_mov_b32_e32 v227, v72
	s_mul_hi_i32 s1, s0, 0xc000
	s_mul_i32 s0, s0, 0xc000
	v_readlane_b32 s14, v248, 19
	s_add_u32 s0, s14, s0
	v_readlane_b32 s14, v248, 20
	v_lshlrev_b32_e32 v86, 2, v227
	s_addc_u32 s1, s14, s1
	v_ashrrev_i32_e32 v87, 31, v86
	s_ashr_i32 s43, s42, 31
	s_lshl_b64 s[18:19], s[42:43], 11
	v_lshlrev_b64 v[32:33], 2, v[86:87]
	v_lshl_add_u64 v[20:21], s[18:19], 0, v[86:87]
	v_lshl_add_u64 v[88:89], s[0:1], 0, v[32:33]
	s_movk_i32 s22, 0x5000
	v_lshl_add_u64 v[28:29], v[20:21], 1, s[26:27]
	v_add_co_u32_e32 v64, vcc, s22, v88
	s_mov_b64 s[0:1], 0x4000
	global_load_dwordx2 v[62:63], v[28:29], off nt
	global_load_dwordx2 v[68:69], v[28:29], off offset:512 nt
	global_load_dwordx2 v[70:71], v[28:29], off offset:1024 nt
	global_load_dwordx2 v[82:83], v[28:29], off offset:1536 nt
	global_load_dwordx2 v[84:85], v[28:29], off offset:2048 nt
	v_addc_co_u32_e32 v65, vcc, 0, v89, vcc
	global_load_dwordx2 v[106:107], v[28:29], off offset:2560 nt
	global_load_dwordx4 v[0:3], v[64:65], off offset:-4096
	v_lshl_add_u64 v[66:67], v[88:89], 0, s[0:1]
	global_load_dwordx4 v[16:19], v[66:67], off offset:1024
	global_load_dwordx4 v[12:15], v[66:67], off offset:2048
	global_load_dwordx4 v[8:11], v[66:67], off offset:3072
	global_load_dwordx4 v[4:7], v[64:65], off
	v_lshl_add_u64 v[20:21], v[20:21], 2, s[20:21]
	global_load_dwordx4 v[34:37], v[20:21], off nt
	global_load_dwordx4 v[38:41], v[20:21], off offset:1024 nt
	global_load_dwordx4 v[42:45], v[20:21], off offset:2048 nt
	global_load_dwordx4 v[46:49], v[20:21], off offset:3072 nt
	v_add_co_u32_e32 v90, vcc, s87, v20
	v_readlane_b32 s0, v248, 13
	s_nop 0
	v_addc_co_u32_e32 v91, vcc, 0, v21, vcc
	global_load_dwordx4 v[50:53], v[90:91], off nt
	global_load_dwordx4 v[20:23], v[64:65], off offset:1024
	global_load_dwordx4 v[54:57], v[90:91], off offset:1024 nt
	global_load_dwordx2 v[112:113], v[28:29], off offset:3072 nt
	global_load_dwordx4 v[24:27], v[64:65], off offset:2048
	global_load_dwordx4 v[58:61], v[90:91], off offset:2048 nt
	global_load_dwordx2 v[114:115], v[28:29], off offset:3584 nt
	s_nop 0
	global_load_dwordx4 v[28:31], v[64:65], off offset:3072
	global_load_dwordx4 v[92:95], v[90:91], off offset:3072 nt
	v_readlane_b32 s1, v248, 14
	s_or_b32 s44, s42, 1
	s_ashr_i32 s45, s44, 31
	s_lshl_b64 s[16:17], s[44:45], 11
	s_mov_b32 s23, 0x9000
	s_movk_i32 s28, 0x7000
	v_mov_b32_e32 v158, 0
	v_mov_b32_e32 v174, 0
	v_mov_b32_e32 v246, 0
	s_waitcnt vmcnt(23)
	s_waitcnt lgkmcnt(0)
	v_lshlrev_b32_e32 v90, 16, v62
	v_and_b32_e32 v91, 0xffff0000, v62
	v_lshlrev_b32_e32 v62, 16, v63
	v_and_b32_e32 v63, 0xffff0000, v63
	s_waitcnt vmcnt(19)
	s_waitcnt lgkmcnt(0)
	v_lshlrev_b32_e32 v102, 16, v84
	v_and_b32_e32 v103, 0xffff0000, v84
	v_lshlrev_b32_e32 v84, 16, v85
	v_and_b32_e32 v85, 0xffff0000, v85
	s_waitcnt vmcnt(17)
	s_waitcnt lgkmcnt(0)
	v_pk_mul_f32 v[90:91], v[0:1], v[90:91]
	v_lshlrev_b32_e32 v96, 16, v68
	v_and_b32_e32 v97, 0xffff0000, v68
	v_lshlrev_b32_e32 v100, 16, v82
	v_and_b32_e32 v101, 0xffff0000, v82
	v_lshlrev_b32_e32 v82, 16, v83
	v_and_b32_e32 v83, 0xffff0000, v83
	v_lshlrev_b32_e32 v116, 16, v106
	v_pk_mul_f32 v[62:63], v[2:3], v[62:63]
	s_waitcnt vmcnt(13)
	s_waitcnt lgkmcnt(0)
	v_pk_mul_f32 v[122:123], v[6:7], v[84:85]
	s_waitcnt vmcnt(12)
	s_waitcnt lgkmcnt(0)
	v_pk_fma_f32 v[84:85], v[34:35], s[40:41], v[90:91] op_sel_hi:[1,0,1]
	v_and_b32_e32 v117, 0xffff0000, v106
	v_lshlrev_b32_e32 v34, 16, v107
	v_and_b32_e32 v35, 0xffff0000, v107
	v_lshlrev_b32_e32 v98, 16, v70
	v_and_b32_e32 v99, 0xffff0000, v70
	v_pk_mul_f32 v[104:105], v[16:17], v[96:97]
	v_pk_mul_f32 v[110:111], v[10:11], v[82:83]
	v_pk_mul_f32 v[118:119], v[8:9], v[100:101]
	v_pk_fma_f32 v[82:83], v[36:37], s[40:41], v[62:63] op_sel_hi:[1,0,1]
	s_waitcnt vmcnt(7)
	s_waitcnt lgkmcnt(0)
	v_pk_mul_f32 v[36:37], v[20:21], v[116:117]
	v_pk_mul_f32 v[34:35], v[22:23], v[34:35]
	v_pk_mul_f32 v[108:109], v[12:13], v[98:99]
	v_pk_fma_f32 v[98:99], v[38:39], s[40:41], v[104:105] op_sel_hi:[1,0,1]
	v_pk_fma_f32 v[104:105], v[46:47], s[40:41], v[118:119] op_sel_hi:[1,0,1]
	s_waitcnt vmcnt(6)
	s_waitcnt lgkmcnt(0)
	v_pk_fma_f32 v[116:117], v[56:57], s[40:41], v[34:35] op_sel_hi:[1,0,1]
	v_pk_fma_f32 v[118:119], v[54:55], s[40:41], v[36:37] op_sel_hi:[1,0,1]
	s_waitcnt vmcnt(5)
	s_waitcnt lgkmcnt(0)
	v_lshlrev_b32_e32 v34, 16, v112
	v_and_b32_e32 v35, 0xffff0000, v112
	v_lshlrev_b32_e32 v36, 16, v113
	v_and_b32_e32 v37, 0xffff0000, v113
	s_waitcnt vmcnt(4)
	s_waitcnt lgkmcnt(0)
	v_pk_mul_f32 v[34:35], v[24:25], v[34:35]
	v_pk_mul_f32 v[36:37], v[26:27], v[36:37]
	v_lshlrev_b32_e32 v68, 16, v69
	v_and_b32_e32 v69, 0xffff0000, v69
	v_lshlrev_b32_e32 v70, 16, v71
	v_and_b32_e32 v71, 0xffff0000, v71
	s_waitcnt vmcnt(3)
	s_waitcnt lgkmcnt(0)
	v_pk_fma_f32 v[124:125], v[60:61], s[40:41], v[36:37] op_sel_hi:[1,0,1]
	v_pk_fma_f32 v[126:127], v[58:59], s[40:41], v[34:35] op_sel_hi:[1,0,1]
	s_waitcnt vmcnt(2)
	s_waitcnt lgkmcnt(0)
	v_lshlrev_b32_e32 v34, 16, v114
	v_and_b32_e32 v35, 0xffff0000, v114
	v_lshlrev_b32_e32 v36, 16, v115
	v_and_b32_e32 v37, 0xffff0000, v115
	v_pk_mul_f32 v[68:69], v[18:19], v[68:69]
	v_pk_mul_f32 v[70:71], v[14:15], v[70:71]
	s_waitcnt vmcnt(1)
	s_waitcnt lgkmcnt(0)
	v_pk_mul_f32 v[34:35], v[28:29], v[34:35]
	v_pk_mul_f32 v[36:37], v[30:31], v[36:37]
	v_pk_fma_f32 v[96:97], v[40:41], s[40:41], v[68:69] op_sel_hi:[1,0,1]
	v_pk_fma_f32 v[100:101], v[44:45], s[40:41], v[70:71] op_sel_hi:[1,0,1]
	s_waitcnt vmcnt(0)
	s_waitcnt lgkmcnt(0)
; #define GAS __attribute__((address_space(1)))
; template <int l>
; __device__ __forceinline__ void layer_phases(Frame& F, const XcdBarrier& bar, const int lo, const int hi) {
;     ...
;                     f32x4 (&v)[8] = vv[rq]; float s = 0.f;
; #pragma unroll
;                     for (int j = 0; j < 8; ++j) s += (v[j].x + v[j].y) + (v[j].z + v[j].w);
;                     const float mean = wave_sum(s) * (1.f / D); float s2 = 0.f;
; #pragma unroll
;                     for (int j = 0; j < 8; ++j) { v[j] = v[j] - mean; s2 += (v[j].x * v[j].x + v[j].y * v[j].y) + (v[j].z * v[j].z + v[j].w * v[j].w); }
;                     const float rstd = 1.f / sqrtf(wave_sum(s2) * (1.f / D) + LN_EPS);
; #pragma unroll
;                     for (int j = 0; j < 8; ++j) { const int k = 4 * lq + 256 * j;
;                         const f32x4 xv = v[j] * rstd * *(const GAS f32x4*)(g1 + k) + *(const GAS f32x4*)(b1 + k);
	v_pk_fma_f32 v[68:69], v[94:95], s[40:41], v[36:37] op_sel_hi:[1,0,1]
	v_pk_fma_f32 v[70:71], v[92:93], s[40:41], v[34:35] op_sel_hi:[1,0,1]
	v_mov_b32_e32 v34, v84
	v_mov_b32_e32 v35, v98
	v_mov_b32_e32 v36, v85
	v_mov_b32_e32 v37, v99
	v_pk_add_f32 v[34:35], v[34:35], v[36:37]
	v_mov_b32_e32 v36, v82
	v_mov_b32_e32 v37, v96
	v_mov_b32_e32 v38, v83
	v_mov_b32_e32 v39, v97
	v_pk_mul_f32 v[120:121], v[4:5], v[102:103]
	v_pk_fma_f32 v[102:103], v[42:43], s[40:41], v[108:109] op_sel_hi:[1,0,1]
	v_pk_add_f32 v[36:37], v[36:37], v[38:39]
	v_mov_b32_e32 v38, v102
	v_pk_add_f32 v[34:35], v[34:35], v[36:37]
	v_pk_mov_b32 v[36:37], v[102:103], v[100:101] op_sel:[1,0]
	v_mov_b32_e32 v39, v101
	v_pk_add_f32 v[36:37], v[36:37], v[38:39]
	v_pk_fma_f32 v[90:91], v[48:49], s[40:41], v[110:111] op_sel_hi:[1,0,1]
	v_pk_fma_f32 v[108:109], v[52:53], s[40:41], v[122:123] op_sel_hi:[1,0,1]
	v_pk_fma_f32 v[110:111], v[50:51], s[40:41], v[120:121] op_sel_hi:[1,0,1]
	v_add_f32_e32 v34, 0, v34
	v_pk_add_f32 v[36:37], v[36:37], v[36:37] op_sel:[0,1] op_sel_hi:[1,0]
	v_add_f32_e32 v34, v34, v35
	v_add_f32_e32 v38, v104, v105
	v_add_f32_e32 v40, v90, v91
	v_mov_b32_e32 v35, v110
	v_mov_b32_e32 v37, v111
	v_mov_b32_e32 v39, v108
	v_mov_b32_e32 v41, v109
	v_pk_add_f32 v[34:35], v[34:35], v[36:37]
	v_pk_add_f32 v[36:37], v[38:39], v[40:41]
	v_mov_b32_e32 v38, v118
	v_pk_add_f32 v[34:35], v[34:35], v[36:37]
	v_pk_mov_b32 v[36:37], v[118:119], v[116:117] op_sel:[1,0]
	v_mov_b32_e32 v39, v117
	v_pk_add_f32 v[36:37], v[36:37], v[38:39]
	v_pk_add_f32 v[34:35], v[34:35], v[34:35] op_sel:[0,1] op_sel_hi:[1,0]
	v_pk_add_f32 v[36:37], v[36:37], v[36:37] op_sel:[0,1] op_sel_hi:[1,0]
	v_add_f32_e32 v38, v126, v127
	v_add_f32_e32 v40, v124, v125
	v_mov_b32_e32 v35, v70
	v_mov_b32_e32 v37, v71
	v_mov_b32_e32 v39, v68
	v_mov_b32_e32 v41, v69
	v_pk_add_f32 v[34:35], v[34:35], v[36:37]
	v_pk_add_f32 v[36:37], v[38:39], v[40:41]
	v_lshl_add_u64 v[112:113], s[0:1], 0, v[32:33]
	v_pk_add_f32 v[34:35], v[34:35], v[36:37]
	v_lshl_add_u64 v[114:115], s[24:25], 0, v[32:33]
	v_add_f32_e32 v34, v34, v35
	ds_bpermute_b32 v35, v73, v34
	ds_read_b128 v[92:95], v252 offset:0
	ds_read_b128 v[120:123], v252 offset:8192
	s_waitcnt lgkmcnt(0)
	v_add_f32_e32 v34, v34, v35
	ds_bpermute_b32 v35, v217, v34
	s_waitcnt lgkmcnt(0)
	v_add_f32_e32 v34, v34, v35
	ds_bpermute_b32 v35, v218, v34
	s_waitcnt lgkmcnt(0)
	v_add_f32_e32 v34, v34, v35
	ds_bpermute_b32 v35, v219, v34
	s_waitcnt lgkmcnt(0)
	v_add_f32_e32 v34, v34, v35
	ds_bpermute_b32 v35, v220, v34
	s_waitcnt lgkmcnt(0)
	v_add_f32_e32 v34, v34, v35
	ds_bpermute_b32 v35, v221, v34
	s_waitcnt lgkmcnt(0)
	v_add_f32_e32 v42, v34, v35
	v_fmamk_f32 v85, v42, 0xba000000, v85
	v_fmamk_f32 v99, v42, 0xba000000, v99
	v_fmamk_f32 v83, v42, 0xba000000, v83
	v_fmac_f32_e32 v84, 0xba000000, v42
	v_fmamk_f32 v97, v42, 0xba000000, v97
	v_fmac_f32_e32 v98, 0xba000000, v42
	v_mov_b32_e32 v36, v85
	v_mov_b32_e32 v37, v99
	v_fmac_f32_e32 v82, 0xba000000, v42
	v_fmac_f32_e32 v96, 0xba000000, v42
	v_mov_b32_e32 v34, v84
	v_mov_b32_e32 v35, v98
	v_pk_mul_f32 v[36:37], v[36:37], v[36:37]
	v_mov_b32_e32 v38, v83
	v_mov_b32_e32 v39, v97
	v_pk_fma_f32 v[34:35], v[34:35], v[34:35], v[36:37]
	v_mov_b32_e32 v36, v82
	v_mov_b32_e32 v37, v96
	v_pk_mul_f32 v[38:39], v[38:39], v[38:39]
	v_fmamk_f32 v103, v42, 0xba000000, v103
	v_pk_fma_f32 v[36:37], v[36:37], v[36:37], v[38:39]
	v_fmac_f32_e32 v102, 0xba000000, v42
	v_pk_add_f32 v[34:35], v[34:35], v[36:37]
	v_fmamk_f32 v101, v42, 0xba000000, v101
	v_fmac_f32_e32 v100, 0xba000000, v42
	v_pk_add_f32 v[34:35], v[34:35], v[34:35] op_sel_hi:[0,1]
	v_pk_mul_f32 v[36:37], v[100:101], v[100:101]
	v_pk_mul_f32 v[38:39], v[102:103], v[102:103]
	v_fmac_f32_e32 v104, 0xba000000, v42
	v_pk_mov_b32 v[40:41], v[38:39], v[36:37] op_sel:[1,0]
	v_mov_b32_e32 v39, v37
	v_fmamk_f32 v105, v42, 0xba000000, v105
	v_fmac_f32_e32 v90, 0xba000000, v42
	v_mul_f32_e32 v34, v104, v104
	v_pk_add_f32 v[36:37], v[40:41], v[38:39]
	v_fmamk_f32 v91, v42, 0xba000000, v91
	v_pk_fma_f32 v[38:39], v[104:105], v[104:105], v[34:35] op_sel_hi:[1,1,0]
	v_mul_f32_e32 v34, v90, v90
	v_pk_add_f32 v[36:37], v[36:37], v[36:37] op_sel_hi:[0,1]
	v_pk_fma_f32 v[40:41], v[90:91], v[90:91], v[34:35] op_sel_hi:[1,1,0]
	v_fmamk_f32 v109, v42, 0xba000000, v109
	v_fmac_f32_e32 v108, 0xba000000, v42
	v_fmamk_f32 v111, v42, 0xba000000, v111
	v_fmac_f32_e32 v110, 0xba000000, v42
	v_mul_f32_e32 v38, v110, v110
	v_mul_f32_e32 v40, v111, v111
	v_mul_f32_e32 v36, v108, v108
	v_mul_f32_e32 v34, v109, v109
	v_pk_add_f32 v[38:39], v[38:39], v[40:41]
	v_pk_add_f32 v[34:35], v[36:37], v[34:35]
	v_fmamk_f32 v119, v42, 0xba000000, v119
	v_pk_add_f32 v[34:35], v[38:39], v[34:35]
	v_fmac_f32_e32 v118, 0xba000000, v42
	v_fmamk_f32 v117, v42, 0xba000000, v117
	v_fmac_f32_e32 v116, 0xba000000, v42
	v_pk_add_f32 v[34:35], v[34:35], v[34:35] op_sel_hi:[0,1]
	v_pk_mul_f32 v[36:37], v[116:117], v[116:117]
	v_pk_mul_f32 v[38:39], v[118:119], v[118:119]
	v_fmac_f32_e32 v126, 0xba000000, v42
	v_pk_mov_b32 v[40:41], v[38:39], v[36:37] op_sel:[1,0]
	v_mov_b32_e32 v39, v37
	v_fmamk_f32 v127, v42, 0xba000000, v127
	v_fmac_f32_e32 v124, 0xba000000, v42
	v_mul_f32_e32 v34, v126, v126
	v_pk_add_f32 v[36:37], v[40:41], v[38:39]
	v_fmamk_f32 v125, v42, 0xba000000, v125
	v_pk_fma_f32 v[38:39], v[126:127], v[126:127], v[34:35] op_sel_hi:[1,1,0]
	v_mul_f32_e32 v34, v124, v124
	v_pk_add_f32 v[36:37], v[36:37], v[36:37] op_sel_hi:[0,1]
	v_pk_fma_f32 v[40:41], v[124:125], v[124:125], v[34:35] op_sel_hi:[1,1,0]
	v_fmamk_f32 v69, v42, 0xba000000, v69
	v_fmac_f32_e32 v68, 0xba000000, v42
	v_fmamk_f32 v71, v42, 0xba000000, v71
	v_fmac_f32_e32 v70, 0xba000000, v42
	v_mul_f32_e32 v38, v70, v70
	v_mul_f32_e32 v40, v71, v71
	v_mul_f32_e32 v36, v68, v68
	v_mul_f32_e32 v34, v69, v69
	v_pk_add_f32 v[38:39], v[38:39], v[40:41]
	v_pk_add_f32 v[34:35], v[36:37], v[34:35]
	s_nop 0
	v_pk_add_f32 v[34:35], v[38:39], v[34:35]
	s_nop 0
	v_add_f32_e32 v34, v34, v35
	ds_bpermute_b32 v35, v73, v34
	s_waitcnt lgkmcnt(0)
; #define GAS __attribute__((address_space(1)))
; __device__ __forceinline__ unsigned pk2(float lo, float hi) { return f2bf(lo) | (f2bf(hi) << 16); }
; __device__ __forceinline__ unsigned pk4_fp8(float a, float b, float c, float d) { int r = __builtin_amdgcn_cvt_pk_fp8_f32(a, b, 0, false); r = __builtin_amdgcn_cvt_pk_fp8_f32(c, d, r, true); return (unsigned)r; }
; template <int l>
; __device__ __forceinline__ void layer_phases(Frame& F, const XcdBarrier& bar, const int lo, const int hi) {
;     ...
;                     const float mean = wave_sum(s) * (1.f / D); float s2 = 0.f;
; #pragma unroll
;                     for (int j = 0; j < 8; ++j) { v[j] = v[j] - mean; s2 += (v[j].x * v[j].x + v[j].y * v[j].y) + (v[j].z * v[j].z + v[j].w * v[j].w); }
;                     const float rstd = 1.f / sqrtf(wave_sum(s2) * (1.f / D) + LN_EPS);
; #pragma unroll
;                     for (int j = 0; j < 8; ++j) { const int k = 4 * lq + 256 * j;
;                         const f32x4 xv = v[j] * rstd * *(const GAS f32x4*)(g1 + k) + *(const GAS f32x4*)(b1 + k);
;                         { v2u xo; xo.x = pk2(xv.x, xv.y); xo.y = pk2(xv.z, xv.w); *(GAS v2u*)(x1 + (size_t)m * D + k) = xo; }
;                         const f32x4 hv = xv * (*(const GAS f32x4*)(mrow + 8192 + k) + 1.0f) + *(const GAS f32x4*)(mrow + 6144 + k);
;                         v2u o; o.x = pk2(hv.x, hv.y); o.y = pk2(hv.z, hv.w);
;                         *(GAS unsigned*)(h2q + (size_t)m * D + k) = pk4_fp8(hv.x, hv.y, hv.z, hv.w);
	v_add_f32_e32 v32, v34, v35
	ds_bpermute_b32 v33, v217, v32
	s_waitcnt lgkmcnt(0)
	v_add_f32_e32 v36, v32, v33
	ds_bpermute_b32 v37, v218, v36
	v_lshl_add_u64 v[32:33], s[16:17], 0, v[86:87]
	v_lshl_add_u64 v[34:35], v[32:33], 2, s[20:21]
	v_lshl_add_u64 v[106:107], v[32:33], 1, s[26:27]
	global_load_dwordx4 v[60:63], v[34:35], off nt
	global_load_dwordx4 v[56:59], v[34:35], off offset:1024 nt
	global_load_dwordx4 v[48:51], v[34:35], off offset:2048 nt
	global_load_dwordx4 v[40:43], v[34:35], off offset:3072 nt
	s_waitcnt lgkmcnt(0)
	v_add_f32_e32 v32, v36, v37
	ds_bpermute_b32 v33, v219, v32
	global_load_dwordx2 v[140:141], v[106:107], off nt
	global_load_dwordx2 v[138:139], v[106:107], off offset:512 nt
	global_load_dwordx2 v[136:137], v[106:107], off offset:1024 nt
	global_load_dwordx2 v[132:133], v[106:107], off offset:1536 nt
	s_waitcnt lgkmcnt(0)
	v_add_f32_e32 v32, v32, v33
	ds_bpermute_b32 v33, v220, v32
	s_waitcnt lgkmcnt(0)
	v_add_f32_e32 v36, v32, v33
	ds_bpermute_b32 v37, v221, v36
	v_add_co_u32_e32 v32, vcc, s87, v34
	s_waitcnt lgkmcnt(0)
	v_add_f32_e32 v34, v36, v37
	v_addc_co_u32_e32 v33, vcc, 0, v35, vcc
	v_fmamk_f32 v34, v34, 0x3a000000, v223
	v_mul_f32_e32 v35, 0x4f800000, v34
	v_cmp_gt_f32_e32 vcc, s89, v34
	s_waitcnt vmcnt(3)
	s_waitcnt lgkmcnt(0)
	v_and_b32_e32 v159, 0xffff0000, v140
	v_cndmask_b32_e32 v80, v34, v35, vcc
	v_sqrt_f32_e32 v128, v80
	global_load_dwordx4 v[52:55], v[32:33], off nt
	global_load_dwordx4 v[44:47], v[32:33], off offset:1024 nt
	global_load_dwordx4 v[36:39], v[32:33], off offset:2048 nt
	s_nop 0
	global_load_dwordx4 v[32:35], v[32:33], off offset:3072 nt
	s_nop 0
	global_load_dwordx2 v[148:149], v[106:107], off offset:2048 nt
	global_load_dwordx2 v[146:147], v[106:107], off offset:2560 nt
	global_load_dwordx2 v[144:145], v[106:107], off offset:3072 nt
	global_load_dwordx2 v[142:143], v[106:107], off offset:3584 nt
	s_waitcnt vmcnt(10)
	s_waitcnt lgkmcnt(0)
	v_lshlrev_b32_e32 v160, 16, v138
	v_add_u32_e32 v129, -1, v128
	v_fma_f32 v130, -v129, v128, v80
	v_cmp_ge_f32_e64 s[14:15], 0, v130
	v_add_u32_e32 v130, 1, v128
	v_and_b32_e32 v161, 0xffff0000, v138
	v_cndmask_b32_e64 v129, v128, v129, s[14:15]
	v_fma_f32 v128, -v130, v128, v80
	v_cmp_lt_f32_e64 s[14:15], 0, v128
	v_lshlrev_b32_e32 v138, 16, v139
	v_and_b32_e32 v139, 0xffff0000, v139
	v_cndmask_b32_e64 v128, v129, v130, s[14:15]
	v_mul_f32_e32 v129, 0x37800000, v128
	v_cndmask_b32_e32 v128, v128, v129, vcc
	v_cmp_class_f32_e32 vcc, v80, v224
	s_waitcnt vmcnt(9)
	s_waitcnt lgkmcnt(0)
	v_lshlrev_b32_e32 v162, 16, v136
	v_and_b32_e32 v163, 0xffff0000, v136
	v_cndmask_b32_e32 v80, v128, v80, vcc
	v_div_scale_f32 v128, s[0:1], v80, v80, 1.0
	v_rcp_f32_e32 v129, v128
	s_lshl_b64 s[0:1], s[42:43], 12
	s_add_u32 s0, s3, s0
	s_addc_u32 s1, s41, s1
	v_fma_f32 v106, -v128, v129, 1.0
	v_fmac_f32_e32 v129, v106, v129
	v_div_scale_f32 v106, vcc, 1.0, v80, 1.0
	v_mul_f32_e32 v107, v106, v129
	v_fma_f32 v130, -v128, v107, v106
	v_fmac_f32_e32 v107, v130, v129
	v_fma_f32 v106, -v128, v107, v106
	v_div_fmas_f32 v106, v106, v129, v107
	v_div_fixup_f32 v80, v106, v80, 1.0
	v_pk_mul_f32 v[84:85], v[84:85], v[80:81] op_sel_hi:[1,0]
	v_pk_mul_f32 v[82:83], v[82:83], v[80:81] op_sel_hi:[1,0]
	v_pk_fma_f32 v[134:135], v[92:93], v[84:85], v[120:121]
	v_pk_fma_f32 v[106:107], v[94:95], v[82:83], v[122:123]
	v_bfe_u32 v82, v134, 16, 1
	v_add3_u32 v82, v134, v82, s90
	v_bfe_u32 v83, v135, 16, 1
	v_lshrrev_b32_e32 v82, 16, v82
	v_add3_u32 v83, v135, v83, s90
	v_and_or_b32 v82, v83, s86, v82
	v_bfe_u32 v83, v106, 16, 1
	v_add3_u32 v83, v106, v83, s90
	v_bfe_u32 v84, v107, 16, 1
	v_lshrrev_b32_e32 v83, 16, v83
	v_add3_u32 v84, v107, v84, s90
	v_lshlrev_b64 v[128:129], 1, v[86:87]
	v_and_or_b32 v83, v84, s86, v83
	v_lshl_add_u64 v[130:131], s[0:1], 0, v[128:129]
	global_store_dwordx2 v[130:131], v[82:83], off
	v_add_co_u32_e32 v82, vcc, s23, v88
	s_add_u32 s0, s50, s18
	s_nop 0
	v_addc_co_u32_e32 v83, vcc, 0, v89, vcc
	v_add_co_u32_e32 v84, vcc, s28, v88
	s_addc_u32 s1, s51, s19
	s_nop 0
	v_addc_co_u32_e32 v85, vcc, 0, v89, vcc
	ds_read_b128 v[92:95], v252 offset:16384
	ds_read_b128 v[120:123], v252 offset:24576
	v_pk_mul_f32 v[96:97], v[96:97], v[80:81] op_sel_hi:[1,0]
	v_pk_mul_f32 v[100:101], v[100:101], v[80:81] op_sel_hi:[1,0]
	v_pk_mul_f32 v[90:91], v[90:91], v[80:81] op_sel_hi:[1,0]
	v_pk_mul_f32 v[110:111], v[110:111], v[80:81] op_sel_hi:[1,0]
	v_pk_mul_f32 v[108:109], v[108:109], v[80:81] op_sel_hi:[1,0]
	v_pk_mul_f32 v[118:119], v[118:119], v[80:81] op_sel_hi:[1,0]
	v_pk_mul_f32 v[116:117], v[116:117], v[80:81] op_sel_hi:[1,0]
	v_pk_mul_f32 v[126:127], v[126:127], v[80:81] op_sel_hi:[1,0]
	v_pk_mul_f32 v[124:125], v[124:125], v[80:81] op_sel_hi:[1,0]
	v_lshlrev_b32_e32 v136, 16, v137
	v_and_b32_e32 v137, 0xffff0000, v137
	s_waitcnt vmcnt(9)
	s_waitcnt lgkmcnt(0)
	v_lshlrev_b32_e32 v164, 16, v132
	v_and_b32_e32 v165, 0xffff0000, v132
	v_lshlrev_b32_e32 v132, 16, v133
	v_and_b32_e32 v133, 0xffff0000, v133
	s_waitcnt vmcnt(1)
	s_waitcnt lgkmcnt(0)
; #define GAS __attribute__((address_space(1)))
; #define LAS __attribute__((address_space(3)))
; __device__ __forceinline__ unsigned pk2(float lo, float hi) { return f2bf(lo) | (f2bf(hi) << 16); }
; __device__ __forceinline__ unsigned pk4_fp8(float a, float b, float c, float d) { int r = __builtin_amdgcn_cvt_pk_fp8_f32(a, b, 0, false); r = __builtin_amdgcn_cvt_pk_fp8_f32(c, d, r, true); return (unsigned)r; }
; template <int l>
; __device__ __forceinline__ void layer_phases(Frame& F, const XcdBarrier& bar, const int lo, const int hi) {
;     ...
;                     for (int j = 0; j < 8; ++j) { const int k = 4 * lq + 256 * j;
;                         const f32x4 xv = v[j] * rstd * *(const GAS f32x4*)(g1 + k) + *(const GAS f32x4*)(b1 + k);
;                         { v2u xo; xo.x = pk2(xv.x, xv.y); xo.y = pk2(xv.z, xv.w); *(GAS v2u*)(x1 + (size_t)m * D + k) = xo; }
;                         const f32x4 hv = xv * (*(const GAS f32x4*)(mrow + 8192 + k) + 1.0f) + *(const GAS f32x4*)(mrow + 6144 + k);
;                         v2u o; o.x = pk2(hv.x, hv.y); o.y = pk2(hv.z, hv.w);
;                         *(GAS unsigned*)(h2q + (size_t)m * D + k) = pk4_fp8(hv.x, hv.y, hv.z, hv.w);
;                         const int chunk = (lq >> 1) + 32 * j;
;                         *(LAS v2u*)(h2s + rloc * 4096 + ((chunk ^ (rloc & 15)) << 4) + (lq & 1) * 8) = o; }
	v_lshlrev_b32_e32 v172, 16, v142
	v_and_b32_e32 v173, 0xffff0000, v142
	v_lshlrev_b32_e32 v142, 16, v143
	v_and_b32_e32 v143, 0xffff0000, v143
	v_pk_mul_f32 v[142:143], v[30:31], v[142:143]
	v_lshlrev_b32_e32 v168, 16, v146
	v_and_b32_e32 v169, 0xffff0000, v146
	v_lshlrev_b32_e32 v146, 16, v147
	v_and_b32_e32 v147, 0xffff0000, v147
	v_lshlrev_b32_e32 v170, 16, v144
	v_and_b32_e32 v171, 0xffff0000, v144
	v_lshlrev_b32_e32 v144, 16, v145
	v_and_b32_e32 v145, 0xffff0000, v145
	v_pk_mul_f32 v[18:19], v[18:19], v[138:139]
	v_pk_mul_f32 v[16:17], v[16:17], v[160:161]
	v_pk_mul_f32 v[14:15], v[14:15], v[136:137]
	v_pk_mul_f32 v[10:11], v[10:11], v[132:133]
	v_pk_mul_f32 v[8:9], v[8:9], v[164:165]
	v_pk_mul_f32 v[132:133], v[20:21], v[168:169]
	v_pk_mul_f32 v[136:137], v[22:23], v[146:147]
	v_pk_mul_f32 v[138:139], v[24:25], v[170:171]
	v_pk_fma_f32 v[24:25], v[58:59], s[40:41], v[18:19] op_sel_hi:[1,0,1]
	v_pk_fma_f32 v[18:19], v[40:41], s[40:41], v[8:9] op_sel_hi:[1,0,1]
	v_pk_fma_f32 v[8:9], v[46:47], s[40:41], v[136:137] op_sel_hi:[1,0,1]
	v_lshlrev_b32_e32 v166, 16, v148
	v_and_b32_e32 v167, 0xffff0000, v148
	v_lshlrev_b32_e32 v148, 16, v149
	v_and_b32_e32 v149, 0xffff0000, v149
	v_pk_mul_f32 v[12:13], v[12:13], v[162:163]
	v_pk_mul_f32 v[4:5], v[4:5], v[166:167]
	v_pk_mul_f32 v[6:7], v[6:7], v[148:149]
	v_pk_fma_f32 v[20:21], v[50:51], s[40:41], v[14:15] op_sel_hi:[1,0,1]
	v_pk_fma_f32 v[22:23], v[48:49], s[40:41], v[12:13] op_sel_hi:[1,0,1]
	v_pk_fma_f32 v[12:13], v[54:55], s[40:41], v[6:7] op_sel_hi:[1,0,1]
	v_pk_fma_f32 v[14:15], v[52:53], s[40:41], v[4:5] op_sel_hi:[1,0,1]
	v_pk_fma_f32 v[6:7], v[36:37], s[40:41], v[138:139] op_sel_hi:[1,0,1]
	v_mov_b32_e32 v37, v24
	v_pk_mov_b32 v[48:49], v[22:23], v[20:21] op_sel:[1,0]
	v_mov_b32_e32 v50, v22
	v_mov_b32_e32 v51, v21
	v_add_f32_e32 v52, v18, v19
	v_mov_b32_e32 v53, v12
	v_mov_b32_e32 v55, v13
	s_waitcnt lgkmcnt(0)
	v_pk_add_f32 v[92:93], v[92:93], 1.0 op_sel_hi:[1,0]
	s_waitcnt lgkmcnt(0)
	v_pk_fma_f32 v[92:93], v[92:93], v[134:135], v[120:121]
	v_mov_b32_e32 v120, 0
	v_cvt_pk_fp8_f32 v120, v92, v93
	v_pk_add_f32 v[94:95], v[94:95], 1.0 op_sel_hi:[1,0]
	v_lshl_add_u64 v[134:135], s[0:1], 0, v[86:87]
	v_pk_fma_f32 v[94:95], v[94:95], v[106:107], v[122:123]
	s_mov_b64 s[0:1], 0x8000
	v_cvt_pk_fp8_f32 v120, v94, v95 op_sel:[0,0,1]
	v_lshl_add_u64 v[122:123], v[88:89], 0, s[0:1]
	s_mov_b64 s[0:1], 0x6000
	global_store_dword v[134:135], v120, off
	ds_read_b128 v[150:153], v252 offset:1024
	ds_read_b128 v[154:157], v252 offset:9216
	v_lshl_add_u64 v[120:121], v[88:89], 0, s[0:1]
	v_pk_mul_f32 v[88:89], v[98:99], v[80:81] op_sel_hi:[1,0]
	s_lshl_b64 s[0:1], s[44:45], 12
	s_add_u32 s0, s3, s0
	s_addc_u32 s1, s41, s1
	s_waitcnt lgkmcnt(0)
	v_pk_fma_f32 v[106:107], v[152:153], v[96:97], v[156:157]
	v_pk_fma_f32 v[88:89], v[150:151], v[88:89], v[154:155]
	v_bfe_u32 v98, v106, 16, 1
	v_bfe_u32 v96, v88, 16, 1
	v_bfe_u32 v97, v89, 16, 1
	v_bfe_u32 v99, v107, 16, 1
	v_add3_u32 v96, v88, v96, s90
	v_add3_u32 v98, v106, v98, s90
	v_add3_u32 v97, v89, v97, s90
	v_add3_u32 v99, v107, v99, s90
	v_lshrrev_b32_e32 v96, 16, v96
	v_lshrrev_b32_e32 v98, 16, v98
	v_and_or_b32 v96, v97, s86, v96
	v_and_or_b32 v97, v99, s86, v98
	global_store_dwordx2 v[130:131], v[96:97], off offset:512
	ds_read_b128 v[96:99], v252 offset:17408
	s_nop 0
	ds_read_b128 v[150:153], v252 offset:25600
	v_mov_b32_e32 v154, 0
	s_waitcnt lgkmcnt(0)
	v_pk_add_f32 v[96:97], v[96:97], 1.0 op_sel_hi:[1,0]
	s_waitcnt lgkmcnt(0)
	v_pk_fma_f32 v[96:97], v[96:97], v[88:89], v[150:151]
	v_pk_add_f32 v[88:89], v[98:99], 1.0 op_sel_hi:[1,0]
	v_cvt_pk_fp8_f32 v154, v96, v97
	v_pk_fma_f32 v[98:99], v[88:89], v[106:107], v[152:153]
	v_pk_mul_f32 v[88:89], v[102:103], v[80:81] op_sel_hi:[1,0]
	v_cvt_pk_fp8_f32 v154, v98, v99 op_sel:[0,0,1]
	global_store_dword v[134:135], v154, off offset:256
	ds_read_b128 v[150:153], v252 offset:2048
	s_nop 0
	ds_read_b128 v[154:157], v252 offset:10240
	s_waitcnt lgkmcnt(0)
	v_pk_fma_f32 v[106:107], v[152:153], v[100:101], v[156:157]
	v_pk_fma_f32 v[88:89], v[150:151], v[88:89], v[154:155]
	v_bfe_u32 v102, v106, 16, 1
	v_bfe_u32 v100, v88, 16, 1
	v_bfe_u32 v101, v89, 16, 1
	v_bfe_u32 v103, v107, 16, 1
	v_add3_u32 v100, v88, v100, s90
	v_add3_u32 v102, v106, v102, s90
	v_add3_u32 v101, v89, v101, s90
	v_add3_u32 v103, v107, v103, s90
	v_lshrrev_b32_e32 v100, 16, v100
	v_lshrrev_b32_e32 v102, 16, v102
	v_and_or_b32 v100, v101, s86, v100
	v_and_or_b32 v101, v103, s86, v102
	global_store_dwordx2 v[130:131], v[100:101], off offset:1024
	ds_read_b128 v[100:103], v252 offset:18432
	s_nop 0
	ds_read_b128 v[150:153], v252 offset:26624
	v_mov_b32_e32 v154, 0
	s_waitcnt lgkmcnt(0)
	v_pk_add_f32 v[100:101], v[100:101], 1.0 op_sel_hi:[1,0]
	s_waitcnt lgkmcnt(0)
	v_pk_fma_f32 v[100:101], v[100:101], v[88:89], v[150:151]
	v_pk_add_f32 v[88:89], v[102:103], 1.0 op_sel_hi:[1,0]
	v_cvt_pk_fp8_f32 v154, v100, v101
	v_pk_fma_f32 v[102:103], v[88:89], v[106:107], v[152:153]
	v_pk_mul_f32 v[88:89], v[104:105], v[80:81] op_sel_hi:[1,0]
	v_cvt_pk_fp8_f32 v154, v102, v103 op_sel:[0,0,1]
	global_store_dword v[134:135], v154, off offset:512
	ds_read_b128 v[150:153], v252 offset:3072
	s_nop 0
	ds_read_b128 v[154:157], v252 offset:11264
	s_waitcnt lgkmcnt(0)
	v_pk_fma_f32 v[152:153], v[90:91], v[152:153], v[156:157]
	v_pk_fma_f32 v[150:151], v[88:89], v[150:151], v[154:155]
	v_bfe_u32 v90, v152, 16, 1
	v_bfe_u32 v88, v150, 16, 1
	v_bfe_u32 v89, v151, 16, 1
	v_bfe_u32 v91, v153, 16, 1
	v_add3_u32 v88, v150, v88, s90
	v_add3_u32 v90, v152, v90, s90
	v_add3_u32 v89, v151, v89, s90
	v_add3_u32 v91, v153, v91, s90
	v_lshrrev_b32_e32 v88, 16, v88
	v_lshrrev_b32_e32 v90, 16, v90
	v_and_or_b32 v88, v89, s86, v88
	v_and_or_b32 v89, v91, s86, v90
	global_store_dwordx2 v[130:131], v[88:89], off offset:1536
	ds_read_b128 v[88:91], v252 offset:19456
	s_nop 0
	ds_read_b128 v[104:107], v252 offset:27648
	v_mov_b32_e32 v154, 0
	s_waitcnt lgkmcnt(0)
; #define GAS __attribute__((address_space(1)))
; #define LAS __attribute__((address_space(3)))
; __device__ __forceinline__ unsigned pk2(float lo, float hi) { return f2bf(lo) | (f2bf(hi) << 16); }
; __device__ __forceinline__ unsigned pk4_fp8(float a, float b, float c, float d) { int r = __builtin_amdgcn_cvt_pk_fp8_f32(a, b, 0, false); r = __builtin_amdgcn_cvt_pk_fp8_f32(c, d, r, true); return (unsigned)r; }
; __device__ __forceinline__ f32x4 bf4(unsigned a, unsigned b) { return (f32x4){bflo(a), bfhi(a), bflo(b), bfhi(b)}; }
; template <int l>
; __device__ __forceinline__ void layer_phases(Frame& F, const XcdBarrier& bar, const int lo, const int hi) {
;     ...
;                     for (int j = 0; j < 8; ++j) { const size_t off = (size_t)(m0 + 2 * rp + rr) * D + 4 * lq + 256 * j;
;                         f32x4 xv; if (l == 0) xv = __builtin_nontemporal_load((const GAS f32x4*)(xin + off)); else { const v2u xw_ = __builtin_nontemporal_load((const GAS v2u*)(xinb + off)); xv = bf4(xw_.x, xw_.y); } const v2u mw = __builtin_nontemporal_load((const GAS v2u*)(mixb + off)); const f32x4 gv = *(const GAS f32x4*)(mrow + 4096 + 4 * lq + 256 * j);
;                         vv[rr][j] = xv * ALPHA + gv * (f32x4){bflo(mw.x), bfhi(mw.x), bflo(mw.y), bfhi(mw.y)}; }
;     ...
;                     for (int j = 0; j < 8; ++j) { const int k = 4 * lq + 256 * j;
;                         const f32x4 xv = v[j] * rstd * *(const GAS f32x4*)(g1 + k) + *(const GAS f32x4*)(b1 + k);
;                         { v2u xo; xo.x = pk2(xv.x, xv.y); xo.y = pk2(xv.z, xv.w); *(GAS v2u*)(x1 + (size_t)m * D + k) = xo; }
;                         const f32x4 hv = xv * (*(const GAS f32x4*)(mrow + 8192 + k) + 1.0f) + *(const GAS f32x4*)(mrow + 6144 + k);
;                         v2u o; o.x = pk2(hv.x, hv.y); o.y = pk2(hv.z, hv.w);
;                         *(GAS unsigned*)(h2q + (size_t)m * D + k) = pk4_fp8(hv.x, hv.y, hv.z, hv.w);
;                         const int chunk = (lq >> 1) + 32 * j;
;                         *(LAS v2u*)(h2s + rloc * 4096 + ((chunk ^ (rloc & 15)) << 4) + (lq & 1) * 8) = o; }
	v_pk_add_f32 v[88:89], v[88:89], 1.0 op_sel_hi:[1,0]
	s_waitcnt lgkmcnt(0)
	v_pk_fma_f32 v[104:105], v[150:151], v[88:89], v[104:105]
	v_pk_add_f32 v[90:91], v[90:91], 1.0 op_sel_hi:[1,0]
	v_cvt_pk_fp8_f32 v154, v104, v105
	v_pk_fma_f32 v[106:107], v[152:153], v[90:91], v[106:107]
	v_add_co_u32_e32 v88, vcc, s87, v112
	v_cvt_pk_fp8_f32 v154, v106, v107 op_sel:[0,0,1]
	s_nop 0
	v_addc_co_u32_e32 v89, vcc, 0, v113, vcc
	v_add_co_u32_e32 v90, vcc, s87, v114
	global_store_dword v[134:135], v154, off offset:768
	s_nop 0
	v_addc_co_u32_e32 v91, vcc, 0, v115, vcc
	ds_read_b128 v[150:153], v252 offset:4096
	ds_read_b128 v[154:157], v252 offset:12288
	s_waitcnt lgkmcnt(0)
	v_pk_fma_f32 v[156:157], v[108:109], v[152:153], v[156:157]
	v_pk_fma_f32 v[154:155], v[110:111], v[150:151], v[154:155]
	v_bfe_u32 v110, v156, 16, 1
	v_bfe_u32 v108, v154, 16, 1
	v_bfe_u32 v109, v155, 16, 1
	v_bfe_u32 v111, v157, 16, 1
	v_add3_u32 v108, v154, v108, s90
	v_add3_u32 v110, v156, v110, s90
	v_add3_u32 v109, v155, v109, s90
	v_add3_u32 v111, v157, v111, s90
	v_lshrrev_b32_e32 v108, 16, v108
	v_lshrrev_b32_e32 v110, 16, v110
	v_and_or_b32 v108, v109, s86, v108
	v_and_or_b32 v109, v111, s86, v110
	global_store_dwordx2 v[130:131], v[108:109], off offset:2048
	ds_read_b128 v[108:111], v252 offset:20480
	s_nop 0
	ds_read_b128 v[150:153], v252 offset:28672
	s_waitcnt lgkmcnt(0)
	v_pk_add_f32 v[108:109], v[108:109], 1.0 op_sel_hi:[1,0]
	s_waitcnt lgkmcnt(0)
	v_pk_fma_f32 v[108:109], v[154:155], v[108:109], v[150:151]
	v_pk_add_f32 v[110:111], v[110:111], 1.0 op_sel_hi:[1,0]
	v_cvt_pk_fp8_f32 v158, v108, v109
	v_pk_fma_f32 v[110:111], v[156:157], v[110:111], v[152:153]
	s_nop 0
	v_cvt_pk_fp8_f32 v158, v110, v111 op_sel:[0,0,1]
	global_store_dword v[134:135], v158, off offset:1024
	ds_read_b128 v[150:153], v252 offset:5120
	ds_read_b128 v[154:157], v252 offset:13312
	v_mov_b32_e32 v158, 0
	s_waitcnt lgkmcnt(0)
	v_pk_fma_f32 v[156:157], v[116:117], v[152:153], v[156:157]
	v_pk_fma_f32 v[154:155], v[118:119], v[150:151], v[154:155]
	v_bfe_u32 v118, v156, 16, 1
	v_bfe_u32 v116, v154, 16, 1
	v_bfe_u32 v117, v155, 16, 1
	v_bfe_u32 v119, v157, 16, 1
	v_add3_u32 v116, v154, v116, s90
	v_add3_u32 v118, v156, v118, s90
	v_add3_u32 v117, v155, v117, s90
	v_add3_u32 v119, v157, v119, s90
	v_lshrrev_b32_e32 v116, 16, v116
	v_lshrrev_b32_e32 v118, 16, v118
	v_and_or_b32 v116, v117, s86, v116
	v_and_or_b32 v117, v119, s86, v118
	global_store_dwordx2 v[130:131], v[116:117], off offset:2560
	ds_read_b128 v[116:119], v252 offset:21504
	s_nop 0
	ds_read_b128 v[150:153], v252 offset:29696
	s_waitcnt lgkmcnt(0)
	v_pk_add_f32 v[116:117], v[116:117], 1.0 op_sel_hi:[1,0]
	s_waitcnt lgkmcnt(0)
	v_pk_fma_f32 v[116:117], v[154:155], v[116:117], v[150:151]
	v_pk_add_f32 v[118:119], v[118:119], 1.0 op_sel_hi:[1,0]
	v_cvt_pk_fp8_f32 v158, v116, v117
	v_pk_fma_f32 v[118:119], v[156:157], v[118:119], v[152:153]
	s_nop 0
	v_cvt_pk_fp8_f32 v158, v118, v119 op_sel:[0,0,1]
	global_store_dword v[134:135], v158, off offset:1280
	ds_read_b128 v[150:153], v252 offset:6144
	ds_read_b128 v[154:157], v252 offset:14336
	v_lshlrev_b32_e32 v158, 16, v140
	v_pk_mul_f32 v[0:1], v[0:1], v[158:159]
	v_lshlrev_b32_e32 v140, 16, v141
	v_pk_fma_f32 v[30:31], v[60:61], s[40:41], v[0:1] op_sel_hi:[1,0,1]
	v_and_b32_e32 v141, 0xffff0000, v141
	v_pk_mul_f32 v[2:3], v[2:3], v[140:141]
	v_pk_mul_f32 v[140:141], v[26:27], v[144:145]
	v_pk_fma_f32 v[26:27], v[56:57], s[40:41], v[16:17] op_sel_hi:[1,0,1]
	v_pk_fma_f32 v[16:17], v[42:43], s[40:41], v[10:11] op_sel_hi:[1,0,1]
	v_pk_fma_f32 v[10:11], v[44:45], s[40:41], v[132:133] op_sel_hi:[1,0,1]
	v_pk_mul_f32 v[144:145], v[28:29], v[172:173]
	v_pk_fma_f32 v[28:29], v[62:63], s[40:41], v[2:3] op_sel_hi:[1,0,1]
	v_pk_fma_f32 v[4:5], v[38:39], s[40:41], v[140:141] op_sel_hi:[1,0,1]
	v_pk_fma_f32 v[2:3], v[32:33], s[40:41], v[144:145] op_sel_hi:[1,0,1]
	v_mov_b32_e32 v32, v30
	v_mov_b32_e32 v33, v26
	v_mov_b32_e32 v36, v28
	v_mov_b32_e32 v38, v29
	v_mov_b32_e32 v39, v25
	v_add_f32_e32 v54, v16, v17
	v_mov_b32_e32 v57, v14
	v_pk_mov_b32 v[58:59], v[10:11], v[8:9] op_sel:[1,0]
	v_mov_b32_e32 v60, v10
	v_mov_b32_e32 v61, v9
	v_add_f32_e32 v62, v6, v7
	v_add_f32_e32 v132, v4, v5
	s_waitcnt lgkmcnt(0)
	v_pk_fma_f32 v[156:157], v[124:125], v[152:153], v[156:157]
	v_pk_fma_f32 v[154:155], v[126:127], v[150:151], v[154:155]
	v_bfe_u32 v126, v156, 16, 1
	v_bfe_u32 v124, v154, 16, 1
	v_bfe_u32 v125, v155, 16, 1
	v_bfe_u32 v127, v157, 16, 1
	v_add3_u32 v124, v154, v124, s90
	v_add3_u32 v126, v156, v126, s90
	v_add3_u32 v125, v155, v125, s90
	v_add3_u32 v127, v157, v127, s90
	v_lshrrev_b32_e32 v124, 16, v124
	v_lshrrev_b32_e32 v126, 16, v126
	v_and_or_b32 v124, v125, s86, v124
	v_and_or_b32 v125, v127, s86, v126
	global_store_dwordx2 v[130:131], v[124:125], off offset:3072
	ds_read_b128 v[124:127], v252 offset:22528
	s_nop 0
	ds_read_b128 v[150:153], v252 offset:30720
	s_waitcnt lgkmcnt(0)
	v_pk_add_f32 v[0:1], v[124:125], 1.0 op_sel_hi:[1,0]
	s_waitcnt lgkmcnt(0)
; #define GAS __attribute__((address_space(1)))
; #define LAS __attribute__((address_space(3)))
; __device__ __forceinline__ unsigned pk2(float lo, float hi) { return f2bf(lo) | (f2bf(hi) << 16); }
; __device__ __forceinline__ unsigned pk4_fp8(float a, float b, float c, float d) { int r = __builtin_amdgcn_cvt_pk_fp8_f32(a, b, 0, false); r = __builtin_amdgcn_cvt_pk_fp8_f32(c, d, r, true); return (unsigned)r; }
; template <int l>
; __device__ __forceinline__ void layer_phases(Frame& F, const XcdBarrier& bar, const int lo, const int hi) {
;     ...
; #pragma unroll
;                 for (int rq = 0; rq < 2; ++rq) { const int rr = 2 * rp + rq, m = m0 + rr, rloc = 4 * F.wave + rr;
;                     f32x4 (&v)[8] = vv[rq]; float s = 0.f;
; #pragma unroll
;                     for (int j = 0; j < 8; ++j) s += (v[j].x + v[j].y) + (v[j].z + v[j].w);
;                     const float mean = wave_sum(s) * (1.f / D); float s2 = 0.f;
; #pragma unroll
;                     for (int j = 0; j < 8; ++j) { v[j] = v[j] - mean; s2 += (v[j].x * v[j].x + v[j].y * v[j].y) + (v[j].z * v[j].z + v[j].w * v[j].w); }
;                     const float rstd = 1.f / sqrtf(wave_sum(s2) * (1.f / D) + LN_EPS);
; #pragma unroll
;                     for (int j = 0; j < 8; ++j) { const int k = 4 * lq + 256 * j;
;                         const f32x4 xv = v[j] * rstd * *(const GAS f32x4*)(g1 + k) + *(const GAS f32x4*)(b1 + k);
;                         { v2u xo; xo.x = pk2(xv.x, xv.y); xo.y = pk2(xv.z, xv.w); *(GAS v2u*)(x1 + (size_t)m * D + k) = xo; }
;                         const f32x4 hv = xv * (*(const GAS f32x4*)(mrow + 8192 + k) + 1.0f) + *(const GAS f32x4*)(mrow + 6144 + k);
;                         v2u o; o.x = pk2(hv.x, hv.y); o.y = pk2(hv.z, hv.w);
;                         *(GAS unsigned*)(h2q + (size_t)m * D + k) = pk4_fp8(hv.x, hv.y, hv.z, hv.w);
;                         const int chunk = (lq >> 1) + 32 * j;
;                         *(LAS v2u*)(h2s + rloc * 4096 + ((chunk ^ (rloc & 15)) << 4) + (lq & 1) * 8) = o; }
	v_pk_fma_f32 v[124:125], v[154:155], v[0:1], v[150:151]
	v_pk_add_f32 v[0:1], v[126:127], 1.0 op_sel_hi:[1,0]
	v_cvt_pk_fp8_f32 v174, v124, v125
	v_pk_fma_f32 v[126:127], v[156:157], v[0:1], v[152:153]
	v_pk_fma_f32 v[0:1], v[34:35], s[40:41], v[142:143] op_sel_hi:[1,0,1]
	v_mov_b32_e32 v34, v31
	v_cvt_pk_fp8_f32 v174, v126, v127 op_sel:[0,0,1]
	v_mov_b32_e32 v35, v27
	v_pk_add_f32 v[32:33], v[32:33], v[34:35]
	v_pk_add_f32 v[34:35], v[36:37], v[38:39]
	global_store_dword v[134:135], v174, off offset:1536
	ds_read_b128 v[40:43], v252 offset:7168
	ds_read_b128 v[44:47], v252 offset:15360
	v_pk_add_f32 v[36:37], v[48:49], v[50:51]
	v_pk_add_f32 v[32:33], v[32:33], v[34:35]
	v_pk_add_f32 v[34:35], v[36:37], v[36:37] op_sel:[0,1] op_sel_hi:[1,0]
	v_add_f32_e32 v32, 0, v32
	v_mov_b32_e32 v35, v15
	v_add_f32_e32 v56, v32, v33
	v_pk_add_f32 v[38:39], v[52:53], v[54:55]
	v_pk_add_f32 v[32:33], v[56:57], v[34:35]
	v_pk_add_f32 v[48:49], v[58:59], v[60:61]
	v_pk_add_f32 v[32:33], v[32:33], v[38:39]
	v_pk_add_f32 v[36:37], v[48:49], v[48:49] op_sel:[0,1] op_sel_hi:[1,0]
	v_pk_add_f32 v[32:33], v[32:33], v[32:33] op_sel:[0,1] op_sel_hi:[1,0]
	v_mov_b32_e32 v63, v0
	v_mov_b32_e32 v133, v1
	v_mov_b32_e32 v37, v3
	v_mov_b32_e32 v33, v2
	v_pk_add_f32 v[50:51], v[62:63], v[132:133]
	v_pk_add_f32 v[32:33], v[32:33], v[36:37]
	v_pk_mul_f32 v[34:35], v[68:69], v[80:81] op_sel_hi:[1,0]
	v_pk_add_f32 v[32:33], v[32:33], v[50:51]
	s_waitcnt lgkmcnt(0)
	v_pk_fma_f32 v[42:43], v[34:35], v[42:43], v[46:47]
	v_add_f32_e32 v32, v32, v33
	ds_bpermute_b32 v33, v73, v32
	v_bfe_u32 v34, v42, 16, 1
	v_bfe_u32 v35, v43, 16, 1
	v_add3_u32 v34, v42, v34, s90
	v_add3_u32 v35, v43, v35, s90
	s_waitcnt lgkmcnt(0)
	v_add_f32_e32 v32, v32, v33
	ds_bpermute_b32 v33, v217, v32
	v_lshrrev_b32_e32 v34, 16, v34
	s_waitcnt lgkmcnt(0)
	v_add_f32_e32 v32, v32, v33
	ds_bpermute_b32 v33, v218, v32
	s_waitcnt lgkmcnt(0)
	v_add_f32_e32 v32, v32, v33
	ds_bpermute_b32 v33, v219, v32
	s_waitcnt lgkmcnt(0)
	v_add_f32_e32 v32, v32, v33
	ds_bpermute_b32 v33, v220, v32
	s_waitcnt lgkmcnt(0)
	v_add_f32_e32 v48, v32, v33
	v_pk_mul_f32 v[32:33], v[70:71], v[80:81] op_sel_hi:[1,0]
	v_mov_b32_e32 v71, 0
	v_pk_fma_f32 v[40:41], v[32:33], v[40:41], v[44:45]
	ds_bpermute_b32 v44, v221, v48
	v_bfe_u32 v32, v40, 16, 1
	v_bfe_u32 v33, v41, 16, 1
	v_add3_u32 v32, v40, v32, s90
	v_add3_u32 v33, v41, v33, s90
	v_lshrrev_b32_e32 v32, 16, v32
	v_and_or_b32 v32, v33, s86, v32
	v_and_or_b32 v33, v35, s86, v34
	global_store_dwordx2 v[130:131], v[32:33], off offset:3584
	ds_read_b128 v[32:35], v252 offset:23552
	s_nop 0
	ds_read_b128 v[36:39], v252 offset:31744
	s_waitcnt lgkmcnt(0)
	v_add_f32_e32 v44, v48, v44
	v_fmamk_f32 v29, v44, 0xba000000, v29
	v_fmamk_f32 v31, v44, 0xba000000, v31
	v_fmamk_f32 v25, v44, 0xba000000, v25
	v_fmamk_f32 v27, v44, 0xba000000, v27
	v_fmamk_f32 v23, v44, 0xba000000, v23
	v_fmac_f32_e32 v22, 0xba000000, v44
	v_fmamk_f32 v21, v44, 0xba000000, v21
	v_fmac_f32_e32 v20, 0xba000000, v44
	v_fmac_f32_e32 v28, 0xba000000, v44
	v_fmac_f32_e32 v30, 0xba000000, v44
	v_fmac_f32_e32 v24, 0xba000000, v44
	v_fmac_f32_e32 v26, 0xba000000, v44
	v_mov_b32_e32 v46, v31
	v_mov_b32_e32 v47, v27
	v_mov_b32_e32 v50, v29
	v_mov_b32_e32 v51, v25
	v_pk_mul_f32 v[52:53], v[20:21], v[20:21]
	v_pk_mul_f32 v[54:55], v[22:23], v[22:23]
	v_fmamk_f32 v19, v44, 0xba000000, v19
	v_fmac_f32_e32 v18, 0xba000000, v44
	v_fmamk_f32 v17, v44, 0xba000000, v17
	v_fmac_f32_e32 v16, 0xba000000, v44
	v_fmamk_f32 v13, v44, 0xba000000, v13
	v_fmac_f32_e32 v12, 0xba000000, v44
	v_fmamk_f32 v15, v44, 0xba000000, v15
	v_fmac_f32_e32 v14, 0xba000000, v44
	v_fmamk_f32 v11, v44, 0xba000000, v11
	v_fmac_f32_e32 v10, 0xba000000, v44
	v_fmamk_f32 v9, v44, 0xba000000, v9
	v_fmac_f32_e32 v8, 0xba000000, v44
	v_fmamk_f32 v7, v44, 0xba000000, v7
	v_fmac_f32_e32 v6, 0xba000000, v44
	v_fmamk_f32 v5, v44, 0xba000000, v5
	v_fmac_f32_e32 v4, 0xba000000, v44
	v_fmamk_f32 v1, v44, 0xba000000, v1
	v_fmac_f32_e32 v0, 0xba000000, v44
	v_fmamk_f32 v3, v44, 0xba000000, v3
	v_fmac_f32_e32 v2, 0xba000000, v44
	v_mov_b32_e32 v44, v30
	v_mov_b32_e32 v45, v26
	v_mov_b32_e32 v48, v28
	v_mov_b32_e32 v49, v24
	v_pk_mul_f32 v[46:47], v[46:47], v[46:47]
	v_pk_mul_f32 v[50:51], v[50:51], v[50:51]
	v_pk_mov_b32 v[130:131], v[54:55], v[52:53] op_sel:[1,0]
	v_mov_b32_e32 v55, v53
	v_mul_f32_e32 v56, v18, v18
	v_mul_f32_e32 v58, v16, v16
	v_pk_mul_f32 v[60:61], v[8:9], v[8:9]
	v_pk_mul_f32 v[62:63], v[10:11], v[10:11]
	v_mul_f32_e32 v68, v6, v6
	v_mul_f32_e32 v70, v4, v4
	v_pk_fma_f32 v[44:45], v[44:45], v[44:45], v[46:47]
	v_pk_fma_f32 v[46:47], v[48:49], v[48:49], v[50:51]
	v_pk_add_f32 v[48:49], v[130:131], v[54:55]
	v_pk_fma_f32 v[52:53], v[18:19], v[18:19], v[56:57] op_sel_hi:[1,1,0]
	v_pk_fma_f32 v[56:57], v[16:17], v[16:17], v[58:59] op_sel_hi:[1,1,0]
	v_pk_mov_b32 v[58:59], v[62:63], v[60:61] op_sel:[1,0]
	v_mov_b32_e32 v63, v61
	v_pk_fma_f32 v[60:61], v[6:7], v[6:7], v[68:69] op_sel_hi:[1,1,0]
	v_pk_fma_f32 v[68:69], v[4:5], v[4:5], v[70:71] op_sel_hi:[1,1,0]
	v_pk_add_f32 v[44:45], v[44:45], v[46:47]
	v_pk_add_f32 v[46:47], v[48:49], v[48:49] op_sel_hi:[0,1]
	v_pk_add_f32 v[44:45], v[44:45], v[44:45] op_sel_hi:[0,1]
	v_mul_f32_e32 v52, v14, v14
	v_mul_f32_e32 v56, v15, v15
	v_mul_f32_e32 v46, v12, v12
	v_mul_f32_e32 v44, v13, v13
	v_pk_add_f32 v[48:49], v[52:53], v[56:57]
	v_pk_add_f32 v[50:51], v[58:59], v[62:63]
	v_mul_f32_e32 v60, v2, v2
	v_pk_add_f32 v[50:51], v[50:51], v[50:51] op_sel_hi:[0,1]
	v_mul_f32_e32 v68, v3, v3
	v_mul_f32_e32 v50, v0, v0
	v_pk_add_f32 v[52:53], v[60:61], v[68:69]
	s_waitcnt lgkmcnt(0)
	v_pk_add_f32 v[32:33], v[32:33], 1.0 op_sel_hi:[1,0]
	s_waitcnt lgkmcnt(0)
; #define GAS __attribute__((address_space(1)))
; #define LAS __attribute__((address_space(3)))
; __device__ __forceinline__ unsigned pk2(float lo, float hi) { return f2bf(lo) | (f2bf(hi) << 16); }
; __device__ __forceinline__ unsigned pk4_fp8(float a, float b, float c, float d) { int r = __builtin_amdgcn_cvt_pk_fp8_f32(a, b, 0, false); r = __builtin_amdgcn_cvt_pk_fp8_f32(c, d, r, true); return (unsigned)r; }
; template <int l>
; __device__ __forceinline__ void layer_phases(Frame& F, const XcdBarrier& bar, const int lo, const int hi) {
;     ...
;                     const float mean = wave_sum(s) * (1.f / D); float s2 = 0.f;
; #pragma unroll
;                     for (int j = 0; j < 8; ++j) { v[j] = v[j] - mean; s2 += (v[j].x * v[j].x + v[j].y * v[j].y) + (v[j].z * v[j].z + v[j].w * v[j].w); }
;                     const float rstd = 1.f / sqrtf(wave_sum(s2) * (1.f / D) + LN_EPS);
; #pragma unroll
;                     for (int j = 0; j < 8; ++j) { const int k = 4 * lq + 256 * j;
;                         const f32x4 xv = v[j] * rstd * *(const GAS f32x4*)(g1 + k) + *(const GAS f32x4*)(b1 + k);
;                         { v2u xo; xo.x = pk2(xv.x, xv.y); xo.y = pk2(xv.z, xv.w); *(GAS v2u*)(x1 + (size_t)m * D + k) = xo; }
;                         const f32x4 hv = xv * (*(const GAS f32x4*)(mrow + 8192 + k) + 1.0f) + *(const GAS f32x4*)(mrow + 6144 + k);
;                         v2u o; o.x = pk2(hv.x, hv.y); o.y = pk2(hv.z, hv.w);
;                         *(GAS unsigned*)(h2q + (size_t)m * D + k) = pk4_fp8(hv.x, hv.y, hv.z, hv.w);
;                         const int chunk = (lq >> 1) + 32 * j;
;                         *(LAS v2u*)(h2s + rloc * 4096 + ((chunk ^ (rloc & 15)) << 4) + (lq & 1) * 8) = o; }
	v_pk_fma_f32 v[130:131], v[40:41], v[32:33], v[36:37]
	v_pk_add_f32 v[32:33], v[34:35], 1.0 op_sel_hi:[1,0]
	v_cvt_pk_fp8_f32 v71, v130, v131
	v_pk_fma_f32 v[132:133], v[42:43], v[32:33], v[38:39]
	v_pk_add_f32 v[32:33], v[46:47], v[44:45]
	v_cvt_pk_fp8_f32 v71, v132, v133 op_sel:[0,0,1]
	v_pk_add_f32 v[32:33], v[48:49], v[32:33]
	global_store_dword v[134:135], v71, off offset:1792
	ds_read_b128 v[36:39], v252 offset:0
	ds_read_b128 v[40:43], v252 offset:8192
	v_pk_add_f32 v[32:33], v[32:33], v[32:33] op_sel_hi:[0,1]
	v_mul_f32_e32 v32, v1, v1
	v_pk_add_f32 v[32:33], v[50:51], v[32:33]
	s_nop 0
	v_pk_add_f32 v[32:33], v[52:53], v[32:33]
	s_nop 0
	v_add_f32_e32 v32, v32, v33
	ds_bpermute_b32 v33, v73, v32
	s_waitcnt lgkmcnt(0)
	v_add_f32_e32 v32, v32, v33
	ds_bpermute_b32 v33, v217, v32
	s_waitcnt lgkmcnt(0)
	v_add_f32_e32 v32, v32, v33
	ds_bpermute_b32 v33, v218, v32
	s_waitcnt lgkmcnt(0)
	v_add_f32_e32 v32, v32, v33
	ds_bpermute_b32 v33, v219, v32
	s_waitcnt lgkmcnt(0)
	v_add_f32_e32 v32, v32, v33
	ds_bpermute_b32 v33, v220, v32
	s_waitcnt lgkmcnt(0)
	v_add_f32_e32 v32, v32, v33
	ds_bpermute_b32 v33, v221, v32
	s_waitcnt lgkmcnt(0)
	v_add_f32_e32 v32, v32, v33
	v_fmamk_f32 v32, v32, 0x3a000000, v223
	v_mul_f32_e32 v33, 0x4f800000, v32
	v_cmp_gt_f32_e32 vcc, s89, v32
	s_nop 1
	v_cndmask_b32_e32 v32, v32, v33, vcc
	v_sqrt_f32_e32 v33, v32
	s_nop 0
	v_add_u32_e32 v34, -1, v33
	v_add_u32_e32 v35, 1, v33
	v_fma_f32 v44, -v34, v33, v32
	v_fma_f32 v45, -v35, v33, v32
	v_cmp_ge_f32_e64 s[14:15], 0, v44
	s_nop 1
	v_cndmask_b32_e64 v33, v33, v34, s[14:15]
	v_cmp_lt_f32_e64 s[14:15], 0, v45
	s_nop 1
	v_cndmask_b32_e64 v33, v33, v35, s[14:15]
	v_mul_f32_e32 v34, 0x37800000, v33
	v_cndmask_b32_e32 v33, v33, v34, vcc
	v_cmp_class_f32_e32 vcc, v32, v224
	s_nop 1
	v_cndmask_b32_e32 v34, v33, v32, vcc
	v_div_scale_f32 v35, s[14:15], v34, v34, 1.0
	v_rcp_f32_e32 v44, v35
	v_div_scale_f32 v45, vcc, 1.0, v34, 1.0
	v_lshl_add_u64 v[32:33], s[0:1], 0, v[128:129]
	v_fma_f32 v46, -v35, v44, 1.0
	v_fmac_f32_e32 v44, v46, v44
	v_mul_f32_e32 v46, v45, v44
	v_fma_f32 v47, -v35, v46, v45
	v_fmac_f32_e32 v46, v47, v44
	v_fma_f32 v35, -v35, v46, v45
	v_div_fmas_f32 v35, v35, v44, v46
	v_div_fixup_f32 v34, v35, v34, 1.0
	v_pk_mul_f32 v[30:31], v[30:31], v[34:35] op_sel_hi:[1,0]
	v_pk_mul_f32 v[28:29], v[28:29], v[34:35] op_sel_hi:[1,0]
	s_waitcnt lgkmcnt(0)
	v_pk_fma_f32 v[40:41], v[36:37], v[30:31], v[40:41]
	v_pk_fma_f32 v[42:43], v[38:39], v[28:29], v[42:43]
	v_bfe_u32 v28, v40, 16, 1
	v_bfe_u32 v30, v42, 16, 1
	v_bfe_u32 v29, v41, 16, 1
	v_bfe_u32 v31, v43, 16, 1
	v_add3_u32 v28, v40, v28, s90
	v_add3_u32 v30, v42, v30, s90
	v_add3_u32 v29, v41, v29, s90
	v_add3_u32 v31, v43, v31, s90
	v_lshrrev_b32_e32 v28, 16, v28
	v_lshrrev_b32_e32 v30, 16, v30
	v_and_or_b32 v28, v29, s86, v28
	v_and_or_b32 v29, v31, s86, v30
	global_store_dwordx2 v[32:33], v[28:29], off
	ds_read_b128 v[28:31], v252 offset:16384
	s_nop 0
	ds_read_b128 v[36:39], v252 offset:24576
	v_mov_b32_e32 v35, 0
	s_add_u32 s0, s50, s16
	s_addc_u32 s1, s51, s17
	s_or_b32 s46, s42, 2
	s_ashr_i32 s47, s46, 31
	s_lshl_b64 s[18:19], s[46:47], 11
	s_or_b32 s48, s42, 3
	s_ashr_i32 s49, s48, 31
	s_lshl_b64 s[16:17], s[48:49], 11
	s_waitcnt lgkmcnt(0)
	v_pk_add_f32 v[28:29], v[28:29], 1.0 op_sel_hi:[1,0]
	s_waitcnt lgkmcnt(0)
	v_pk_fma_f32 v[134:135], v[28:29], v[40:41], v[36:37]
	v_pk_add_f32 v[28:29], v[30:31], 1.0 op_sel_hi:[1,0]
	v_cvt_pk_fp8_f32 v35, v134, v135
	v_pk_fma_f32 v[136:137], v[28:29], v[42:43], v[38:39]
	v_lshl_add_u64 v[28:29], s[0:1], 0, v[86:87]
	s_lshl_b64 s[0:1], s[46:47], 12
	v_cvt_pk_fp8_f32 v35, v136, v137 op_sel:[0,0,1]
	s_add_u32 s0, s3, s0
	s_addc_u32 s1, s41, s1
	global_store_dword v[28:29], v35, off
	ds_read_b128 v[36:39], v252 offset:1024
	ds_read_b128 v[40:43], v252 offset:9216
	v_pk_mul_f32 v[26:27], v[26:27], v[34:35] op_sel_hi:[1,0]
	v_pk_mul_f32 v[24:25], v[24:25], v[34:35] op_sel_hi:[1,0]
	v_mov_b32_e32 v35, 0
	s_waitcnt lgkmcnt(0)
	v_pk_fma_f32 v[30:31], v[38:39], v[24:25], v[42:43]
	v_pk_fma_f32 v[40:41], v[36:37], v[26:27], v[40:41]
	v_bfe_u32 v26, v30, 16, 1
	v_bfe_u32 v24, v40, 16, 1
	v_bfe_u32 v25, v41, 16, 1
	v_bfe_u32 v27, v31, 16, 1
	v_add3_u32 v24, v40, v24, s90
	v_add3_u32 v26, v30, v26, s90
	v_add3_u32 v25, v41, v25, s90
	v_add3_u32 v27, v31, v27, s90
	v_lshrrev_b32_e32 v24, 16, v24
	v_lshrrev_b32_e32 v26, 16, v26
	v_and_or_b32 v24, v25, s86, v24
	v_and_or_b32 v25, v27, s86, v26
	global_store_dwordx2 v[32:33], v[24:25], off offset:512
	ds_read_b128 v[24:27], v252 offset:17408
	s_nop 0
	ds_read_b128 v[36:39], v252 offset:25600
	s_waitcnt lgkmcnt(0)
	v_pk_add_f32 v[24:25], v[24:25], 1.0 op_sel_hi:[1,0]
	s_waitcnt lgkmcnt(0)
	v_pk_fma_f32 v[138:139], v[24:25], v[40:41], v[36:37]
	v_pk_add_f32 v[24:25], v[26:27], 1.0 op_sel_hi:[1,0]
	v_cvt_pk_fp8_f32 v35, v138, v139
	v_pk_fma_f32 v[140:141], v[24:25], v[30:31], v[38:39]
	s_nop 0
	v_cvt_pk_fp8_f32 v35, v140, v141 op_sel:[0,0,1]
	global_store_dword v[28:29], v35, off offset:256
	ds_read_b128 v[24:27], v252 offset:2048
	ds_read_b128 v[36:39], v252 offset:10240
	v_pk_mul_f32 v[22:23], v[22:23], v[34:35] op_sel_hi:[1,0]
	v_pk_mul_f32 v[20:21], v[20:21], v[34:35] op_sel_hi:[1,0]
	v_mov_b32_e32 v35, 0
	s_waitcnt lgkmcnt(0)
	v_pk_fma_f32 v[30:31], v[26:27], v[20:21], v[38:39]
	v_pk_fma_f32 v[36:37], v[24:25], v[22:23], v[36:37]
	v_bfe_u32 v22, v30, 16, 1
	v_bfe_u32 v20, v36, 16, 1
	v_bfe_u32 v21, v37, 16, 1
	v_bfe_u32 v23, v31, 16, 1
	v_add3_u32 v20, v36, v20, s90
	v_add3_u32 v22, v30, v22, s90
	v_add3_u32 v21, v37, v21, s90
	v_add3_u32 v23, v31, v23, s90
	v_lshrrev_b32_e32 v20, 16, v20
	v_lshrrev_b32_e32 v22, 16, v22
	v_and_or_b32 v20, v21, s86, v20
	v_and_or_b32 v21, v23, s86, v22
	global_store_dwordx2 v[32:33], v[20:21], off offset:1024
	ds_read_b128 v[20:23], v252 offset:18432
	s_nop 0
	ds_read_b128 v[24:27], v252 offset:26624
	s_waitcnt lgkmcnt(0)
; #define GAS __attribute__((address_space(1)))
; #define LAS __attribute__((address_space(3)))
; __device__ __forceinline__ unsigned pk2(float lo, float hi) { return f2bf(lo) | (f2bf(hi) << 16); }
; __device__ __forceinline__ unsigned pk4_fp8(float a, float b, float c, float d) { int r = __builtin_amdgcn_cvt_pk_fp8_f32(a, b, 0, false); r = __builtin_amdgcn_cvt_pk_fp8_f32(c, d, r, true); return (unsigned)r; }
; template <int l>
; __device__ __forceinline__ void layer_phases(Frame& F, const XcdBarrier& bar, const int lo, const int hi) {
;     ...
;                     for (int j = 0; j < 8; ++j) { const int k = 4 * lq + 256 * j;
;                         const f32x4 xv = v[j] * rstd * *(const GAS f32x4*)(g1 + k) + *(const GAS f32x4*)(b1 + k);
;                         { v2u xo; xo.x = pk2(xv.x, xv.y); xo.y = pk2(xv.z, xv.w); *(GAS v2u*)(x1 + (size_t)m * D + k) = xo; }
;                         const f32x4 hv = xv * (*(const GAS f32x4*)(mrow + 8192 + k) + 1.0f) + *(const GAS f32x4*)(mrow + 6144 + k);
;                         v2u o; o.x = pk2(hv.x, hv.y); o.y = pk2(hv.z, hv.w);
;                         *(GAS unsigned*)(h2q + (size_t)m * D + k) = pk4_fp8(hv.x, hv.y, hv.z, hv.w);
;                         const int chunk = (lq >> 1) + 32 * j;
;                         *(LAS v2u*)(h2s + rloc * 4096 + ((chunk ^ (rloc & 15)) << 4) + (lq & 1) * 8) = o; }
	v_pk_add_f32 v[20:21], v[20:21], 1.0 op_sel_hi:[1,0]
	s_waitcnt lgkmcnt(0)
	v_pk_fma_f32 v[142:143], v[20:21], v[36:37], v[24:25]
	v_pk_add_f32 v[20:21], v[22:23], 1.0 op_sel_hi:[1,0]
	v_cvt_pk_fp8_f32 v35, v142, v143
	v_pk_fma_f32 v[144:145], v[20:21], v[30:31], v[26:27]
	v_mov_b32_e32 v30, 0
	v_cvt_pk_fp8_f32 v35, v144, v145 op_sel:[0,0,1]
	global_store_dword v[28:29], v35, off offset:512
	ds_read_b128 v[20:23], v252 offset:3072
	ds_read_b128 v[24:27], v252 offset:11264
	v_pk_mul_f32 v[18:19], v[18:19], v[34:35] op_sel_hi:[1,0]
	v_pk_mul_f32 v[16:17], v[16:17], v[34:35] op_sel_hi:[1,0]
	v_pk_mul_f32 v[14:15], v[14:15], v[34:35] op_sel_hi:[1,0]
	v_pk_mul_f32 v[12:13], v[12:13], v[34:35] op_sel_hi:[1,0]
	v_pk_mul_f32 v[10:11], v[10:11], v[34:35] op_sel_hi:[1,0]
	v_pk_mul_f32 v[8:9], v[8:9], v[34:35] op_sel_hi:[1,0]
	v_pk_mul_f32 v[6:7], v[6:7], v[34:35] op_sel_hi:[1,0]
	v_pk_mul_f32 v[4:5], v[4:5], v[34:35] op_sel_hi:[1,0]
	v_pk_mul_f32 v[2:3], v[2:3], v[34:35] op_sel_hi:[1,0]
	v_pk_mul_f32 v[0:1], v[0:1], v[34:35] op_sel_hi:[1,0]
	s_waitcnt lgkmcnt(0)
	v_pk_fma_f32 v[26:27], v[16:17], v[22:23], v[26:27]
	v_pk_fma_f32 v[24:25], v[18:19], v[20:21], v[24:25]
	v_bfe_u32 v18, v26, 16, 1
	v_bfe_u32 v16, v24, 16, 1
	v_bfe_u32 v17, v25, 16, 1
	v_bfe_u32 v19, v27, 16, 1
	v_add3_u32 v16, v24, v16, s90
	v_add3_u32 v18, v26, v18, s90
	v_add3_u32 v17, v25, v17, s90
	v_add3_u32 v19, v27, v19, s90
	v_lshrrev_b32_e32 v16, 16, v16
	v_lshrrev_b32_e32 v18, 16, v18
	v_and_or_b32 v16, v17, s86, v16
	v_and_or_b32 v17, v19, s86, v18
	global_store_dwordx2 v[32:33], v[16:17], off offset:1536
	ds_read_b128 v[16:19], v252 offset:19456
	s_nop 0
	ds_read_b128 v[20:23], v252 offset:27648
	s_waitcnt lgkmcnt(0)
	v_pk_add_f32 v[16:17], v[16:17], 1.0 op_sel_hi:[1,0]
	s_waitcnt lgkmcnt(0)
	v_pk_fma_f32 v[146:147], v[24:25], v[16:17], v[20:21]
	v_pk_add_f32 v[16:17], v[18:19], 1.0 op_sel_hi:[1,0]
	v_cvt_pk_fp8_f32 v30, v146, v147
	v_pk_fma_f32 v[148:149], v[26:27], v[16:17], v[22:23]
	v_mov_b32_e32 v24, 0
	v_cvt_pk_fp8_f32 v30, v148, v149 op_sel:[0,0,1]
	global_store_dword v[28:29], v30, off offset:768
	ds_read_b128 v[16:19], v252 offset:4096
	ds_read_b128 v[20:23], v252 offset:12288
	s_waitcnt lgkmcnt(0)
	v_pk_fma_f32 v[22:23], v[12:13], v[18:19], v[22:23]
	v_pk_fma_f32 v[20:21], v[14:15], v[16:17], v[20:21]
	v_bfe_u32 v14, v22, 16, 1
	v_bfe_u32 v12, v20, 16, 1
	v_bfe_u32 v13, v21, 16, 1
	v_bfe_u32 v15, v23, 16, 1
	v_add3_u32 v12, v20, v12, s90
	v_add3_u32 v14, v22, v14, s90
	v_add3_u32 v13, v21, v13, s90
	v_add3_u32 v15, v23, v15, s90
	v_lshrrev_b32_e32 v12, 16, v12
	v_lshrrev_b32_e32 v14, 16, v14
	v_and_or_b32 v12, v13, s86, v12
	v_and_or_b32 v13, v15, s86, v14
	global_store_dwordx2 v[32:33], v[12:13], off offset:2048
	ds_read_b128 v[12:15], v252 offset:20480
	s_nop 0
	ds_read_b128 v[16:19], v252 offset:28672
	s_waitcnt lgkmcnt(0)
	v_pk_add_f32 v[12:13], v[12:13], 1.0 op_sel_hi:[1,0]
	s_waitcnt lgkmcnt(0)
	v_pk_fma_f32 v[150:151], v[20:21], v[12:13], v[16:17]
	v_pk_add_f32 v[12:13], v[14:15], 1.0 op_sel_hi:[1,0]
	v_cvt_pk_fp8_f32 v24, v150, v151
	v_pk_fma_f32 v[152:153], v[22:23], v[12:13], v[18:19]
	v_mov_b32_e32 v20, 0
	v_cvt_pk_fp8_f32 v24, v152, v153 op_sel:[0,0,1]
	global_store_dword v[28:29], v24, off offset:1024
	ds_read_b128 v[12:15], v252 offset:5120
	ds_read_b128 v[16:19], v252 offset:13312
	s_waitcnt lgkmcnt(0)
	v_pk_fma_f32 v[18:19], v[8:9], v[14:15], v[18:19]
	v_pk_fma_f32 v[16:17], v[10:11], v[12:13], v[16:17]
	v_bfe_u32 v10, v18, 16, 1
	v_bfe_u32 v8, v16, 16, 1
	v_bfe_u32 v9, v17, 16, 1
	v_bfe_u32 v11, v19, 16, 1
	v_add3_u32 v8, v16, v8, s90
	v_add3_u32 v10, v18, v10, s90
	v_add3_u32 v9, v17, v9, s90
	v_add3_u32 v11, v19, v11, s90
	v_lshrrev_b32_e32 v8, 16, v8
	v_lshrrev_b32_e32 v10, 16, v10
	v_and_or_b32 v8, v9, s86, v8
	v_and_or_b32 v9, v11, s86, v10
	global_store_dwordx2 v[32:33], v[8:9], off offset:2560
	ds_read_b128 v[8:11], v252 offset:21504
	s_nop 0
	ds_read_b128 v[12:15], v252 offset:29696
	s_waitcnt lgkmcnt(0)
	v_pk_add_f32 v[8:9], v[8:9], 1.0 op_sel_hi:[1,0]
	s_waitcnt lgkmcnt(0)
	v_pk_fma_f32 v[154:155], v[16:17], v[8:9], v[12:13]
	v_pk_add_f32 v[8:9], v[10:11], 1.0 op_sel_hi:[1,0]
	v_cvt_pk_fp8_f32 v20, v154, v155
	v_pk_fma_f32 v[156:157], v[18:19], v[8:9], v[14:15]
	v_mov_b32_e32 v16, 0
	v_cvt_pk_fp8_f32 v20, v156, v157 op_sel:[0,0,1]
	global_store_dword v[28:29], v20, off offset:1280
	ds_read_b128 v[8:11], v252 offset:6144
	ds_read_b128 v[12:15], v252 offset:14336
	s_waitcnt lgkmcnt(0)
	v_pk_fma_f32 v[14:15], v[4:5], v[10:11], v[14:15]
	v_pk_fma_f32 v[12:13], v[6:7], v[8:9], v[12:13]
	v_bfe_u32 v6, v14, 16, 1
	v_bfe_u32 v4, v12, 16, 1
	v_bfe_u32 v5, v13, 16, 1
	v_bfe_u32 v7, v15, 16, 1
	v_add3_u32 v4, v12, v4, s90
	v_add3_u32 v6, v14, v6, s90
	v_add3_u32 v5, v13, v5, s90
	v_add3_u32 v7, v15, v7, s90
	v_lshrrev_b32_e32 v4, 16, v4
	v_lshrrev_b32_e32 v6, 16, v6
	v_and_or_b32 v4, v5, s86, v4
	v_and_or_b32 v5, v7, s86, v6
	global_store_dwordx2 v[32:33], v[4:5], off offset:3072
	ds_read_b128 v[4:7], v252 offset:22528
	s_nop 0
	ds_read_b128 v[8:11], v252 offset:30720
	s_waitcnt lgkmcnt(0)
	v_pk_add_f32 v[4:5], v[4:5], 1.0 op_sel_hi:[1,0]
	s_waitcnt lgkmcnt(0)
	v_pk_fma_f32 v[158:159], v[12:13], v[4:5], v[8:9]
	v_pk_add_f32 v[4:5], v[6:7], 1.0 op_sel_hi:[1,0]
	v_cvt_pk_fp8_f32 v16, v158, v159
	v_pk_fma_f32 v[160:161], v[14:15], v[4:5], v[10:11]
	v_mov_b32_e32 v12, 0
	v_cvt_pk_fp8_f32 v16, v160, v161 op_sel:[0,0,1]
	global_store_dword v[28:29], v16, off offset:1536
	ds_read_b128 v[4:7], v252 offset:7168
	ds_read_b128 v[8:11], v252 offset:15360
	s_waitcnt lgkmcnt(0)
; #define GAS __attribute__((address_space(1)))
; #define LAS __attribute__((address_space(3)))
; __device__ __forceinline__ unsigned pk2(float lo, float hi) { return f2bf(lo) | (f2bf(hi) << 16); }
; __device__ __forceinline__ unsigned pk4_fp8(float a, float b, float c, float d) { int r = __builtin_amdgcn_cvt_pk_fp8_f32(a, b, 0, false); r = __builtin_amdgcn_cvt_pk_fp8_f32(c, d, r, true); return (unsigned)r; }
; __device__ __forceinline__ f32x4 bf4(unsigned a, unsigned b) { return (f32x4){bflo(a), bfhi(a), bflo(b), bfhi(b)}; }
; template <int l>
; __device__ __forceinline__ void layer_phases(Frame& F, const XcdBarrier& bar, const int lo, const int hi) {
;     ...
;                 for (int rp = 0; rp < 2; ++rp) {
;                 f32x4 vv[2][8];
; #pragma unroll
;                 for (int rr = 0; rr < 2; ++rr)
; #pragma unroll
;                     for (int j = 0; j < 8; ++j) { const size_t off = (size_t)(m0 + 2 * rp + rr) * D + 4 * lq + 256 * j;
;                         f32x4 xv; if (l == 0) xv = __builtin_nontemporal_load((const GAS f32x4*)(xin + off)); else { const v2u xw_ = __builtin_nontemporal_load((const GAS v2u*)(xinb + off)); xv = bf4(xw_.x, xw_.y); } const v2u mw = __builtin_nontemporal_load((const GAS v2u*)(mixb + off)); const f32x4 gv = *(const GAS f32x4*)(mrow + 4096 + 4 * lq + 256 * j);
;                         vv[rr][j] = xv * ALPHA + gv * (f32x4){bflo(mw.x), bfhi(mw.x), bflo(mw.y), bfhi(mw.y)}; }
;     ...
;                     for (int j = 0; j < 8; ++j) { const int k = 4 * lq + 256 * j;
;                         const f32x4 xv = v[j] * rstd * *(const GAS f32x4*)(g1 + k) + *(const GAS f32x4*)(b1 + k);
;                         { v2u xo; xo.x = pk2(xv.x, xv.y); xo.y = pk2(xv.z, xv.w); *(GAS v2u*)(x1 + (size_t)m * D + k) = xo; }
;                         const f32x4 hv = xv * (*(const GAS f32x4*)(mrow + 8192 + k) + 1.0f) + *(const GAS f32x4*)(mrow + 6144 + k);
;                         v2u o; o.x = pk2(hv.x, hv.y); o.y = pk2(hv.z, hv.w);
;                         *(GAS unsigned*)(h2q + (size_t)m * D + k) = pk4_fp8(hv.x, hv.y, hv.z, hv.w);
;                         const int chunk = (lq >> 1) + 32 * j;
;                         *(LAS v2u*)(h2s + rloc * 4096 + ((chunk ^ (rloc & 15)) << 4) + (lq & 1) * 8) = o; }
	v_pk_fma_f32 v[10:11], v[0:1], v[6:7], v[10:11]
	v_pk_fma_f32 v[8:9], v[2:3], v[4:5], v[8:9]
	v_bfe_u32 v2, v10, 16, 1
	v_bfe_u32 v0, v8, 16, 1
	v_bfe_u32 v1, v9, 16, 1
	v_bfe_u32 v3, v11, 16, 1
	v_add3_u32 v0, v8, v0, s90
	v_add3_u32 v2, v10, v2, s90
	v_add3_u32 v1, v9, v1, s90
	v_add3_u32 v3, v11, v3, s90
	v_lshrrev_b32_e32 v0, 16, v0
	v_lshrrev_b32_e32 v2, 16, v2
	v_and_or_b32 v0, v1, s86, v0
	v_and_or_b32 v1, v3, s86, v2
	global_store_dwordx2 v[32:33], v[0:1], off offset:3584
	ds_read_b128 v[0:3], v252 offset:23552
	s_nop 0
	ds_read_b128 v[4:7], v252 offset:31744
	v_lshl_add_u64 v[32:33], s[18:19], 0, v[86:87]
	v_lshl_add_u64 v[48:49], v[32:33], 2, s[20:21]
	v_add_co_u32_e32 v60, vcc, s87, v48
	s_waitcnt lgkmcnt(0)
	v_pk_add_f32 v[0:1], v[0:1], 1.0 op_sel_hi:[1,0]
	s_waitcnt lgkmcnt(0)
	v_pk_fma_f32 v[162:163], v[8:9], v[0:1], v[4:5]
	v_pk_add_f32 v[0:1], v[2:3], 1.0 op_sel_hi:[1,0]
	v_cvt_pk_fp8_f32 v12, v162, v163
	v_pk_fma_f32 v[164:165], v[10:11], v[0:1], v[6:7]
	v_lshl_add_u64 v[0:1], v[32:33], 1, s[26:27]
	v_addc_co_u32_e32 v61, vcc, 0, v49, vcc
	v_cvt_pk_fp8_f32 v12, v164, v165 op_sel:[0,0,1]
	global_store_dword v[28:29], v12, off offset:1792
	global_load_dwordx2 v[68:69], v[0:1], off nt
	global_load_dwordx2 v[70:71], v[0:1], off offset:512 nt
	global_load_dwordx2 v[166:167], v[0:1], off offset:1024 nt
	global_load_dwordx2 v[168:169], v[0:1], off offset:1536 nt
	global_load_dwordx2 v[170:171], v[0:1], off offset:2048 nt
	global_load_dwordx2 v[172:173], v[0:1], off offset:2560 nt
	global_load_dwordx2 v[174:175], v[0:1], off offset:3072 nt
	global_load_dwordx2 v[176:177], v[0:1], off offset:3584 nt
	global_load_dwordx4 v[28:31], v[64:65], off offset:-4096
	global_load_dwordx4 v[24:27], v[66:67], off offset:1024
	global_load_dwordx4 v[20:23], v[66:67], off offset:2048
	global_load_dwordx4 v[16:19], v[66:67], off offset:3072
	global_load_dwordx4 v[12:15], v[64:65], off
	global_load_dwordx4 v[8:11], v[64:65], off offset:1024
	global_load_dwordx4 v[4:7], v[64:65], off offset:2048
	global_load_dwordx4 v[0:3], v[64:65], off offset:3072
	global_load_dwordx4 v[32:35], v[48:49], off nt
	global_load_dwordx4 v[36:39], v[48:49], off offset:1024 nt
	global_load_dwordx4 v[40:43], v[48:49], off offset:2048 nt
	global_load_dwordx4 v[44:47], v[48:49], off offset:3072 nt
	s_nop 0
	global_load_dwordx4 v[48:51], v[60:61], off nt
	global_load_dwordx4 v[52:55], v[60:61], off offset:1024 nt
	global_load_dwordx4 v[56:59], v[60:61], off offset:2048 nt
	s_nop 0
	global_load_dwordx4 v[60:63], v[60:61], off offset:3072 nt
	s_waitcnt vmcnt(23)
	s_waitcnt lgkmcnt(0)
	v_lshlrev_b32_e32 v64, 16, v68
	v_and_b32_e32 v65, 0xffff0000, v68
	v_lshlrev_b32_e32 v66, 16, v69
	v_and_b32_e32 v67, 0xffff0000, v69
	s_waitcnt vmcnt(22)
	s_waitcnt lgkmcnt(0)
	v_lshlrev_b32_e32 v68, 16, v70
	v_and_b32_e32 v69, 0xffff0000, v70
	v_lshlrev_b32_e32 v70, 16, v71
	v_and_b32_e32 v71, 0xffff0000, v71
	s_waitcnt vmcnt(21)
	s_waitcnt lgkmcnt(0)
	v_lshlrev_b32_e32 v178, 16, v166
	v_and_b32_e32 v179, 0xffff0000, v166
	v_lshlrev_b32_e32 v166, 16, v167
	v_and_b32_e32 v167, 0xffff0000, v167
	s_waitcnt vmcnt(15)
	s_waitcnt lgkmcnt(0)
	v_pk_mul_f32 v[64:65], v[28:29], v[64:65]
	v_pk_mul_f32 v[66:67], v[30:31], v[66:67]
	s_waitcnt vmcnt(14)
	s_waitcnt lgkmcnt(0)
	v_pk_mul_f32 v[70:71], v[26:27], v[70:71]
	v_pk_mul_f32 v[68:69], v[24:25], v[68:69]
	v_lshlrev_b32_e32 v180, 16, v168
	v_and_b32_e32 v181, 0xffff0000, v168
	v_lshlrev_b32_e32 v168, 16, v169
	v_and_b32_e32 v169, 0xffff0000, v169
	s_waitcnt vmcnt(13)
	s_waitcnt lgkmcnt(0)
	v_pk_mul_f32 v[166:167], v[22:23], v[166:167]
	v_pk_mul_f32 v[178:179], v[20:21], v[178:179]
	s_waitcnt vmcnt(7)
	s_waitcnt lgkmcnt(0)
	v_pk_fma_f32 v[190:191], v[34:35], s[40:41], v[66:67] op_sel_hi:[1,0,1]
	v_pk_fma_f32 v[198:199], v[32:33], s[40:41], v[64:65] op_sel_hi:[1,0,1]
	s_waitcnt vmcnt(6)
	s_waitcnt lgkmcnt(0)
	v_pk_fma_f32 v[192:193], v[38:39], s[40:41], v[70:71] op_sel_hi:[1,0,1]
	v_pk_fma_f32 v[194:195], v[36:37], s[40:41], v[68:69] op_sel_hi:[1,0,1]
	v_pk_mul_f32 v[196:197], v[18:19], v[168:169]
	s_waitcnt vmcnt(5)
	s_waitcnt lgkmcnt(0)
	v_pk_fma_f32 v[166:167], v[42:43], s[40:41], v[166:167] op_sel_hi:[1,0,1]
	v_pk_fma_f32 v[168:169], v[40:41], s[40:41], v[178:179] op_sel_hi:[1,0,1]
	v_mov_b32_e32 v32, v198
	v_mov_b32_e32 v33, v194
	v_mov_b32_e32 v34, v199
	v_mov_b32_e32 v35, v195
	v_mov_b32_e32 v36, v190
	v_mov_b32_e32 v37, v192
	v_mov_b32_e32 v38, v191
	v_mov_b32_e32 v39, v193
	v_lshlrev_b32_e32 v182, 16, v170
	v_and_b32_e32 v183, 0xffff0000, v170
	v_lshlrev_b32_e32 v170, 16, v171
	v_and_b32_e32 v171, 0xffff0000, v171
	v_pk_mov_b32 v[40:41], v[168:169], v[166:167] op_sel:[1,0]
	v_mov_b32_e32 v42, v168
	v_mov_b32_e32 v43, v167
	v_pk_add_f32 v[32:33], v[32:33], v[34:35]
	v_pk_add_f32 v[34:35], v[36:37], v[38:39]
	v_lshlrev_b32_e32 v184, 16, v172
	v_and_b32_e32 v185, 0xffff0000, v172
	v_lshlrev_b32_e32 v172, 16, v173
	v_and_b32_e32 v173, 0xffff0000, v173
	v_lshlrev_b32_e32 v186, 16, v174
	v_and_b32_e32 v187, 0xffff0000, v174
	v_lshlrev_b32_e32 v174, 16, v175
	v_and_b32_e32 v175, 0xffff0000, v175
	v_lshlrev_b32_e32 v188, 16, v176
	v_and_b32_e32 v189, 0xffff0000, v176
	v_lshlrev_b32_e32 v176, 16, v177
	v_and_b32_e32 v177, 0xffff0000, v177
	v_pk_mul_f32 v[180:181], v[16:17], v[180:181]
	v_pk_mul_f32 v[182:183], v[12:13], v[182:183]
	v_pk_mul_f32 v[200:201], v[14:15], v[170:171]
	v_pk_add_f32 v[36:37], v[40:41], v[42:43]
	v_pk_add_f32 v[32:33], v[32:33], v[34:35]
	v_pk_mul_f32 v[184:185], v[8:9], v[184:185]
	v_pk_mul_f32 v[202:203], v[10:11], v[172:173]
	v_pk_mul_f32 v[204:205], v[4:5], v[186:187]
	v_pk_mul_f32 v[186:187], v[6:7], v[174:175]
	v_pk_mul_f32 v[208:209], v[2:3], v[176:177]
	s_waitcnt vmcnt(4)
; template <int l>
; __device__ __forceinline__ void layer_phases(Frame& F, const XcdBarrier& bar, const int lo, const int hi) {
;     ...
; #pragma unroll
;                 for (int rq = 0; rq < 2; ++rq) { const int rr = 2 * rp + rq, m = m0 + rr, rloc = 4 * F.wave + rr;
;                     f32x4 (&v)[8] = vv[rq]; float s = 0.f;
; #pragma unroll
;                     for (int j = 0; j < 8; ++j) s += (v[j].x + v[j].y) + (v[j].z + v[j].w);
;                     const float mean = wave_sum(s) * (1.f / D); float s2 = 0.f;
; #pragma unroll
;                     for (int j = 0; j < 8; ++j) { v[j] = v[j] - mean; s2 += (v[j].x * v[j].x + v[j].y * v[j].y) + (v[j].z * v[j].z + v[j].w * v[j].w); }
;                     const float rstd = 1.f / sqrtf(wave_sum(s2) * (1.f / D) + LN_EPS);
	s_waitcnt lgkmcnt(0)
	v_pk_fma_f32 v[170:171], v[46:47], s[40:41], v[196:197] op_sel_hi:[1,0,1]
	v_pk_fma_f32 v[172:173], v[44:45], s[40:41], v[180:181] op_sel_hi:[1,0,1]
	s_waitcnt vmcnt(3)
	s_waitcnt lgkmcnt(0)
	v_pk_fma_f32 v[174:175], v[50:51], s[40:41], v[200:201] op_sel_hi:[1,0,1]
	v_pk_fma_f32 v[176:177], v[48:49], s[40:41], v[182:183] op_sel_hi:[1,0,1]
	v_pk_add_f32 v[34:35], v[36:37], v[36:37] op_sel:[0,1] op_sel_hi:[1,0]
	v_add_f32_e32 v32, 0, v32
	s_waitcnt vmcnt(2)
	s_waitcnt lgkmcnt(0)
	v_pk_fma_f32 v[178:179], v[54:55], s[40:41], v[202:203] op_sel_hi:[1,0,1]
	v_pk_fma_f32 v[180:181], v[52:53], s[40:41], v[184:185] op_sel_hi:[1,0,1]
	v_add_f32_e32 v44, v172, v173
	v_add_f32_e32 v46, v170, v171
	v_mov_b32_e32 v49, v176
	v_mov_b32_e32 v45, v174
	v_mov_b32_e32 v47, v175
	v_mov_b32_e32 v35, v177
	v_add_f32_e32 v48, v32, v33
	v_pk_mov_b32 v[50:51], v[180:181], v[178:179] op_sel:[1,0]
	v_mov_b32_e32 v52, v180
	v_mov_b32_e32 v53, v179
	v_pk_add_f32 v[38:39], v[44:45], v[46:47]
	v_pk_add_f32 v[32:33], v[48:49], v[34:35]
	v_pk_mul_f32 v[206:207], v[0:1], v[188:189]
	v_pk_add_f32 v[40:41], v[50:51], v[52:53]
	v_pk_add_f32 v[32:33], v[32:33], v[38:39]
	s_waitcnt vmcnt(1)
	s_waitcnt lgkmcnt(0)
	v_pk_fma_f32 v[186:187], v[58:59], s[40:41], v[186:187] op_sel_hi:[1,0,1]
	v_pk_fma_f32 v[188:189], v[56:57], s[40:41], v[204:205] op_sel_hi:[1,0,1]
	s_waitcnt vmcnt(0)
	s_waitcnt lgkmcnt(0)
	v_pk_fma_f32 v[182:183], v[62:63], s[40:41], v[208:209] op_sel_hi:[1,0,1]
	v_pk_fma_f32 v[184:185], v[60:61], s[40:41], v[206:207] op_sel_hi:[1,0,1]
	v_pk_add_f32 v[36:37], v[40:41], v[40:41] op_sel:[0,1] op_sel_hi:[1,0]
	v_pk_add_f32 v[32:33], v[32:33], v[32:33] op_sel:[0,1] op_sel_hi:[1,0]
	v_add_f32_e32 v54, v188, v189
	v_add_f32_e32 v56, v186, v187
	v_mov_b32_e32 v55, v182
	v_mov_b32_e32 v57, v183
	v_mov_b32_e32 v37, v185
	v_mov_b32_e32 v33, v184
	v_pk_add_f32 v[42:43], v[54:55], v[56:57]
	v_pk_add_f32 v[32:33], v[32:33], v[36:37]
	ds_read_b128 v[64:67], v252 offset:0
	ds_read_b128 v[68:71], v252 offset:8192
	v_pk_add_f32 v[32:33], v[32:33], v[42:43]
	v_lshl_add_u64 v[196:197], s[0:1], 0, v[128:129]
	v_add_f32_e32 v32, v32, v33
	ds_bpermute_b32 v33, v73, v32
	s_waitcnt lgkmcnt(0)
	v_add_f32_e32 v32, v32, v33
	ds_bpermute_b32 v33, v217, v32
	s_waitcnt lgkmcnt(0)
	v_add_f32_e32 v32, v32, v33
	ds_bpermute_b32 v33, v218, v32
	s_waitcnt lgkmcnt(0)
	v_add_f32_e32 v32, v32, v33
	ds_bpermute_b32 v33, v219, v32
	s_waitcnt lgkmcnt(0)
	v_add_f32_e32 v32, v32, v33
	ds_bpermute_b32 v33, v220, v32
	s_waitcnt lgkmcnt(0)
	v_add_f32_e32 v32, v32, v33
	ds_bpermute_b32 v33, v221, v32
	s_waitcnt lgkmcnt(0)
	v_add_f32_e32 v32, v32, v33
	v_fmamk_f32 v191, v32, 0xba000000, v191
	v_fmamk_f32 v199, v32, 0xba000000, v199
	v_fmamk_f32 v193, v32, 0xba000000, v193
	v_fmamk_f32 v195, v32, 0xba000000, v195
	v_fmac_f32_e32 v190, 0xba000000, v32
	v_fmac_f32_e32 v198, 0xba000000, v32
	v_fmac_f32_e32 v192, 0xba000000, v32
	v_fmac_f32_e32 v194, 0xba000000, v32
	v_fmamk_f32 v169, v32, 0xba000000, v169
	v_fmac_f32_e32 v168, 0xba000000, v32
	v_fmamk_f32 v167, v32, 0xba000000, v167
	v_fmac_f32_e32 v166, 0xba000000, v32
	v_mov_b32_e32 v34, v199
	v_mov_b32_e32 v35, v195
	v_mov_b32_e32 v38, v191
	v_mov_b32_e32 v39, v193
	v_fmamk_f32 v173, v32, 0xba000000, v173
	v_fmac_f32_e32 v172, 0xba000000, v32
	v_fmamk_f32 v171, v32, 0xba000000, v171
	v_fmac_f32_e32 v170, 0xba000000, v32
	v_fmamk_f32 v175, v32, 0xba000000, v175
	v_fmac_f32_e32 v174, 0xba000000, v32
	v_fmamk_f32 v177, v32, 0xba000000, v177
	v_fmac_f32_e32 v176, 0xba000000, v32
	v_fmamk_f32 v181, v32, 0xba000000, v181
	v_fmac_f32_e32 v180, 0xba000000, v32
	v_fmamk_f32 v179, v32, 0xba000000, v179
	v_fmac_f32_e32 v178, 0xba000000, v32
	v_fmamk_f32 v189, v32, 0xba000000, v189
	v_fmac_f32_e32 v188, 0xba000000, v32
	v_fmamk_f32 v187, v32, 0xba000000, v187
	v_fmac_f32_e32 v186, 0xba000000, v32
	v_fmamk_f32 v183, v32, 0xba000000, v183
	v_fmac_f32_e32 v182, 0xba000000, v32
	v_fmamk_f32 v185, v32, 0xba000000, v185
	v_fmac_f32_e32 v184, 0xba000000, v32
	v_mov_b32_e32 v32, v198
	v_mov_b32_e32 v33, v194
	v_mov_b32_e32 v36, v190
	v_mov_b32_e32 v37, v192
	v_pk_mul_f32 v[40:41], v[166:167], v[166:167]
	v_pk_mul_f32 v[42:43], v[168:169], v[168:169]
	v_pk_mul_f32 v[34:35], v[34:35], v[34:35]
	v_pk_mul_f32 v[38:39], v[38:39], v[38:39]
	v_pk_mov_b32 v[56:57], v[42:43], v[40:41] op_sel:[1,0]
	v_mov_b32_e32 v43, v41
	v_pk_fma_f32 v[32:33], v[32:33], v[32:33], v[34:35]
	v_pk_fma_f32 v[34:35], v[36:37], v[36:37], v[38:39]
	v_mul_f32_e32 v44, v172, v172
	v_mul_f32_e32 v46, v170, v170
	v_pk_add_f32 v[36:37], v[56:57], v[42:43]
	v_pk_add_f32 v[32:33], v[32:33], v[34:35]
	v_pk_fma_f32 v[40:41], v[172:173], v[172:173], v[44:45] op_sel_hi:[1,1,0]
	v_pk_fma_f32 v[44:45], v[170:171], v[170:171], v[46:47] op_sel_hi:[1,1,0]
	v_pk_add_f32 v[34:35], v[36:37], v[36:37] op_sel_hi:[0,1]
	v_pk_add_f32 v[32:33], v[32:33], v[32:33] op_sel_hi:[0,1]
	v_pk_mul_f32 v[48:49], v[178:179], v[178:179]
	v_pk_mul_f32 v[50:51], v[180:181], v[180:181]
	v_mul_f32_e32 v40, v176, v176
	v_mul_f32_e32 v44, v177, v177
	v_mul_f32_e32 v34, v174, v174
	v_mul_f32_e32 v32, v175, v175
	v_pk_mov_b32 v[46:47], v[50:51], v[48:49] op_sel:[1,0]
	v_mov_b32_e32 v51, v49
	v_pk_add_f32 v[36:37], v[40:41], v[44:45]
	v_pk_add_f32 v[32:33], v[34:35], v[32:33]
	v_mul_f32_e32 v52, v188, v188
	v_mul_f32_e32 v54, v186, v186
	v_pk_add_f32 v[38:39], v[46:47], v[50:51]
	v_pk_add_f32 v[32:33], v[36:37], v[32:33]
	v_pk_fma_f32 v[48:49], v[188:189], v[188:189], v[52:53] op_sel_hi:[1,1,0]
	v_pk_fma_f32 v[52:53], v[186:187], v[186:187], v[54:55] op_sel_hi:[1,1,0]
	v_pk_add_f32 v[38:39], v[38:39], v[38:39] op_sel_hi:[0,1]
	v_pk_add_f32 v[32:33], v[32:33], v[32:33] op_sel_hi:[0,1]
	v_mul_f32_e32 v48, v184, v184
	v_mul_f32_e32 v52, v185, v185
	v_mul_f32_e32 v38, v182, v182
	v_mul_f32_e32 v32, v183, v183
	v_pk_add_f32 v[40:41], v[48:49], v[52:53]
	v_pk_add_f32 v[32:33], v[38:39], v[32:33]
	s_nop 0
	v_pk_add_f32 v[32:33], v[40:41], v[32:33]
	s_nop 0
	v_add_f32_e32 v32, v32, v33
	ds_bpermute_b32 v33, v73, v32
	s_waitcnt lgkmcnt(0)
; #define GAS __attribute__((address_space(1)))
; __device__ __forceinline__ unsigned pk2(float lo, float hi) { return f2bf(lo) | (f2bf(hi) << 16); }
; __device__ __forceinline__ unsigned pk4_fp8(float a, float b, float c, float d) { int r = __builtin_amdgcn_cvt_pk_fp8_f32(a, b, 0, false); r = __builtin_amdgcn_cvt_pk_fp8_f32(c, d, r, true); return (unsigned)r; }
; template <int l>
; __device__ __forceinline__ void layer_phases(Frame& F, const XcdBarrier& bar, const int lo, const int hi) {
;     ...
;                     const float mean = wave_sum(s) * (1.f / D); float s2 = 0.f;
; #pragma unroll
;                     for (int j = 0; j < 8; ++j) { v[j] = v[j] - mean; s2 += (v[j].x * v[j].x + v[j].y * v[j].y) + (v[j].z * v[j].z + v[j].w * v[j].w); }
;                     const float rstd = 1.f / sqrtf(wave_sum(s2) * (1.f / D) + LN_EPS);
; #pragma unroll
;                     for (int j = 0; j < 8; ++j) { const int k = 4 * lq + 256 * j;
;                         const f32x4 xv = v[j] * rstd * *(const GAS f32x4*)(g1 + k) + *(const GAS f32x4*)(b1 + k);
;                         { v2u xo; xo.x = pk2(xv.x, xv.y); xo.y = pk2(xv.z, xv.w); *(GAS v2u*)(x1 + (size_t)m * D + k) = xo; }
;                         const f32x4 hv = xv * (*(const GAS f32x4*)(mrow + 8192 + k) + 1.0f) + *(const GAS f32x4*)(mrow + 6144 + k);
;                         v2u o; o.x = pk2(hv.x, hv.y); o.y = pk2(hv.z, hv.w);
;                         *(GAS unsigned*)(h2q + (size_t)m * D + k) = pk4_fp8(hv.x, hv.y, hv.z, hv.w);
	v_add_f32_e32 v34, v32, v33
	ds_bpermute_b32 v35, v217, v34
	v_lshl_add_u64 v[32:33], s[16:17], 0, v[86:87]
	v_lshl_add_u64 v[214:215], v[32:33], 1, s[26:27]
	s_waitcnt lgkmcnt(0)
	v_add_f32_e32 v36, v34, v35
	ds_bpermute_b32 v37, v218, v36
	v_lshl_add_u64 v[34:35], v[32:33], 2, s[20:21]
	v_add_co_u32_e32 v32, vcc, s87, v34
	global_load_dwordx4 v[44:47], v[34:35], off nt
	global_load_dwordx4 v[52:55], v[34:35], off offset:1024 nt
	global_load_dwordx4 v[48:51], v[34:35], off offset:2048 nt
	global_load_dwordx4 v[40:43], v[34:35], off offset:3072 nt
	s_waitcnt lgkmcnt(0)
	v_add_f32_e32 v36, v36, v37
	ds_bpermute_b32 v37, v219, v36
	v_addc_co_u32_e32 v33, vcc, 0, v35, vcc
	global_load_dwordx2 v[206:207], v[214:215], off nt
	global_load_dwordx2 v[204:205], v[214:215], off offset:512 nt
	global_load_dwordx2 v[202:203], v[214:215], off offset:1024 nt
	global_load_dwordx2 v[200:201], v[214:215], off offset:1536 nt
	s_waitcnt lgkmcnt(0)
	v_add_f32_e32 v36, v36, v37
	ds_bpermute_b32 v37, v220, v36
	s_waitcnt lgkmcnt(0)
	v_add_f32_e32 v34, v36, v37
	ds_bpermute_b32 v35, v221, v34
	s_waitcnt lgkmcnt(0)
	v_add_f32_e32 v34, v34, v35
	v_fmamk_f32 v34, v34, 0x3a000000, v223
	v_mul_f32_e32 v35, 0x4f800000, v34
	v_cmp_gt_f32_e32 vcc, s89, v34
	s_waitcnt vmcnt(2)
	s_waitcnt lgkmcnt(0)
	v_and_b32_e32 v233, 0xffff0000, v204
	v_cndmask_b32_e32 v80, v34, v35, vcc
	v_sqrt_f32_e32 v208, v80
	global_load_dwordx4 v[56:59], v[32:33], off nt
	global_load_dwordx4 v[60:63], v[32:33], off offset:1024 nt
	global_load_dwordx4 v[36:39], v[32:33], off offset:2048 nt
	s_nop 0
	global_load_dwordx4 v[32:35], v[32:33], off offset:3072 nt
	s_waitcnt vmcnt(4)
	s_waitcnt lgkmcnt(0)
	v_lshlrev_b32_e32 v236, 16, v200
	v_and_b32_e32 v237, 0xffff0000, v200
	v_add_u32_e32 v209, -1, v208
	v_add_u32_e32 v210, 1, v208
	v_fma_f32 v211, -v209, v208, v80
	v_fma_f32 v212, -v210, v208, v80
	v_cmp_ge_f32_e64 s[14:15], 0, v211
	v_lshlrev_b32_e32 v200, 16, v201
	v_and_b32_e32 v201, 0xffff0000, v201
	v_cndmask_b32_e64 v208, v208, v209, s[14:15]
	v_cmp_lt_f32_e64 s[14:15], 0, v212
	v_pk_mul_f32 v[18:19], v[18:19], v[200:201]
	v_lshlrev_b32_e32 v234, 16, v202
	v_cndmask_b32_e64 v208, v208, v210, s[14:15]
	v_mul_f32_e32 v209, 0x37800000, v208
	v_cndmask_b32_e32 v208, v208, v209, vcc
	v_cmp_class_f32_e32 vcc, v80, v224
	v_and_b32_e32 v235, 0xffff0000, v202
	v_lshlrev_b32_e32 v202, 16, v203
	v_cndmask_b32_e32 v80, v208, v80, vcc
	v_div_scale_f32 v228, s[0:1], v80, v80, 1.0
	v_rcp_f32_e32 v229, v228
	v_div_scale_f32 v230, vcc, 1.0, v80, 1.0
	global_load_dwordx2 v[208:209], v[214:215], off offset:2048 nt
	global_load_dwordx2 v[212:213], v[214:215], off offset:2560 nt
	global_load_dwordx2 v[210:211], v[214:215], off offset:3072 nt
	s_nop 0
	global_load_dwordx2 v[214:215], v[214:215], off offset:3584 nt
	v_fma_f32 v231, -v228, v229, 1.0
	v_fmac_f32_e32 v229, v231, v229
	v_mul_f32_e32 v231, v230, v229
	v_fma_f32 v232, -v228, v231, v230
	v_fmac_f32_e32 v231, v232, v229
	v_fma_f32 v228, -v228, v231, v230
	v_div_fmas_f32 v228, v228, v229, v231
	v_div_fixup_f32 v80, v228, v80, 1.0
	v_pk_mul_f32 v[198:199], v[198:199], v[80:81] op_sel_hi:[1,0]
	v_pk_mul_f32 v[190:191], v[190:191], v[80:81] op_sel_hi:[1,0]
	v_pk_fma_f32 v[198:199], v[64:65], v[198:199], v[68:69]
	v_pk_fma_f32 v[190:191], v[66:67], v[190:191], v[70:71]
	v_bfe_u32 v64, v198, 16, 1
	v_bfe_u32 v66, v190, 16, 1
	v_bfe_u32 v65, v199, 16, 1
	v_bfe_u32 v67, v191, 16, 1
	v_add3_u32 v64, v198, v64, s90
	v_add3_u32 v66, v190, v66, s90
	v_add3_u32 v65, v199, v65, s90
	v_add3_u32 v67, v191, v67, s90
	v_lshrrev_b32_e32 v64, 16, v64
	v_lshrrev_b32_e32 v66, 16, v66
	v_and_or_b32 v64, v65, s86, v64
	v_and_or_b32 v65, v67, s86, v66
	global_store_dwordx2 v[196:197], v[64:65], off
	ds_read_b128 v[64:67], v252 offset:16384
	s_nop 0
	ds_read_b128 v[68:71], v252 offset:24576
	v_mov_b32_e32 v228, 0
	s_add_u32 s0, s50, s18
	s_addc_u32 s1, s51, s19
	v_pk_mul_f32 v[194:195], v[194:195], v[80:81] op_sel_hi:[1,0]
	v_pk_mul_f32 v[192:193], v[192:193], v[80:81] op_sel_hi:[1,0]
	v_pk_mul_f32 v[168:169], v[168:169], v[80:81] op_sel_hi:[1,0]
	v_pk_mul_f32 v[166:167], v[166:167], v[80:81] op_sel_hi:[1,0]
	v_pk_mul_f32 v[172:173], v[172:173], v[80:81] op_sel_hi:[1,0]
	v_pk_mul_f32 v[170:171], v[170:171], v[80:81] op_sel_hi:[1,0]
	v_pk_mul_f32 v[176:177], v[176:177], v[80:81] op_sel_hi:[1,0]
	v_pk_mul_f32 v[174:175], v[174:175], v[80:81] op_sel_hi:[1,0]
	v_pk_mul_f32 v[180:181], v[180:181], v[80:81] op_sel_hi:[1,0]
	v_pk_mul_f32 v[178:179], v[178:179], v[80:81] op_sel_hi:[1,0]
	v_pk_mul_f32 v[188:189], v[188:189], v[80:81] op_sel_hi:[1,0]
	v_pk_mul_f32 v[186:187], v[186:187], v[80:81] op_sel_hi:[1,0]
	v_lshlrev_b32_e32 v232, 16, v204
	v_lshlrev_b32_e32 v204, 16, v205
	v_and_b32_e32 v205, 0xffff0000, v205
	v_and_b32_e32 v203, 0xffff0000, v203
	v_pk_mul_f32 v[26:27], v[26:27], v[204:205]
	v_pk_mul_f32 v[204:205], v[24:25], v[232:233]
	v_pk_mul_f32 v[16:17], v[16:17], v[236:237]
	v_pk_mul_f32 v[22:23], v[22:23], v[202:203]
	v_pk_mul_f32 v[202:203], v[20:21], v[234:235]
	v_pk_fma_f32 v[50:51], v[50:51], s[40:41], v[22:23] op_sel_hi:[1,0,1]
	v_pk_fma_f32 v[48:49], v[48:49], s[40:41], v[202:203] op_sel_hi:[1,0,1]
	s_waitcnt vmcnt(4)
	s_waitcnt lgkmcnt(0)
	v_lshlrev_b32_e32 v238, 16, v208
	v_and_b32_e32 v239, 0xffff0000, v208
	v_lshlrev_b32_e32 v208, 16, v209
	s_waitcnt vmcnt(1)
	s_waitcnt lgkmcnt(0)
; #define GAS __attribute__((address_space(1)))
; #define LAS __attribute__((address_space(3)))
; __device__ __forceinline__ unsigned pk2(float lo, float hi) { return f2bf(lo) | (f2bf(hi) << 16); }
; __device__ __forceinline__ unsigned pk4_fp8(float a, float b, float c, float d) { int r = __builtin_amdgcn_cvt_pk_fp8_f32(a, b, 0, false); r = __builtin_amdgcn_cvt_pk_fp8_f32(c, d, r, true); return (unsigned)r; }
; template <int l>
; __device__ __forceinline__ void layer_phases(Frame& F, const XcdBarrier& bar, const int lo, const int hi) {
;     ...
;                     for (int j = 0; j < 8; ++j) { const int k = 4 * lq + 256 * j;
;                         const f32x4 xv = v[j] * rstd * *(const GAS f32x4*)(g1 + k) + *(const GAS f32x4*)(b1 + k);
;                         { v2u xo; xo.x = pk2(xv.x, xv.y); xo.y = pk2(xv.z, xv.w); *(GAS v2u*)(x1 + (size_t)m * D + k) = xo; }
;                         const f32x4 hv = xv * (*(const GAS f32x4*)(mrow + 8192 + k) + 1.0f) + *(const GAS f32x4*)(mrow + 6144 + k);
;                         v2u o; o.x = pk2(hv.x, hv.y); o.y = pk2(hv.z, hv.w);
;                         *(GAS unsigned*)(h2q + (size_t)m * D + k) = pk4_fp8(hv.x, hv.y, hv.z, hv.w);
;                         const int chunk = (lq >> 1) + 32 * j;
;                         *(LAS v2u*)(h2s + rloc * 4096 + ((chunk ^ (rloc & 15)) << 4) + (lq & 1) * 8) = o; }
	v_lshlrev_b32_e32 v244, 16, v214
	v_and_b32_e32 v245, 0xffff0000, v214
	v_pk_mul_f32 v[200:201], v[0:1], v[244:245]
	v_lshlrev_b32_e32 v214, 16, v215
	v_and_b32_e32 v215, 0xffff0000, v215
	v_and_b32_e32 v209, 0xffff0000, v209
	v_lshlrev_b32_e32 v240, 16, v212
	v_and_b32_e32 v241, 0xffff0000, v212
	v_lshlrev_b32_e32 v212, 16, v213
	v_and_b32_e32 v213, 0xffff0000, v213
	v_lshlrev_b32_e32 v242, 16, v210
	v_and_b32_e32 v243, 0xffff0000, v210
	v_lshlrev_b32_e32 v210, 16, v211
	v_and_b32_e32 v211, 0xffff0000, v211
	v_pk_mul_f32 v[12:13], v[12:13], v[238:239]
	v_pk_mul_f32 v[14:15], v[14:15], v[208:209]
	v_pk_mul_f32 v[8:9], v[8:9], v[240:241]
	v_pk_mul_f32 v[10:11], v[10:11], v[212:213]
	v_pk_mul_f32 v[4:5], v[4:5], v[242:243]
	v_pk_mul_f32 v[6:7], v[6:7], v[210:211]
	s_waitcnt lgkmcnt(0)
	v_pk_add_f32 v[64:65], v[64:65], 1.0 op_sel_hi:[1,0]
	s_waitcnt lgkmcnt(0)
	v_pk_fma_f32 v[64:65], v[64:65], v[198:199], v[68:69]
	v_pk_add_f32 v[66:67], v[66:67], 1.0 op_sel_hi:[1,0]
	v_cvt_pk_fp8_f32 v228, v64, v65
	v_pk_fma_f32 v[66:67], v[66:67], v[190:191], v[70:71]
	v_lshl_add_u64 v[190:191], s[0:1], 0, v[86:87]
	s_lshl_b64 s[0:1], s[48:49], 12
	v_cvt_pk_fp8_f32 v228, v66, v67 op_sel:[0,0,1]
	s_add_u32 s0, s3, s0
	s_addc_u32 s1, s41, s1
	global_store_dword v[190:191], v228, off
	ds_read_b128 v[68:71], v252 offset:1024
	s_nop 0
	ds_read_b128 v[228:231], v252 offset:9216
	s_waitcnt lgkmcnt(0)
	v_pk_fma_f32 v[198:199], v[70:71], v[192:193], v[230:231]
	v_pk_fma_f32 v[228:229], v[68:69], v[194:195], v[228:229]
	v_bfe_u32 v70, v198, 16, 1
	v_bfe_u32 v68, v228, 16, 1
	v_bfe_u32 v69, v229, 16, 1
	v_bfe_u32 v71, v199, 16, 1
	v_add3_u32 v68, v228, v68, s90
	v_add3_u32 v70, v198, v70, s90
	v_add3_u32 v69, v229, v69, s90
	v_add3_u32 v71, v199, v71, s90
	v_lshrrev_b32_e32 v68, 16, v68
	v_lshrrev_b32_e32 v70, 16, v70
	v_and_or_b32 v68, v69, s86, v68
	v_and_or_b32 v69, v71, s86, v70
	global_store_dwordx2 v[196:197], v[68:69], off offset:512
	ds_read_b128 v[68:71], v252 offset:17408
	s_nop 0
	ds_read_b128 v[192:195], v252 offset:25600
	v_mov_b32_e32 v230, 0
	s_waitcnt lgkmcnt(0)
	v_pk_add_f32 v[68:69], v[68:69], 1.0 op_sel_hi:[1,0]
	s_waitcnt lgkmcnt(0)
	v_pk_fma_f32 v[68:69], v[68:69], v[228:229], v[192:193]
	v_pk_add_f32 v[70:71], v[70:71], 1.0 op_sel_hi:[1,0]
	v_cvt_pk_fp8_f32 v230, v68, v69
	v_pk_fma_f32 v[70:71], v[70:71], v[198:199], v[194:195]
	s_nop 0
	v_cvt_pk_fp8_f32 v230, v70, v71 op_sel:[0,0,1]
	global_store_dword v[190:191], v230, off offset:256
	ds_read_b128 v[192:195], v252 offset:2048
	s_nop 0
	ds_read_b128 v[228:231], v252 offset:10240
	s_waitcnt lgkmcnt(0)
	v_pk_fma_f32 v[198:199], v[194:195], v[166:167], v[230:231]
	v_pk_fma_f32 v[228:229], v[192:193], v[168:169], v[228:229]
	v_bfe_u32 v168, v198, 16, 1
	v_bfe_u32 v166, v228, 16, 1
	v_bfe_u32 v167, v229, 16, 1
	v_bfe_u32 v169, v199, 16, 1
	v_add3_u32 v166, v228, v166, s90
	v_add3_u32 v168, v198, v168, s90
	v_add3_u32 v167, v229, v167, s90
	v_add3_u32 v169, v199, v169, s90
	v_lshrrev_b32_e32 v166, 16, v166
	v_lshrrev_b32_e32 v168, 16, v168
	v_and_or_b32 v166, v167, s86, v166
	v_and_or_b32 v167, v169, s86, v168
	global_store_dwordx2 v[196:197], v[166:167], off offset:1024
	ds_read_b128 v[166:169], v252 offset:18432
	s_nop 0
	ds_read_b128 v[192:195], v252 offset:26624
	v_mov_b32_e32 v230, 0
	s_waitcnt lgkmcnt(0)
	v_pk_add_f32 v[166:167], v[166:167], 1.0 op_sel_hi:[1,0]
	s_waitcnt lgkmcnt(0)
	v_pk_fma_f32 v[166:167], v[166:167], v[228:229], v[192:193]
	v_pk_add_f32 v[168:169], v[168:169], 1.0 op_sel_hi:[1,0]
	v_cvt_pk_fp8_f32 v230, v166, v167
	v_pk_fma_f32 v[168:169], v[168:169], v[198:199], v[194:195]
	s_nop 0
	v_cvt_pk_fp8_f32 v230, v168, v169 op_sel:[0,0,1]
	global_store_dword v[190:191], v230, off offset:512
	ds_read_b128 v[192:195], v252 offset:3072
	s_nop 0
	ds_read_b128 v[228:231], v252 offset:11264
	s_waitcnt lgkmcnt(0)
	v_pk_fma_f32 v[198:199], v[170:171], v[194:195], v[230:231]
	v_pk_fma_f32 v[228:229], v[172:173], v[192:193], v[228:229]
	v_bfe_u32 v172, v198, 16, 1
	v_bfe_u32 v170, v228, 16, 1
	v_bfe_u32 v171, v229, 16, 1
	v_bfe_u32 v173, v199, 16, 1
	v_add3_u32 v170, v228, v170, s90
	v_add3_u32 v172, v198, v172, s90
	v_add3_u32 v171, v229, v171, s90
	v_add3_u32 v173, v199, v173, s90
	v_lshrrev_b32_e32 v170, 16, v170
	v_lshrrev_b32_e32 v172, 16, v172
	v_and_or_b32 v170, v171, s86, v170
	v_and_or_b32 v171, v173, s86, v172
	global_store_dwordx2 v[196:197], v[170:171], off offset:1536
	ds_read_b128 v[170:173], v252 offset:19456
	s_nop 0
	ds_read_b128 v[192:195], v252 offset:27648
	v_mov_b32_e32 v230, 0
	s_waitcnt lgkmcnt(0)
	v_pk_add_f32 v[170:171], v[170:171], 1.0 op_sel_hi:[1,0]
	s_waitcnt lgkmcnt(0)
	v_pk_fma_f32 v[170:171], v[228:229], v[170:171], v[192:193]
	v_pk_add_f32 v[172:173], v[172:173], 1.0 op_sel_hi:[1,0]
	v_cvt_pk_fp8_f32 v230, v170, v171
	v_pk_fma_f32 v[172:173], v[198:199], v[172:173], v[194:195]
	s_nop 0
	v_cvt_pk_fp8_f32 v230, v172, v173 op_sel:[0,0,1]
	global_store_dword v[190:191], v230, off offset:768
	ds_read_b128 v[192:195], v252 offset:4096
	s_nop 0
	ds_read_b128 v[228:231], v252 offset:12288
	s_waitcnt lgkmcnt(0)
	v_pk_fma_f32 v[198:199], v[174:175], v[194:195], v[230:231]
	v_pk_fma_f32 v[228:229], v[176:177], v[192:193], v[228:229]
	v_bfe_u32 v176, v198, 16, 1
	v_bfe_u32 v174, v228, 16, 1
	v_bfe_u32 v175, v229, 16, 1
	v_bfe_u32 v177, v199, 16, 1
	v_add3_u32 v174, v228, v174, s90
	v_add3_u32 v176, v198, v176, s90
	v_add3_u32 v175, v229, v175, s90
	v_add3_u32 v177, v199, v177, s90
	v_lshrrev_b32_e32 v174, 16, v174
	v_lshrrev_b32_e32 v176, 16, v176
	v_and_or_b32 v174, v175, s86, v174
	v_and_or_b32 v175, v177, s86, v176
	global_store_dwordx2 v[196:197], v[174:175], off offset:2048
	ds_read_b128 v[174:177], v252 offset:20480
	s_nop 0
	ds_read_b128 v[192:195], v252 offset:28672
	v_mov_b32_e32 v230, 0
	s_waitcnt lgkmcnt(0)
; #define GAS __attribute__((address_space(1)))
; #define LAS __attribute__((address_space(3)))
; __device__ __forceinline__ unsigned pk2(float lo, float hi) { return f2bf(lo) | (f2bf(hi) << 16); }
; __device__ __forceinline__ unsigned pk4_fp8(float a, float b, float c, float d) { int r = __builtin_amdgcn_cvt_pk_fp8_f32(a, b, 0, false); r = __builtin_amdgcn_cvt_pk_fp8_f32(c, d, r, true); return (unsigned)r; }
; __device__ __forceinline__ f32x4 bf4(unsigned a, unsigned b) { return (f32x4){bflo(a), bfhi(a), bflo(b), bfhi(b)}; }
; template <int l>
; __device__ __forceinline__ void layer_phases(Frame& F, const XcdBarrier& bar, const int lo, const int hi) {
;     ...
;                     for (int j = 0; j < 8; ++j) { const size_t off = (size_t)(m0 + 2 * rp + rr) * D + 4 * lq + 256 * j;
;                         f32x4 xv; if (l == 0) xv = __builtin_nontemporal_load((const GAS f32x4*)(xin + off)); else { const v2u xw_ = __builtin_nontemporal_load((const GAS v2u*)(xinb + off)); xv = bf4(xw_.x, xw_.y); } const v2u mw = __builtin_nontemporal_load((const GAS v2u*)(mixb + off)); const f32x4 gv = *(const GAS f32x4*)(mrow + 4096 + 4 * lq + 256 * j);
;                         vv[rr][j] = xv * ALPHA + gv * (f32x4){bflo(mw.x), bfhi(mw.x), bflo(mw.y), bfhi(mw.y)}; }
; #pragma unroll
;                 for (int rq = 0; rq < 2; ++rq) { const int rr = 2 * rp + rq, m = m0 + rr, rloc = 4 * F.wave + rr;
;                     f32x4 (&v)[8] = vv[rq]; float s = 0.f;
; #pragma unroll
;                     for (int j = 0; j < 8; ++j) s += (v[j].x + v[j].y) + (v[j].z + v[j].w);
;     ...
;                     for (int j = 0; j < 8; ++j) { const int k = 4 * lq + 256 * j;
;                         const f32x4 xv = v[j] * rstd * *(const GAS f32x4*)(g1 + k) + *(const GAS f32x4*)(b1 + k);
;                         { v2u xo; xo.x = pk2(xv.x, xv.y); xo.y = pk2(xv.z, xv.w); *(GAS v2u*)(x1 + (size_t)m * D + k) = xo; }
;                         const f32x4 hv = xv * (*(const GAS f32x4*)(mrow + 8192 + k) + 1.0f) + *(const GAS f32x4*)(mrow + 6144 + k);
;                         v2u o; o.x = pk2(hv.x, hv.y); o.y = pk2(hv.z, hv.w);
;                         *(GAS unsigned*)(h2q + (size_t)m * D + k) = pk4_fp8(hv.x, hv.y, hv.z, hv.w);
;                         const int chunk = (lq >> 1) + 32 * j;
;                         *(LAS v2u*)(h2s + rloc * 4096 + ((chunk ^ (rloc & 15)) << 4) + (lq & 1) * 8) = o; }
	v_pk_add_f32 v[174:175], v[174:175], 1.0 op_sel_hi:[1,0]
	s_waitcnt lgkmcnt(0)
	v_pk_fma_f32 v[174:175], v[228:229], v[174:175], v[192:193]
	v_pk_add_f32 v[176:177], v[176:177], 1.0 op_sel_hi:[1,0]
	v_cvt_pk_fp8_f32 v230, v174, v175
	v_pk_fma_f32 v[176:177], v[198:199], v[176:177], v[194:195]
	s_nop 0
	v_cvt_pk_fp8_f32 v230, v176, v177 op_sel:[0,0,1]
	global_store_dword v[190:191], v230, off offset:1024
	ds_read_b128 v[192:195], v252 offset:5120
	s_nop 0
	ds_read_b128 v[228:231], v252 offset:13312
	s_waitcnt lgkmcnt(0)
	v_pk_fma_f32 v[198:199], v[178:179], v[194:195], v[230:231]
	v_pk_fma_f32 v[228:229], v[180:181], v[192:193], v[228:229]
	v_bfe_u32 v180, v198, 16, 1
	v_bfe_u32 v178, v228, 16, 1
	v_bfe_u32 v179, v229, 16, 1
	v_bfe_u32 v181, v199, 16, 1
	v_add3_u32 v178, v228, v178, s90
	v_add3_u32 v180, v198, v180, s90
	v_add3_u32 v179, v229, v179, s90
	v_add3_u32 v181, v199, v181, s90
	v_lshrrev_b32_e32 v178, 16, v178
	v_lshrrev_b32_e32 v180, 16, v180
	v_and_or_b32 v178, v179, s86, v178
	v_and_or_b32 v179, v181, s86, v180
	global_store_dwordx2 v[196:197], v[178:179], off offset:2560
	ds_read_b128 v[178:181], v252 offset:21504
	s_nop 0
	ds_read_b128 v[192:195], v252 offset:29696
	v_mov_b32_e32 v230, 0
	s_waitcnt lgkmcnt(0)
	v_pk_add_f32 v[178:179], v[178:179], 1.0 op_sel_hi:[1,0]
	s_waitcnt lgkmcnt(0)
	v_pk_fma_f32 v[178:179], v[228:229], v[178:179], v[192:193]
	v_pk_add_f32 v[180:181], v[180:181], 1.0 op_sel_hi:[1,0]
	v_cvt_pk_fp8_f32 v230, v178, v179
	v_pk_fma_f32 v[180:181], v[198:199], v[180:181], v[194:195]
	s_nop 0
	v_cvt_pk_fp8_f32 v230, v180, v181 op_sel:[0,0,1]
	global_store_dword v[190:191], v230, off offset:1280
	ds_read_b128 v[192:195], v252 offset:6144
	s_nop 0
	ds_read_b128 v[228:231], v252 offset:14336
	s_waitcnt lgkmcnt(0)
	v_pk_fma_f32 v[198:199], v[186:187], v[194:195], v[230:231]
	v_pk_fma_f32 v[228:229], v[188:189], v[192:193], v[228:229]
	v_bfe_u32 v188, v198, 16, 1
	v_bfe_u32 v186, v228, 16, 1
	v_bfe_u32 v187, v229, 16, 1
	v_bfe_u32 v189, v199, 16, 1
	v_add3_u32 v186, v228, v186, s90
	v_add3_u32 v188, v198, v188, s90
	v_add3_u32 v187, v229, v187, s90
	v_add3_u32 v189, v199, v189, s90
	v_lshrrev_b32_e32 v186, 16, v186
	v_lshrrev_b32_e32 v188, 16, v188
	v_and_or_b32 v186, v187, s86, v186
	v_and_or_b32 v187, v189, s86, v188
	global_store_dwordx2 v[196:197], v[186:187], off offset:3072
	ds_read_b128 v[186:189], v252 offset:22528
	s_nop 0
	ds_read_b128 v[192:195], v252 offset:30720
	v_lshlrev_b32_e32 v230, 16, v206
	v_and_b32_e32 v231, 0xffff0000, v206
	v_lshlrev_b32_e32 v206, 16, v207
	v_and_b32_e32 v207, 0xffff0000, v207
	v_pk_mul_f32 v[30:31], v[30:31], v[206:207]
	v_pk_mul_f32 v[206:207], v[2:3], v[214:215]
	v_pk_mul_f32 v[28:29], v[28:29], v[230:231]
	v_pk_fma_f32 v[20:21], v[46:47], s[40:41], v[30:31] op_sel_hi:[1,0,1]
	v_pk_fma_f32 v[24:25], v[44:45], s[40:41], v[28:29] op_sel_hi:[1,0,1]
	v_pk_fma_f32 v[28:29], v[54:55], s[40:41], v[26:27] op_sel_hi:[1,0,1]
	v_pk_fma_f32 v[30:31], v[52:53], s[40:41], v[204:205] op_sel_hi:[1,0,1]
	v_pk_fma_f32 v[44:45], v[42:43], s[40:41], v[18:19] op_sel_hi:[1,0,1]
	v_pk_fma_f32 v[46:47], v[40:41], s[40:41], v[16:17] op_sel_hi:[1,0,1]
	v_pk_fma_f32 v[40:41], v[58:59], s[40:41], v[14:15] op_sel_hi:[1,0,1]
	v_pk_fma_f32 v[42:43], v[56:57], s[40:41], v[12:13] op_sel_hi:[1,0,1]
	v_pk_fma_f32 v[12:13], v[62:63], s[40:41], v[10:11] op_sel_hi:[1,0,1]
	v_pk_fma_f32 v[14:15], v[60:61], s[40:41], v[8:9] op_sel_hi:[1,0,1]
	v_pk_fma_f32 v[8:9], v[38:39], s[40:41], v[6:7] op_sel_hi:[1,0,1]
	v_pk_fma_f32 v[10:11], v[36:37], s[40:41], v[4:5] op_sel_hi:[1,0,1]
	v_pk_fma_f32 v[4:5], v[34:35], s[40:41], v[206:207] op_sel_hi:[1,0,1]
	v_pk_fma_f32 v[6:7], v[32:33], s[40:41], v[200:201] op_sel_hi:[1,0,1]
	v_mov_b32_e32 v22, v24
	v_mov_b32_e32 v23, v30
	v_mov_b32_e32 v26, v25
	v_mov_b32_e32 v27, v31
	v_mov_b32_e32 v32, v20
	v_mov_b32_e32 v33, v28
	v_mov_b32_e32 v34, v21
	v_mov_b32_e32 v35, v29
	v_pk_mov_b32 v[36:37], v[48:49], v[50:51] op_sel:[1,0]
	v_mov_b32_e32 v38, v48
	v_mov_b32_e32 v39, v51
	v_pk_add_f32 v[22:23], v[22:23], v[26:27]
	v_pk_add_f32 v[26:27], v[32:33], v[34:35]
	v_pk_add_f32 v[32:33], v[36:37], v[38:39]
	v_pk_add_f32 v[22:23], v[22:23], v[26:27]
	v_pk_add_f32 v[26:27], v[32:33], v[32:33] op_sel:[0,1] op_sel_hi:[1,0]
	v_add_f32_e32 v22, 0, v22
	v_add_f32_e32 v56, v46, v47
	v_add_f32_e32 v58, v44, v45
	v_mov_b32_e32 v61, v42
	v_mov_b32_e32 v57, v40
	v_mov_b32_e32 v59, v41
	v_mov_b32_e32 v27, v43
	v_add_f32_e32 v60, v22, v23
	v_pk_mov_b32 v[62:63], v[14:15], v[12:13] op_sel:[1,0]
	v_pk_add_f32 v[34:35], v[56:57], v[58:59]
	v_pk_add_f32 v[22:23], v[60:61], v[26:27]
	v_pk_mul_f32 v[26:27], v[182:183], v[80:81] op_sel_hi:[1,0]
	v_pk_add_f32 v[22:23], v[22:23], v[34:35]
	s_waitcnt lgkmcnt(0)
	v_pk_add_f32 v[0:1], v[186:187], 1.0 op_sel_hi:[1,0]
	s_waitcnt lgkmcnt(0)
	v_pk_fma_f32 v[0:1], v[228:229], v[0:1], v[192:193]
	v_pk_add_f32 v[2:3], v[188:189], 1.0 op_sel_hi:[1,0]
	v_cvt_pk_fp8_f32 v246, v0, v1
	v_pk_fma_f32 v[2:3], v[198:199], v[2:3], v[194:195]
	v_mov_b32_e32 v186, v14
	v_mov_b32_e32 v187, v13
	v_cvt_pk_fp8_f32 v246, v2, v3 op_sel:[0,0,1]
	v_pk_add_f32 v[36:37], v[62:63], v[186:187]
	v_pk_add_f32 v[22:23], v[22:23], v[22:23] op_sel:[0,1] op_sel_hi:[1,0]
	v_pk_add_f32 v[32:33], v[36:37], v[36:37] op_sel:[0,1] op_sel_hi:[1,0]
	global_store_dword v[190:191], v246, off offset:1536
	ds_read_b128 v[16:19], v252 offset:7168
	ds_read_b128 v[52:55], v252 offset:15360
	v_add_f32_e32 v188, v10, v11
	v_add_f32_e32 v192, v8, v9
	v_mov_b32_e32 v189, v4
	v_mov_b32_e32 v193, v5
	v_mov_b32_e32 v33, v7
	v_mov_b32_e32 v23, v6
	v_pk_add_f32 v[38:39], v[188:189], v[192:193]
	v_pk_add_f32 v[22:23], v[22:23], v[32:33]
	v_mov_b32_e32 v192, 0
	v_pk_add_f32 v[22:23], v[22:23], v[38:39]
	s_waitcnt lgkmcnt(0)
; #define LAS __attribute__((address_space(3)))
; template <int l>
; __device__ __forceinline__ void layer_phases(Frame& F, const XcdBarrier& bar, const int lo, const int hi) {
;     ...
;                     f32x4 (&v)[8] = vv[rq]; float s = 0.f;
; #pragma unroll
;                     for (int j = 0; j < 8; ++j) s += (v[j].x + v[j].y) + (v[j].z + v[j].w);
;                     const float mean = wave_sum(s) * (1.f / D); float s2 = 0.f;
; #pragma unroll
;                     for (int j = 0; j < 8; ++j) { v[j] = v[j] - mean; s2 += (v[j].x * v[j].x + v[j].y * v[j].y) + (v[j].z * v[j].z + v[j].w * v[j].w); }
;                     const float rstd = 1.f / sqrtf(wave_sum(s2) * (1.f / D) + LN_EPS);
;     ...
;                         const int chunk = (lq >> 1) + 32 * j;
;                         *(LAS v2u*)(h2s + rloc * 4096 + ((chunk ^ (rloc & 15)) << 4) + (lq & 1) * 8) = o; }
	v_pk_fma_f32 v[26:27], v[26:27], v[18:19], v[54:55]
	v_add_f32_e32 v22, v22, v23
	ds_bpermute_b32 v23, v73, v22
	v_bfe_u32 v18, v26, 16, 1
	v_bfe_u32 v19, v27, 16, 1
	v_add3_u32 v18, v26, v18, s90
	v_add3_u32 v19, v27, v19, s90
	s_waitcnt lgkmcnt(0)
	v_add_f32_e32 v22, v22, v23
	ds_bpermute_b32 v23, v217, v22
	v_lshrrev_b32_e32 v18, 16, v18
	s_waitcnt lgkmcnt(0)
	v_add_f32_e32 v22, v22, v23
	ds_bpermute_b32 v23, v218, v22
	s_waitcnt lgkmcnt(0)
	v_add_f32_e32 v22, v22, v23
	ds_bpermute_b32 v23, v219, v22
	s_waitcnt lgkmcnt(0)
	v_add_f32_e32 v22, v22, v23
	ds_bpermute_b32 v23, v220, v22
	s_waitcnt lgkmcnt(0)
	v_add_f32_e32 v36, v22, v23
	v_pk_mul_f32 v[22:23], v[184:185], v[80:81] op_sel_hi:[1,0]
	ds_bpermute_b32 v37, v221, v36
	v_pk_fma_f32 v[22:23], v[22:23], v[16:17], v[52:53]
	s_waitcnt lgkmcnt(0)
	v_add_f32_e32 v36, v36, v37
	v_bfe_u32 v16, v22, 16, 1
	v_bfe_u32 v17, v23, 16, 1
	v_add3_u32 v16, v22, v16, s90
	v_add3_u32 v17, v23, v17, s90
	v_lshrrev_b32_e32 v16, 16, v16
	v_and_or_b32 v16, v17, s86, v16
	v_and_or_b32 v17, v19, s86, v18
	global_store_dwordx2 v[196:197], v[16:17], off offset:3584
	ds_read_b128 v[16:19], v252 offset:23552
	s_nop 0
	ds_read_b128 v[32:35], v252 offset:31744
	v_fmamk_f32 v21, v36, 0xba000000, v21
	v_fmamk_f32 v25, v36, 0xba000000, v25
	v_fmamk_f32 v29, v36, 0xba000000, v29
	v_fmamk_f32 v31, v36, 0xba000000, v31
	v_fmac_f32_e32 v20, 0xba000000, v36
	v_fmac_f32_e32 v24, 0xba000000, v36
	v_fmac_f32_e32 v28, 0xba000000, v36
	v_fmac_f32_e32 v30, 0xba000000, v36
	v_fmamk_f32 v49, v36, 0xba000000, v49
	v_fmac_f32_e32 v48, 0xba000000, v36
	v_fmamk_f32 v51, v36, 0xba000000, v51
	v_fmac_f32_e32 v50, 0xba000000, v36
	v_mov_b32_e32 v38, v25
	v_mov_b32_e32 v39, v31
	v_mov_b32_e32 v54, v21
	v_mov_b32_e32 v55, v29
	v_fmamk_f32 v47, v36, 0xba000000, v47
	v_fmac_f32_e32 v46, 0xba000000, v36
	v_fmamk_f32 v45, v36, 0xba000000, v45
	v_fmac_f32_e32 v44, 0xba000000, v36
	v_fmamk_f32 v41, v36, 0xba000000, v41
	v_fmac_f32_e32 v40, 0xba000000, v36
	v_fmamk_f32 v43, v36, 0xba000000, v43
	v_fmac_f32_e32 v42, 0xba000000, v36
	v_fmamk_f32 v15, v36, 0xba000000, v15
	v_fmac_f32_e32 v14, 0xba000000, v36
	v_fmamk_f32 v13, v36, 0xba000000, v13
	v_fmac_f32_e32 v12, 0xba000000, v36
	v_fmamk_f32 v11, v36, 0xba000000, v11
	v_fmac_f32_e32 v10, 0xba000000, v36
	v_fmamk_f32 v9, v36, 0xba000000, v9
	v_fmac_f32_e32 v8, 0xba000000, v36
	v_fmamk_f32 v5, v36, 0xba000000, v5
	v_fmac_f32_e32 v4, 0xba000000, v36
	v_fmamk_f32 v7, v36, 0xba000000, v7
	v_fmac_f32_e32 v6, 0xba000000, v36
	v_mov_b32_e32 v36, v24
	v_mov_b32_e32 v37, v30
	v_mov_b32_e32 v52, v20
	v_mov_b32_e32 v53, v28
	v_pk_mul_f32 v[56:57], v[50:51], v[50:51]
	v_pk_mul_f32 v[58:59], v[48:49], v[48:49]
	v_pk_mul_f32 v[38:39], v[38:39], v[38:39]
	v_pk_mul_f32 v[54:55], v[54:55], v[54:55]
	v_pk_mov_b32 v[188:189], v[58:59], v[56:57] op_sel:[1,0]
	v_mov_b32_e32 v59, v57
	v_pk_fma_f32 v[36:37], v[36:37], v[36:37], v[38:39]
	v_pk_fma_f32 v[38:39], v[52:53], v[52:53], v[54:55]
	v_mul_f32_e32 v60, v46, v46
	v_mul_f32_e32 v62, v44, v44
	v_pk_mul_f32 v[182:183], v[12:13], v[12:13]
	v_pk_mul_f32 v[184:185], v[14:15], v[14:15]
	v_pk_add_f32 v[52:53], v[188:189], v[58:59]
	v_pk_add_f32 v[36:37], v[36:37], v[38:39]
	v_pk_fma_f32 v[56:57], v[46:47], v[46:47], v[60:61] op_sel_hi:[1,1,0]
	v_pk_fma_f32 v[60:61], v[44:45], v[44:45], v[62:63] op_sel_hi:[1,1,0]
	v_pk_mov_b32 v[62:63], v[184:185], v[182:183] op_sel:[1,0]
	v_mov_b32_e32 v185, v183
	v_pk_add_f32 v[38:39], v[52:53], v[52:53] op_sel_hi:[0,1]
	v_pk_add_f32 v[36:37], v[36:37], v[36:37] op_sel_hi:[0,1]
	v_pk_add_f32 v[54:55], v[62:63], v[184:185]
	v_mul_f32_e32 v38, v40, v40
	v_mul_f32_e32 v36, v41, v41
	v_pk_add_f32 v[58:59], v[54:55], v[54:55] op_sel_hi:[0,1]
	v_mul_f32_e32 v56, v42, v42
	v_mul_f32_e32 v60, v43, v43
	v_pk_add_f32 v[56:57], v[56:57], v[60:61]
	v_mul_f32_e32 v80, v10, v10
	v_mul_f32_e32 v186, v8, v8
	v_pk_fma_f32 v[182:183], v[10:11], v[10:11], v[80:81] op_sel_hi:[1,1,0]
	v_pk_fma_f32 v[186:187], v[8:9], v[8:9], v[186:187] op_sel_hi:[1,1,0]
	v_mul_f32_e32 v182, v6, v6
	v_mul_f32_e32 v186, v7, v7
	v_mul_f32_e32 v58, v4, v4
	v_pk_add_f32 v[60:61], v[182:183], v[186:187]
	v_mov_b32_e32 v62, 0
	v_lshlrev_b32_e32 v80, 4, v227
	s_waitcnt lgkmcnt(0)
	v_pk_add_f32 v[16:17], v[16:17], 1.0 op_sel_hi:[1,0]
	s_waitcnt lgkmcnt(0)
	v_pk_fma_f32 v[16:17], v[22:23], v[16:17], v[32:33]
	v_pk_add_f32 v[18:19], v[18:19], 1.0 op_sel_hi:[1,0]
	v_cvt_pk_fp8_f32 v192, v16, v17
	v_pk_fma_f32 v[18:19], v[26:27], v[18:19], v[34:35]
	v_pk_add_f32 v[22:23], v[38:39], v[36:37]
	v_cvt_pk_fp8_f32 v192, v18, v19 op_sel:[0,0,1]
	v_pk_add_f32 v[22:23], v[56:57], v[22:23]
	v_mov_b32_e32 v56, 0
	v_pk_add_f32 v[22:23], v[22:23], v[22:23] op_sel_hi:[0,1]
	global_store_dword v[190:191], v192, off offset:1792
	ds_read_b128 v[34:37], v252 offset:0
	ds_read_b128 v[52:55], v252 offset:8192
	v_mul_f32_e32 v22, v5, v5
	v_pk_add_f32 v[22:23], v[58:59], v[22:23]
	v_lshlrev_b32_e32 v57, 3, v227
	v_pk_add_f32 v[22:23], v[60:61], v[22:23]
	v_and_b32_e32 v63, 8, v57
	v_add_f32_e32 v22, v22, v23
	ds_bpermute_b32 v23, v73, v22
	v_add_u32_e32 v63, 0, v63
	v_lshrrev_b32_e32 v61, 1, v227
	v_mov_b32_e32 v60, 0
	s_waitcnt lgkmcnt(0)
	v_add_f32_e32 v22, v22, v23
	ds_bpermute_b32 v23, v217, v22
	s_waitcnt lgkmcnt(0)
	v_add_f32_e32 v22, v22, v23
	ds_bpermute_b32 v23, v218, v22
	s_waitcnt lgkmcnt(0)
	v_add_f32_e32 v22, v22, v23
	ds_bpermute_b32 v23, v219, v22
	s_waitcnt lgkmcnt(0)
	v_add_f32_e32 v22, v22, v23
	ds_bpermute_b32 v23, v220, v22
	s_waitcnt lgkmcnt(0)
	v_add_f32_e32 v22, v22, v23
	ds_bpermute_b32 v23, v221, v22
	s_waitcnt lgkmcnt(0)
; #define GAS __attribute__((address_space(1)))
; #define LAS __attribute__((address_space(3)))
; __device__ __forceinline__ unsigned pk2(float lo, float hi) { return f2bf(lo) | (f2bf(hi) << 16); }
; __device__ __forceinline__ unsigned pk4_fp8(float a, float b, float c, float d) { int r = __builtin_amdgcn_cvt_pk_fp8_f32(a, b, 0, false); r = __builtin_amdgcn_cvt_pk_fp8_f32(c, d, r, true); return (unsigned)r; }
; template <int l>
; __device__ __forceinline__ void layer_phases(Frame& F, const XcdBarrier& bar, const int lo, const int hi) {
;     ...
;                     const float mean = wave_sum(s) * (1.f / D); float s2 = 0.f;
; #pragma unroll
;                     for (int j = 0; j < 8; ++j) { v[j] = v[j] - mean; s2 += (v[j].x * v[j].x + v[j].y * v[j].y) + (v[j].z * v[j].z + v[j].w * v[j].w); }
;                     const float rstd = 1.f / sqrtf(wave_sum(s2) * (1.f / D) + LN_EPS);
; #pragma unroll
;                     for (int j = 0; j < 8; ++j) { const int k = 4 * lq + 256 * j;
;                         const f32x4 xv = v[j] * rstd * *(const GAS f32x4*)(g1 + k) + *(const GAS f32x4*)(b1 + k);
;                         { v2u xo; xo.x = pk2(xv.x, xv.y); xo.y = pk2(xv.z, xv.w); *(GAS v2u*)(x1 + (size_t)m * D + k) = xo; }
;                         const f32x4 hv = xv * (*(const GAS f32x4*)(mrow + 8192 + k) + 1.0f) + *(const GAS f32x4*)(mrow + 6144 + k);
;                         v2u o; o.x = pk2(hv.x, hv.y); o.y = pk2(hv.z, hv.w);
;                         *(GAS unsigned*)(h2q + (size_t)m * D + k) = pk4_fp8(hv.x, hv.y, hv.z, hv.w);
;                         const int chunk = (lq >> 1) + 32 * j;
;                         *(LAS v2u*)(h2s + rloc * 4096 + ((chunk ^ (rloc & 15)) << 4) + (lq & 1) * 8) = o; }
	v_add_f32_e32 v22, v22, v23
	v_fmamk_f32 v22, v22, 0x3a000000, v223
	v_mul_f32_e32 v23, 0x4f800000, v22
	v_cmp_gt_f32_e32 vcc, s89, v22
	s_nop 1
	v_cndmask_b32_e32 v22, v22, v23, vcc
	v_sqrt_f32_e32 v23, v22
	s_nop 0
	v_add_u32_e32 v26, -1, v23
	v_add_u32_e32 v27, 1, v23
	v_fma_f32 v32, -v26, v23, v22
	v_fma_f32 v33, -v27, v23, v22
	v_cmp_ge_f32_e64 s[14:15], 0, v32
	s_nop 1
	v_cndmask_b32_e64 v23, v23, v26, s[14:15]
	v_cmp_lt_f32_e64 s[14:15], 0, v33
	s_nop 1
	v_cndmask_b32_e64 v23, v23, v27, s[14:15]
	v_mul_f32_e32 v26, 0x37800000, v23
	v_cndmask_b32_e32 v23, v23, v26, vcc
	v_cmp_class_f32_e32 vcc, v22, v224
	s_nop 1
	v_cndmask_b32_e32 v26, v23, v22, vcc
	v_div_scale_f32 v27, s[14:15], v26, v26, 1.0
	v_rcp_f32_e32 v32, v27
	v_div_scale_f32 v33, vcc, 1.0, v26, 1.0
	v_lshl_add_u64 v[22:23], s[0:1], 0, v[128:129]
	v_fma_f32 v38, -v27, v32, 1.0
	v_fmac_f32_e32 v32, v38, v32
	v_mul_f32_e32 v38, v33, v32
	v_fma_f32 v39, -v27, v38, v33
	v_fmac_f32_e32 v38, v39, v32
	v_fma_f32 v27, -v27, v38, v33
	v_div_fmas_f32 v27, v27, v32, v38
	v_div_fixup_f32 v32, v27, v26, 1.0
	v_pk_mul_f32 v[24:25], v[24:25], v[32:33] op_sel_hi:[1,0]
	v_pk_mul_f32 v[20:21], v[20:21], v[32:33] op_sel_hi:[1,0]
	s_waitcnt lgkmcnt(0)
	v_pk_fma_f32 v[38:39], v[34:35], v[24:25], v[52:53]
	v_pk_fma_f32 v[20:21], v[36:37], v[20:21], v[54:55]
	v_bfe_u32 v24, v38, 16, 1
	v_bfe_u32 v26, v20, 16, 1
	v_bfe_u32 v25, v39, 16, 1
	v_bfe_u32 v27, v21, 16, 1
	v_add3_u32 v24, v38, v24, s90
	v_add3_u32 v26, v20, v26, s90
	v_add3_u32 v25, v39, v25, s90
	v_add3_u32 v27, v21, v27, s90
	v_lshrrev_b32_e32 v24, 16, v24
	v_lshrrev_b32_e32 v26, 16, v26
	v_and_or_b32 v24, v25, s86, v24
	v_and_or_b32 v25, v27, s86, v26
	global_store_dwordx2 v[22:23], v[24:25], off
	ds_read_b128 v[24:27], v252 offset:16384
	s_nop 0
	ds_read_b128 v[34:37], v252 offset:24576
	v_mov_b32_e32 v33, 0
	s_add_u32 s0, s50, s16
	s_addc_u32 s1, s51, s17
	s_mov_b32 s14, 0x8000
	s_waitcnt lgkmcnt(0)
	v_pk_add_f32 v[24:25], v[24:25], 1.0 op_sel_hi:[1,0]
	s_waitcnt lgkmcnt(0)
	v_pk_fma_f32 v[24:25], v[24:25], v[38:39], v[34:35]
	v_pk_add_f32 v[26:27], v[26:27], 1.0 op_sel_hi:[1,0]
	v_cvt_pk_fp8_f32 v33, v24, v25
	v_pk_fma_f32 v[26:27], v[26:27], v[20:21], v[36:37]
	v_lshl_add_u64 v[20:21], s[0:1], 0, v[86:87]
	v_readlane_b32 s0, v248, 24
	v_cvt_pk_fp8_f32 v33, v26, v27 op_sel:[0,0,1]
	v_add_u32_e32 v87, 32, v61
	v_add_u32_e32 v199, s0, v63
	v_readlane_b32 s0, v248, 25
	global_store_dword v[20:21], v33, off
	ds_read_b128 v[34:37], v252 offset:1024
	ds_read_b128 v[52:55], v252 offset:9216
	v_pk_mul_f32 v[30:31], v[30:31], v[32:33] op_sel_hi:[1,0]
	v_pk_mul_f32 v[28:29], v[28:29], v[32:33] op_sel_hi:[1,0]
	v_mov_b32_e32 v33, 0
	v_add_u32_e32 v200, s0, v63
	v_readlane_b32 s0, v248, 26
	v_xor_b32_e32 v185, s66, v87
	v_xor_b32_e32 v192, s68, v87
	v_add_u32_e32 v201, s0, v63
	v_readlane_b32 s0, v248, 27
	v_lshl_add_u32 v185, v185, 4, v200
	v_lshl_add_u32 v192, v192, 4, v201
	v_add_u32_e32 v63, s0, v63
	v_xor_b32_e32 v86, s64, v61
	v_lshl_add_u32 v86, v86, 4, v199
	v_readlane_b32 s0, v248, 30
	s_waitcnt lgkmcnt(0)
	v_pk_fma_f32 v[38:39], v[36:37], v[28:29], v[54:55]
	v_pk_fma_f32 v[52:53], v[34:35], v[30:31], v[52:53]
	v_bfe_u32 v30, v38, 16, 1
	v_bfe_u32 v28, v52, 16, 1
	v_bfe_u32 v29, v53, 16, 1
	v_bfe_u32 v31, v39, 16, 1
	v_add3_u32 v28, v52, v28, s90
	v_add3_u32 v30, v38, v30, s90
	v_add3_u32 v29, v53, v29, s90
	v_add3_u32 v31, v39, v31, s90
	v_lshrrev_b32_e32 v28, 16, v28
	v_lshrrev_b32_e32 v30, 16, v30
	v_and_or_b32 v28, v29, s86, v28
	v_and_or_b32 v29, v31, s86, v30
	global_store_dwordx2 v[22:23], v[28:29], off offset:512
	ds_read_b128 v[28:31], v252 offset:17408
	s_nop 0
	ds_read_b128 v[34:37], v252 offset:25600
	s_waitcnt lgkmcnt(0)
	v_pk_add_f32 v[28:29], v[28:29], 1.0 op_sel_hi:[1,0]
	s_waitcnt lgkmcnt(0)
	v_pk_fma_f32 v[28:29], v[28:29], v[52:53], v[34:35]
	v_pk_add_f32 v[30:31], v[30:31], 1.0 op_sel_hi:[1,0]
	v_cvt_pk_fp8_f32 v33, v28, v29
	v_pk_fma_f32 v[30:31], v[30:31], v[38:39], v[36:37]
	s_nop 0
	v_cvt_pk_fp8_f32 v33, v30, v31 op_sel:[0,0,1]
	global_store_dword v[20:21], v33, off offset:256
	ds_read_b128 v[34:37], v252 offset:2048
	ds_read_b128 v[52:55], v252 offset:10240
	v_pk_mul_f32 v[38:39], v[48:49], v[32:33] op_sel_hi:[1,0]
	v_pk_mul_f32 v[48:49], v[50:51], v[32:33] op_sel_hi:[1,0]
	s_waitcnt lgkmcnt(0)
	v_pk_fma_f32 v[38:39], v[34:35], v[38:39], v[52:53]
	v_pk_fma_f32 v[54:55], v[36:37], v[48:49], v[54:55]
	v_bfe_u32 v33, v38, 16, 1
	v_bfe_u32 v35, v54, 16, 1
	v_bfe_u32 v34, v39, 16, 1
	v_bfe_u32 v36, v55, 16, 1
	v_add3_u32 v33, v38, v33, s90
	v_add3_u32 v35, v54, v35, s90
	v_add3_u32 v34, v39, v34, s90
	v_add3_u32 v36, v55, v36, s90
	v_lshrrev_b32_e32 v33, 16, v33
	v_lshrrev_b32_e32 v35, 16, v35
	v_and_or_b32 v34, v34, s86, v33
	v_and_or_b32 v35, v36, s86, v35
	global_store_dwordx2 v[22:23], v[34:35], off offset:1024
	ds_read_b128 v[34:37], v252 offset:18432
	s_nop 0
	ds_read_b128 v[48:51], v252 offset:26624
	v_mov_b32_e32 v33, 0
	s_waitcnt lgkmcnt(0)
	v_pk_add_f32 v[34:35], v[34:35], 1.0 op_sel_hi:[1,0]
	s_waitcnt lgkmcnt(0)
; #define GAS __attribute__((address_space(1)))
; #define LAS __attribute__((address_space(3)))
; __device__ __forceinline__ unsigned pk2(float lo, float hi) { return f2bf(lo) | (f2bf(hi) << 16); }
; __device__ __forceinline__ unsigned pk4_fp8(float a, float b, float c, float d) { int r = __builtin_amdgcn_cvt_pk_fp8_f32(a, b, 0, false); r = __builtin_amdgcn_cvt_pk_fp8_f32(c, d, r, true); return (unsigned)r; }
; template <int l>
; __device__ __forceinline__ void layer_phases(Frame& F, const XcdBarrier& bar, const int lo, const int hi) {
;     ...
;                     for (int j = 0; j < 8; ++j) { const int k = 4 * lq + 256 * j;
;                         const f32x4 xv = v[j] * rstd * *(const GAS f32x4*)(g1 + k) + *(const GAS f32x4*)(b1 + k);
;                         { v2u xo; xo.x = pk2(xv.x, xv.y); xo.y = pk2(xv.z, xv.w); *(GAS v2u*)(x1 + (size_t)m * D + k) = xo; }
;                         const f32x4 hv = xv * (*(const GAS f32x4*)(mrow + 8192 + k) + 1.0f) + *(const GAS f32x4*)(mrow + 6144 + k);
;                         v2u o; o.x = pk2(hv.x, hv.y); o.y = pk2(hv.z, hv.w);
;                         *(GAS unsigned*)(h2q + (size_t)m * D + k) = pk4_fp8(hv.x, hv.y, hv.z, hv.w);
;                         const int chunk = (lq >> 1) + 32 * j;
;                         *(LAS v2u*)(h2s + rloc * 4096 + ((chunk ^ (rloc & 15)) << 4) + (lq & 1) * 8) = o; }
	v_pk_fma_f32 v[34:35], v[34:35], v[38:39], v[48:49]
	v_pk_add_f32 v[36:37], v[36:37], 1.0 op_sel_hi:[1,0]
	v_cvt_pk_fp8_f32 v33, v34, v35
	v_pk_fma_f32 v[36:37], v[36:37], v[54:55], v[50:51]
	s_nop 0
	v_cvt_pk_fp8_f32 v33, v36, v37 op_sel:[0,0,1]
	global_store_dword v[20:21], v33, off offset:512
	ds_read_b128 v[48:51], v252 offset:3072
	ds_read_b128 v[52:55], v252 offset:11264
	v_pk_mul_f32 v[38:39], v[46:47], v[32:33] op_sel_hi:[1,0]
	v_pk_mul_f32 v[44:45], v[44:45], v[32:33] op_sel_hi:[1,0]
	v_add_u32_e32 v112, 64, v61
	v_add_u32_e32 v113, 0xa0, v61
	v_add_u32_e32 v114, 0xc0, v61
	v_add_u32_e32 v115, 0xe0, v61
	v_xor_b32_e32 v186, s66, v112
	v_xor_b32_e32 v189, s66, v113
	v_xor_b32_e32 v190, s66, v114
	v_xor_b32_e32 v191, s66, v115
	v_xor_b32_e32 v193, s68, v112
	v_xor_b32_e32 v196, s68, v113
	v_xor_b32_e32 v197, s68, v114
	v_xor_b32_e32 v198, s68, v115
	v_lshl_add_u32 v186, v186, 4, v200
	v_lshl_add_u32 v189, v189, 4, v200
	v_lshl_add_u32 v190, v190, 4, v200
	v_lshl_add_u32 v191, v191, 4, v200
	v_lshl_add_u32 v193, v193, 4, v201
	v_lshl_add_u32 v196, v196, 4, v201
	v_lshl_add_u32 v197, v197, 4, v201
	v_lshl_add_u32 v198, v198, 4, v201
	v_xor_b32_e32 v182, s64, v113
	v_xor_b32_e32 v183, s64, v114
	v_xor_b32_e32 v184, s64, v115
	v_xor_b32_e32 v113, s70, v113
	v_xor_b32_e32 v114, s70, v114
	v_xor_b32_e32 v115, s70, v115
	v_lshl_add_u32 v182, v182, 4, v199
	v_lshl_add_u32 v183, v183, 4, v199
	v_lshl_add_u32 v184, v184, 4, v199
	v_lshl_add_u32 v113, v113, 4, v63
	v_lshl_add_u32 v114, v114, 4, v63
	s_waitcnt lgkmcnt(0)
	v_pk_fma_f32 v[54:55], v[44:45], v[50:51], v[54:55]
	v_pk_fma_f32 v[38:39], v[38:39], v[48:49], v[52:53]
	v_bfe_u32 v45, v54, 16, 1
	v_bfe_u32 v33, v38, 16, 1
	v_bfe_u32 v44, v39, 16, 1
	v_bfe_u32 v46, v55, 16, 1
	v_add3_u32 v33, v38, v33, s90
	v_add3_u32 v45, v54, v45, s90
	v_add3_u32 v44, v39, v44, s90
	v_add3_u32 v46, v55, v46, s90
	v_lshrrev_b32_e32 v33, 16, v33
	v_lshrrev_b32_e32 v45, 16, v45
	v_and_or_b32 v44, v44, s86, v33
	v_and_or_b32 v45, v46, s86, v45
	global_store_dwordx2 v[22:23], v[44:45], off offset:1536
	ds_read_b128 v[44:47], v252 offset:19456
	s_nop 0
	ds_read_b128 v[48:51], v252 offset:27648
	v_mov_b32_e32 v33, 0
	v_xor_b32_e32 v120, s66, v61
	v_xor_b32_e32 v121, s68, v61
	v_lshl_add_u32 v120, v120, 4, v200
	v_lshl_add_u32 v121, v121, 4, v201
	v_xor_b32_e32 v122, s64, v87
	v_xor_b32_e32 v123, s64, v112
	v_xor_b32_e32 v87, s70, v87
	v_xor_b32_e32 v112, s70, v112
	v_lshl_add_u32 v122, v122, 4, v199
	v_lshl_add_u32 v123, v123, 4, v199
	v_lshl_add_u32 v87, v87, 4, v63
	v_lshl_add_u32 v112, v112, 4, v63
	s_waitcnt lgkmcnt(0)
	v_pk_add_f32 v[44:45], v[44:45], 1.0 op_sel_hi:[1,0]
	s_waitcnt lgkmcnt(0)
	v_pk_fma_f32 v[38:39], v[38:39], v[44:45], v[48:49]
	v_pk_add_f32 v[44:45], v[46:47], 1.0 op_sel_hi:[1,0]
	v_cvt_pk_fp8_f32 v33, v38, v39
	v_pk_fma_f32 v[44:45], v[54:55], v[44:45], v[50:51]
	v_ashrrev_i32_e32 v55, 5, v227
	v_and_b32_e32 v54, 31, v227
	v_cvt_pk_fp8_f32 v33, v44, v45 op_sel:[0,0,1]
	global_store_dword v[20:21], v33, off offset:768
	ds_read_b128 v[46:49], v252 offset:4096
	ds_read_b128 v[50:53], v252 offset:12288
	v_pk_mul_f32 v[42:43], v[42:43], v[32:33] op_sel_hi:[1,0]
	v_pk_mul_f32 v[40:41], v[40:41], v[32:33] op_sel_hi:[1,0]
	s_waitcnt lgkmcnt(0)
	v_pk_fma_f32 v[50:51], v[42:43], v[46:47], v[50:51]
	v_pk_fma_f32 v[52:53], v[40:41], v[48:49], v[52:53]
	v_bfe_u32 v33, v50, 16, 1
	v_bfe_u32 v41, v52, 16, 1
	v_bfe_u32 v40, v51, 16, 1
	v_bfe_u32 v42, v53, 16, 1
	v_add3_u32 v33, v50, v33, s90
	v_add3_u32 v41, v52, v41, s90
	v_add3_u32 v40, v51, v40, s90
	v_add3_u32 v42, v53, v42, s90
	v_lshrrev_b32_e32 v33, 16, v33
	v_lshrrev_b32_e32 v41, 16, v41
	v_and_or_b32 v40, v40, s86, v33
	v_and_or_b32 v41, v42, s86, v41
	global_store_dwordx2 v[22:23], v[40:41], off offset:2048
	ds_read_b128 v[40:43], v252 offset:20480
	s_nop 0
	ds_read_b128 v[46:49], v252 offset:28672
	v_mov_b32_e32 v33, 0
	v_pk_mul_f32 v[14:15], v[14:15], v[32:33] op_sel_hi:[1,0]
	v_pk_mul_f32 v[12:13], v[12:13], v[32:33] op_sel_hi:[1,0]
	v_pk_mul_f32 v[10:11], v[10:11], v[32:33] op_sel_hi:[1,0]
	v_pk_mul_f32 v[8:9], v[8:9], v[32:33] op_sel_hi:[1,0]
	s_waitcnt lgkmcnt(0)
	v_pk_add_f32 v[40:41], v[40:41], 1.0 op_sel_hi:[1,0]
	s_waitcnt lgkmcnt(0)
	v_pk_fma_f32 v[40:41], v[50:51], v[40:41], v[46:47]
	v_pk_add_f32 v[42:43], v[42:43], 1.0 op_sel_hi:[1,0]
	v_cvt_pk_fp8_f32 v56, v40, v41
	v_pk_fma_f32 v[42:43], v[52:53], v[42:43], v[48:49]
	v_add_u32_e32 v50, 0x60, v61
	v_add_u32_e32 v51, 0x80, v61
	v_cvt_pk_fp8_f32 v56, v42, v43 op_sel:[0,0,1]
	v_xor_b32_e32 v128, s64, v50
	v_xor_b32_e32 v129, s64, v51
	v_xor_b32_e32 v187, s66, v50
	global_store_dword v[20:21], v56, off offset:1024
	ds_read_b128 v[46:49], v252 offset:5120
	s_nop 0
	ds_read_b128 v[56:59], v252 offset:13312
	v_xor_b32_e32 v188, s66, v51
	v_xor_b32_e32 v194, s68, v50
	v_xor_b32_e32 v195, s68, v51
	v_xor_b32_e32 v50, s70, v50
	v_xor_b32_e32 v51, s70, v51
	v_lshl_add_u32 v187, v187, 4, v200
	v_lshl_add_u32 v188, v188, 4, v200
	v_lshl_add_u32 v194, v194, 4, v201
	v_lshl_add_u32 v195, v195, 4, v201
	v_lshl_add_u32 v200, v50, 4, v63
	v_lshl_add_u32 v201, v51, 4, v63
	v_and_b32_sdwa v50, v94, v226 dst_sel:DWORD dst_unused:UNUSED_PAD src0_sel:WORD_1 src1_sel:DWORD
	v_and_b32_sdwa v51, v92, v226 dst_sel:DWORD dst_unused:UNUSED_PAD src0_sel:WORD_1 src1_sel:DWORD
	v_add3_u32 v92, v92, v51, s90
	v_add3_u32 v94, v94, v50, s90
	v_xor_b32_e32 v61, s70, v61
	v_lshl_add_u32 v128, v128, 4, v199
	v_lshl_add_u32 v129, v129, 4, v199
	v_lshl_add_u32 v199, v61, 4, v63
	v_lshl_add_u32 v63, v115, 4, v63
	v_and_b32_sdwa v61, v95, v226 dst_sel:DWORD dst_unused:UNUSED_PAD src0_sel:WORD_1 src1_sel:DWORD
	v_and_b32_sdwa v115, v93, v226 dst_sel:DWORD dst_unused:UNUSED_PAD src0_sel:WORD_1 src1_sel:DWORD
	v_add3_u32 v61, v95, v61, s90
	v_lshl_add_u64 v[52:53], s[36:37], 0, v[80:81]
	s_waitcnt lgkmcnt(0)
; #define GAS __attribute__((address_space(1)))
; #define LAS __attribute__((address_space(3)))
; __device__ __forceinline__ unsigned pk2(float lo, float hi) { return f2bf(lo) | (f2bf(hi) << 16); }
; __device__ __forceinline__ unsigned pk4_fp8(float a, float b, float c, float d) { int r = __builtin_amdgcn_cvt_pk_fp8_f32(a, b, 0, false); r = __builtin_amdgcn_cvt_pk_fp8_f32(c, d, r, true); return (unsigned)r; }
; template <int l>
; __device__ __forceinline__ void layer_phases(Frame& F, const XcdBarrier& bar, const int lo, const int hi) {
;     ...
;                     for (int j = 0; j < 8; ++j) { const int k = 4 * lq + 256 * j;
;                         const f32x4 xv = v[j] * rstd * *(const GAS f32x4*)(g1 + k) + *(const GAS f32x4*)(b1 + k);
;                         { v2u xo; xo.x = pk2(xv.x, xv.y); xo.y = pk2(xv.z, xv.w); *(GAS v2u*)(x1 + (size_t)m * D + k) = xo; }
;                         const f32x4 hv = xv * (*(const GAS f32x4*)(mrow + 8192 + k) + 1.0f) + *(const GAS f32x4*)(mrow + 6144 + k);
;                         v2u o; o.x = pk2(hv.x, hv.y); o.y = pk2(hv.z, hv.w);
;                         *(GAS unsigned*)(h2q + (size_t)m * D + k) = pk4_fp8(hv.x, hv.y, hv.z, hv.w);
;                         const int chunk = (lq >> 1) + 32 * j;
;                         *(LAS v2u*)(h2s + rloc * 4096 + ((chunk ^ (rloc & 15)) << 4) + (lq & 1) * 8) = o; }
	v_pk_fma_f32 v[50:51], v[12:13], v[48:49], v[58:59]
	v_pk_fma_f32 v[56:57], v[14:15], v[46:47], v[56:57]
	v_bfe_u32 v14, v50, 16, 1
	v_bfe_u32 v12, v56, 16, 1
	v_bfe_u32 v13, v57, 16, 1
	v_bfe_u32 v15, v51, 16, 1
	v_add3_u32 v12, v56, v12, s90
	v_add3_u32 v14, v50, v14, s90
	v_add3_u32 v13, v57, v13, s90
	v_add3_u32 v15, v51, v15, s90
	v_lshrrev_b32_e32 v12, 16, v12
	v_lshrrev_b32_e32 v14, 16, v14
	v_and_or_b32 v12, v13, s86, v12
	v_and_or_b32 v13, v15, s86, v14
	global_store_dwordx2 v[22:23], v[12:13], off offset:2560
	ds_read_b128 v[12:15], v252 offset:21504
	s_nop 0
	ds_read_b128 v[46:49], v252 offset:29696
	v_add3_u32 v58, v93, v115, s90
	v_and_b32_e32 v59, 0xffff0000, v61
	v_and_b32_e32 v58, 0xffff0000, v58
	v_or_b32_sdwa v59, v59, v94 dst_sel:DWORD dst_unused:UNUSED_PAD src0_sel:DWORD src1_sel:WORD_1
	v_or_b32_sdwa v58, v58, v92 dst_sel:DWORD dst_unused:UNUSED_PAD src0_sel:DWORD src1_sel:WORD_1
	ds_write_b64 v86, v[58:59]
	v_and_b32_sdwa v59, v96, v226 dst_sel:DWORD dst_unused:UNUSED_PAD src0_sel:WORD_1 src1_sel:DWORD
	v_and_b32_sdwa v61, v99, v226 dst_sel:DWORD dst_unused:UNUSED_PAD src0_sel:WORD_1 src1_sel:DWORD
	v_and_b32_sdwa v86, v97, v226 dst_sel:DWORD dst_unused:UNUSED_PAD src0_sel:WORD_1 src1_sel:DWORD
	v_and_b32_sdwa v58, v98, v226 dst_sel:DWORD dst_unused:UNUSED_PAD src0_sel:WORD_1 src1_sel:DWORD
	v_add3_u32 v92, v96, v59, s90
	v_add3_u32 v59, v99, v61, s90
	v_add3_u32 v61, v97, v86, s90
	v_add3_u32 v58, v98, v58, s90
	v_and_b32_e32 v59, 0xffff0000, v59
	v_and_b32_e32 v61, 0xffff0000, v61
	v_or_b32_sdwa v59, v59, v58 dst_sel:DWORD dst_unused:UNUSED_PAD src0_sel:DWORD src1_sel:WORD_1
	v_or_b32_sdwa v58, v61, v92 dst_sel:DWORD dst_unused:UNUSED_PAD src0_sel:DWORD src1_sel:WORD_1
	ds_write_b64 v122, v[58:59]
	v_and_b32_sdwa v59, v100, v226 dst_sel:DWORD dst_unused:UNUSED_PAD src0_sel:WORD_1 src1_sel:DWORD
	v_and_b32_sdwa v61, v103, v226 dst_sel:DWORD dst_unused:UNUSED_PAD src0_sel:WORD_1 src1_sel:DWORD
	v_and_b32_sdwa v86, v101, v226 dst_sel:DWORD dst_unused:UNUSED_PAD src0_sel:WORD_1 src1_sel:DWORD
	v_and_b32_sdwa v58, v102, v226 dst_sel:DWORD dst_unused:UNUSED_PAD src0_sel:WORD_1 src1_sel:DWORD
	v_add3_u32 v92, v100, v59, s90
	v_add3_u32 v59, v103, v61, s90
	v_add3_u32 v61, v101, v86, s90
	v_add3_u32 v58, v102, v58, s90
	v_and_b32_e32 v59, 0xffff0000, v59
	v_and_b32_e32 v61, 0xffff0000, v61
	v_or_b32_sdwa v59, v59, v58 dst_sel:DWORD dst_unused:UNUSED_PAD src0_sel:DWORD src1_sel:WORD_1
	v_or_b32_sdwa v58, v61, v92 dst_sel:DWORD dst_unused:UNUSED_PAD src0_sel:DWORD src1_sel:WORD_1
	ds_write_b64 v123, v[58:59]
	v_and_b32_sdwa v59, v104, v226 dst_sel:DWORD dst_unused:UNUSED_PAD src0_sel:WORD_1 src1_sel:DWORD
	v_and_b32_sdwa v61, v107, v226 dst_sel:DWORD dst_unused:UNUSED_PAD src0_sel:WORD_1 src1_sel:DWORD
	v_and_b32_sdwa v86, v105, v226 dst_sel:DWORD dst_unused:UNUSED_PAD src0_sel:WORD_1 src1_sel:DWORD
	v_and_b32_sdwa v58, v106, v226 dst_sel:DWORD dst_unused:UNUSED_PAD src0_sel:WORD_1 src1_sel:DWORD
	v_add3_u32 v92, v104, v59, s90
	v_add3_u32 v59, v107, v61, s90
	v_add3_u32 v61, v105, v86, s90
	v_add3_u32 v58, v106, v58, s90
	v_and_b32_e32 v59, 0xffff0000, v59
	v_and_b32_e32 v61, 0xffff0000, v61
	v_or_b32_sdwa v59, v59, v58 dst_sel:DWORD dst_unused:UNUSED_PAD src0_sel:DWORD src1_sel:WORD_1
	v_or_b32_sdwa v58, v61, v92 dst_sel:DWORD dst_unused:UNUSED_PAD src0_sel:DWORD src1_sel:WORD_1
	ds_write_b64 v128, v[58:59]
	v_and_b32_sdwa v59, v108, v226 dst_sel:DWORD dst_unused:UNUSED_PAD src0_sel:WORD_1 src1_sel:DWORD
	v_and_b32_sdwa v61, v111, v226 dst_sel:DWORD dst_unused:UNUSED_PAD src0_sel:WORD_1 src1_sel:DWORD
	v_and_b32_sdwa v86, v109, v226 dst_sel:DWORD dst_unused:UNUSED_PAD src0_sel:WORD_1 src1_sel:DWORD
	v_and_b32_sdwa v58, v110, v226 dst_sel:DWORD dst_unused:UNUSED_PAD src0_sel:WORD_1 src1_sel:DWORD
	v_add3_u32 v92, v108, v59, s90
	v_add3_u32 v59, v111, v61, s90
	v_add3_u32 v61, v109, v86, s90
	v_add3_u32 v58, v110, v58, s90
	v_and_b32_e32 v59, 0xffff0000, v59
	v_and_b32_e32 v61, 0xffff0000, v61
	v_or_b32_sdwa v59, v59, v58 dst_sel:DWORD dst_unused:UNUSED_PAD src0_sel:DWORD src1_sel:WORD_1
	v_or_b32_sdwa v58, v61, v92 dst_sel:DWORD dst_unused:UNUSED_PAD src0_sel:DWORD src1_sel:WORD_1
	ds_write_b64 v129, v[58:59]
	v_and_b32_sdwa v59, v116, v226 dst_sel:DWORD dst_unused:UNUSED_PAD src0_sel:WORD_1 src1_sel:DWORD
	v_and_b32_sdwa v61, v119, v226 dst_sel:DWORD dst_unused:UNUSED_PAD src0_sel:WORD_1 src1_sel:DWORD
	v_and_b32_sdwa v86, v117, v226 dst_sel:DWORD dst_unused:UNUSED_PAD src0_sel:WORD_1 src1_sel:DWORD
	v_and_b32_sdwa v58, v118, v226 dst_sel:DWORD dst_unused:UNUSED_PAD src0_sel:WORD_1 src1_sel:DWORD
	v_add3_u32 v92, v116, v59, s90
	v_add3_u32 v59, v119, v61, s90
	v_add3_u32 v61, v117, v86, s90
	v_add3_u32 v58, v118, v58, s90
	v_and_b32_e32 v59, 0xffff0000, v59
	v_and_b32_e32 v61, 0xffff0000, v61
	v_or_b32_sdwa v59, v59, v58 dst_sel:DWORD dst_unused:UNUSED_PAD src0_sel:DWORD src1_sel:WORD_1
	v_or_b32_sdwa v58, v61, v92 dst_sel:DWORD dst_unused:UNUSED_PAD src0_sel:DWORD src1_sel:WORD_1
	ds_write_b64 v182, v[58:59]
	v_and_b32_sdwa v59, v124, v226 dst_sel:DWORD dst_unused:UNUSED_PAD src0_sel:WORD_1 src1_sel:DWORD
	v_and_b32_sdwa v61, v127, v226 dst_sel:DWORD dst_unused:UNUSED_PAD src0_sel:WORD_1 src1_sel:DWORD
	v_and_b32_sdwa v58, v126, v226 dst_sel:DWORD dst_unused:UNUSED_PAD src0_sel:WORD_1 src1_sel:DWORD
	v_and_b32_sdwa v86, v125, v226 dst_sel:DWORD dst_unused:UNUSED_PAD src0_sel:WORD_1 src1_sel:DWORD
	v_add3_u32 v92, v124, v59, s90
	v_add3_u32 v59, v127, v61, s90
	v_add3_u32 v58, v126, v58, s90
	s_waitcnt lgkmcnt(0)
	v_pk_add_f32 v[12:13], v[12:13], 1.0 op_sel_hi:[1,0]
	v_pk_add_f32 v[14:15], v[14:15], 1.0 op_sel_hi:[1,0]
	s_waitcnt lgkmcnt(0)
; #define GAS __attribute__((address_space(1)))
; #define LAS __attribute__((address_space(3)))
; __device__ __forceinline__ unsigned pk2(float lo, float hi) { return f2bf(lo) | (f2bf(hi) << 16); }
; __device__ __forceinline__ unsigned pk4_fp8(float a, float b, float c, float d) { int r = __builtin_amdgcn_cvt_pk_fp8_f32(a, b, 0, false); r = __builtin_amdgcn_cvt_pk_fp8_f32(c, d, r, true); return (unsigned)r; }
; template <int l>
; __device__ __forceinline__ void layer_phases(Frame& F, const XcdBarrier& bar, const int lo, const int hi) {
;     ...
;                     for (int j = 0; j < 8; ++j) { const int k = 4 * lq + 256 * j;
;                         const f32x4 xv = v[j] * rstd * *(const GAS f32x4*)(g1 + k) + *(const GAS f32x4*)(b1 + k);
;                         { v2u xo; xo.x = pk2(xv.x, xv.y); xo.y = pk2(xv.z, xv.w); *(GAS v2u*)(x1 + (size_t)m * D + k) = xo; }
;                         const f32x4 hv = xv * (*(const GAS f32x4*)(mrow + 8192 + k) + 1.0f) + *(const GAS f32x4*)(mrow + 6144 + k);
;                         v2u o; o.x = pk2(hv.x, hv.y); o.y = pk2(hv.z, hv.w);
;                         *(GAS unsigned*)(h2q + (size_t)m * D + k) = pk4_fp8(hv.x, hv.y, hv.z, hv.w);
;                         const int chunk = (lq >> 1) + 32 * j;
;                         *(LAS v2u*)(h2s + rloc * 4096 + ((chunk ^ (rloc & 15)) << 4) + (lq & 1) * 8) = o; }
	v_pk_fma_f32 v[12:13], v[56:57], v[12:13], v[46:47]
	v_pk_fma_f32 v[14:15], v[50:51], v[14:15], v[48:49]
	v_cvt_pk_fp8_f32 v60, v12, v13
	v_add3_u32 v46, v125, v86, s90
	v_and_b32_e32 v47, 0xffff0000, v59
	v_and_b32_e32 v50, 0xffff0000, v46
	v_cvt_pk_fp8_f32 v60, v14, v15 op_sel:[0,0,1]
	v_or_b32_sdwa v51, v47, v58 dst_sel:DWORD dst_unused:UNUSED_PAD src0_sel:DWORD src1_sel:WORD_1
	v_or_b32_sdwa v50, v50, v92 dst_sel:DWORD dst_unused:UNUSED_PAD src0_sel:DWORD src1_sel:WORD_1
	v_and_b32_sdwa v61, v131, v226 dst_sel:DWORD dst_unused:UNUSED_PAD src0_sel:WORD_1 src1_sel:DWORD
	global_store_dword v[20:21], v60, off offset:1280
	ds_read_b128 v[46:49], v252 offset:6144
	ds_read_b128 v[56:59], v252 offset:14336
	ds_write_b64 v183, v[50:51]
	v_and_b32_sdwa v51, v130, v226 dst_sel:DWORD dst_unused:UNUSED_PAD src0_sel:WORD_1 src1_sel:DWORD
	v_and_b32_sdwa v60, v133, v226 dst_sel:DWORD dst_unused:UNUSED_PAD src0_sel:WORD_1 src1_sel:DWORD
	v_and_b32_sdwa v50, v132, v226 dst_sel:DWORD dst_unused:UNUSED_PAD src0_sel:WORD_1 src1_sel:DWORD
	v_add3_u32 v86, v130, v51, s90
	v_add3_u32 v51, v133, v60, s90
	v_add3_u32 v60, v131, v61, s90
	v_add3_u32 v50, v132, v50, s90
	v_and_b32_e32 v51, 0xffff0000, v51
	v_and_b32_e32 v60, 0xffff0000, v60
	v_or_b32_sdwa v51, v51, v50 dst_sel:DWORD dst_unused:UNUSED_PAD src0_sel:DWORD src1_sel:WORD_1
	v_or_b32_sdwa v50, v60, v86 dst_sel:DWORD dst_unused:UNUSED_PAD src0_sel:DWORD src1_sel:WORD_1
	ds_write_b64 v184, v[50:51]
	v_and_b32_sdwa v51, v134, v226 dst_sel:DWORD dst_unused:UNUSED_PAD src0_sel:WORD_1 src1_sel:DWORD
	v_and_b32_sdwa v60, v137, v226 dst_sel:DWORD dst_unused:UNUSED_PAD src0_sel:WORD_1 src1_sel:DWORD
	v_and_b32_sdwa v61, v135, v226 dst_sel:DWORD dst_unused:UNUSED_PAD src0_sel:WORD_1 src1_sel:DWORD
	v_and_b32_sdwa v50, v136, v226 dst_sel:DWORD dst_unused:UNUSED_PAD src0_sel:WORD_1 src1_sel:DWORD
	v_add3_u32 v86, v134, v51, s90
	v_add3_u32 v51, v137, v60, s90
	v_add3_u32 v60, v135, v61, s90
	v_add3_u32 v50, v136, v50, s90
	v_and_b32_e32 v51, 0xffff0000, v51
	v_and_b32_e32 v60, 0xffff0000, v60
	v_or_b32_sdwa v51, v51, v50 dst_sel:DWORD dst_unused:UNUSED_PAD src0_sel:DWORD src1_sel:WORD_1
	v_or_b32_sdwa v50, v60, v86 dst_sel:DWORD dst_unused:UNUSED_PAD src0_sel:DWORD src1_sel:WORD_1
	ds_write_b64 v120, v[50:51]
	v_and_b32_sdwa v51, v138, v226 dst_sel:DWORD dst_unused:UNUSED_PAD src0_sel:WORD_1 src1_sel:DWORD
	v_and_b32_sdwa v60, v141, v226 dst_sel:DWORD dst_unused:UNUSED_PAD src0_sel:WORD_1 src1_sel:DWORD
	v_and_b32_sdwa v61, v139, v226 dst_sel:DWORD dst_unused:UNUSED_PAD src0_sel:WORD_1 src1_sel:DWORD
	v_and_b32_sdwa v50, v140, v226 dst_sel:DWORD dst_unused:UNUSED_PAD src0_sel:WORD_1 src1_sel:DWORD
	v_add3_u32 v86, v138, v51, s90
	v_add3_u32 v51, v141, v60, s90
	v_add3_u32 v60, v139, v61, s90
	v_add3_u32 v50, v140, v50, s90
	v_and_b32_e32 v51, 0xffff0000, v51
	v_and_b32_e32 v60, 0xffff0000, v60
	v_or_b32_sdwa v51, v51, v50 dst_sel:DWORD dst_unused:UNUSED_PAD src0_sel:DWORD src1_sel:WORD_1
	v_or_b32_sdwa v50, v60, v86 dst_sel:DWORD dst_unused:UNUSED_PAD src0_sel:DWORD src1_sel:WORD_1
	ds_write_b64 v185, v[50:51]
	v_and_b32_sdwa v51, v142, v226 dst_sel:DWORD dst_unused:UNUSED_PAD src0_sel:WORD_1 src1_sel:DWORD
	v_and_b32_sdwa v60, v145, v226 dst_sel:DWORD dst_unused:UNUSED_PAD src0_sel:WORD_1 src1_sel:DWORD
	v_and_b32_sdwa v61, v143, v226 dst_sel:DWORD dst_unused:UNUSED_PAD src0_sel:WORD_1 src1_sel:DWORD
	v_and_b32_sdwa v50, v144, v226 dst_sel:DWORD dst_unused:UNUSED_PAD src0_sel:WORD_1 src1_sel:DWORD
	v_add3_u32 v86, v142, v51, s90
	v_add3_u32 v51, v145, v60, s90
	v_add3_u32 v60, v143, v61, s90
	v_add3_u32 v50, v144, v50, s90
	v_and_b32_e32 v51, 0xffff0000, v51
	v_and_b32_e32 v60, 0xffff0000, v60
	v_or_b32_sdwa v51, v51, v50 dst_sel:DWORD dst_unused:UNUSED_PAD src0_sel:DWORD src1_sel:WORD_1
	v_or_b32_sdwa v50, v60, v86 dst_sel:DWORD dst_unused:UNUSED_PAD src0_sel:DWORD src1_sel:WORD_1
	ds_write_b64 v186, v[50:51]
	v_and_b32_sdwa v51, v146, v226 dst_sel:DWORD dst_unused:UNUSED_PAD src0_sel:WORD_1 src1_sel:DWORD
	v_and_b32_sdwa v60, v149, v226 dst_sel:DWORD dst_unused:UNUSED_PAD src0_sel:WORD_1 src1_sel:DWORD
	v_and_b32_sdwa v61, v147, v226 dst_sel:DWORD dst_unused:UNUSED_PAD src0_sel:WORD_1 src1_sel:DWORD
	v_and_b32_sdwa v50, v148, v226 dst_sel:DWORD dst_unused:UNUSED_PAD src0_sel:WORD_1 src1_sel:DWORD
	v_add3_u32 v86, v146, v51, s90
	v_add3_u32 v51, v149, v60, s90
	v_add3_u32 v60, v147, v61, s90
	v_add3_u32 v50, v148, v50, s90
	v_and_b32_e32 v51, 0xffff0000, v51
	v_and_b32_e32 v60, 0xffff0000, v60
	v_or_b32_sdwa v51, v51, v50 dst_sel:DWORD dst_unused:UNUSED_PAD src0_sel:DWORD src1_sel:WORD_1
	v_or_b32_sdwa v50, v60, v86 dst_sel:DWORD dst_unused:UNUSED_PAD src0_sel:DWORD src1_sel:WORD_1
	ds_write_b64 v187, v[50:51]
	v_and_b32_sdwa v50, v152, v226 dst_sel:DWORD dst_unused:UNUSED_PAD src0_sel:WORD_1 src1_sel:DWORD
	v_and_b32_sdwa v51, v150, v226 dst_sel:DWORD dst_unused:UNUSED_PAD src0_sel:WORD_1 src1_sel:DWORD
	v_and_b32_sdwa v60, v153, v226 dst_sel:DWORD dst_unused:UNUSED_PAD src0_sel:WORD_1 src1_sel:DWORD
	v_and_b32_sdwa v61, v151, v226 dst_sel:DWORD dst_unused:UNUSED_PAD src0_sel:WORD_1 src1_sel:DWORD
	v_add3_u32 v86, v150, v51, s90
	v_add3_u32 v92, v152, v50, s90
	v_add3_u32 v50, v153, v60, s90
	v_add3_u32 v51, v151, v61, s90
	v_and_b32_e32 v60, 0xffff0000, v50
	v_and_b32_e32 v61, 0xffff0000, v51
	s_waitcnt lgkmcnt(0)
; #define GAS __attribute__((address_space(1)))
; #define LAS __attribute__((address_space(3)))
; __device__ __forceinline__ unsigned pk2(float lo, float hi) { return f2bf(lo) | (f2bf(hi) << 16); }
; __device__ __forceinline__ unsigned pk4_fp8(float a, float b, float c, float d) { int r = __builtin_amdgcn_cvt_pk_fp8_f32(a, b, 0, false); r = __builtin_amdgcn_cvt_pk_fp8_f32(c, d, r, true); return (unsigned)r; }
; template <int l>
; __device__ __forceinline__ void layer_phases(Frame& F, const XcdBarrier& bar, const int lo, const int hi) {
;     ...
;                     for (int j = 0; j < 8; ++j) { const int k = 4 * lq + 256 * j;
;                         const f32x4 xv = v[j] * rstd * *(const GAS f32x4*)(g1 + k) + *(const GAS f32x4*)(b1 + k);
;                         { v2u xo; xo.x = pk2(xv.x, xv.y); xo.y = pk2(xv.z, xv.w); *(GAS v2u*)(x1 + (size_t)m * D + k) = xo; }
;                         const f32x4 hv = xv * (*(const GAS f32x4*)(mrow + 8192 + k) + 1.0f) + *(const GAS f32x4*)(mrow + 6144 + k);
;                         v2u o; o.x = pk2(hv.x, hv.y); o.y = pk2(hv.z, hv.w);
;                         *(GAS unsigned*)(h2q + (size_t)m * D + k) = pk4_fp8(hv.x, hv.y, hv.z, hv.w);
;                         const int chunk = (lq >> 1) + 32 * j;
;                         *(LAS v2u*)(h2s + rloc * 4096 + ((chunk ^ (rloc & 15)) << 4) + (lq & 1) * 8) = o; }
	v_pk_fma_f32 v[50:51], v[8:9], v[48:49], v[58:59]
	v_pk_fma_f32 v[56:57], v[10:11], v[46:47], v[56:57]
	v_bfe_u32 v10, v50, 16, 1
	v_bfe_u32 v8, v56, 16, 1
	v_bfe_u32 v9, v57, 16, 1
	v_bfe_u32 v11, v51, 16, 1
	v_add3_u32 v8, v56, v8, s90
	v_add3_u32 v10, v50, v10, s90
	v_add3_u32 v9, v57, v9, s90
	v_add3_u32 v11, v51, v11, s90
	v_lshrrev_b32_e32 v8, 16, v8
	v_lshrrev_b32_e32 v10, 16, v10
	v_and_or_b32 v8, v9, s86, v8
	v_and_or_b32 v9, v11, s86, v10
	global_store_dwordx2 v[22:23], v[8:9], off offset:3072
	ds_read_b128 v[8:11], v252 offset:22528
	s_nop 0
	ds_read_b128 v[46:49], v252 offset:30720
	v_or_b32_sdwa v59, v60, v92 dst_sel:DWORD dst_unused:UNUSED_PAD src0_sel:DWORD src1_sel:WORD_1
	v_or_b32_sdwa v58, v61, v86 dst_sel:DWORD dst_unused:UNUSED_PAD src0_sel:DWORD src1_sel:WORD_1
	ds_write_b64 v188, v[58:59]
	v_and_b32_sdwa v59, v154, v226 dst_sel:DWORD dst_unused:UNUSED_PAD src0_sel:WORD_1 src1_sel:DWORD
	v_and_b32_sdwa v60, v157, v226 dst_sel:DWORD dst_unused:UNUSED_PAD src0_sel:WORD_1 src1_sel:DWORD
	v_and_b32_sdwa v61, v155, v226 dst_sel:DWORD dst_unused:UNUSED_PAD src0_sel:WORD_1 src1_sel:DWORD
	v_and_b32_sdwa v58, v156, v226 dst_sel:DWORD dst_unused:UNUSED_PAD src0_sel:WORD_1 src1_sel:DWORD
	v_add3_u32 v86, v154, v59, s90
	v_add3_u32 v59, v157, v60, s90
	v_add3_u32 v60, v155, v61, s90
	v_add3_u32 v58, v156, v58, s90
	v_and_b32_e32 v59, 0xffff0000, v59
	v_and_b32_e32 v60, 0xffff0000, v60
	v_or_b32_sdwa v59, v59, v58 dst_sel:DWORD dst_unused:UNUSED_PAD src0_sel:DWORD src1_sel:WORD_1
	v_or_b32_sdwa v58, v60, v86 dst_sel:DWORD dst_unused:UNUSED_PAD src0_sel:DWORD src1_sel:WORD_1
	ds_write_b64 v189, v[58:59]
	v_and_b32_sdwa v59, v158, v226 dst_sel:DWORD dst_unused:UNUSED_PAD src0_sel:WORD_1 src1_sel:DWORD
	v_and_b32_sdwa v60, v161, v226 dst_sel:DWORD dst_unused:UNUSED_PAD src0_sel:WORD_1 src1_sel:DWORD
	v_and_b32_sdwa v61, v159, v226 dst_sel:DWORD dst_unused:UNUSED_PAD src0_sel:WORD_1 src1_sel:DWORD
	v_and_b32_sdwa v58, v160, v226 dst_sel:DWORD dst_unused:UNUSED_PAD src0_sel:WORD_1 src1_sel:DWORD
	v_add3_u32 v86, v158, v59, s90
	v_add3_u32 v59, v161, v60, s90
	v_add3_u32 v60, v159, v61, s90
	v_add3_u32 v58, v160, v58, s90
	v_and_b32_e32 v59, 0xffff0000, v59
	v_and_b32_e32 v60, 0xffff0000, v60
	v_or_b32_sdwa v59, v59, v58 dst_sel:DWORD dst_unused:UNUSED_PAD src0_sel:DWORD src1_sel:WORD_1
	v_or_b32_sdwa v58, v60, v86 dst_sel:DWORD dst_unused:UNUSED_PAD src0_sel:DWORD src1_sel:WORD_1
	ds_write_b64 v190, v[58:59]
	v_and_b32_sdwa v59, v162, v226 dst_sel:DWORD dst_unused:UNUSED_PAD src0_sel:WORD_1 src1_sel:DWORD
	v_and_b32_sdwa v60, v165, v226 dst_sel:DWORD dst_unused:UNUSED_PAD src0_sel:WORD_1 src1_sel:DWORD
	v_and_b32_sdwa v61, v163, v226 dst_sel:DWORD dst_unused:UNUSED_PAD src0_sel:WORD_1 src1_sel:DWORD
	v_and_b32_sdwa v58, v164, v226 dst_sel:DWORD dst_unused:UNUSED_PAD src0_sel:WORD_1 src1_sel:DWORD
	v_add3_u32 v86, v162, v59, s90
	v_add3_u32 v59, v165, v60, s90
	v_add3_u32 v60, v163, v61, s90
	v_add3_u32 v58, v164, v58, s90
	v_and_b32_e32 v59, 0xffff0000, v59
	v_and_b32_e32 v60, 0xffff0000, v60
	v_or_b32_sdwa v59, v59, v58 dst_sel:DWORD dst_unused:UNUSED_PAD src0_sel:DWORD src1_sel:WORD_1
	v_or_b32_sdwa v58, v60, v86 dst_sel:DWORD dst_unused:UNUSED_PAD src0_sel:DWORD src1_sel:WORD_1
	ds_write_b64 v191, v[58:59]
	v_pk_mul_f32 v[58:59], v[6:7], v[32:33] op_sel_hi:[1,0]
	v_pk_mul_f32 v[60:61], v[4:5], v[32:33] op_sel_hi:[1,0]
	v_and_b32_sdwa v5, v64, v226 dst_sel:DWORD dst_unused:UNUSED_PAD src0_sel:WORD_1 src1_sel:DWORD
	v_and_b32_sdwa v6, v67, v226 dst_sel:DWORD dst_unused:UNUSED_PAD src0_sel:WORD_1 src1_sel:DWORD
	v_and_b32_sdwa v7, v65, v226 dst_sel:DWORD dst_unused:UNUSED_PAD src0_sel:WORD_1 src1_sel:DWORD
	v_and_b32_sdwa v4, v66, v226 dst_sel:DWORD dst_unused:UNUSED_PAD src0_sel:WORD_1 src1_sel:DWORD
	v_add3_u32 v32, v64, v5, s90
	v_add3_u32 v5, v67, v6, s90
	v_add3_u32 v6, v65, v7, s90
	v_add3_u32 v4, v66, v4, s90
	v_and_b32_e32 v5, 0xffff0000, v5
	v_and_b32_e32 v6, 0xffff0000, v6
	v_or_b32_sdwa v5, v5, v4 dst_sel:DWORD dst_unused:UNUSED_PAD src0_sel:DWORD src1_sel:WORD_1
	v_or_b32_sdwa v4, v6, v32 dst_sel:DWORD dst_unused:UNUSED_PAD src0_sel:DWORD src1_sel:WORD_1
	ds_write_b64 v121, v[4:5]
	v_and_b32_sdwa v5, v68, v226 dst_sel:DWORD dst_unused:UNUSED_PAD src0_sel:WORD_1 src1_sel:DWORD
	v_and_b32_sdwa v6, v71, v226 dst_sel:DWORD dst_unused:UNUSED_PAD src0_sel:WORD_1 src1_sel:DWORD
	v_and_b32_sdwa v7, v69, v226 dst_sel:DWORD dst_unused:UNUSED_PAD src0_sel:WORD_1 src1_sel:DWORD
	v_and_b32_sdwa v4, v70, v226 dst_sel:DWORD dst_unused:UNUSED_PAD src0_sel:WORD_1 src1_sel:DWORD
	v_add3_u32 v32, v68, v5, s90
	v_add3_u32 v5, v71, v6, s90
	v_add3_u32 v6, v69, v7, s90
	v_add3_u32 v4, v70, v4, s90
	v_and_b32_e32 v5, 0xffff0000, v5
	v_and_b32_e32 v6, 0xffff0000, v6
	v_or_b32_sdwa v5, v5, v4 dst_sel:DWORD dst_unused:UNUSED_PAD src0_sel:DWORD src1_sel:WORD_1
	v_or_b32_sdwa v4, v6, v32 dst_sel:DWORD dst_unused:UNUSED_PAD src0_sel:DWORD src1_sel:WORD_1
	ds_write_b64 v192, v[4:5]
	v_and_b32_sdwa v4, v168, v226 dst_sel:DWORD dst_unused:UNUSED_PAD src0_sel:WORD_1 src1_sel:DWORD
	v_and_b32_sdwa v5, v166, v226 dst_sel:DWORD dst_unused:UNUSED_PAD src0_sel:WORD_1 src1_sel:DWORD
	v_add3_u32 v32, v166, v5, s90
	v_add3_u32 v64, v168, v4, s90
	v_and_b32_sdwa v6, v169, v226 dst_sel:DWORD dst_unused:UNUSED_PAD src0_sel:WORD_1 src1_sel:DWORD
	v_and_b32_sdwa v7, v167, v226 dst_sel:DWORD dst_unused:UNUSED_PAD src0_sel:WORD_1 src1_sel:DWORD
	v_add3_u32 v6, v169, v6, s90
	v_add3_u32 v7, v167, v7, s90
	s_waitcnt lgkmcnt(0)
	v_pk_add_f32 v[4:5], v[8:9], 1.0 op_sel_hi:[1,0]
	v_and_b32_e32 v6, 0xffff0000, v6
	s_waitcnt lgkmcnt(0)
; #define GAS __attribute__((address_space(1)))
; #define LAS __attribute__((address_space(3)))
; __device__ __forceinline__ unsigned pk2(float lo, float hi) { return f2bf(lo) | (f2bf(hi) << 16); }
; __device__ __forceinline__ unsigned pk4_fp8(float a, float b, float c, float d) { int r = __builtin_amdgcn_cvt_pk_fp8_f32(a, b, 0, false); r = __builtin_amdgcn_cvt_pk_fp8_f32(c, d, r, true); return (unsigned)r; }
; template <int l>
; __device__ __forceinline__ void layer_phases(Frame& F, const XcdBarrier& bar, const int lo, const int hi) {
;     ...
;                     for (int j = 0; j < 8; ++j) { const int k = 4 * lq + 256 * j;
;                         const f32x4 xv = v[j] * rstd * *(const GAS f32x4*)(g1 + k) + *(const GAS f32x4*)(b1 + k);
;                         { v2u xo; xo.x = pk2(xv.x, xv.y); xo.y = pk2(xv.z, xv.w); *(GAS v2u*)(x1 + (size_t)m * D + k) = xo; }
;                         const f32x4 hv = xv * (*(const GAS f32x4*)(mrow + 8192 + k) + 1.0f) + *(const GAS f32x4*)(mrow + 6144 + k);
;                         v2u o; o.x = pk2(hv.x, hv.y); o.y = pk2(hv.z, hv.w);
;                         *(GAS unsigned*)(h2q + (size_t)m * D + k) = pk4_fp8(hv.x, hv.y, hv.z, hv.w);
;                         const int chunk = (lq >> 1) + 32 * j;
;                         *(LAS v2u*)(h2s + rloc * 4096 + ((chunk ^ (rloc & 15)) << 4) + (lq & 1) * 8) = o; }
	v_pk_fma_f32 v[46:47], v[56:57], v[4:5], v[46:47]
	v_pk_add_f32 v[4:5], v[10:11], 1.0 op_sel_hi:[1,0]
	v_cvt_pk_fp8_f32 v62, v46, v47
	v_pk_fma_f32 v[48:49], v[50:51], v[4:5], v[48:49]
	v_and_b32_e32 v4, 0xffff0000, v7
	v_or_b32_sdwa v51, v6, v64 dst_sel:DWORD dst_unused:UNUSED_PAD src0_sel:DWORD src1_sel:WORD_1
	v_cvt_pk_fp8_f32 v62, v48, v49 op_sel:[0,0,1]
	v_or_b32_sdwa v50, v4, v32 dst_sel:DWORD dst_unused:UNUSED_PAD src0_sel:DWORD src1_sel:WORD_1
	v_and_b32_sdwa v56, v171, v226 dst_sel:DWORD dst_unused:UNUSED_PAD src0_sel:WORD_1 src1_sel:DWORD
	v_and_b32_sdwa v32, v172, v226 dst_sel:DWORD dst_unused:UNUSED_PAD src0_sel:WORD_1 src1_sel:DWORD
	global_store_dword v[20:21], v62, off offset:1536
	ds_read_b128 v[4:7], v252 offset:7168
	ds_read_b128 v[8:11], v252 offset:15360
	ds_write_b64 v193, v[50:51]
	v_and_b32_sdwa v51, v173, v226 dst_sel:DWORD dst_unused:UNUSED_PAD src0_sel:WORD_1 src1_sel:DWORD
	v_and_b32_sdwa v50, v170, v226 dst_sel:DWORD dst_unused:UNUSED_PAD src0_sel:WORD_1 src1_sel:DWORD
	v_add3_u32 v51, v173, v51, s90
	v_add3_u32 v56, v171, v56, s90
	v_add3_u32 v50, v170, v50, s90
	v_add3_u32 v32, v172, v32, s90
	v_and_b32_e32 v51, 0xffff0000, v51
	v_and_b32_e32 v56, 0xffff0000, v56
	v_or_b32_sdwa v51, v51, v32 dst_sel:DWORD dst_unused:UNUSED_PAD src0_sel:DWORD src1_sel:WORD_1
	v_or_b32_sdwa v50, v56, v50 dst_sel:DWORD dst_unused:UNUSED_PAD src0_sel:DWORD src1_sel:WORD_1
	ds_write_b64 v194, v[50:51]
	v_and_b32_sdwa v51, v177, v226 dst_sel:DWORD dst_unused:UNUSED_PAD src0_sel:WORD_1 src1_sel:DWORD
	v_and_b32_sdwa v56, v175, v226 dst_sel:DWORD dst_unused:UNUSED_PAD src0_sel:WORD_1 src1_sel:DWORD
	v_and_b32_sdwa v32, v176, v226 dst_sel:DWORD dst_unused:UNUSED_PAD src0_sel:WORD_1 src1_sel:DWORD
	v_and_b32_sdwa v50, v174, v226 dst_sel:DWORD dst_unused:UNUSED_PAD src0_sel:WORD_1 src1_sel:DWORD
	v_add3_u32 v51, v177, v51, s90
	v_add3_u32 v56, v175, v56, s90
	v_add3_u32 v50, v174, v50, s90
	v_add3_u32 v32, v176, v32, s90
	v_and_b32_e32 v51, 0xffff0000, v51
	v_and_b32_e32 v56, 0xffff0000, v56
	v_or_b32_sdwa v51, v51, v32 dst_sel:DWORD dst_unused:UNUSED_PAD src0_sel:DWORD src1_sel:WORD_1
	v_or_b32_sdwa v50, v56, v50 dst_sel:DWORD dst_unused:UNUSED_PAD src0_sel:DWORD src1_sel:WORD_1
	ds_write_b64 v195, v[50:51]
	v_and_b32_sdwa v51, v181, v226 dst_sel:DWORD dst_unused:UNUSED_PAD src0_sel:WORD_1 src1_sel:DWORD
	v_and_b32_sdwa v56, v179, v226 dst_sel:DWORD dst_unused:UNUSED_PAD src0_sel:WORD_1 src1_sel:DWORD
	v_and_b32_sdwa v32, v180, v226 dst_sel:DWORD dst_unused:UNUSED_PAD src0_sel:WORD_1 src1_sel:DWORD
	v_and_b32_sdwa v50, v178, v226 dst_sel:DWORD dst_unused:UNUSED_PAD src0_sel:WORD_1 src1_sel:DWORD
	v_add3_u32 v51, v181, v51, s90
	v_add3_u32 v56, v179, v56, s90
	v_add3_u32 v50, v178, v50, s90
	v_add3_u32 v32, v180, v32, s90
	v_and_b32_e32 v51, 0xffff0000, v51
	v_and_b32_e32 v56, 0xffff0000, v56
	v_or_b32_sdwa v51, v51, v32 dst_sel:DWORD dst_unused:UNUSED_PAD src0_sel:DWORD src1_sel:WORD_1
	v_or_b32_sdwa v50, v56, v50 dst_sel:DWORD dst_unused:UNUSED_PAD src0_sel:DWORD src1_sel:WORD_1
	ds_write_b64 v196, v[50:51]
	v_and_b32_sdwa v51, v3, v226 dst_sel:DWORD dst_unused:UNUSED_PAD src0_sel:WORD_1 src1_sel:DWORD
	v_and_b32_sdwa v56, v1, v226 dst_sel:DWORD dst_unused:UNUSED_PAD src0_sel:WORD_1 src1_sel:DWORD
	v_and_b32_sdwa v32, v2, v226 dst_sel:DWORD dst_unused:UNUSED_PAD src0_sel:WORD_1 src1_sel:DWORD
	v_and_b32_sdwa v50, v0, v226 dst_sel:DWORD dst_unused:UNUSED_PAD src0_sel:WORD_1 src1_sel:DWORD
	v_add3_u32 v3, v3, v51, s90
	v_add3_u32 v1, v1, v56, s90
	v_add3_u32 v0, v0, v50, s90
	v_add3_u32 v2, v2, v32, s90
	v_and_b32_e32 v3, 0xffff0000, v3
	v_and_b32_e32 v32, 0xffff0000, v1
	v_or_b32_sdwa v1, v3, v2 dst_sel:DWORD dst_unused:UNUSED_PAD src0_sel:DWORD src1_sel:WORD_1
	v_or_b32_sdwa v0, v32, v0 dst_sel:DWORD dst_unused:UNUSED_PAD src0_sel:DWORD src1_sel:WORD_1
	ds_write_b64 v197, v[0:1]
	v_and_b32_sdwa v1, v16, v226 dst_sel:DWORD dst_unused:UNUSED_PAD src0_sel:WORD_1 src1_sel:DWORD
	v_and_b32_sdwa v2, v19, v226 dst_sel:DWORD dst_unused:UNUSED_PAD src0_sel:WORD_1 src1_sel:DWORD
	v_and_b32_sdwa v3, v17, v226 dst_sel:DWORD dst_unused:UNUSED_PAD src0_sel:WORD_1 src1_sel:DWORD
	v_and_b32_sdwa v0, v18, v226 dst_sel:DWORD dst_unused:UNUSED_PAD src0_sel:WORD_1 src1_sel:DWORD
	v_add3_u32 v16, v16, v1, s90
	v_add3_u32 v1, v19, v2, s90
	v_add3_u32 v2, v17, v3, s90
	v_add3_u32 v0, v18, v0, s90
	v_and_b32_e32 v1, 0xffff0000, v1
	v_and_b32_e32 v2, 0xffff0000, v2
	v_or_b32_sdwa v1, v1, v0 dst_sel:DWORD dst_unused:UNUSED_PAD src0_sel:DWORD src1_sel:WORD_1
	v_or_b32_sdwa v0, v2, v16 dst_sel:DWORD dst_unused:UNUSED_PAD src0_sel:DWORD src1_sel:WORD_1
	ds_write_b64 v198, v[0:1]
	v_and_b32_sdwa v1, v24, v226 dst_sel:DWORD dst_unused:UNUSED_PAD src0_sel:WORD_1 src1_sel:DWORD
	v_and_b32_sdwa v2, v27, v226 dst_sel:DWORD dst_unused:UNUSED_PAD src0_sel:WORD_1 src1_sel:DWORD
	v_and_b32_sdwa v3, v25, v226 dst_sel:DWORD dst_unused:UNUSED_PAD src0_sel:WORD_1 src1_sel:DWORD
	v_and_b32_sdwa v0, v26, v226 dst_sel:DWORD dst_unused:UNUSED_PAD src0_sel:WORD_1 src1_sel:DWORD
	v_add3_u32 v16, v24, v1, s90
	v_add3_u32 v1, v27, v2, s90
	v_add3_u32 v2, v25, v3, s90
	v_add3_u32 v0, v26, v0, s90
	v_and_b32_e32 v1, 0xffff0000, v1
	v_and_b32_e32 v2, 0xffff0000, v2
	v_or_b32_sdwa v1, v1, v0 dst_sel:DWORD dst_unused:UNUSED_PAD src0_sel:DWORD src1_sel:WORD_1
	v_or_b32_sdwa v0, v2, v16 dst_sel:DWORD dst_unused:UNUSED_PAD src0_sel:DWORD src1_sel:WORD_1
	ds_write_b64 v199, v[0:1]
	v_and_b32_sdwa v17, v28, v226 dst_sel:DWORD dst_unused:UNUSED_PAD src0_sel:WORD_1 src1_sel:DWORD
	v_and_b32_sdwa v18, v31, v226 dst_sel:DWORD dst_unused:UNUSED_PAD src0_sel:WORD_1 src1_sel:DWORD
	s_waitcnt lgkmcnt(0)
; #define GAS __attribute__((address_space(1)))
; #define LAS __attribute__((address_space(3)))
; __device__ __forceinline__ unsigned pk2(float lo, float hi) { return f2bf(lo) | (f2bf(hi) << 16); }
; __device__ __forceinline__ unsigned pk4_fp8(float a, float b, float c, float d) { int r = __builtin_amdgcn_cvt_pk_fp8_f32(a, b, 0, false); r = __builtin_amdgcn_cvt_pk_fp8_f32(c, d, r, true); return (unsigned)r; }
; template <int l>
; __device__ __forceinline__ void layer_phases(Frame& F, const XcdBarrier& bar, const int lo, const int hi) {
;     ...
;                     for (int j = 0; j < 8; ++j) { const int k = 4 * lq + 256 * j;
;                         const f32x4 xv = v[j] * rstd * *(const GAS f32x4*)(g1 + k) + *(const GAS f32x4*)(b1 + k);
;                         { v2u xo; xo.x = pk2(xv.x, xv.y); xo.y = pk2(xv.z, xv.w); *(GAS v2u*)(x1 + (size_t)m * D + k) = xo; }
;                         const f32x4 hv = xv * (*(const GAS f32x4*)(mrow + 8192 + k) + 1.0f) + *(const GAS f32x4*)(mrow + 6144 + k);
;                         v2u o; o.x = pk2(hv.x, hv.y); o.y = pk2(hv.z, hv.w);
;                         *(GAS unsigned*)(h2q + (size_t)m * D + k) = pk4_fp8(hv.x, hv.y, hv.z, hv.w);
;                         const int chunk = (lq >> 1) + 32 * j;
;                         *(LAS v2u*)(h2s + rloc * 4096 + ((chunk ^ (rloc & 15)) << 4) + (lq & 1) * 8) = o; }
	v_pk_fma_f32 v[10:11], v[60:61], v[6:7], v[10:11]
	v_pk_fma_f32 v[8:9], v[58:59], v[4:5], v[8:9]
	v_bfe_u32 v2, v10, 16, 1
	v_bfe_u32 v0, v8, 16, 1
	v_bfe_u32 v1, v9, 16, 1
	v_bfe_u32 v3, v11, 16, 1
	v_add3_u32 v0, v8, v0, s90
	v_add3_u32 v2, v10, v2, s90
	v_add3_u32 v1, v9, v1, s90
	v_add3_u32 v3, v11, v3, s90
	v_lshrrev_b32_e32 v0, 16, v0
	v_lshrrev_b32_e32 v2, 16, v2
	v_and_or_b32 v0, v1, s86, v0
	v_and_or_b32 v1, v3, s86, v2
	global_store_dwordx2 v[22:23], v[0:1], off offset:3584
	ds_read_b128 v[0:3], v252 offset:23552
	v_and_b32_sdwa v19, v29, v226 dst_sel:DWORD dst_unused:UNUSED_PAD src0_sel:WORD_1 src1_sel:DWORD
	ds_read_b128 v[4:7], v252 offset:31744
	v_and_b32_sdwa v16, v30, v226 dst_sel:DWORD dst_unused:UNUSED_PAD src0_sel:WORD_1 src1_sel:DWORD
	v_add3_u32 v22, v28, v17, s90
	v_add3_u32 v17, v31, v18, s90
	v_add3_u32 v18, v29, v19, s90
	v_add3_u32 v16, v30, v16, s90
	v_and_b32_e32 v17, 0xffff0000, v17
	v_and_b32_e32 v18, 0xffff0000, v18
	v_or_b32_sdwa v17, v17, v16 dst_sel:DWORD dst_unused:UNUSED_PAD src0_sel:DWORD src1_sel:WORD_1
	v_or_b32_sdwa v16, v18, v22 dst_sel:DWORD dst_unused:UNUSED_PAD src0_sel:DWORD src1_sel:WORD_1
	ds_write_b64 v87, v[16:17]
	v_and_b32_sdwa v17, v34, v226 dst_sel:DWORD dst_unused:UNUSED_PAD src0_sel:WORD_1 src1_sel:DWORD
	v_and_b32_sdwa v18, v37, v226 dst_sel:DWORD dst_unused:UNUSED_PAD src0_sel:WORD_1 src1_sel:DWORD
	v_and_b32_sdwa v19, v35, v226 dst_sel:DWORD dst_unused:UNUSED_PAD src0_sel:WORD_1 src1_sel:DWORD
	v_and_b32_sdwa v16, v36, v226 dst_sel:DWORD dst_unused:UNUSED_PAD src0_sel:WORD_1 src1_sel:DWORD
	v_add3_u32 v22, v34, v17, s90
	v_add3_u32 v17, v37, v18, s90
	v_add3_u32 v18, v35, v19, s90
	v_add3_u32 v16, v36, v16, s90
	v_and_b32_e32 v17, 0xffff0000, v17
	v_and_b32_e32 v18, 0xffff0000, v18
	v_or_b32_sdwa v17, v17, v16 dst_sel:DWORD dst_unused:UNUSED_PAD src0_sel:DWORD src1_sel:WORD_1
	v_or_b32_sdwa v16, v18, v22 dst_sel:DWORD dst_unused:UNUSED_PAD src0_sel:DWORD src1_sel:WORD_1
	ds_write_b64 v112, v[16:17]
	v_and_b32_sdwa v17, v38, v226 dst_sel:DWORD dst_unused:UNUSED_PAD src0_sel:WORD_1 src1_sel:DWORD
	v_and_b32_sdwa v18, v45, v226 dst_sel:DWORD dst_unused:UNUSED_PAD src0_sel:WORD_1 src1_sel:DWORD
	v_and_b32_sdwa v19, v39, v226 dst_sel:DWORD dst_unused:UNUSED_PAD src0_sel:WORD_1 src1_sel:DWORD
	v_and_b32_sdwa v16, v44, v226 dst_sel:DWORD dst_unused:UNUSED_PAD src0_sel:WORD_1 src1_sel:DWORD
	v_add3_u32 v22, v38, v17, s90
	v_add3_u32 v17, v45, v18, s90
	v_add3_u32 v18, v39, v19, s90
	v_add3_u32 v16, v44, v16, s90
	v_and_b32_e32 v17, 0xffff0000, v17
	v_and_b32_e32 v18, 0xffff0000, v18
	v_or_b32_sdwa v17, v17, v16 dst_sel:DWORD dst_unused:UNUSED_PAD src0_sel:DWORD src1_sel:WORD_1
	v_or_b32_sdwa v16, v18, v22 dst_sel:DWORD dst_unused:UNUSED_PAD src0_sel:DWORD src1_sel:WORD_1
	ds_write_b64 v200, v[16:17]
	v_and_b32_sdwa v17, v40, v226 dst_sel:DWORD dst_unused:UNUSED_PAD src0_sel:WORD_1 src1_sel:DWORD
	v_and_b32_sdwa v18, v43, v226 dst_sel:DWORD dst_unused:UNUSED_PAD src0_sel:WORD_1 src1_sel:DWORD
	v_and_b32_sdwa v19, v41, v226 dst_sel:DWORD dst_unused:UNUSED_PAD src0_sel:WORD_1 src1_sel:DWORD
	v_and_b32_sdwa v16, v42, v226 dst_sel:DWORD dst_unused:UNUSED_PAD src0_sel:WORD_1 src1_sel:DWORD
	v_add3_u32 v22, v40, v17, s90
	v_add3_u32 v17, v43, v18, s90
	v_add3_u32 v18, v41, v19, s90
	v_add3_u32 v16, v42, v16, s90
	v_and_b32_e32 v17, 0xffff0000, v17
	v_and_b32_e32 v18, 0xffff0000, v18
	v_or_b32_sdwa v17, v17, v16 dst_sel:DWORD dst_unused:UNUSED_PAD src0_sel:DWORD src1_sel:WORD_1
	v_or_b32_sdwa v16, v18, v22 dst_sel:DWORD dst_unused:UNUSED_PAD src0_sel:DWORD src1_sel:WORD_1
	v_and_b32_sdwa v18, v15, v226 dst_sel:DWORD dst_unused:UNUSED_PAD src0_sel:WORD_1 src1_sel:DWORD
	v_and_b32_sdwa v19, v13, v226 dst_sel:DWORD dst_unused:UNUSED_PAD src0_sel:WORD_1 src1_sel:DWORD
	ds_write_b64 v201, v[16:17]
	v_and_b32_sdwa v16, v14, v226 dst_sel:DWORD dst_unused:UNUSED_PAD src0_sel:WORD_1 src1_sel:DWORD
	v_and_b32_sdwa v17, v12, v226 dst_sel:DWORD dst_unused:UNUSED_PAD src0_sel:WORD_1 src1_sel:DWORD
	v_add3_u32 v15, v15, v18, s90
	v_add3_u32 v13, v13, v19, s90
	v_add3_u32 v12, v12, v17, s90
	v_add3_u32 v14, v14, v16, s90
	v_and_b32_e32 v15, 0xffff0000, v15
	v_and_b32_e32 v16, 0xffff0000, v13
	v_or_b32_sdwa v13, v15, v14 dst_sel:DWORD dst_unused:UNUSED_PAD src0_sel:DWORD src1_sel:WORD_1
	v_or_b32_sdwa v12, v16, v12 dst_sel:DWORD dst_unused:UNUSED_PAD src0_sel:DWORD src1_sel:WORD_1
	ds_write_b64 v113, v[12:13]
	v_and_b32_sdwa v13, v46, v226 dst_sel:DWORD dst_unused:UNUSED_PAD src0_sel:WORD_1 src1_sel:DWORD
	v_and_b32_sdwa v14, v49, v226 dst_sel:DWORD dst_unused:UNUSED_PAD src0_sel:WORD_1 src1_sel:DWORD
	v_and_b32_sdwa v15, v47, v226 dst_sel:DWORD dst_unused:UNUSED_PAD src0_sel:WORD_1 src1_sel:DWORD
	v_and_b32_sdwa v12, v48, v226 dst_sel:DWORD dst_unused:UNUSED_PAD src0_sel:WORD_1 src1_sel:DWORD
	v_add3_u32 v16, v46, v13, s90
	v_add3_u32 v13, v49, v14, s90
	v_add3_u32 v14, v47, v15, s90
	v_add3_u32 v12, v48, v12, s90
	v_and_b32_e32 v13, 0xffff0000, v13
	v_and_b32_e32 v14, 0xffff0000, v14
	v_or_b32_sdwa v13, v13, v12 dst_sel:DWORD dst_unused:UNUSED_PAD src0_sel:DWORD src1_sel:WORD_1
	v_or_b32_sdwa v12, v14, v16 dst_sel:DWORD dst_unused:UNUSED_PAD src0_sel:DWORD src1_sel:WORD_1
	ds_write_b64 v114, v[12:13]
	v_add_u32_e32 v57, s0, v55
	s_movk_i32 s0, 0x2000
	s_waitcnt lgkmcnt(0)
	v_pk_add_f32 v[0:1], v[0:1], 1.0 op_sel_hi:[1,0]
	v_pk_add_f32 v[2:3], v[2:3], 1.0 op_sel_hi:[1,0]
	s_waitcnt lgkmcnt(0)
; #define GAS __attribute__((address_space(1)))
; #define LAS __attribute__((address_space(3)))
; __device__ __forceinline__ unsigned pk2(float lo, float hi) { return f2bf(lo) | (f2bf(hi) << 16); }
; __device__ __forceinline__ unsigned pk4_fp8(float a, float b, float c, float d) { int r = __builtin_amdgcn_cvt_pk_fp8_f32(a, b, 0, false); r = __builtin_amdgcn_cvt_pk_fp8_f32(c, d, r, true); return (unsigned)r; }
; #define P5_LDB(dst, q0) do { _Pragma("unroll") for (int q_ = 0; q_ < 4; ++q_) _Pragma("unroll") for (int c_ = 0; c_ < 4; ++c_) dst[q_][c_] = *(const GAS bf16x8*)(wbase + (size_t)((q0) + q_) * 4096 + c_ * 1024); } while (0)
; template <int l>
; __device__ __forceinline__ void layer_phases(Frame& F, const XcdBarrier& bar, const int lo, const int hi) {
;     ...
;                     for (int j = 0; j < 8; ++j) { const int k = 4 * lq + 256 * j;
;                         const f32x4 xv = v[j] * rstd * *(const GAS f32x4*)(g1 + k) + *(const GAS f32x4*)(b1 + k);
;                         { v2u xo; xo.x = pk2(xv.x, xv.y); xo.y = pk2(xv.z, xv.w); *(GAS v2u*)(x1 + (size_t)m * D + k) = xo; }
;                         const f32x4 hv = xv * (*(const GAS f32x4*)(mrow + 8192 + k) + 1.0f) + *(const GAS f32x4*)(mrow + 6144 + k);
;                         v2u o; o.x = pk2(hv.x, hv.y); o.y = pk2(hv.z, hv.w);
;                         *(GAS unsigned*)(h2q + (size_t)m * D + k) = pk4_fp8(hv.x, hv.y, hv.z, hv.w);
;                         const int chunk = (lq >> 1) + 32 * j;
;                         *(LAS v2u*)(h2s + rloc * 4096 + ((chunk ^ (rloc & 15)) << 4) + (lq & 1) * 8) = o; }
;     ...
;                 bf16x8 bqa[4][4], bqb[4][4];
;                 const unsigned lo_ = lq * 16;
;                 const unsigned char* wbase = wrf + (size_t)(16 * F.wave) * 4096 + lo_;
;     ...
;                 asm volatile("" ::: "memory");
;                 P5_LDB(bqa, 0); P5_LDB(bqb, 4);
;                 __syncthreads();
;                 att::f32x16 acc0 = att::f32x16{}, acc1 = att::f32x16{};
;                 P5_MMA(bqa, 0); asm volatile("" ::: "memory"); P5_LDB(bqa, 8);
;                 P5_MMA(bqb, 4); asm volatile("" ::: "memory"); P5_LDB(bqb, 12);
;                 P5_MMA(bqa, 8); P5_MMA(bqb, 12);
	v_pk_fma_f32 v[0:1], v[8:9], v[0:1], v[4:5]
	v_pk_fma_f32 v[2:3], v[10:11], v[2:3], v[6:7]
	v_cvt_pk_fp8_f32 v33, v0, v1
	v_and_b32_sdwa v5, v0, v226 dst_sel:DWORD dst_unused:UNUSED_PAD src0_sel:WORD_1 src1_sel:DWORD
	v_and_b32_sdwa v6, v3, v226 dst_sel:DWORD dst_unused:UNUSED_PAD src0_sel:WORD_1 src1_sel:DWORD
	v_and_b32_sdwa v7, v1, v226 dst_sel:DWORD dst_unused:UNUSED_PAD src0_sel:WORD_1 src1_sel:DWORD
	v_cvt_pk_fp8_f32 v33, v2, v3 op_sel:[0,0,1]
	v_and_b32_sdwa v4, v2, v226 dst_sel:DWORD dst_unused:UNUSED_PAD src0_sel:WORD_1 src1_sel:DWORD
	v_add3_u32 v0, v0, v5, s90
	v_add3_u32 v5, v3, v6, s90
	v_add3_u32 v1, v1, v7, s90
	v_add3_u32 v4, v2, v4, s90
	v_and_b32_e32 v5, 0xffff0000, v5
	v_and_b32_e32 v6, 0xffff0000, v1
	v_or_b32_sdwa v1, v5, v4 dst_sel:DWORD dst_unused:UNUSED_PAD src0_sel:DWORD src1_sel:WORD_1
	v_or_b32_sdwa v0, v6, v0 dst_sel:DWORD dst_unused:UNUSED_PAD src0_sel:DWORD src1_sel:WORD_1
	ds_write_b64 v63, v[0:1]
	global_store_dword v[20:21], v33, off offset:1792
	global_load_dwordx4 v[0:3], v80, s[36:37]
	global_load_dwordx4 v[36:39], v80, s[36:37] offset:1024
	global_load_dwordx4 v[16:19], v80, s[36:37] offset:2048
	global_load_dwordx4 v[32:35], v80, s[36:37] offset:3072
	v_add_co_u32_e32 v4, vcc, s87, v52
	v_lshl_add_u32 v56, v54, 12, 0
	s_nop 0
	v_addc_co_u32_e32 v5, vcc, 0, v53, vcc
	v_add_co_u32_e32 v8, vcc, s0, v52
	s_movk_i32 s0, 0x3000
	s_nop 0
	v_addc_co_u32_e32 v9, vcc, 0, v53, vcc
	global_load_dwordx4 v[40:43], v[8:9], off offset:-4096
	global_load_dwordx4 v[58:61], v[4:5], off offset:1024
	global_load_dwordx4 v[62:65], v[4:5], off offset:2048
	v_add_co_u32_e32 v12, vcc, s0, v52
	s_movk_i32 s0, 0x6000
	s_nop 0
	v_addc_co_u32_e32 v13, vcc, 0, v53, vcc
	v_add_co_u32_e32 v10, vcc, s85, v52
	v_bitop3_b32 v22, v57, v227, 15 bitop3:0x78
	s_nop 0
	v_addc_co_u32_e32 v11, vcc, 0, v53, vcc
	v_add_co_u32_e32 v6, vcc, s22, v52
	v_lshl_add_u32 v22, v22, 4, v56
	s_nop 0
	v_addc_co_u32_e32 v7, vcc, 0, v53, vcc
	v_add_co_u32_e32 v20, vcc, s0, v52
	v_readlane_b32 s0, v248, 28
	s_nop 0
	v_addc_co_u32_e32 v21, vcc, 0, v53, vcc
	v_add_co_u32_e32 v14, vcc, s28, v52
	s_nop 1
	v_addc_co_u32_e32 v15, vcc, 0, v53, vcc
	v_add_co_u32_e32 v70, vcc, s14, v52
	s_nop 1
	v_addc_co_u32_e32 v71, vcc, 0, v53, vcc
	global_load_dwordx4 v[66:69], v[8:9], off
	global_load_dwordx4 v[82:85], v[8:9], off offset:1024
	global_load_dwordx4 v[86:89], v[8:9], off offset:2048
	global_load_dwordx4 v[90:93], v[8:9], off offset:3072
	global_load_dwordx4 v[94:97], v[10:11], off offset:-4096
	global_load_dwordx4 v[98:101], v[4:5], off offset:3072
	global_load_dwordx4 v[102:105], v[12:13], off offset:1024
	global_load_dwordx4 v[106:109], v[12:13], off offset:2048
	global_load_dwordx4 v[110:113], v[12:13], off offset:3072
	global_load_dwordx4 v[114:117], v[10:11], off
	global_load_dwordx4 v[118:121], v[10:11], off offset:1024
	global_load_dwordx4 v[122:125], v[10:11], off offset:2048
	global_load_dwordx4 v[126:129], v[10:11], off offset:3072
	global_load_dwordx4 v[130:133], v[6:7], off offset:1024
	global_load_dwordx4 v[134:137], v[6:7], off offset:2048
	global_load_dwordx4 v[138:141], v[20:21], off offset:-4096
	global_load_dwordx4 v[142:145], v[20:21], off
	global_load_dwordx4 v[146:149], v[20:21], off offset:1024
	global_load_dwordx4 v[150:153], v[20:21], off offset:2048
	global_load_dwordx4 v[154:157], v[20:21], off offset:3072
	global_load_dwordx4 v[158:161], v[70:71], off offset:-4096
	global_load_dwordx4 v[162:165], v[6:7], off offset:3072
	global_load_dwordx4 v[48:51], v[14:15], off offset:1024
	global_load_dwordx4 v[166:169], v[14:15], off offset:2048
	global_load_dwordx4 v[44:47], v[14:15], off offset:3072
	s_waitcnt lgkmcnt(0)
	s_barrier
	ds_read_b128 v[170:173], v22
	v_add_u32_e32 v4, 2, v57
	v_bitop3_b32 v4, v4, v227, 15 bitop3:0x78
	v_lshl_add_u32 v4, v4, 4, v56
	ds_read_b128 v[174:177], v4
	s_waitcnt vmcnt(31)
	s_waitcnt lgkmcnt(0)
	v_mfma_f32_32x32x16_bf16 v[0:15], v[170:173], v[0:3], 0
	s_waitcnt vmcnt(29)
	s_waitcnt lgkmcnt(0)
	v_mfma_f32_32x32x16_bf16 v[16:31], v[170:173], v[16:19], 0
	v_mfma_f32_32x32x16_bf16 v[0:15], v[170:173], v[36:39], v[0:15]
	v_add_u32_e32 v36, 6, v57
	v_bitop3_b32 v36, v36, v227, 15 bitop3:0x78
	v_lshl_add_u32 v36, v36, 4, v56
	ds_read_b128 v[36:39], v36
	s_waitcnt vmcnt(28)
	s_waitcnt lgkmcnt(0)
	v_mfma_f32_32x32x16_bf16 v[16:31], v[170:173], v[32:35], v[16:31]
	v_add_u32_e32 v32, 4, v57
	v_bitop3_b32 v32, v32, v227, 15 bitop3:0x78
	v_lshl_add_u32 v32, v32, 4, v56
	ds_read_b128 v[32:35], v32
	s_waitcnt vmcnt(27)
	s_waitcnt lgkmcnt(0)
	v_mfma_f32_32x32x16_bf16 v[0:15], v[174:177], v[40:43], v[0:15]
	v_add_u32_e32 v40, s0, v55
	s_mov_b32 s0, 0xa000
	s_waitcnt vmcnt(25)
	s_waitcnt lgkmcnt(0)
	v_mfma_f32_32x32x16_bf16 v[16:31], v[174:177], v[62:65], v[16:31]
	v_mfma_f32_32x32x16_bf16 v[0:15], v[174:177], v[58:61], v[0:15]
	global_load_dwordx4 v[58:61], v[70:71], off offset:2048
	s_waitcnt vmcnt(20)
	s_waitcnt lgkmcnt(0)
	v_mfma_f32_32x32x16_bf16 v[16:31], v[174:177], v[98:101], v[16:31]
	s_waitcnt lgkmcnt(0)
	v_mfma_f32_32x32x16_bf16 v[0:15], v[32:35], v[66:69], v[0:15]
	v_mfma_f32_32x32x16_bf16 v[16:31], v[32:35], v[86:89], v[16:31]
	v_mfma_f32_32x32x16_bf16 v[0:15], v[32:35], v[82:85], v[0:15]
	v_mfma_f32_32x32x16_bf16 v[16:31], v[32:35], v[90:93], v[16:31]
	v_bitop3_b32 v32, v40, v227, 15 bitop3:0x78
	v_lshl_add_u32 v32, v32, 4, v56
	ds_read_b128 v[32:35], v32
	v_mfma_f32_32x32x16_bf16 v[0:15], v[36:39], v[94:97], v[0:15]
	s_waitcnt vmcnt(18)
	s_waitcnt lgkmcnt(0)
	v_mfma_f32_32x32x16_bf16 v[16:31], v[36:39], v[106:109], v[16:31]
	v_mfma_f32_32x32x16_bf16 v[0:15], v[36:39], v[102:105], v[0:15]
	s_waitcnt vmcnt(17)
; #define P5_LDB(dst, q0) do { _Pragma("unroll") for (int q_ = 0; q_ < 4; ++q_) _Pragma("unroll") for (int c_ = 0; c_ < 4; ++c_) dst[q_][c_] = *(const GAS bf16x8*)(wbase + (size_t)((q0) + q_) * 4096 + c_ * 1024); } while (0)
; template <int l>
; __device__ __forceinline__ void layer_phases(Frame& F, const XcdBarrier& bar, const int lo, const int hi) {
;     ...
;                 P5_MMA(bqa, 0); asm volatile("" ::: "memory"); P5_LDB(bqa, 8);
;                 P5_MMA(bqb, 4); asm volatile("" ::: "memory"); P5_LDB(bqb, 12);
;                 P5_MMA(bqa, 8); P5_MMA(bqb, 12);
	s_waitcnt lgkmcnt(0)
	v_mfma_f32_32x32x16_bf16 v[16:31], v[36:39], v[110:113], v[16:31]
	v_add_u32_e32 v36, 2, v40
	v_bitop3_b32 v36, v36, v227, 15 bitop3:0x78
	v_lshl_add_u32 v36, v36, 4, v56
	ds_read_b128 v[36:39], v36
	s_waitcnt vmcnt(16)
	s_waitcnt lgkmcnt(0)
	v_mfma_f32_32x32x16_bf16 v[0:15], v[32:35], v[114:117], v[0:15]
	s_waitcnt vmcnt(14)
	s_waitcnt lgkmcnt(0)
	v_mfma_f32_32x32x16_bf16 v[16:31], v[32:35], v[122:125], v[16:31]
	v_mfma_f32_32x32x16_bf16 v[0:15], v[32:35], v[118:121], v[0:15]
	s_waitcnt vmcnt(13)
	s_waitcnt lgkmcnt(0)
	v_mfma_f32_32x32x16_bf16 v[16:31], v[32:35], v[126:129], v[16:31]
	v_add_u32_e32 v32, 4, v40
	v_bitop3_b32 v32, v32, v227, 15 bitop3:0x78
	v_lshl_add_u32 v32, v32, 4, v56
	ds_read_b128 v[32:35], v32
	v_add_u32_e32 v40, 6, v40
	v_bitop3_b32 v40, v40, v227, 15 bitop3:0x78
	v_lshl_add_u32 v40, v40, 4, v56
	s_waitcnt vmcnt(10)
	s_waitcnt lgkmcnt(0)
	v_mfma_f32_32x32x16_bf16 v[0:15], v[36:39], v[138:141], v[0:15]
	ds_read_b128 v[40:43], v40
	v_mfma_f32_32x32x16_bf16 v[16:31], v[36:39], v[134:137], v[16:31]
	v_mfma_f32_32x32x16_bf16 v[0:15], v[36:39], v[130:133], v[0:15]
	s_waitcnt vmcnt(4)
	s_waitcnt lgkmcnt(0)
	v_mfma_f32_32x32x16_bf16 v[16:31], v[36:39], v[162:165], v[16:31]
	global_load_dwordx4 v[36:39], v[70:71], off
	global_load_dwordx4 v[62:65], v[70:71], off offset:1024
	global_load_dwordx4 v[66:69], v[70:71], off offset:3072
	v_add_co_u32_e32 v70, vcc, s0, v52
	v_readlane_b32 s0, v248, 29
	s_nop 0
	v_addc_co_u32_e32 v71, vcc, 0, v53, vcc
	s_waitcnt lgkmcnt(1)
	v_mfma_f32_32x32x16_bf16 v[0:15], v[32:35], v[142:145], v[0:15]
	v_add_co_u32_e32 v90, vcc, s23, v52
	global_load_dwordx4 v[82:85], v[70:71], off offset:-4096
	global_load_dwordx4 v[94:97], v[70:71], off
	v_addc_co_u32_e32 v91, vcc, 0, v53, vcc
	global_load_dwordx4 v[86:89], v[90:91], off offset:1024
	v_mfma_f32_32x32x16_bf16 v[16:31], v[32:35], v[150:153], v[16:31]
	v_add_u32_e32 v57, s0, v55
	s_mov_b32 s0, 0xb000
	v_add_co_u32_e32 v118, vcc, s0, v52
	s_mov_b32 s0, 0xc000
	s_nop 0
	v_addc_co_u32_e32 v119, vcc, 0, v53, vcc
	v_mfma_f32_32x32x16_bf16 v[0:15], v[32:35], v[146:149], v[0:15]
	v_add_co_u32_e32 v122, vcc, s0, v52
	v_bitop3_b32 v80, v57, v227, 15 bitop3:0x78
	s_nop 0
	v_addc_co_u32_e32 v123, vcc, 0, v53, vcc
	v_lshl_add_u32 v80, v80, 4, v56
	v_readlane_b32 s0, v248, 31
	v_mfma_f32_32x32x16_bf16 v[16:31], v[32:35], v[154:157], v[16:31]
	global_load_dwordx4 v[32:35], v[90:91], off offset:2048
	s_nop 0
	global_load_dwordx4 v[90:93], v[90:91], off offset:3072
	s_waitcnt lgkmcnt(0)
	v_mfma_f32_32x32x16_bf16 v[0:15], v[40:43], v[158:161], v[0:15]
	s_waitcnt vmcnt(11)
	s_waitcnt lgkmcnt(0)
	v_mfma_f32_32x32x16_bf16 v[0:15], v[40:43], v[48:51], v[0:15]
	global_load_dwordx4 v[48:51], v[70:71], off offset:1024
	global_load_dwordx4 v[98:101], v[70:71], off offset:2048
	global_load_dwordx4 v[102:105], v[70:71], off offset:3072
	global_load_dwordx4 v[106:109], v[122:123], off offset:-4096
	global_load_dwordx4 v[110:113], v[118:119], off offset:1024
	global_load_dwordx4 v[114:117], v[118:119], off offset:2048
	s_nop 0
	global_load_dwordx4 v[118:121], v[118:119], off offset:3072
	s_waitcnt vmcnt(17)
	s_waitcnt lgkmcnt(0)
	v_mfma_f32_32x32x16_bf16 v[16:31], v[40:43], v[166:169], v[16:31]
	s_waitcnt vmcnt(16)
	s_waitcnt lgkmcnt(0)
	v_mfma_f32_32x32x16_bf16 v[16:31], v[40:43], v[44:47], v[16:31]
	ds_read_b128 v[40:43], v80
	v_add_u32_e32 v44, 2, v57
	v_bitop3_b32 v44, v44, v227, 15 bitop3:0x78
	v_lshl_add_u32 v44, v44, 4, v56
	ds_read_b128 v[44:47], v44
	s_waitcnt vmcnt(14)
	s_waitcnt lgkmcnt(0)
	v_mfma_f32_32x32x16_bf16 v[0:15], v[40:43], v[36:39], v[0:15]
	v_add_u32_e32 v36, 6, v57
	v_bitop3_b32 v36, v36, v227, 15 bitop3:0x78
	v_lshl_add_u32 v36, v36, 4, v56
	ds_read_b128 v[36:39], v36
	v_mfma_f32_32x32x16_bf16 v[16:31], v[40:43], v[58:61], v[16:31]
	s_waitcnt vmcnt(13)
	s_waitcnt lgkmcnt(0)
	v_mfma_f32_32x32x16_bf16 v[0:15], v[40:43], v[62:65], v[0:15]
	s_waitcnt vmcnt(12)
	s_waitcnt lgkmcnt(0)
	v_mfma_f32_32x32x16_bf16 v[16:31], v[40:43], v[66:69], v[16:31]
	global_load_dwordx4 v[40:43], v[122:123], off offset:2048
	s_waitcnt vmcnt(12)
	s_waitcnt lgkmcnt(0)
	v_mfma_f32_32x32x16_bf16 v[0:15], v[44:47], v[82:85], v[0:15]
	s_waitcnt vmcnt(9)
	s_waitcnt lgkmcnt(0)
	v_mfma_f32_32x32x16_bf16 v[16:31], v[44:47], v[32:35], v[16:31]
	v_add_u32_e32 v32, 4, v57
	v_bitop3_b32 v32, v32, v227, 15 bitop3:0x78
	v_lshl_add_u32 v32, v32, 4, v56
	ds_read_b128 v[32:35], v32
	v_add_u32_e32 v57, s0, v55
	s_mov_b32 s0, 0xe000
	v_add_co_u32_e32 v58, vcc, s0, v52
	v_mfma_f32_32x32x16_bf16 v[0:15], v[44:47], v[86:89], v[0:15]
	s_nop 0
	v_addc_co_u32_e32 v59, vcc, 0, v53, vcc
	s_mov_b32 s0, 0xd000
	v_add_co_u32_e32 v60, vcc, s0, v52
	s_mov_b32 s0, 0xf000
	s_nop 0
	v_addc_co_u32_e32 v61, vcc, 0, v53, vcc
	s_waitcnt vmcnt(8)
	s_waitcnt lgkmcnt(0)
	v_mfma_f32_32x32x16_bf16 v[16:31], v[44:47], v[90:93], v[16:31]
	v_bitop3_b32 v44, v57, v227, 15 bitop3:0x78
	v_lshl_add_u32 v44, v44, 4, v56
	ds_read_b128 v[44:47], v44
	v_add_co_u32_e32 v52, vcc, s0, v52
	v_readlane_b32 s0, v248, 32
	s_nop 0
	v_addc_co_u32_e32 v53, vcc, 0, v53, vcc
	s_waitcnt lgkmcnt(1)
	v_mfma_f32_32x32x16_bf16 v[0:15], v[32:35], v[94:97], v[0:15]
	s_waitcnt vmcnt(6)
	s_waitcnt lgkmcnt(0)
	v_mfma_f32_32x32x16_bf16 v[16:31], v[32:35], v[98:101], v[16:31]
	v_mfma_f32_32x32x16_bf16 v[0:15], v[32:35], v[48:51], v[0:15]
	v_add_u32_e32 v48, 2, v57
	v_bitop3_b32 v48, v48, v227, 15 bitop3:0x78
	v_lshl_add_u32 v48, v48, 4, v56
	ds_read_b128 v[48:51], v48
	s_waitcnt vmcnt(5)
	s_waitcnt lgkmcnt(0)
	v_mfma_f32_32x32x16_bf16 v[16:31], v[32:35], v[102:105], v[16:31]
	global_load_dwordx4 v[32:35], v[122:123], off
	s_waitcnt vmcnt(5)
; __device__ __forceinline__ int crow(int r, int hi) { return (r & 3) + 8 * (r >> 2) + 4 * hi; }
; template <int l>
; __device__ __forceinline__ void layer_phases(Frame& F, const XcdBarrier& bar, const int lo, const int hi) {
;     ...
;                 P5_MMA(bqa, 8); P5_MMA(bqb, 12);
;     ...
;                 __syncthreads();
; #pragma unroll
;                 for (int r = 0; r < 16; ++r) { const int row = att::crow(r, hi5); part[(F.wave * 32 + row) * 64 + r32] = acc0[r]; part[(F.wave * 32 + row) * 64 + 32 + r32] = acc1[r]; }
;                 __syncthreads();
;                 float score[4]; unsigned key[4]; int ek[4][6]; float sk[4][6];
; #pragma unroll
;                 for (int rr = 0; rr < 4; ++rr) { const int rloc = 4 * F.wave + rr; float lg = 0.f;
; #pragma unroll
;                     for (int w = 0; w < 8; ++w) lg += part[(w * 32 + rloc) * 64 + F.lane];
	s_waitcnt lgkmcnt(0)
	v_mfma_f32_32x32x16_bf16 v[0:15], v[36:39], v[106:109], v[0:15]
	s_waitcnt vmcnt(3)
	s_waitcnt lgkmcnt(0)
	v_mfma_f32_32x32x16_bf16 v[16:31], v[36:39], v[114:117], v[16:31]
	v_mfma_f32_32x32x16_bf16 v[0:15], v[36:39], v[110:113], v[0:15]
	s_waitcnt vmcnt(2)
	s_waitcnt lgkmcnt(0)
	v_mfma_f32_32x32x16_bf16 v[16:31], v[36:39], v[118:121], v[16:31]
	global_load_dwordx4 v[36:39], v[122:123], off offset:1024
	s_waitcnt vmcnt(1)
	s_waitcnt lgkmcnt(0)
	v_mfma_f32_32x32x16_bf16 v[0:15], v[44:47], v[32:35], v[0:15]
	global_load_dwordx4 v[32:35], v[122:123], off offset:3072
	s_waitcnt vmcnt(1)
	s_waitcnt lgkmcnt(0)
	v_mfma_f32_32x32x16_bf16 v[0:15], v[44:47], v[36:39], v[0:15]
	global_load_dwordx4 v[36:39], v[58:59], off offset:-4096
	v_mfma_f32_32x32x16_bf16 v[16:31], v[44:47], v[40:43], v[16:31]
	s_waitcnt vmcnt(1)
	s_waitcnt lgkmcnt(0)
	v_mfma_f32_32x32x16_bf16 v[16:31], v[44:47], v[32:35], v[16:31]
	global_load_dwordx4 v[32:35], v[60:61], off offset:2048
	global_load_dwordx4 v[40:43], v[58:59], off
	s_waitcnt vmcnt(2)
	s_waitcnt lgkmcnt(0)
	v_mfma_f32_32x32x16_bf16 v[0:15], v[48:51], v[36:39], v[0:15]
	global_load_dwordx4 v[36:39], v[60:61], off offset:1024
	s_waitcnt vmcnt(2)
	s_waitcnt lgkmcnt(0)
	v_mfma_f32_32x32x16_bf16 v[16:31], v[48:51], v[32:35], v[16:31]
	global_load_dwordx4 v[32:35], v[60:61], off offset:3072
	s_waitcnt vmcnt(0)
	s_waitcnt lgkmcnt(0)
	v_mfma_f32_32x32x16_bf16 v[16:31], v[48:51], v[32:35], v[16:31]
	global_load_dwordx4 v[32:35], v[58:59], off offset:2048
	v_mfma_f32_32x32x16_bf16 v[0:15], v[48:51], v[36:39], v[0:15]
	v_add_u32_e32 v36, 4, v57
	v_bitop3_b32 v36, v36, v227, 15 bitop3:0x78
	v_lshl_add_u32 v44, v36, 4, v56
	ds_read_b128 v[44:47], v44
	v_add_u32_e32 v48, 6, v57
	v_bitop3_b32 v48, v48, v227, 15 bitop3:0x78
	v_lshl_add_u32 v48, v48, 4, v56
	ds_read_b128 v[48:51], v48
	s_waitcnt lgkmcnt(1)
	v_mfma_f32_32x32x16_bf16 v[0:15], v[44:47], v[40:43], v[0:15]
	global_load_dwordx4 v[40:43], v[58:59], off offset:1024
	global_load_dwordx4 v[36:39], v[52:53], off
	s_waitcnt vmcnt(2)
	s_waitcnt lgkmcnt(0)
	v_mfma_f32_32x32x16_bf16 v[16:31], v[44:47], v[32:35], v[16:31]
	global_load_dwordx4 v[32:35], v[58:59], off offset:3072
	s_waitcnt vmcnt(0)
	s_waitcnt lgkmcnt(0)
	v_mfma_f32_32x32x16_bf16 v[16:31], v[44:47], v[32:35], v[16:31]
	global_load_dwordx4 v[32:35], v[52:53], off offset:2048
	v_mfma_f32_32x32x16_bf16 v[0:15], v[44:47], v[40:43], v[0:15]
	v_lshlrev_b32_e32 v40, 10, v55
	v_lshlrev_b32_e32 v41, 2, v54
	s_waitcnt lgkmcnt(0)
	v_mfma_f32_32x32x16_bf16 v[0:15], v[48:51], v[36:39], v[0:15]
	global_load_dwordx4 v[36:39], v[52:53], off offset:1024
	s_waitcnt vmcnt(1)
	s_waitcnt lgkmcnt(0)
	v_mfma_f32_32x32x16_bf16 v[16:31], v[48:51], v[32:35], v[16:31]
	global_load_dwordx4 v[32:35], v[52:53], off offset:3072
	s_barrier
	s_waitcnt vmcnt(1)
	s_waitcnt lgkmcnt(0)
	v_mfma_f32_32x32x16_bf16 v[0:15], v[48:51], v[36:39], v[0:15]
	v_add3_u32 v36, s0, v40, v41
	v_add_u32_e32 v37, 0x800, v36
	v_add_u32_e32 v38, 0x1000, v36
	v_add_u32_e32 v39, 0x1800, v36
	s_waitcnt vmcnt(0)
	s_waitcnt lgkmcnt(0)
	v_mfma_f32_32x32x16_bf16 v[16:31], v[48:51], v[32:35], v[16:31]
	s_nop 11
	ds_write2_b32 v36, v0, v16 offset1:32
	ds_write2_b32 v36, v1, v17 offset0:64 offset1:96
	ds_write2_b32 v36, v2, v18 offset0:128 offset1:160
	ds_write2_b32 v36, v3, v19 offset0:192 offset1:224
	ds_write2_b32 v37, v4, v20 offset1:32
	ds_write2_b32 v37, v5, v21 offset0:64 offset1:96
	ds_write2_b32 v37, v6, v22 offset0:128 offset1:160
	ds_write2_b32 v37, v7, v23 offset0:192 offset1:224
	ds_write2_b32 v38, v8, v24 offset1:32
	ds_write2_b32 v38, v9, v25 offset0:64 offset1:96
	ds_write2_b32 v38, v10, v26 offset0:128 offset1:160
	ds_write2_b32 v38, v11, v27 offset0:192 offset1:224
	ds_write2_b32 v39, v12, v28 offset1:32
	ds_write2_b32 v39, v13, v29 offset0:64 offset1:96
	ds_write2_b32 v39, v14, v30 offset0:128 offset1:160
	ds_write2_b32 v39, v15, v31 offset0:192 offset1:224
	s_waitcnt lgkmcnt(0)
	s_barrier
	ds_read2st64_b32 v[0:1], v225 offset1:1
	ds_read2st64_b32 v[2:3], v225 offset0:32 offset1:33
	ds_read2st64_b32 v[4:5], v225 offset0:34 offset1:35
	ds_read2st64_b32 v[6:7], v225 offset0:2 offset1:3
	ds_read2st64_b32 v[8:9], v225 offset0:64 offset1:65
	ds_read2st64_b32 v[10:11], v225 offset0:96 offset1:97
	ds_read2st64_b32 v[12:13], v225 offset0:98 offset1:99
	ds_read2st64_b32 v[14:15], v225 offset0:66 offset1:67
	ds_read2st64_b32 v[16:17], v225 offset0:128 offset1:129
	ds_read2st64_b32 v[18:19], v225 offset0:160 offset1:161
	ds_read2st64_b32 v[20:21], v225 offset0:162 offset1:163
	ds_read2st64_b32 v[22:23], v225 offset0:130 offset1:131
	ds_read2st64_b32 v[24:25], v225 offset0:192 offset1:193
	ds_read2st64_b32 v[26:27], v225 offset0:224 offset1:225
	ds_read2st64_b32 v[28:29], v225 offset0:226 offset1:227
	ds_read2st64_b32 v[30:31], v225 offset0:194 offset1:195
	s_waitcnt lgkmcnt(14)
	v_add_f32_e32 v0, 0, v0
	v_add_f32_e32 v1, 0, v1
	v_add_f32_e32 v0, v0, v2
	v_add_f32_e32 v1, v1, v3
	s_waitcnt lgkmcnt(12)
	v_add_f32_e32 v6, 0, v6
	v_add_f32_e32 v7, 0, v7
	s_waitcnt lgkmcnt(11)
	v_add_f32_e32 v0, v0, v8
	v_add_f32_e32 v1, v1, v9
	v_add_f32_e32 v2, v6, v4
	v_add_f32_e32 v3, v7, v5
	s_waitcnt lgkmcnt(10)
	v_add_f32_e32 v0, v0, v10
	v_add_f32_e32 v1, v1, v11
	s_waitcnt lgkmcnt(8)
	v_add_f32_e32 v2, v2, v14
	v_add_f32_e32 v3, v3, v15
	s_waitcnt lgkmcnt(7)
	v_add_f32_e32 v0, v0, v16
	v_add_f32_e32 v1, v1, v17
	v_add_f32_e32 v2, v2, v12
	v_add_f32_e32 v3, v3, v13
	s_waitcnt lgkmcnt(6)
	v_add_f32_e32 v0, v0, v18
	v_add_f32_e32 v1, v1, v19
	s_waitcnt lgkmcnt(4)
	v_add_f32_e32 v2, v2, v22
	v_add_f32_e32 v3, v3, v23
	s_waitcnt lgkmcnt(3)
; template <int l>
; __device__ __forceinline__ void layer_phases(Frame& F, const XcdBarrier& bar, const int lo, const int hi) {
;     ...
;                 for (int rr = 0; rr < 4; ++rr) { const int rloc = 4 * F.wave + rr; float lg = 0.f;
; #pragma unroll
;                     for (int w = 0; w < 8; ++w) lg += part[(w * 32 + rloc) * 64 + F.lane];
;                     score[rr] = 1.0f / (1.0f + __expf(-lg)); const float sel = score[rr] + rb;
;                     unsigned ob = __float_as_uint(sel); ob = (ob & 0x80000000u) ? ~ob : (ob | 0x80000000u);
;                     key[rr] = (ob & ~63u) | (unsigned)(63 - F.lane); }
; #pragma unroll
;                 for (int k = 0; k < 6; ++k) {
;                     unsigned mx[4];
; #pragma unroll
;                     for (int rr = 0; rr < 4; ++rr) mx[rr] = key[rr];
; #pragma unroll
;                     for (int o = 1; o < 64; o <<= 1) {
; #pragma unroll
;                         for (int rr = 0; rr < 4; ++rr) { const unsigned t = __shfl_xor(mx[rr], o); mx[rr] = t > mx[rr] ? t : mx[rr]; } }
; #pragma unroll
;                     for (int rr = 0; rr < 4; ++rr) { const int win = 63 - (int)(__builtin_amdgcn_readfirstlane((int)mx[rr]) & 63);
;                         ek[rr][k] = win; sk[rr][k] = __uint_as_float((unsigned)__builtin_amdgcn_readlane((int)__float_as_uint(score[rr]), win)); if (F.lane == win) key[rr] = 0u; }
	v_add_f32_e32 v0, v0, v24
	v_add_f32_e32 v1, v1, v25
	v_add_f32_e32 v2, v2, v20
	v_add_f32_e32 v3, v3, v21
	s_waitcnt lgkmcnt(2)
	v_add_f32_e32 v0, v0, v26
	v_add_f32_e32 v1, v1, v27
	s_waitcnt lgkmcnt(0)
	v_add_f32_e32 v2, v2, v30
	v_add_f32_e32 v3, v3, v31
	v_mul_f32_e32 v0, 0xbfb8aa3b, v0
	v_mul_f32_e32 v4, 0xbfb8aa3b, v1
	v_add_f32_e32 v2, v2, v28
	v_add_f32_e32 v3, v3, v29
	v_exp_f32_e32 v1, v0
	v_exp_f32_e32 v0, v4
	v_mul_f32_e32 v2, 0xbfb8aa3b, v2
	v_mul_f32_e32 v5, 0xbfb8aa3b, v3
	v_exp_f32_e32 v3, v2
	v_exp_f32_e32 v2, v5
	v_pk_add_f32 v[0:1], v[0:1], 1.0 op_sel_hi:[1,0]
	v_pk_add_f32 v[2:3], v[2:3], 1.0 op_sel_hi:[1,0]
	v_div_scale_f32 v4, s[0:1], v1, v1, 1.0
	v_div_scale_f32 v6, s[0:1], v0, v0, 1.0
	v_rcp_f32_e32 v12, v4
	v_div_scale_f32 v8, s[0:1], v3, v3, 1.0
	v_rcp_f32_e32 v13, v6
	v_div_scale_f32 v10, s[0:1], v2, v2, 1.0
	v_rcp_f32_e32 v14, v8
	v_rcp_f32_e32 v15, v10
	v_fma_f32 v16, -v4, v12, 1.0
	v_div_scale_f32 v5, vcc, 1.0, v1, 1.0
	v_fma_f32 v17, -v6, v13, 1.0
	v_fmac_f32_e32 v12, v16, v12
	v_div_scale_f32 v7, s[14:15], 1.0, v0, 1.0
	v_fma_f32 v18, -v8, v14, 1.0
	v_fmac_f32_e32 v13, v17, v13
	v_mul_f32_e32 v16, v5, v12
	v_div_scale_f32 v9, s[16:17], 1.0, v3, 1.0
	v_fma_f32 v19, -v10, v15, 1.0
	v_fmac_f32_e32 v14, v18, v14
	v_mul_f32_e32 v17, v7, v13
	v_fma_f32 v20, -v4, v16, v5
	v_div_scale_f32 v11, s[18:19], 1.0, v2, 1.0
	v_fmac_f32_e32 v15, v19, v15
	v_mul_f32_e32 v18, v9, v14
	v_fma_f32 v21, -v6, v17, v7
	v_fmac_f32_e32 v16, v20, v12
	v_mul_f32_e32 v19, v11, v15
	v_fma_f32 v22, -v8, v18, v9
	v_fmac_f32_e32 v17, v21, v13
	v_fma_f32 v4, -v4, v16, v5
	v_fma_f32 v23, -v10, v19, v11
	v_fmac_f32_e32 v18, v22, v14
	v_fma_f32 v5, -v6, v17, v7
	v_div_fmas_f32 v4, v4, v12, v16
	s_mov_b64 vcc, s[14:15]
	v_fmac_f32_e32 v19, v23, v15
	v_fma_f32 v6, -v8, v18, v9
	v_div_fixup_f32 v1, v4, v1, 1.0
	v_div_fmas_f32 v4, v5, v13, v17
	s_mov_b64 vcc, s[16:17]
	v_fma_f32 v7, -v10, v19, v11
	v_div_fixup_f32 v0, v4, v0, 1.0
	v_div_fmas_f32 v6, v6, v14, v18
	s_mov_b64 vcc, s[18:19]
	v_pk_add_f32 v[4:5], v[74:75], v[0:1]
	v_div_fixup_f32 v3, v6, v3, 1.0
	v_div_fmas_f32 v6, v7, v15, v19
	v_not_b32_e32 v7, v5
	v_or_b32_e32 v8, 0x80000000, v5
	v_div_fixup_f32 v2, v6, v2, 1.0
	v_cmp_gt_i32_e32 vcc, 0, v5
	v_not_b32_e32 v9, v4
	v_or_b32_e32 v10, 0x80000000, v4
	v_cndmask_b32_e32 v6, v8, v7, vcc
	v_cmp_gt_i32_e32 vcc, 0, v4
	v_pk_add_f32 v[4:5], v[74:75], v[2:3]
	v_and_or_b32 v6, v6, s93, v222
	v_cndmask_b32_e32 v7, v10, v9, vcc
	v_not_b32_e32 v8, v5
	v_or_b32_e32 v9, 0x80000000, v5
	v_cmp_gt_i32_e32 vcc, 0, v5
	v_and_or_b32 v7, v7, s93, v222
	v_not_b32_e32 v10, v4
	v_or_b32_e32 v11, 0x80000000, v4
	v_cndmask_b32_e32 v5, v9, v8, vcc
	v_cmp_gt_i32_e32 vcc, 0, v4
	ds_bpermute_b32 v8, v73, v6
	ds_bpermute_b32 v9, v73, v7
	v_cndmask_b32_e32 v4, v11, v10, vcc
	v_and_or_b32 v5, v5, s93, v222
	v_and_or_b32 v4, v4, s93, v222
	ds_bpermute_b32 v10, v73, v5
	ds_bpermute_b32 v11, v73, v4
	s_waitcnt lgkmcnt(3)
	v_max_u32_e32 v8, v8, v6
	s_waitcnt lgkmcnt(2)
	v_max_u32_e32 v9, v9, v7
	ds_bpermute_b32 v12, v217, v8
	ds_bpermute_b32 v13, v217, v9
	s_waitcnt lgkmcnt(3)
	v_max_u32_e32 v10, v10, v5
	s_waitcnt lgkmcnt(2)
	v_max_u32_e32 v11, v11, v4
	ds_bpermute_b32 v14, v217, v10
	ds_bpermute_b32 v15, v217, v11
	s_waitcnt lgkmcnt(3)
	v_max_u32_e32 v8, v12, v8
	s_waitcnt lgkmcnt(2)
	v_max_u32_e32 v9, v13, v9
	ds_bpermute_b32 v12, v218, v8
	ds_bpermute_b32 v13, v218, v9
	s_waitcnt lgkmcnt(3)
	v_max_u32_e32 v10, v14, v10
	s_waitcnt lgkmcnt(2)
	v_max_u32_e32 v11, v15, v11
	ds_bpermute_b32 v14, v218, v10
	ds_bpermute_b32 v15, v218, v11
	s_waitcnt lgkmcnt(3)
	v_max_u32_e32 v8, v12, v8
	s_waitcnt lgkmcnt(2)
	v_max_u32_e32 v9, v13, v9
	ds_bpermute_b32 v12, v219, v8
	ds_bpermute_b32 v13, v219, v9
	s_waitcnt lgkmcnt(3)
	v_max_u32_e32 v10, v14, v10
	s_waitcnt lgkmcnt(2)
	v_max_u32_e32 v11, v15, v11
	ds_bpermute_b32 v14, v219, v10
	ds_bpermute_b32 v15, v219, v11
	s_waitcnt lgkmcnt(3)
	v_max_u32_e32 v8, v12, v8
	s_waitcnt lgkmcnt(2)
	v_max_u32_e32 v9, v13, v9
	ds_bpermute_b32 v12, v220, v8
	ds_bpermute_b32 v13, v220, v9
	s_waitcnt lgkmcnt(3)
	v_max_u32_e32 v10, v14, v10
	s_waitcnt lgkmcnt(2)
	v_max_u32_e32 v11, v15, v11
	ds_bpermute_b32 v14, v220, v10
	ds_bpermute_b32 v15, v220, v11
	s_waitcnt lgkmcnt(3)
	v_max_u32_e32 v8, v12, v8
	s_waitcnt lgkmcnt(2)
	v_max_u32_e32 v9, v13, v9
	ds_bpermute_b32 v12, v221, v8
	ds_bpermute_b32 v13, v221, v9
	s_waitcnt lgkmcnt(3)
	v_max_u32_e32 v10, v14, v10
	s_waitcnt lgkmcnt(2)
	v_max_u32_e32 v11, v15, v11
	ds_bpermute_b32 v14, v221, v10
	ds_bpermute_b32 v15, v221, v11
	s_waitcnt lgkmcnt(3)
	v_max_u32_e32 v8, v12, v8
	s_waitcnt lgkmcnt(2)
	v_max_u32_e32 v9, v13, v9
	v_readfirstlane_b32 s0, v8
	v_readfirstlane_b32 s1, v9
	s_waitcnt lgkmcnt(1)
	v_max_u32_e32 v8, v14, v10
	s_andn2_b32 s16, 63, s0
	s_waitcnt lgkmcnt(0)
	v_max_u32_e32 v9, v15, v11
	s_andn2_b32 s82, 63, s1
	v_cmp_ne_u32_e32 vcc, s16, v72
	v_readfirstlane_b32 s0, v8
	v_readfirstlane_b32 s1, v9
	v_cndmask_b32_e32 v6, 0, v6, vcc
	v_cmp_ne_u32_e32 vcc, s82, v72
	s_andn2_b32 s45, 63, s0
	s_andn2_b32 s19, 63, s1
	v_cndmask_b32_e32 v7, 0, v7, vcc
	ds_bpermute_b32 v8, v73, v6
	v_cmp_ne_u32_e32 vcc, s45, v72
	ds_bpermute_b32 v9, v73, v7
	v_readlane_b32 s95, v1, s16
	v_cndmask_b32_e32 v5, 0, v5, vcc
	v_cmp_ne_u32_e32 vcc, s19, v72
	ds_bpermute_b32 v10, v73, v5
	s_waitcnt lgkmcnt(2)
	v_max_u32_e32 v8, v8, v6
	v_cndmask_b32_e32 v4, 0, v4, vcc
	ds_bpermute_b32 v11, v73, v4
	s_waitcnt lgkmcnt(2)
	v_max_u32_e32 v9, v9, v7
	ds_bpermute_b32 v12, v217, v8
	ds_bpermute_b32 v13, v217, v9
	s_waitcnt lgkmcnt(3)
	v_max_u32_e32 v10, v10, v5
	s_waitcnt lgkmcnt(2)
; template <int l>
; __device__ __forceinline__ void layer_phases(Frame& F, const XcdBarrier& bar, const int lo, const int hi) {
;     ...
;                 for (int k = 0; k < 6; ++k) {
;                     unsigned mx[4];
; #pragma unroll
;                     for (int rr = 0; rr < 4; ++rr) mx[rr] = key[rr];
; #pragma unroll
;                     for (int o = 1; o < 64; o <<= 1) {
; #pragma unroll
;                         for (int rr = 0; rr < 4; ++rr) { const unsigned t = __shfl_xor(mx[rr], o); mx[rr] = t > mx[rr] ? t : mx[rr]; } }
; #pragma unroll
;                     for (int rr = 0; rr < 4; ++rr) { const int win = 63 - (int)(__builtin_amdgcn_readfirstlane((int)mx[rr]) & 63);
;                         ek[rr][k] = win; sk[rr][k] = __uint_as_float((unsigned)__builtin_amdgcn_readlane((int)__float_as_uint(score[rr]), win)); if (F.lane == win) key[rr] = 0u; }
	v_max_u32_e32 v11, v11, v4
	ds_bpermute_b32 v14, v217, v10
	ds_bpermute_b32 v15, v217, v11
	s_waitcnt lgkmcnt(3)
	v_max_u32_e32 v8, v12, v8
	s_waitcnt lgkmcnt(2)
	v_max_u32_e32 v9, v13, v9
	ds_bpermute_b32 v12, v218, v8
	ds_bpermute_b32 v13, v218, v9
	s_waitcnt lgkmcnt(3)
	v_max_u32_e32 v10, v14, v10
	s_waitcnt lgkmcnt(2)
	v_max_u32_e32 v11, v15, v11
	ds_bpermute_b32 v14, v218, v10
	ds_bpermute_b32 v15, v218, v11
	s_waitcnt lgkmcnt(3)
	v_max_u32_e32 v8, v12, v8
	s_waitcnt lgkmcnt(2)
	v_max_u32_e32 v9, v13, v9
	ds_bpermute_b32 v12, v219, v8
	ds_bpermute_b32 v13, v219, v9
	s_waitcnt lgkmcnt(3)
	v_max_u32_e32 v10, v14, v10
	s_waitcnt lgkmcnt(2)
	v_max_u32_e32 v11, v15, v11
	ds_bpermute_b32 v14, v219, v10
	ds_bpermute_b32 v15, v219, v11
	s_waitcnt lgkmcnt(3)
	v_max_u32_e32 v8, v12, v8
	s_waitcnt lgkmcnt(2)
	v_max_u32_e32 v9, v13, v9
	ds_bpermute_b32 v12, v220, v8
	ds_bpermute_b32 v13, v220, v9
	s_waitcnt lgkmcnt(3)
	v_max_u32_e32 v10, v14, v10
	s_waitcnt lgkmcnt(2)
	v_max_u32_e32 v11, v15, v11
	ds_bpermute_b32 v14, v220, v10
	ds_bpermute_b32 v15, v220, v11
	s_waitcnt lgkmcnt(3)
	v_max_u32_e32 v8, v12, v8
	s_waitcnt lgkmcnt(2)
	v_max_u32_e32 v9, v13, v9
	ds_bpermute_b32 v12, v221, v8
	ds_bpermute_b32 v13, v221, v9
	s_waitcnt lgkmcnt(3)
	v_max_u32_e32 v10, v14, v10
	s_waitcnt lgkmcnt(2)
	v_max_u32_e32 v11, v15, v11
	ds_bpermute_b32 v14, v221, v10
	ds_bpermute_b32 v15, v221, v11
	s_waitcnt lgkmcnt(3)
	v_max_u32_e32 v8, v12, v8
	s_waitcnt lgkmcnt(2)
	v_max_u32_e32 v9, v13, v9
	v_readfirstlane_b32 s0, v8
	v_readfirstlane_b32 s1, v9
	s_waitcnt lgkmcnt(1)
	v_max_u32_e32 v8, v14, v10
	s_andn2_b32 s17, 63, s0
	s_waitcnt lgkmcnt(0)
	v_max_u32_e32 v9, v15, v11
	s_andn2_b32 s60, 63, s1
	v_cmp_ne_u32_e32 vcc, s17, v72
	v_readfirstlane_b32 s0, v8
	v_readfirstlane_b32 s1, v9
	v_cndmask_b32_e32 v6, 0, v6, vcc
	v_cmp_ne_u32_e32 vcc, s60, v72
	s_andn2_b32 s97, 63, s0
	s_andn2_b32 s49, 63, s1
	v_cndmask_b32_e32 v7, 0, v7, vcc
	ds_bpermute_b32 v8, v73, v6
	v_cmp_ne_u32_e32 vcc, s97, v72
	ds_bpermute_b32 v9, v73, v7
	v_readlane_b32 s47, v0, s82
	v_cndmask_b32_e32 v5, 0, v5, vcc
	v_cmp_ne_u32_e32 vcc, s49, v72
	ds_bpermute_b32 v10, v73, v5
	s_waitcnt lgkmcnt(2)
	v_max_u32_e32 v8, v8, v6
	v_cndmask_b32_e32 v4, 0, v4, vcc
	ds_bpermute_b32 v11, v73, v4
	s_waitcnt lgkmcnt(2)
	v_max_u32_e32 v9, v9, v7
	ds_bpermute_b32 v12, v217, v8
	ds_bpermute_b32 v13, v217, v9
	s_waitcnt lgkmcnt(3)
	v_max_u32_e32 v10, v10, v5
	s_waitcnt lgkmcnt(2)
	v_max_u32_e32 v11, v11, v4
	ds_bpermute_b32 v14, v217, v10
	ds_bpermute_b32 v15, v217, v11
	s_waitcnt lgkmcnt(3)
	v_max_u32_e32 v8, v12, v8
	s_waitcnt lgkmcnt(2)
	v_max_u32_e32 v9, v13, v9
	ds_bpermute_b32 v12, v218, v8
	ds_bpermute_b32 v13, v218, v9
	s_waitcnt lgkmcnt(3)
	v_max_u32_e32 v10, v14, v10
	s_waitcnt lgkmcnt(2)
	v_max_u32_e32 v11, v15, v11
	ds_bpermute_b32 v14, v218, v10
	ds_bpermute_b32 v15, v218, v11
	s_waitcnt lgkmcnt(3)
	v_max_u32_e32 v8, v12, v8
	s_waitcnt lgkmcnt(2)
	v_max_u32_e32 v9, v13, v9
	ds_bpermute_b32 v12, v219, v8
	ds_bpermute_b32 v13, v219, v9
	s_waitcnt lgkmcnt(3)
	v_max_u32_e32 v10, v14, v10
	s_waitcnt lgkmcnt(2)
	v_max_u32_e32 v11, v15, v11
	ds_bpermute_b32 v14, v219, v10
	ds_bpermute_b32 v15, v219, v11
	s_waitcnt lgkmcnt(3)
	v_max_u32_e32 v8, v12, v8
	s_waitcnt lgkmcnt(2)
	v_max_u32_e32 v9, v13, v9
	ds_bpermute_b32 v12, v220, v8
	ds_bpermute_b32 v13, v220, v9
	s_waitcnt lgkmcnt(3)
	v_max_u32_e32 v10, v14, v10
	s_waitcnt lgkmcnt(2)
	v_max_u32_e32 v11, v15, v11
	ds_bpermute_b32 v14, v220, v10
	ds_bpermute_b32 v15, v220, v11
	s_waitcnt lgkmcnt(3)
	v_max_u32_e32 v8, v12, v8
	s_waitcnt lgkmcnt(2)
	v_max_u32_e32 v9, v13, v9
	ds_bpermute_b32 v12, v221, v8
	ds_bpermute_b32 v13, v221, v9
	s_waitcnt lgkmcnt(3)
	v_max_u32_e32 v10, v14, v10
	s_waitcnt lgkmcnt(2)
	v_max_u32_e32 v11, v15, v11
	ds_bpermute_b32 v14, v221, v10
	ds_bpermute_b32 v15, v221, v11
	s_waitcnt lgkmcnt(3)
	v_max_u32_e32 v8, v12, v8
	s_waitcnt lgkmcnt(2)
	v_max_u32_e32 v9, v13, v9
	v_readfirstlane_b32 s0, v8
	v_readfirstlane_b32 s1, v9
	s_waitcnt lgkmcnt(1)
	v_max_u32_e32 v8, v14, v10
	s_andn2_b32 s80, 63, s0
	s_waitcnt lgkmcnt(0)
	v_max_u32_e32 v9, v15, v11
	s_andn2_b32 s33, 63, s1
	v_cmp_ne_u32_e32 vcc, s80, v72
	v_readfirstlane_b32 s0, v8
	v_readfirstlane_b32 s1, v9
	v_cndmask_b32_e32 v6, 0, v6, vcc
	v_cmp_ne_u32_e32 vcc, s33, v72
	s_andn2_b32 s61, 63, s0
	s_andn2_b32 s96, 63, s1
	v_cndmask_b32_e32 v7, 0, v7, vcc
	ds_bpermute_b32 v8, v73, v6
	v_cmp_ne_u32_e32 vcc, s61, v72
	ds_bpermute_b32 v9, v73, v7
	v_readlane_b32 s43, v3, s45
	v_cndmask_b32_e32 v5, 0, v5, vcc
	v_cmp_ne_u32_e32 vcc, s96, v72
	ds_bpermute_b32 v10, v73, v5
	s_waitcnt lgkmcnt(2)
	v_max_u32_e32 v8, v8, v6
	v_cndmask_b32_e32 v4, 0, v4, vcc
	ds_bpermute_b32 v11, v73, v4
	s_waitcnt lgkmcnt(2)
	v_max_u32_e32 v9, v9, v7
	ds_bpermute_b32 v12, v217, v8
	ds_bpermute_b32 v13, v217, v9
	s_waitcnt lgkmcnt(3)
	v_max_u32_e32 v10, v10, v5
	s_waitcnt lgkmcnt(2)
	v_max_u32_e32 v11, v11, v4
	ds_bpermute_b32 v14, v217, v10
	ds_bpermute_b32 v15, v217, v11
	s_waitcnt lgkmcnt(3)
	v_max_u32_e32 v8, v12, v8
	s_waitcnt lgkmcnt(2)
	v_max_u32_e32 v9, v13, v9
	ds_bpermute_b32 v12, v218, v8
	ds_bpermute_b32 v13, v218, v9
	s_waitcnt lgkmcnt(3)
	v_max_u32_e32 v10, v14, v10
	s_waitcnt lgkmcnt(2)
	v_max_u32_e32 v11, v15, v11
	ds_bpermute_b32 v14, v218, v10
	ds_bpermute_b32 v15, v218, v11
	s_waitcnt lgkmcnt(3)
	v_max_u32_e32 v8, v12, v8
	s_waitcnt lgkmcnt(2)
	v_max_u32_e32 v9, v13, v9
	ds_bpermute_b32 v12, v219, v8
	ds_bpermute_b32 v13, v219, v9
	s_waitcnt lgkmcnt(3)
	v_max_u32_e32 v10, v14, v10
	s_waitcnt lgkmcnt(2)
	v_max_u32_e32 v11, v15, v11
	ds_bpermute_b32 v14, v219, v10
	ds_bpermute_b32 v15, v219, v11
	s_waitcnt lgkmcnt(3)
; template <int l>
; __device__ __forceinline__ void layer_phases(Frame& F, const XcdBarrier& bar, const int lo, const int hi) {
;     ...
;                 for (int k = 0; k < 6; ++k) {
;                     unsigned mx[4];
; #pragma unroll
;                     for (int rr = 0; rr < 4; ++rr) mx[rr] = key[rr];
; #pragma unroll
;                     for (int o = 1; o < 64; o <<= 1) {
; #pragma unroll
;                         for (int rr = 0; rr < 4; ++rr) { const unsigned t = __shfl_xor(mx[rr], o); mx[rr] = t > mx[rr] ? t : mx[rr]; } }
; #pragma unroll
;                     for (int rr = 0; rr < 4; ++rr) { const int win = 63 - (int)(__builtin_amdgcn_readfirstlane((int)mx[rr]) & 63);
;                         ek[rr][k] = win; sk[rr][k] = __uint_as_float((unsigned)__builtin_amdgcn_readlane((int)__float_as_uint(score[rr]), win)); if (F.lane == win) key[rr] = 0u; }
;                 }
; #pragma unroll
;                 for (int rr = 0; rr < 4; ++rr) { const int m = m0 + rr;
;                     const float ssum = ((sk[rr][0] + sk[rr][1]) + (sk[rr][2] + sk[rr][3])) + (sk[rr][4] + sk[rr][5]);
;                     if (F.lane < 6 && rep == 0) { int e = ek[rr][0]; float sc = sk[rr][0];
; #pragma unroll
;                         for (int k = 1; k < 6; ++k) if (F.lane == k) { e = ek[rr][k]; sc = sk[rr][k]; }
;                         const unsigned pos = __hip_atomic_fetch_add(F.ctl + CW_CURSOR + (l * 64 + e) * 16, 1u, RLX_AGENT);
	v_max_u32_e32 v8, v12, v8
	s_waitcnt lgkmcnt(2)
	v_max_u32_e32 v9, v13, v9
	ds_bpermute_b32 v12, v220, v8
	ds_bpermute_b32 v13, v220, v9
	s_waitcnt lgkmcnt(3)
	v_max_u32_e32 v10, v14, v10
	s_waitcnt lgkmcnt(2)
	v_max_u32_e32 v11, v15, v11
	ds_bpermute_b32 v14, v220, v10
	ds_bpermute_b32 v15, v220, v11
	s_waitcnt lgkmcnt(3)
	v_max_u32_e32 v8, v12, v8
	s_waitcnt lgkmcnt(2)
	v_max_u32_e32 v9, v13, v9
	ds_bpermute_b32 v12, v221, v8
	ds_bpermute_b32 v13, v221, v9
	s_waitcnt lgkmcnt(3)
	v_max_u32_e32 v10, v14, v10
	s_waitcnt lgkmcnt(2)
	v_max_u32_e32 v11, v15, v11
	ds_bpermute_b32 v14, v221, v10
	ds_bpermute_b32 v15, v221, v11
	s_waitcnt lgkmcnt(3)
	v_max_u32_e32 v8, v12, v8
	s_waitcnt lgkmcnt(2)
	v_max_u32_e32 v9, v13, v9
	v_readfirstlane_b32 s0, v8
	v_readfirstlane_b32 s1, v9
	s_waitcnt lgkmcnt(1)
	v_max_u32_e32 v8, v14, v10
	s_andn2_b32 s92, 63, s0
	s_waitcnt lgkmcnt(0)
	v_max_u32_e32 v9, v15, v11
	s_andn2_b32 s77, 63, s1
	v_cmp_ne_u32_e32 vcc, s92, v72
	v_readfirstlane_b32 s0, v8
	v_readfirstlane_b32 s1, v9
	v_cndmask_b32_e32 v6, 0, v6, vcc
	v_cmp_ne_u32_e32 vcc, s77, v72
	s_andn2_b32 s79, 63, s0
	s_andn2_b32 s63, 63, s1
	v_cndmask_b32_e32 v7, 0, v7, vcc
	ds_bpermute_b32 v8, v73, v6
	v_cmp_ne_u32_e32 vcc, s79, v72
	ds_bpermute_b32 v9, v73, v7
	v_readlane_b32 s18, v2, s19
	v_cndmask_b32_e32 v5, 0, v5, vcc
	v_cmp_ne_u32_e32 vcc, s63, v72
	ds_bpermute_b32 v10, v73, v5
	s_waitcnt lgkmcnt(2)
	v_max_u32_e32 v8, v8, v6
	v_cndmask_b32_e32 v4, 0, v4, vcc
	ds_bpermute_b32 v11, v73, v4
	s_waitcnt lgkmcnt(2)
	v_max_u32_e32 v9, v9, v7
	ds_bpermute_b32 v12, v217, v8
	ds_bpermute_b32 v13, v217, v9
	s_waitcnt lgkmcnt(3)
	v_max_u32_e32 v10, v10, v5
	s_waitcnt lgkmcnt(2)
	v_max_u32_e32 v11, v11, v4
	ds_bpermute_b32 v14, v217, v10
	ds_bpermute_b32 v15, v217, v11
	s_waitcnt lgkmcnt(3)
	v_max_u32_e32 v8, v12, v8
	s_waitcnt lgkmcnt(2)
	v_max_u32_e32 v9, v13, v9
	ds_bpermute_b32 v12, v218, v8
	ds_bpermute_b32 v13, v218, v9
	s_waitcnt lgkmcnt(3)
	v_max_u32_e32 v10, v14, v10
	s_waitcnt lgkmcnt(2)
	v_max_u32_e32 v11, v15, v11
	ds_bpermute_b32 v14, v218, v10
	ds_bpermute_b32 v15, v218, v11
	s_waitcnt lgkmcnt(3)
	v_max_u32_e32 v8, v12, v8
	s_waitcnt lgkmcnt(2)
	v_max_u32_e32 v9, v13, v9
	ds_bpermute_b32 v12, v219, v8
	ds_bpermute_b32 v13, v219, v9
	s_waitcnt lgkmcnt(3)
	v_max_u32_e32 v10, v14, v10
	s_waitcnt lgkmcnt(2)
	v_max_u32_e32 v11, v15, v11
	ds_bpermute_b32 v14, v219, v10
	ds_bpermute_b32 v15, v219, v11
	s_waitcnt lgkmcnt(3)
	v_max_u32_e32 v8, v12, v8
	s_waitcnt lgkmcnt(2)
	v_max_u32_e32 v9, v13, v9
	ds_bpermute_b32 v12, v220, v8
	ds_bpermute_b32 v13, v220, v9
	s_waitcnt lgkmcnt(3)
	v_max_u32_e32 v10, v14, v10
	s_waitcnt lgkmcnt(2)
	v_max_u32_e32 v11, v15, v11
	ds_bpermute_b32 v14, v220, v10
	ds_bpermute_b32 v15, v220, v11
	s_waitcnt lgkmcnt(3)
	v_max_u32_e32 v8, v12, v8
	s_waitcnt lgkmcnt(2)
	v_max_u32_e32 v9, v13, v9
	ds_bpermute_b32 v12, v221, v8
	ds_bpermute_b32 v13, v221, v9
	s_waitcnt lgkmcnt(3)
	v_max_u32_e32 v10, v14, v10
	s_waitcnt lgkmcnt(2)
	v_max_u32_e32 v11, v15, v11
	ds_bpermute_b32 v14, v221, v10
	ds_bpermute_b32 v15, v221, v11
	s_waitcnt lgkmcnt(3)
	v_max_u32_e32 v8, v12, v8
	s_waitcnt lgkmcnt(2)
	v_max_u32_e32 v9, v13, v9
	v_readfirstlane_b32 s0, v8
	v_readfirstlane_b32 s1, v9
	s_waitcnt lgkmcnt(1)
	v_max_u32_e32 v8, v14, v10
	s_andn2_b32 s53, 63, s0
	s_waitcnt lgkmcnt(0)
	v_max_u32_e32 v9, v15, v11
	s_andn2_b32 s91, 63, s1
	v_cmp_ne_u32_e32 vcc, s53, v72
	v_readfirstlane_b32 s0, v8
	v_readfirstlane_b32 s1, v9
	v_cndmask_b32_e32 v6, 0, v6, vcc
	v_cmp_ne_u32_e32 vcc, s91, v72
	s_andn2_b32 s59, 63, s0
	s_andn2_b32 s78, 63, s1
	v_cndmask_b32_e32 v7, 0, v7, vcc
	v_cmp_ne_u32_e32 vcc, s59, v72
	ds_bpermute_b32 v8, v73, v6
	ds_bpermute_b32 v9, v73, v7
	v_cndmask_b32_e32 v5, 0, v5, vcc
	v_cmp_ne_u32_e32 vcc, s78, v72
	ds_bpermute_b32 v10, v73, v5
	s_waitcnt lgkmcnt(2)
	v_max_u32_e32 v6, v8, v6
	v_cndmask_b32_e32 v4, 0, v4, vcc
	ds_bpermute_b32 v11, v73, v4
	s_waitcnt lgkmcnt(2)
	v_max_u32_e32 v7, v9, v7
	ds_bpermute_b32 v8, v217, v6
	ds_bpermute_b32 v9, v217, v7
	s_waitcnt lgkmcnt(3)
	v_max_u32_e32 v5, v10, v5
	s_waitcnt lgkmcnt(2)
	v_max_u32_e32 v4, v11, v4
	ds_bpermute_b32 v10, v217, v5
	ds_bpermute_b32 v11, v217, v4
	s_waitcnt lgkmcnt(3)
	v_max_u32_e32 v6, v8, v6
	s_waitcnt lgkmcnt(2)
	v_max_u32_e32 v7, v9, v7
	ds_bpermute_b32 v8, v218, v6
	ds_bpermute_b32 v9, v218, v7
	s_waitcnt lgkmcnt(3)
	v_max_u32_e32 v5, v10, v5
	s_waitcnt lgkmcnt(2)
	v_max_u32_e32 v4, v11, v4
	ds_bpermute_b32 v10, v218, v5
	ds_bpermute_b32 v11, v218, v4
	s_waitcnt lgkmcnt(3)
	v_max_u32_e32 v6, v8, v6
	s_waitcnt lgkmcnt(2)
	v_max_u32_e32 v7, v9, v7
	ds_bpermute_b32 v8, v219, v6
	ds_bpermute_b32 v9, v219, v7
	s_waitcnt lgkmcnt(3)
	v_max_u32_e32 v5, v10, v5
	s_waitcnt lgkmcnt(2)
	v_max_u32_e32 v4, v11, v4
	ds_bpermute_b32 v10, v219, v5
	ds_bpermute_b32 v11, v219, v4
	s_waitcnt lgkmcnt(3)
	v_max_u32_e32 v6, v8, v6
	s_waitcnt lgkmcnt(2)
	v_max_u32_e32 v7, v9, v7
	ds_bpermute_b32 v8, v220, v6
	ds_bpermute_b32 v9, v220, v7
	s_waitcnt lgkmcnt(3)
	v_max_u32_e32 v5, v10, v5
	s_waitcnt lgkmcnt(2)
	v_max_u32_e32 v4, v11, v4
	ds_bpermute_b32 v10, v220, v5
	ds_bpermute_b32 v11, v220, v4
	s_waitcnt lgkmcnt(3)
	v_max_u32_e32 v6, v8, v6
	s_waitcnt lgkmcnt(2)
	v_max_u32_e32 v7, v9, v7
	ds_bpermute_b32 v8, v221, v6
	ds_bpermute_b32 v9, v221, v7
	s_waitcnt lgkmcnt(3)
	v_max_u32_e32 v5, v10, v5
	s_waitcnt lgkmcnt(2)
	v_max_u32_e32 v4, v11, v4
	ds_bpermute_b32 v10, v221, v5
	ds_bpermute_b32 v11, v221, v4
	s_waitcnt lgkmcnt(3)
	v_max_u32_e32 v6, v8, v6
	s_waitcnt lgkmcnt(2)
	v_max_u32_e32 v7, v9, v7
	v_readfirstlane_b32 s0, v6
	v_readfirstlane_b32 s1, v7
	s_waitcnt lgkmcnt(1)
	v_max_u32_e32 v5, v10, v5
	s_waitcnt lgkmcnt(0)
	v_max_u32_e32 v4, v11, v4
	s_andn2_b32 vcc_lo, 63, s0
	s_andn2_b32 s52, 63, s1
	v_readfirstlane_b32 s0, v5
	v_readfirstlane_b32 s1, v4
	s_andn2_b32 s88, 63, s0
	s_andn2_b32 s58, 63, s1
	v_readlane_b32 s81, v1, s17
	v_readlane_b32 s62, v0, s60
	v_readlane_b32 s55, v3, s97
	v_readlane_b32 s34, v2, s49
	v_readlane_b32 s0, v1, s80
	v_readlane_b32 s72, v0, s33
	v_readlane_b32 s65, v3, s61
	v_readlane_b32 s35, v2, s96
	v_readlane_b32 s29, v1, s92
	v_readlane_b32 s1, v0, s77
	v_readlane_b32 s73, v3, s79
	v_readlane_b32 s67, v2, s63
	v_readlane_b32 s31, v1, s53
	v_readlane_b32 s28, v0, s91
	v_readlane_b32 s75, v3, s59
	v_readlane_b32 s69, v2, s78
	v_readlane_b32 s71, v1, vcc_lo
	v_readlane_b32 s30, v0, s52
	v_readlane_b32 s84, v3, s88
	v_readlane_b32 s74, v2, s58
	s_mov_b64 s[14:15], exec
	v_readlane_b32 s22, v248, 34
	v_readlane_b32 s23, v248, 35
	s_and_b64 s[22:23], s[14:15], s[22:23]
	s_mov_b64 exec, s[22:23]
	s_cbranch_execz .LBB0_609
; template <int l>
; __device__ __forceinline__ void layer_phases(Frame& F, const XcdBarrier& bar, const int lo, const int hi) {
;     ...
; #pragma unroll
;                 for (int rr = 0; rr < 4; ++rr) { const int m = m0 + rr;
;                     const float ssum = ((sk[rr][0] + sk[rr][1]) + (sk[rr][2] + sk[rr][3])) + (sk[rr][4] + sk[rr][5]);
;                     if (F.lane < 6 && rep == 0) { int e = ek[rr][0]; float sc = sk[rr][0];
; #pragma unroll
;                         for (int k = 1; k < 6; ++k) if (F.lane == k) { e = ek[rr][k]; sc = sk[rr][k]; }
;                         const unsigned pos = __hip_atomic_fetch_add(F.ctl + CW_CURSOR + (l * 64 + e) * 16, 1u, RLX_AGENT);
;                         if (pos < (unsigned)LISTCAP) { list[(size_t)e * LISTCAP + pos] = m; list2[(size_t)e * LISTCAP + pos] = m * 7 + F.lane; }
;                         tinfo[(size_t)m * 6 + F.lane] = e | (int)(pos << 8); gates[(size_t)m * 6 + F.lane] = sc / ssum * ROUTED_SCALE; }
	v_mov_b32_e32 v40, s16
	v_mov_b32_e32 v48, s17
	v_cndmask_b32_e64 v40, v40, v48, s[4:5]
	v_mov_b32_e32 v48, s80
	v_cndmask_b32_e64 v40, v40, v48, s[6:7]
	v_mov_b32_e32 v48, s92
	v_cndmask_b32_e64 v40, v40, v48, s[8:9]
	v_mov_b32_e32 v48, s53
	v_cndmask_b32_e64 v40, v40, v48, s[10:11]
	v_mov_b32_e32 v48, vcc_lo
	v_cndmask_b32_e64 v40, v40, v48, s[12:13]
	v_lshlrev_b32_e32 v34, 6, v40
	global_atomic_add v44, v34, v226, s[38:39] sc0
	v_mov_b32_e32 v41, s82
	v_mov_b32_e32 v48, s60
	v_cndmask_b32_e64 v41, v41, v48, s[4:5]
	v_mov_b32_e32 v48, s33
	v_cndmask_b32_e64 v41, v41, v48, s[6:7]
	v_mov_b32_e32 v48, s77
	v_cndmask_b32_e64 v41, v41, v48, s[8:9]
	v_mov_b32_e32 v48, s91
	v_cndmask_b32_e64 v41, v41, v48, s[10:11]
	v_mov_b32_e32 v48, s52
	v_cndmask_b32_e64 v41, v41, v48, s[12:13]
	v_lshlrev_b32_e32 v34, 6, v41
	global_atomic_add v45, v34, v226, s[38:39] sc0
	v_mov_b32_e32 v42, s45
	v_mov_b32_e32 v48, s97
	v_cndmask_b32_e64 v42, v42, v48, s[4:5]
	v_mov_b32_e32 v48, s61
	v_cndmask_b32_e64 v42, v42, v48, s[6:7]
	v_mov_b32_e32 v48, s79
	v_cndmask_b32_e64 v42, v42, v48, s[8:9]
	v_mov_b32_e32 v48, s59
	v_cndmask_b32_e64 v42, v42, v48, s[10:11]
	v_mov_b32_e32 v48, s88
	v_cndmask_b32_e64 v42, v42, v48, s[12:13]
	v_lshlrev_b32_e32 v34, 6, v42
	global_atomic_add v46, v34, v226, s[38:39] sc0
	v_mov_b32_e32 v43, s19
	v_mov_b32_e32 v48, s49
	v_cndmask_b32_e64 v43, v43, v48, s[4:5]
	v_mov_b32_e32 v48, s96
	v_cndmask_b32_e64 v43, v43, v48, s[6:7]
	v_mov_b32_e32 v48, s63
	v_cndmask_b32_e64 v43, v43, v48, s[8:9]
	v_mov_b32_e32 v48, s78
	v_cndmask_b32_e64 v43, v43, v48, s[10:11]
	v_mov_b32_e32 v48, s58
	v_cndmask_b32_e64 v43, v43, v48, s[12:13]
	v_lshlrev_b32_e32 v34, 6, v43
	global_atomic_add v47, v34, v226, s[38:39] sc0
	s_waitcnt vmcnt(0)
	v_mov_b32_e32 v0, v40
	v_mov_b32_e32 v80, v44
	v_cmp_gt_u32_e32 vcc, s85, v80
	s_and_saveexec_b64 s[16:17], vcc
	s_cbranch_execz .LBB0_615
	v_lshlrev_b64 v[2:3], 2, v[80:81]
	v_readlane_b32 s22, v248, 15
	v_lshl_or_b32 v2, v0, 16, v2
	v_readlane_b32 s23, v248, 16
	v_mov_b32_e32 v1, s42
	s_nop 0
	v_lshl_add_u64 v[4:5], s[22:23], 0, v[2:3]
	global_store_dword v[4:5], v1, off
	v_mad_u64_u32 v[4:5], s[22:23], s42, 7, v[72:73]
	v_readlane_b32 s22, v248, 17
	v_readlane_b32 s23, v248, 18
	s_nop 1
	v_lshl_add_u64 v[2:3], s[22:23], 0, v[2:3]
	global_store_dword v[2:3], v4, off

; #define GRID_BAR() xcd_barrier(bar, F.tid == 0)
; #define GRID_BAR() do { } while (0)
; #define BOTH(k) (IN(k) && IN((k) + 1))
; __device__ __forceinline__ void xcd_barrier(const XcdBarrier& b, bool leader  ) {
;     asm volatile("s_waitcnt vmcnt(0)" ::: "memory");
;     __syncthreads();
;     if (leader) {
;         unsigned* bar = b.bar;
;         __builtin_amdgcn_s_waitcnt(0);
;         unsigned nloc = b.st[0], nx = b.st[1];
;         if (nloc == 0u) { xcd_barrier_complete(bar, b.x, nloc, nx); b.st[0] = nloc; b.st[1] = nx; }
; template <int l>
; __device__ __forceinline__ void layer_phases(Frame& F, const XcdBarrier& bar, const int lo, const int hi) {
;     ...
;                 __syncthreads();
;             }
;             __syncthreads();
;             if (BOTH(pb + 3)) GRID_BAR();
.LBB0_621:
	s_waitcnt lgkmcnt(0)
	s_barrier
	v_lshlrev_b32_e32 v252, 3, v216
	v_add_u32_e32 v252, 0x21400, v252
	ds_write_b64 v252, v[254:255]
	s_waitcnt lgkmcnt(0)
	s_barrier
	v_readlane_b32 s92, v248, 7
	v_readlane_b32 s93, v248, 8
	s_cmp_gt_u32 s93, 6
	v_readlane_b32 s78, v248, 10
	v_readlane_b32 s79, v248, 11
	v_readlane_b32 s90, v248, 6
	s_barrier
	s_cbranch_scc0 .LBB0_675
	s_waitcnt vmcnt(0)
	v_sub_u32_e32 v0, 0, v72
	v_readlane_b32 s0, v248, 0
	s_barrier
	s_nop 0
	v_cmp_eq_u32_e32 vcc, s0, v0
	s_and_saveexec_b64 s[0:1], vcc
	s_cbranch_execz .LBB0_674
	s_add_i32 s3, 0, 0x21520
	v_mov_b32_e32 v0, s3
	s_waitcnt vmcnt(0) expcnt(0) lgkmcnt(0)
	ds_read_b32 v2, v0
	s_add_i32 s3, 0, 0x21524
	v_mov_b32_e32 v0, s3
	ds_read_b32 v0, v0
	s_waitcnt lgkmcnt(1)
	v_cmp_ne_u32_e32 vcc, 0, v2
	s_cbranch_vccnz .LBB0_638
	v_readlane_b32 s4, v248, 1
	v_readlane_b32 s5, v248, 2
	s_load_dwordx2 s[8:9], s[4:5], 0x4
	s_add_u32 s4, s56, 0x4200
	s_addc_u32 s5, s57, 0
	s_add_u32 s6, s56, 0x4400
	s_addc_u32 s7, s57, 0
	s_waitcnt lgkmcnt(0)
	s_mul_i32 s3, s8, s76
	s_add_u32 s8, s56, 0x4500
	s_mul_i32 s3, s3, s9
	s_addc_u32 s9, s57, 0
	s_add_u32 s10, s56, 0x4600
	s_addc_u32 s11, s57, 0
	s_add_u32 s12, s56, 0x4700
	s_addc_u32 s13, s57, 0
	s_add_u32 s14, s56, 0x4800
	s_addc_u32 s15, s57, 0
	s_add_u32 s16, s56, 0x4900
	s_addc_u32 s17, s57, 0
	s_add_u32 s18, s56, 0x4a00
	s_addc_u32 s19, s57, 0
	s_add_u32 s20, s56, 0x4b00
	s_addc_u32 s21, s57, 0
	s_add_u32 s22, s56, 0x4c00
	s_addc_u32 s23, s57, 0
	s_add_u32 s24, s56, 0x4d00
	s_addc_u32 s25, s57, 0
	s_add_u32 s26, s56, 0x4e00
	s_addc_u32 s27, s57, 0
	s_add_u32 s28, s56, 0x4f00
	s_addc_u32 s29, s57, 0
	s_add_u32 s30, s56, 0x5000
	s_addc_u32 s31, s57, 0
	s_add_u32 s34, s56, 0x5100
	s_addc_u32 s35, s57, 0
	s_add_u32 s36, s56, 0x5200
	s_addc_u32 s37, s57, 0
	s_add_u32 s38, s56, 0x5300
	s_addc_u32 s39, s57, 0
	s_mov_b32 s33, 1
	v_mov_b32_e32 v16, 0
	s_branch .LBB0_626

; #define LAS __attribute__((address_space(3)))
; __device__ __forceinline__ void refresh(Frame& F) { int l = (int)__builtin_amdgcn_mbcnt_hi(~0u, __builtin_amdgcn_mbcnt_lo(~0u, 0u)); asm volatile("" : "+v"(l)); F.lane = l; F.tid = F.wave * 64 + l; }
; __device__ __forceinline__ int affine_item(int item_, int G) { if (G != 256) return item_; const int c = item_ & 255, i = item_ >> 8; return 64 * (c & 7) + (c >> 3) + 32 * i; }
; template <int l>
; __device__ __forceinline__ void layer_phases(Frame& F, const XcdBarrier& bar, const int lo, const int hi) {
;     ...
;             refresh(F);
;             const bf16* mixb = (const bf16*)(ws + WS_Y1); const float* xin = inptr<const float>(F, I_X); const bf16* xinb = (const bf16*)(ws + WS_X2B); bf16* x1 = (bf16*)(ws + WS_X1); unsigned char* h2q = ws + WS_H2;
;             const float* g1 = inptr<const float>(F, I_LN1G) + (size_t)l * D; const float* b1 = inptr<const float>(F, I_LN1B) + (size_t)l * D;
;             int* tinfo = (int*)(ws + WS_TINFO); float* gates = (float*)(ws + WS_GATE); int* list = (int*)(ws + WS_LIST); int* list2 = (int*)(ws + WS_LIST2);
;             LAS unsigned char* h2s = F.lds + RING_OFF;
;             LAS float* part = (LAS float*)(F.lds + RING_OFF);
;             const unsigned char* wrf = ws + WS_WR + (size_t)l * 524288;
;             const float rb = inptr<const float>(F, I_RBIAS)[l * NE + F.lane];
;             for (int item_ = blockIdx.x; item_ < T / 32; item_ += F.G) {
;                 const int item = affine_item(item_, F.G);
;                 const int m0 = item * 32 + 4 * F.wave;
;                 int lq = F.lane; asm volatile("" : "+v"(lq));
;                 const int r32 = lq & 31, hi5 = lq >> 5;
;                 const float* mrow = (const float*)(ws + WS_MOD) + ((size_t)l * 8 + (m0 >> 11)) * 12288;
.LBB0_1515:
	s_cmp_gt_i32 s92, 13
	s_cselect_b64 s[0:1], -1, 0
	s_cmp_lt_i32 s93, 14
	s_cselect_b64 s[4:5], -1, 0
	s_or_b64 s[0:1], s[0:1], s[4:5]
	s_and_b64 vcc, exec, s[0:1]
	s_cbranch_vccnz .LBB0_1585
	s_add_i32 s0, 0, 0x21448
	s_waitcnt vmcnt(17)
	v_mov_b32_e32 v0, s0
	s_add_i32 s0, 0, 0x21460
	s_waitcnt vmcnt(4)
	v_mov_b32_e32 v52, v216
	v_mov_b32_e32 v4, s0
	ds_read2_b64 v[0:3], v0 offset1:1
	ds_read_b64 v[4:5], v4
	s_mov_b32 s1, 0
	s_cmpk_gt_i32 s2, 0x1ff
	s_waitcnt lgkmcnt(1)
	v_readfirstlane_b32 s0, v1
	v_readfirstlane_b32 s7, v0
	v_readfirstlane_b32 s6, v3
	v_readfirstlane_b32 s8, v2
	s_waitcnt lgkmcnt(0)
	v_readfirstlane_b32 s5, v5
	v_readfirstlane_b32 s4, v4
	v_lshlrev_b32_e32 v252, 3, v216
	v_add_u32_e32 v252, 0x21400, v252
	ds_read_b64 v[254:255], v252
	s_waitcnt lgkmcnt(0)
	s_cbranch_scc1 .LBB0_1531
	v_ashrrev_i32_e32 v53, 31, v52
	v_lshlrev_b64 v[0:1], 2, v[52:53]
	v_lshl_add_u64 v[2:3], s[4:5], 0, v[0:1]
	flat_load_dword v54, v[2:3] offset:256
	s_add_u32 s20, s56, 0x55c00000
	s_addc_u32 s21, s57, 0
	s_add_u32 s22, s56, 0x3dc00000
	s_addc_u32 s23, s57, 0
	s_add_u32 s3, s56, 0x39c00000
	s_addc_u32 s39, s57, 0
	s_add_u32 s48, s56, 0x41c00000
	s_addc_u32 s49, s57, 0
	s_add_u32 s4, s56, 0xa00000
	s_addc_u32 s5, s57, 0
	v_writelane_b32 v248, s4, 13
	v_and_b32_e32 v2, 64, v216
	v_add_u32_e32 v2, 64, v2
	v_writelane_b32 v248, s5, 14
	s_add_u32 s4, s56, 0x6f600000
	s_addc_u32 s5, s57, 0
	v_writelane_b32 v248, s4, 15
	v_xor_b32_e32 v3, 1, v216
	v_cmp_lt_i32_e32 vcc, v3, v2
	v_writelane_b32 v248, s5, 16
	s_add_u32 s4, s56, 0x100000
	v_writelane_b32 v248, s4, 17
	s_addc_u32 s4, s57, 0
	v_writelane_b32 v248, s4, 19
	s_add_u32 s4, s7, 0x2000
	s_addc_u32 s5, s0, 0
	s_add_u32 s30, s8, 0x2000
	s_addc_u32 s31, s6, 0
	v_writelane_b32 v248, s4, 20
	s_cmpk_eq_i32 s76, 0x100
	v_cndmask_b32_e32 v3, v216, v3, vcc
	v_writelane_b32 v248, s5, 21
	s_cselect_b64 s[4:5], -1, 0
	v_writelane_b32 v248, s4, 22
	s_lshl_b32 s52, s80, 2
	v_lshl_add_u64 v[0:1], s[56:57], 0, v[0:1]
	v_writelane_b32 v248, s5, 23
	s_mov_b64 s[4:5], 0x800000
	s_lshl_b32 s0, s80, 14
	v_lshlrev_b32_e32 v53, 2, v3
	v_xor_b32_e32 v3, 2, v216
	s_waitcnt vmcnt(0)
	v_lshl_add_u64 v[56:57], v[0:1], 0, s[4:5]
	s_mov_b64 s[4:5], 0x900000
	v_writelane_b32 v248, s0, 24
	s_or_b32 s0, s52, 1
	v_cmp_lt_i32_e32 vcc, v3, v2
	v_lshl_add_u64 v[58:59], v[0:1], 0, s[4:5]
	s_lshl_b32 s4, s0, 12
	s_and_b32 s64, s0, 13
	s_or_b32 s0, s52, 2
	v_cndmask_b32_e32 v3, v216, v3, vcc
	v_writelane_b32 v248, s4, 25
	s_lshl_b32 s4, s0, 12
	s_and_b32 s66, s0, 14
	s_or_b32 s0, s52, 3
	v_lshlrev_b32_e32 v194, 2, v3
	v_xor_b32_e32 v3, 4, v216
	v_writelane_b32 v248, s4, 26
	s_lshl_b32 s4, s0, 12
	s_and_b32 s68, s0, 15
	s_lshl_b32 s0, s80, 4
	v_cmp_lt_i32_e32 vcc, v3, v2
	s_and_b32 s54, s52, 12
	s_lshl_b64 s[0:1], s[0:1], 12
	v_cndmask_b32_e32 v3, v216, v3, vcc
	s_add_u32 s0, s56, s0
	v_lshlrev_b32_e32 v195, 2, v3
	v_xor_b32_e32 v3, 8, v216
	s_addc_u32 s1, s57, s1
	v_cmp_lt_i32_e32 vcc, v3, v2
	s_add_u32 s36, s0, 0xe80000
	s_addc_u32 s37, s1, 0
	v_cndmask_b32_e32 v3, v216, v3, vcc
	s_lshl_b32 s69, s80, 5
	v_lshlrev_b32_e32 v196, 2, v3
	v_xor_b32_e32 v3, 16, v216
	v_writelane_b32 v248, s4, 27
	s_or_b32 s0, s69, 8
	v_cmp_lt_i32_e32 vcc, v3, v2
	v_writelane_b32 v248, s0, 30
	s_or_b32 s0, s69, 16
	v_cndmask_b32_e32 v3, v216, v3, vcc
	v_writelane_b32 v248, s0, 28
	s_or_b32 s0, s69, 24
	v_lshlrev_b32_e32 v197, 2, v3
	v_xor_b32_e32 v3, 32, v216
	v_writelane_b32 v248, s0, 29
	s_lshl_b32 s0, s80, 13
	v_cmp_lt_i32_e32 vcc, v3, v2
	s_add_i32 s0, s0, 0
	v_writelane_b32 v248, s0, 31
	v_cndmask_b32_e32 v2, v216, v3, vcc
	v_cmp_gt_i32_e64 s[4:5], 6, v52
	v_lshlrev_b32_e32 v198, 2, v2
	v_lshl_add_u32 v2, v52, 2, 0
	s_lshl_b32 s0, s80, 10
	v_writelane_b32 v248, s4, 32
	v_sub_u32_e32 v199, 63, v52
	v_cmp_eq_u32_e64 s[6:7], 2, v52
	v_writelane_b32 v248, s5, 33
	v_cmp_eq_u32_e64 s[4:5], 1, v52
	v_cmp_eq_u32_e64 s[8:9], 3, v52
	v_cmp_eq_u32_e64 s[10:11], 4, v52
	v_cmp_eq_u32_e64 s[12:13], 5, v52
	s_waitcnt lgkmcnt(0)
	v_mov_b32_e32 v55, v54
	s_lshl_b32 s74, s2, 6
	s_lshl_b32 s1, s76, 6
	s_mov_b32 s82, 0xffff0000
	s_movk_i32 s83, 0x4000
	s_mov_b32 s38, 0x3fb504f3
	v_mov_b32_e32 v200, 0x3727c5ac
	s_mov_b32 s85, 0xf800000
	v_mov_b32_e32 v201, 0x260
	s_movk_i32 s86, 0x7fff
	v_mov_b32_e32 v61, 0
	s_movk_i32 s87, 0x1000
	v_add_u32_e32 v202, s0, v2
	s_movk_i32 s90, 0xffc0
	v_mov_b32_e32 v203, 1
	s_mov_b32 s91, s2
	v_writelane_b32 v248, s1, 34
	s_barrier
	s_lshl_b32 s98, s80, 10
	v_lshl_add_u32 v253, v216, 4, s98
	s_mov_b32 s98, s30
	s_mov_b32 s99, s31
	global_load_dwordx4 v[100:103], v253, s[98:99]
	v_readlane_b32 s98, v248, 20
	v_readlane_b32 s99, v248, 21
	s_nop 4
	global_load_dwordx4 v[104:107], v253, s[98:99]
	s_and_b32 s100, s2, 7
	s_add_u32 s100, s100, 8
	s_mul_i32 s100, s100, 0xc000
	v_readlane_b32 s101, v248, 17
	s_nop 0
	s_add_u32 s100, s101, s100
	v_readlane_b32 s101, v248, 19
	s_nop 0
	s_addc_u32 s101, s101, 0
	s_add_u32 s98, s100, 0x8000
	s_addc_u32 s99, s101, 0
	global_load_dwordx4 v[108:111], v253, s[98:99]
	s_add_u32 s98, s100, 0x6000
	s_addc_u32 s99, s101, 0
	global_load_dwordx4 v[112:115], v253, s[98:99]
	v_add_u32_e32 v253, 0x20000, v253
	s_waitcnt vmcnt(3)
	ds_write_b128 v253, v[100:103]
	s_waitcnt vmcnt(2)
	ds_write_b128 v253, v[104:107] offset:8192
	s_waitcnt vmcnt(1)
	ds_write_b128 v253, v[108:111] offset:16384
	s_waitcnt vmcnt(0)
	ds_write_b128 v253, v[112:115] offset:24576
	v_lshlrev_b32_e32 v252, 4, v216
	v_add_u32_e32 v252, 0x20000, v252
	s_waitcnt lgkmcnt(0)
	s_barrier
	s_branch .LBB0_1520

; #define GAS __attribute__((address_space(1)))
; __device__ __forceinline__ f32x4 bf4(unsigned a, unsigned b) { return (f32x4){bflo(a), bfhi(a), bflo(b), bfhi(b)}; }
; template <int l>
; __device__ __forceinline__ void layer_phases(Frame& F, const XcdBarrier& bar, const int lo, const int hi) {
;     ...
; #pragma unroll
;                 for (int rp = 0; rp < 2; ++rp) {
;                 f32x4 vv[2][8];
; #pragma unroll
;                 for (int rr = 0; rr < 2; ++rr)
; #pragma unroll
;                     for (int j = 0; j < 8; ++j) { const size_t off = (size_t)(m0 + 2 * rp + rr) * D + 4 * lq + 256 * j;
;                         f32x4 xv; if (l == 0) xv = __builtin_nontemporal_load((const GAS f32x4*)(xin + off)); else { const v2u xw_ = __builtin_nontemporal_load((const GAS v2u*)(xinb + off)); xv = bf4(xw_.x, xw_.y); } const v2u mw = __builtin_nontemporal_load((const GAS v2u*)(mixb + off)); const f32x4 gv = *(const GAS f32x4*)(mrow + 4096 + 4 * lq + 256 * j);
;                         vv[rr][j] = xv * ALPHA + gv * (f32x4){bflo(mw.x), bfhi(mw.x), bflo(mw.y), bfhi(mw.y)}; }
.LBB0_1522:
	s_lshl_b32 s0, s0, 5
	s_add_i32 s40, s0, s52
	s_ashr_i32 s0, s40, 11
	s_add_i32 s0, s0, 8
	s_mul_hi_i32 s1, s0, 0xc000
	s_mul_i32 s0, s0, 0xc000
	v_readlane_b32 s14, v248, 17
	v_mov_b32_e32 v204, v52
	s_add_u32 s0, s14, s0
	v_readlane_b32 s14, v248, 19
	s_addc_u32 s1, s14, s1
	v_lshlrev_b32_e32 v36, 2, v204
	s_ashr_i32 s41, s40, 31
	v_ashrrev_i32_e32 v37, 31, v36
	s_lshl_b64 s[18:19], s[40:41], 11
	v_lshl_add_u64 v[0:1], s[18:19], 0, v[36:37]
	v_lshlrev_b64 v[32:33], 2, v[36:37]
	v_lshlrev_b64 v[0:1], 1, v[0:1]
	v_lshl_add_u64 v[38:39], s[0:1], 0, v[32:33]
	s_movk_i32 s24, 0x5000
	v_lshl_add_u64 v[34:35], s[22:23], 0, v[0:1]
	v_add_co_u32_e32 v126, vcc, s24, v38
	global_load_dwordx2 v[40:41], v[34:35], off nt
	v_lshl_add_u64 v[42:43], s[20:21], 0, v[0:1]
	v_addc_co_u32_e32 v127, vcc, 0, v39, vcc
	global_load_dwordx2 v[44:45], v[42:43], off nt
	global_load_dwordx2 v[46:47], v[34:35], off offset:512 nt
	global_load_dwordx2 v[48:49], v[42:43], off offset:512 nt
	global_load_dwordx2 v[50:51], v[34:35], off offset:1024 nt
	global_load_dwordx2 v[62:63], v[42:43], off offset:1024 nt
	global_load_dwordx2 v[64:65], v[34:35], off offset:1536 nt
	global_load_dwordx2 v[66:67], v[42:43], off offset:1536 nt
	global_load_dwordx4 v[0:3], v[126:127], off offset:-4096
	s_mov_b64 s[0:1], 0x4000
	v_lshl_add_u64 v[128:129], v[38:39], 0, s[0:1]
	global_load_dwordx4 v[12:15], v[128:129], off offset:1024
	global_load_dwordx4 v[8:11], v[128:129], off offset:2048
	global_load_dwordx4 v[4:7], v[128:129], off offset:3072
	global_load_dwordx2 v[68:69], v[34:35], off offset:2048 nt
	global_load_dwordx2 v[70:71], v[42:43], off offset:2048 nt
	global_load_dwordx4 v[16:19], v[126:127], off
	global_load_dwordx2 v[72:73], v[34:35], off offset:2560 nt
	global_load_dwordx2 v[74:75], v[42:43], off offset:2560 nt
	global_load_dwordx4 v[28:31], v[126:127], off offset:1024
	global_load_dwordx4 v[24:27], v[126:127], off offset:2048
	global_load_dwordx4 v[20:23], v[126:127], off offset:3072
	global_load_dwordx2 v[80:81], v[34:35], off offset:3072 nt
	global_load_dwordx2 v[82:83], v[34:35], off offset:3584 nt
	global_load_dwordx2 v[86:87], v[42:43], off offset:3072 nt
	global_load_dwordx2 v[88:89], v[42:43], off offset:3584 nt
	v_readlane_b32 s0, v248, 20
	v_readlane_b32 s1, v248, 21
	s_or_b32 s42, s40, 1
	s_ashr_i32 s43, s42, 31
	s_lshl_b64 s[16:17], s[42:43], 11
	s_mov_b32 s25, 0x9000
	s_movk_i32 s26, 0x7000
	v_mov_b32_e32 v142, 0
	v_mov_b32_e32 v174, 0
	s_waitcnt vmcnt(21)
	s_waitcnt lgkmcnt(0)
	v_lshlrev_b32_e32 v76, 16, v46
	v_lshlrev_b32_e32 v42, 16, v40
	v_and_b32_e32 v43, 0xffff0000, v40
	v_lshlrev_b32_e32 v34, 16, v41
	v_and_b32_e32 v35, 0xffff0000, v41
	v_lshlrev_b32_e32 v40, 16, v44
	v_and_b32_e32 v41, 0xffff0000, v44
	v_lshlrev_b32_e32 v44, 16, v45
	v_and_b32_e32 v45, 0xffff0000, v45
	s_waitcnt vmcnt(16)
	s_waitcnt lgkmcnt(0)
	v_lshlrev_b32_e32 v94, 16, v66
	v_and_b32_e32 v95, 0xffff0000, v66
	v_lshlrev_b32_e32 v66, 16, v67
	v_and_b32_e32 v67, 0xffff0000, v67
	s_waitcnt vmcnt(15)
	s_waitcnt lgkmcnt(0)
	v_pk_mul_f32 v[44:45], v[2:3], v[44:45]
	v_lshlrev_b32_e32 v78, 16, v48
	v_and_b32_e32 v79, 0xffff0000, v48
	v_lshlrev_b32_e32 v48, 16, v49
	v_and_b32_e32 v49, 0xffff0000, v49
	v_lshlrev_b32_e32 v92, 16, v64
	v_and_b32_e32 v93, 0xffff0000, v64
	v_lshlrev_b32_e32 v64, 16, v65
	v_and_b32_e32 v65, 0xffff0000, v65
	v_pk_mul_f32 v[40:41], v[0:1], v[40:41]
	s_waitcnt vmcnt(12)
	s_waitcnt lgkmcnt(0)
	v_pk_mul_f32 v[66:67], v[6:7], v[66:67]
	v_pk_fma_f32 v[34:35], v[34:35], s[38:39], v[44:45] op_sel_hi:[1,0,1]
	v_pk_mul_f32 v[44:45], v[4:5], v[94:95]
	v_and_b32_e32 v77, 0xffff0000, v46
	v_lshlrev_b32_e32 v46, 16, v47
	v_and_b32_e32 v47, 0xffff0000, v47
	v_pk_mul_f32 v[48:49], v[14:15], v[48:49]
	v_pk_mul_f32 v[78:79], v[12:13], v[78:79]
	v_pk_fma_f32 v[42:43], v[42:43], s[38:39], v[40:41] op_sel_hi:[1,0,1]
	v_pk_fma_f32 v[40:41], v[64:65], s[38:39], v[66:67] op_sel_hi:[1,0,1]
	v_pk_fma_f32 v[64:65], v[92:93], s[38:39], v[44:45] op_sel_hi:[1,0,1]
	s_waitcnt vmcnt(11)
	s_waitcnt lgkmcnt(0)
	v_lshlrev_b32_e32 v44, 16, v68
	v_and_b32_e32 v45, 0xffff0000, v68
	v_lshlrev_b32_e32 v66, 16, v69
	v_and_b32_e32 v67, 0xffff0000, v69
	s_waitcnt vmcnt(10)
	s_waitcnt lgkmcnt(0)
	v_lshlrev_b32_e32 v68, 16, v70
	v_and_b32_e32 v69, 0xffff0000, v70
	v_pk_fma_f32 v[46:47], v[46:47], s[38:39], v[48:49] op_sel_hi:[1,0,1]
	v_pk_fma_f32 v[48:49], v[76:77], s[38:39], v[78:79] op_sel_hi:[1,0,1]
	v_lshlrev_b32_e32 v70, 16, v71
	v_and_b32_e32 v71, 0xffff0000, v71
	s_waitcnt vmcnt(9)
	s_waitcnt lgkmcnt(0)
	v_pk_mul_f32 v[76:77], v[16:17], v[68:69]
	s_waitcnt vmcnt(7)
	s_waitcnt lgkmcnt(0)
	v_lshlrev_b32_e32 v78, 16, v74
	v_and_b32_e32 v79, 0xffff0000, v74
	v_lshlrev_b32_e32 v74, 16, v75
	v_and_b32_e32 v75, 0xffff0000, v75
	v_pk_mul_f32 v[68:69], v[18:19], v[70:71]
	v_pk_fma_f32 v[70:71], v[44:45], s[38:39], v[76:77] op_sel_hi:[1,0,1]
	v_lshlrev_b32_e32 v76, 16, v72
	v_and_b32_e32 v77, 0xffff0000, v72
	v_lshlrev_b32_e32 v72, 16, v73
	v_and_b32_e32 v73, 0xffff0000, v73
	s_waitcnt vmcnt(6)
	s_waitcnt lgkmcnt(0)
	v_pk_mul_f32 v[74:75], v[30:31], v[74:75]
	v_pk_mul_f32 v[78:79], v[28:29], v[78:79]
	v_lshlrev_b32_e32 v90, 16, v62
	v_pk_fma_f32 v[76:77], v[76:77], s[38:39], v[78:79] op_sel_hi:[1,0,1]
	v_pk_fma_f32 v[78:79], v[72:73], s[38:39], v[74:75] op_sel_hi:[1,0,1]
	s_waitcnt vmcnt(3)
	s_waitcnt lgkmcnt(0)
	v_lshlrev_b32_e32 v72, 16, v80
	v_and_b32_e32 v73, 0xffff0000, v80
	v_lshlrev_b32_e32 v74, 16, v81
	v_and_b32_e32 v75, 0xffff0000, v81
	s_waitcnt vmcnt(1)
	s_waitcnt lgkmcnt(0)
; template <int l>
; __device__ __forceinline__ void layer_phases(Frame& F, const XcdBarrier& bar, const int lo, const int hi) {
;     ...
; #pragma unroll
;                 for (int rq = 0; rq < 2; ++rq) { const int rr = 2 * rp + rq, m = m0 + rr, rloc = 4 * F.wave + rr;
;                     f32x4 (&v)[8] = vv[rq]; float s = 0.f;
; #pragma unroll
;                     for (int j = 0; j < 8; ++j) s += (v[j].x + v[j].y) + (v[j].z + v[j].w);
;                     const float mean = wave_sum(s) * (1.f / D); float s2 = 0.f;
; #pragma unroll
;                     for (int j = 0; j < 8; ++j) { v[j] = v[j] - mean; s2 += (v[j].x * v[j].x + v[j].y * v[j].y) + (v[j].z * v[j].z + v[j].w * v[j].w); }
;                     const float rstd = 1.f / sqrtf(wave_sum(s2) * (1.f / D) + LN_EPS);
	v_lshlrev_b32_e32 v80, 16, v86
	v_and_b32_e32 v81, 0xffff0000, v86
	v_lshlrev_b32_e32 v86, 16, v87
	v_and_b32_e32 v87, 0xffff0000, v87
	v_pk_mul_f32 v[80:81], v[24:25], v[80:81]
	v_pk_mul_f32 v[86:87], v[26:27], v[86:87]
	v_and_b32_e32 v91, 0xffff0000, v62
	v_lshlrev_b32_e32 v62, 16, v63
	v_and_b32_e32 v63, 0xffff0000, v63
	v_pk_fma_f32 v[86:87], v[74:75], s[38:39], v[86:87] op_sel_hi:[1,0,1]
	v_pk_fma_f32 v[94:95], v[72:73], s[38:39], v[80:81] op_sel_hi:[1,0,1]
	v_lshlrev_b32_e32 v72, 16, v82
	v_and_b32_e32 v73, 0xffff0000, v82
	v_lshlrev_b32_e32 v74, 16, v83
	v_and_b32_e32 v75, 0xffff0000, v83
	s_waitcnt vmcnt(0)
	s_waitcnt lgkmcnt(0)
	v_lshlrev_b32_e32 v80, 16, v88
	v_and_b32_e32 v81, 0xffff0000, v88
	v_lshlrev_b32_e32 v82, 16, v89
	v_and_b32_e32 v83, 0xffff0000, v89
	v_lshlrev_b32_e32 v84, 16, v50
	v_and_b32_e32 v85, 0xffff0000, v50
	v_lshlrev_b32_e32 v50, 16, v51
	v_and_b32_e32 v51, 0xffff0000, v51
	v_pk_mul_f32 v[62:63], v[10:11], v[62:63]
	v_pk_mul_f32 v[90:91], v[8:9], v[90:91]
	v_pk_mul_f32 v[80:81], v[20:21], v[80:81]
	v_pk_mul_f32 v[82:83], v[22:23], v[82:83]
	v_pk_fma_f32 v[50:51], v[50:51], s[38:39], v[62:63] op_sel_hi:[1,0,1]
	v_pk_fma_f32 v[62:63], v[84:85], s[38:39], v[90:91] op_sel_hi:[1,0,1]
	v_pk_fma_f32 v[90:91], v[74:75], s[38:39], v[82:83] op_sel_hi:[1,0,1]
	v_pk_fma_f32 v[92:93], v[72:73], s[38:39], v[80:81] op_sel_hi:[1,0,1]
	v_mov_b32_e32 v72, v42
	v_mov_b32_e32 v73, v48
	v_mov_b32_e32 v74, v43
	v_mov_b32_e32 v75, v49
	v_pk_add_f32 v[72:73], v[72:73], v[74:75]
	v_mov_b32_e32 v74, v34
	v_mov_b32_e32 v75, v46
	v_mov_b32_e32 v80, v35
	v_mov_b32_e32 v81, v47
	v_pk_add_f32 v[74:75], v[74:75], v[80:81]
	v_mov_b32_e32 v80, v62
	v_pk_add_f32 v[72:73], v[72:73], v[74:75]
	v_pk_mov_b32 v[74:75], v[62:63], v[50:51] op_sel:[1,0]
	v_mov_b32_e32 v81, v51
	v_pk_add_f32 v[74:75], v[74:75], v[80:81]
	v_pk_fma_f32 v[68:69], v[66:67], s[38:39], v[68:69] op_sel_hi:[1,0,1]
	v_add_f32_e32 v60, 0, v72
	v_pk_add_f32 v[74:75], v[74:75], v[74:75] op_sel:[0,1] op_sel_hi:[1,0]
	v_add_f32_e32 v72, v60, v73
	v_add_f32_e32 v80, v64, v65
	v_add_f32_e32 v82, v40, v41
	v_mov_b32_e32 v73, v70
	v_mov_b32_e32 v75, v71
	v_mov_b32_e32 v81, v68
	v_mov_b32_e32 v83, v69
	v_pk_add_f32 v[72:73], v[72:73], v[74:75]
	v_pk_add_f32 v[74:75], v[80:81], v[82:83]
	v_mov_b32_e32 v80, v76
	v_pk_add_f32 v[72:73], v[72:73], v[74:75]
	v_pk_mov_b32 v[74:75], v[76:77], v[78:79] op_sel:[1,0]
	v_mov_b32_e32 v81, v79
	v_pk_add_f32 v[74:75], v[74:75], v[80:81]
	v_pk_add_f32 v[72:73], v[72:73], v[72:73] op_sel:[0,1] op_sel_hi:[1,0]
	v_pk_add_f32 v[74:75], v[74:75], v[74:75] op_sel:[0,1] op_sel_hi:[1,0]
	v_add_f32_e32 v80, v94, v95
	v_add_f32_e32 v82, v86, v87
	v_mov_b32_e32 v73, v92
	v_mov_b32_e32 v75, v93
	v_mov_b32_e32 v81, v90
	v_mov_b32_e32 v83, v91
	v_pk_add_f32 v[72:73], v[72:73], v[74:75]
	v_pk_add_f32 v[74:75], v[80:81], v[82:83]
	v_lshl_add_u64 v[44:45], s[16:17], 0, v[36:37]
	v_pk_add_f32 v[72:73], v[72:73], v[74:75]
	v_lshlrev_b64 v[66:67], 1, v[44:45]
	v_add_f32_e32 v60, v72, v73
	ds_bpermute_b32 v72, v53, v60
	v_lshl_add_u64 v[44:45], s[22:23], 0, v[66:67]
	global_load_dwordx2 v[84:85], v[44:45], off nt
	s_waitcnt lgkmcnt(0)
	v_add_f32_e32 v60, v60, v72
	ds_bpermute_b32 v72, v194, v60
	s_waitcnt lgkmcnt(0)
	v_add_f32_e32 v60, v60, v72
	ds_bpermute_b32 v72, v195, v60
	s_waitcnt lgkmcnt(0)
	v_add_f32_e32 v60, v60, v72
	ds_bpermute_b32 v72, v196, v60
	s_waitcnt lgkmcnt(0)
	v_add_f32_e32 v60, v60, v72
	ds_bpermute_b32 v72, v197, v60
	s_waitcnt lgkmcnt(0)
	v_add_f32_e32 v60, v60, v72
	ds_bpermute_b32 v72, v198, v60
	s_waitcnt lgkmcnt(0)
	v_add_f32_e32 v88, v60, v72
	v_fmamk_f32 v43, v88, 0xba000000, v43
	v_fmamk_f32 v49, v88, 0xba000000, v49
	v_fmamk_f32 v35, v88, 0xba000000, v35
	v_fmac_f32_e32 v42, 0xba000000, v88
	v_fmamk_f32 v47, v88, 0xba000000, v47
	v_fmac_f32_e32 v48, 0xba000000, v88
	v_mov_b32_e32 v74, v43
	v_mov_b32_e32 v75, v49
	v_fmac_f32_e32 v34, 0xba000000, v88
	v_fmac_f32_e32 v46, 0xba000000, v88
	v_mov_b32_e32 v72, v42
	v_mov_b32_e32 v73, v48
	v_pk_mul_f32 v[74:75], v[74:75], v[74:75]
	v_mov_b32_e32 v80, v35
	v_mov_b32_e32 v81, v47
	v_pk_fma_f32 v[72:73], v[72:73], v[72:73], v[74:75]
	v_mov_b32_e32 v74, v34
	v_mov_b32_e32 v75, v46
	v_pk_mul_f32 v[80:81], v[80:81], v[80:81]
	v_fmamk_f32 v63, v88, 0xba000000, v63
	v_pk_fma_f32 v[74:75], v[74:75], v[74:75], v[80:81]
	v_fmac_f32_e32 v62, 0xba000000, v88
	v_fmamk_f32 v51, v88, 0xba000000, v51
	v_fmac_f32_e32 v50, 0xba000000, v88
	v_pk_add_f32 v[72:73], v[72:73], v[74:75]
	v_pk_mul_f32 v[74:75], v[50:51], v[50:51]
	v_pk_mul_f32 v[80:81], v[62:63], v[62:63]
	v_fmac_f32_e32 v64, 0xba000000, v88
	v_pk_mov_b32 v[82:83], v[80:81], v[74:75] op_sel:[1,0]
	v_mov_b32_e32 v81, v75
	v_fmamk_f32 v65, v88, 0xba000000, v65
	v_fmac_f32_e32 v40, 0xba000000, v88
	v_mul_f32_e32 v60, v64, v64
	v_pk_add_f32 v[74:75], v[82:83], v[80:81]
	v_fmamk_f32 v41, v88, 0xba000000, v41
	v_pk_fma_f32 v[80:81], v[64:65], v[64:65], v[60:61] op_sel_hi:[1,1,0]
	v_mul_f32_e32 v60, v40, v40
	v_pk_add_f32 v[72:73], v[72:73], v[72:73] op_sel_hi:[0,1]
	v_pk_add_f32 v[74:75], v[74:75], v[74:75] op_sel_hi:[0,1]
	v_pk_fma_f32 v[82:83], v[40:41], v[40:41], v[60:61] op_sel_hi:[1,1,0]
	v_fmamk_f32 v69, v88, 0xba000000, v69
	v_fmac_f32_e32 v68, 0xba000000, v88
	v_fmamk_f32 v71, v88, 0xba000000, v71
	v_fmac_f32_e32 v70, 0xba000000, v88
	v_mul_f32_e32 v80, v70, v70
	v_mul_f32_e32 v82, v71, v71
	v_mul_f32_e32 v74, v68, v68
	v_mul_f32_e32 v72, v69, v69
	v_pk_add_f32 v[80:81], v[80:81], v[82:83]
	v_pk_add_f32 v[72:73], v[74:75], v[72:73]
	v_fmamk_f32 v77, v88, 0xba000000, v77
	v_fmac_f32_e32 v76, 0xba000000, v88
	v_fmamk_f32 v79, v88, 0xba000000, v79
; #define GAS __attribute__((address_space(1)))
; #define LAS __attribute__((address_space(3)))
; __device__ __forceinline__ unsigned pk2(float lo, float hi) { return f2bf(lo) | (f2bf(hi) << 16); }
; __device__ __forceinline__ unsigned pk4_fp8(float a, float b, float c, float d) { int r = __builtin_amdgcn_cvt_pk_fp8_f32(a, b, 0, false); r = __builtin_amdgcn_cvt_pk_fp8_f32(c, d, r, true); return (unsigned)r; }
; template <int l>
; __device__ __forceinline__ void layer_phases(Frame& F, const XcdBarrier& bar, const int lo, const int hi) {
;     ...
;                     const float rstd = 1.f / sqrtf(wave_sum(s2) * (1.f / D) + LN_EPS);
; #pragma unroll
;                     for (int j = 0; j < 8; ++j) { const int k = 4 * lq + 256 * j;
;                         const f32x4 xv = v[j] * rstd * *(const GAS f32x4*)(g1 + k) + *(const GAS f32x4*)(b1 + k);
;                         { v2u xo; xo.x = pk2(xv.x, xv.y); xo.y = pk2(xv.z, xv.w); *(GAS v2u*)(x1 + (size_t)m * D + k) = xo; }
;                         const f32x4 hv = xv * (*(const GAS f32x4*)(mrow + 8192 + k) + 1.0f) + *(const GAS f32x4*)(mrow + 6144 + k);
;                         v2u o; o.x = pk2(hv.x, hv.y); o.y = pk2(hv.z, hv.w);
;                         *(GAS unsigned*)(h2q + (size_t)m * D + k) = pk4_fp8(hv.x, hv.y, hv.z, hv.w);
;                         const int chunk = (lq >> 1) + 32 * j;
;                         *(LAS v2u*)(h2s + rloc * 4096 + ((chunk ^ (rloc & 15)) << 4) + (lq & 1) * 8) = o; }
	v_fmac_f32_e32 v78, 0xba000000, v88
	v_pk_add_f32 v[72:73], v[80:81], v[72:73]
	v_pk_mul_f32 v[74:75], v[78:79], v[78:79]
	v_pk_mul_f32 v[80:81], v[76:77], v[76:77]
	v_fmac_f32_e32 v94, 0xba000000, v88
	v_pk_mov_b32 v[82:83], v[80:81], v[74:75] op_sel:[1,0]
	v_mov_b32_e32 v81, v75
	v_fmamk_f32 v95, v88, 0xba000000, v95
	v_fmac_f32_e32 v86, 0xba000000, v88
	v_mul_f32_e32 v60, v94, v94
	v_pk_add_f32 v[74:75], v[82:83], v[80:81]
	v_fmamk_f32 v87, v88, 0xba000000, v87
	v_pk_fma_f32 v[80:81], v[94:95], v[94:95], v[60:61] op_sel_hi:[1,1,0]
	v_mul_f32_e32 v60, v86, v86
	v_pk_add_f32 v[72:73], v[72:73], v[72:73] op_sel_hi:[0,1]
	v_pk_add_f32 v[74:75], v[74:75], v[74:75] op_sel_hi:[0,1]
	v_pk_fma_f32 v[82:83], v[86:87], v[86:87], v[60:61] op_sel_hi:[1,1,0]
	v_fmamk_f32 v91, v88, 0xba000000, v91
	v_fmac_f32_e32 v90, 0xba000000, v88
	v_fmamk_f32 v93, v88, 0xba000000, v93
	v_fmac_f32_e32 v92, 0xba000000, v88
	v_mul_f32_e32 v80, v92, v92
	v_mul_f32_e32 v82, v93, v93
	v_mul_f32_e32 v74, v90, v90
	v_mul_f32_e32 v72, v91, v91
	v_pk_add_f32 v[80:81], v[80:81], v[82:83]
	v_pk_add_f32 v[72:73], v[74:75], v[72:73]
	v_lshl_add_u64 v[74:75], s[30:31], 0, v[32:33]
	v_pk_add_f32 v[72:73], v[80:81], v[72:73]
	ds_read_b128 v[96:99], v252 offset:0
	v_add_f32_e32 v60, v72, v73
	v_lshl_add_u64 v[72:73], s[0:1], 0, v[32:33]
	ds_read_b128 v[80:83], v252 offset:8192
	ds_bpermute_b32 v32, v53, v60
	global_load_dwordx2 v[124:125], v[44:45], off offset:512 nt
	global_load_dwordx2 v[118:119], v[44:45], off offset:1024 nt
	global_load_dwordx2 v[112:113], v[44:45], off offset:1536 nt
	global_load_dwordx2 v[104:105], v[44:45], off offset:2048 nt
	s_waitcnt vmcnt(4)
	s_waitcnt lgkmcnt(0)
	v_and_b32_e32 v143, 0xffff0000, v84
	v_lshlrev_b32_e32 v144, 16, v85
	v_and_b32_e32 v145, 0xffff0000, v85
	s_waitcnt lgkmcnt(0)
	v_add_f32_e32 v32, v60, v32
	ds_bpermute_b32 v33, v194, v32
	s_waitcnt lgkmcnt(0)
	v_add_f32_e32 v32, v32, v33
	ds_bpermute_b32 v33, v195, v32
	s_waitcnt lgkmcnt(0)
	v_add_f32_e32 v60, v32, v33
	ds_bpermute_b32 v88, v196, v60
	v_lshl_add_u64 v[32:33], s[20:21], 0, v[66:67]
	global_load_dwordx2 v[130:131], v[32:33], off offset:512 nt
	global_load_dwordx2 v[120:121], v[32:33], off offset:1024 nt
	global_load_dwordx2 v[114:115], v[32:33], off offset:1536 nt
	global_load_dwordx2 v[106:107], v[32:33], off offset:2048 nt
	global_load_dwordx2 v[132:133], v[32:33], off nt
	global_load_dwordx2 v[110:111], v[44:45], off offset:2560 nt
	global_load_dwordx2 v[102:103], v[44:45], off offset:3072 nt
	global_load_dwordx2 v[100:101], v[44:45], off offset:3584 nt
	global_load_dwordx2 v[122:123], v[32:33], off offset:2560 nt
	global_load_dwordx2 v[116:117], v[32:33], off offset:3072 nt
	global_load_dwordx2 v[108:109], v[32:33], off offset:3584 nt
	s_waitcnt lgkmcnt(0)
	v_add_f32_e32 v60, v60, v88
	ds_bpermute_b32 v66, v197, v60
	v_lshlrev_b64 v[88:89], 1, v[36:37]
	s_waitcnt lgkmcnt(0)
	v_add_f32_e32 v60, v60, v66
	ds_bpermute_b32 v66, v198, v60
	s_waitcnt lgkmcnt(0)
	v_add_f32_e32 v60, v60, v66
	v_fmamk_f32 v60, v60, 0x3a000000, v200
	v_mul_f32_e32 v66, 0x4f800000, v60
	v_cmp_gt_f32_e32 vcc, s85, v60
	s_waitcnt vmcnt(14)
	s_waitcnt lgkmcnt(0)
	v_lshlrev_b32_e32 v150, 16, v124
	v_cndmask_b32_e32 v60, v60, v66, vcc
	v_sqrt_f32_e32 v66, v60
	v_and_b32_e32 v151, 0xffff0000, v124
	s_waitcnt vmcnt(11)
	s_waitcnt lgkmcnt(0)
	v_lshlrev_b32_e32 v158, 16, v104
	v_and_b32_e32 v159, 0xffff0000, v104
	v_add_u32_e32 v44, -1, v66
	v_fma_f32 v45, -v44, v66, v60
	v_cmp_ge_f32_e64 s[14:15], 0, v45
	v_add_u32_e32 v45, 1, v66
	v_lshlrev_b32_e32 v104, 16, v105
	v_cndmask_b32_e64 v44, v66, v44, s[14:15]
	v_fma_f32 v66, -v45, v66, v60
	v_cmp_lt_f32_e64 s[14:15], 0, v66
	v_and_b32_e32 v105, 0xffff0000, v105
	v_lshlrev_b32_e32 v124, 16, v125
	v_cndmask_b32_e64 v44, v44, v45, s[14:15]
	v_mul_f32_e32 v45, 0x37800000, v44
	v_cndmask_b32_e32 v44, v44, v45, vcc
	v_cmp_class_f32_e32 vcc, v60, v201
	s_waitcnt vmcnt(6)
	s_waitcnt lgkmcnt(0)
	v_lshlrev_b32_e32 v146, 16, v132
	v_and_b32_e32 v147, 0xffff0000, v132
	v_cndmask_b32_e32 v44, v44, v60, vcc
	v_div_scale_f32 v45, s[0:1], v44, v44, 1.0
	v_rcp_f32_e32 v60, v45
	s_lshl_b64 s[0:1], s[40:41], 12
	s_add_u32 s0, s3, s0
	s_addc_u32 s1, s39, s1
	v_fma_f32 v32, -v45, v60, 1.0
	v_fmac_f32_e32 v60, v32, v60
	v_div_scale_f32 v32, vcc, 1.0, v44, 1.0
	v_mul_f32_e32 v33, v32, v60
	v_fma_f32 v66, -v45, v33, v32
	v_fmac_f32_e32 v33, v66, v60
	v_fma_f32 v32, -v45, v33, v32
	v_div_fmas_f32 v32, v32, v60, v33
	v_div_fixup_f32 v60, v32, v44, 1.0
	v_pk_mul_f32 v[32:33], v[42:43], v[60:61] op_sel_hi:[1,0]
	v_pk_mul_f32 v[34:35], v[34:35], v[60:61] op_sel_hi:[1,0]
	v_pk_fma_f32 v[96:97], v[80:81], v[32:33], v[96:97]
	v_pk_fma_f32 v[66:67], v[82:83], v[34:35], v[98:99]
	v_bfe_u32 v32, v96, 16, 1
	v_add3_u32 v32, v96, v32, s86
	v_bfe_u32 v33, v97, 16, 1
	v_lshrrev_b32_e32 v32, 16, v32
	v_add3_u32 v33, v97, v33, s86
	v_and_or_b32 v32, v33, s82, v32
	v_bfe_u32 v33, v66, 16, 1
	v_add3_u32 v33, v66, v33, s86
	v_bfe_u32 v34, v67, 16, 1
	v_lshrrev_b32_e32 v33, 16, v33
	v_add3_u32 v34, v67, v34, s86
	v_and_or_b32 v33, v34, s82, v33
	v_lshl_add_u64 v[98:99], s[0:1], 0, v[88:89]
	global_store_dwordx2 v[98:99], v[32:33], off
	v_add_co_u32_e32 v32, vcc, s25, v38
	s_add_u32 s0, s48, s18
	s_nop 0
	v_addc_co_u32_e32 v33, vcc, 0, v39, vcc
	v_add_co_u32_e32 v34, vcc, s26, v38
	s_addc_u32 s1, s49, s19
	s_nop 0
	v_addc_co_u32_e32 v35, vcc, 0, v39, vcc
	ds_read_b128 v[42:45], v252 offset:16384
	ds_read_b128 v[80:83], v252 offset:24576
	v_pk_mul_f32 v[46:47], v[46:47], v[60:61] op_sel_hi:[1,0]
	v_pk_mul_f32 v[50:51], v[50:51], v[60:61] op_sel_hi:[1,0]
	v_pk_mul_f32 v[40:41], v[40:41], v[60:61] op_sel_hi:[1,0]
	v_pk_mul_f32 v[70:71], v[70:71], v[60:61] op_sel_hi:[1,0]
	v_pk_mul_f32 v[68:69], v[68:69], v[60:61] op_sel_hi:[1,0]
	v_pk_mul_f32 v[76:77], v[76:77], v[60:61] op_sel_hi:[1,0]
	v_pk_mul_f32 v[78:79], v[78:79], v[60:61] op_sel_hi:[1,0]
	v_pk_mul_f32 v[86:87], v[86:87], v[60:61] op_sel_hi:[1,0]
	v_lshlrev_b32_e32 v148, 16, v133
	v_and_b32_e32 v149, 0xffff0000, v133
	v_lshlrev_b32_e32 v152, 16, v120
	v_and_b32_e32 v153, 0xffff0000, v120
	v_lshlrev_b32_e32 v120, 16, v121
	v_and_b32_e32 v121, 0xffff0000, v121
	s_waitcnt vmcnt(3)
; #define GAS __attribute__((address_space(1)))
; #define LAS __attribute__((address_space(3)))
; __device__ __forceinline__ unsigned pk2(float lo, float hi) { return f2bf(lo) | (f2bf(hi) << 16); }
; __device__ __forceinline__ unsigned pk4_fp8(float a, float b, float c, float d) { int r = __builtin_amdgcn_cvt_pk_fp8_f32(a, b, 0, false); r = __builtin_amdgcn_cvt_pk_fp8_f32(c, d, r, true); return (unsigned)r; }
; template <int l>
; __device__ __forceinline__ void layer_phases(Frame& F, const XcdBarrier& bar, const int lo, const int hi) {
;     ...
;                     for (int j = 0; j < 8; ++j) { const int k = 4 * lq + 256 * j;
;                         const f32x4 xv = v[j] * rstd * *(const GAS f32x4*)(g1 + k) + *(const GAS f32x4*)(b1 + k);
;                         { v2u xo; xo.x = pk2(xv.x, xv.y); xo.y = pk2(xv.z, xv.w); *(GAS v2u*)(x1 + (size_t)m * D + k) = xo; }
;                         const f32x4 hv = xv * (*(const GAS f32x4*)(mrow + 8192 + k) + 1.0f) + *(const GAS f32x4*)(mrow + 6144 + k);
;                         v2u o; o.x = pk2(hv.x, hv.y); o.y = pk2(hv.z, hv.w);
;                         *(GAS unsigned*)(h2q + (size_t)m * D + k) = pk4_fp8(hv.x, hv.y, hv.z, hv.w);
;                         const int chunk = (lq >> 1) + 32 * j;
;                         *(LAS v2u*)(h2s + rloc * 4096 + ((chunk ^ (rloc & 15)) << 4) + (lq & 1) * 8) = o; }
	s_waitcnt lgkmcnt(0)
	v_lshlrev_b32_e32 v164, 16, v122
	v_and_b32_e32 v165, 0xffff0000, v122
	v_lshlrev_b32_e32 v122, 16, v123
	v_and_b32_e32 v123, 0xffff0000, v123
	v_pk_mul_f32 v[0:1], v[0:1], v[146:147]
	v_pk_mul_f32 v[10:11], v[10:11], v[120:121]
	v_pk_mul_f32 v[120:121], v[30:31], v[122:123]
	v_lshlrev_b32_e32 v160, 16, v106
	v_and_b32_e32 v161, 0xffff0000, v106
	v_lshlrev_b32_e32 v106, 16, v107
	v_and_b32_e32 v107, 0xffff0000, v107
	v_lshlrev_b32_e32 v166, 16, v102
	v_and_b32_e32 v167, 0xffff0000, v102
	v_lshlrev_b32_e32 v168, 16, v103
	v_and_b32_e32 v169, 0xffff0000, v103
	s_waitcnt vmcnt(2)
	s_waitcnt lgkmcnt(0)
	v_lshlrev_b32_e32 v102, 16, v116
	v_and_b32_e32 v103, 0xffff0000, v116
	v_lshlrev_b32_e32 v116, 16, v117
	v_and_b32_e32 v117, 0xffff0000, v117
	v_lshlrev_b32_e32 v170, 16, v100
	v_and_b32_e32 v171, 0xffff0000, v100
	v_lshlrev_b32_e32 v172, 16, v101
	v_and_b32_e32 v173, 0xffff0000, v101
	s_waitcnt vmcnt(1)
	s_waitcnt lgkmcnt(0)
	v_lshlrev_b32_e32 v100, 16, v108
	v_and_b32_e32 v101, 0xffff0000, v108
	v_pk_mul_f32 v[106:107], v[18:19], v[106:107]
	v_pk_mul_f32 v[116:117], v[26:27], v[116:117]
	v_and_b32_e32 v125, 0xffff0000, v125
	v_lshlrev_b32_e32 v156, 16, v114
	v_and_b32_e32 v157, 0xffff0000, v114
	v_lshlrev_b32_e32 v114, 16, v115
	v_and_b32_e32 v115, 0xffff0000, v115
	v_lshlrev_b32_e32 v108, 16, v109
	v_and_b32_e32 v109, 0xffff0000, v109
	v_pk_mul_f32 v[2:3], v[2:3], v[148:149]
	v_lshlrev_b32_e32 v154, 16, v112
	v_and_b32_e32 v155, 0xffff0000, v112
	v_lshlrev_b32_e32 v112, 16, v113
	v_and_b32_e32 v113, 0xffff0000, v113
	v_lshlrev_b32_e32 v162, 16, v110
	v_and_b32_e32 v163, 0xffff0000, v110
	v_lshlrev_b32_e32 v110, 16, v111
	v_and_b32_e32 v111, 0xffff0000, v111
	v_pk_mul_f32 v[8:9], v[8:9], v[152:153]
	v_pk_mul_f32 v[6:7], v[6:7], v[114:115]
	v_pk_mul_f32 v[122:123], v[28:29], v[164:165]
	v_pk_mul_f32 v[108:109], v[22:23], v[108:109]
	v_pk_fma_f32 v[28:29], v[144:145], s[38:39], v[2:3] op_sel_hi:[1,0,1]
	v_pk_mul_f32 v[4:5], v[4:5], v[156:157]
	v_pk_mul_f32 v[114:115], v[16:17], v[160:161]
	v_pk_fma_f32 v[16:17], v[112:113], s[38:39], v[6:7] op_sel_hi:[1,0,1]
	v_mov_b32_e32 v112, v29
	v_pk_fma_f32 v[18:19], v[154:155], s[38:39], v[4:5] op_sel_hi:[1,0,1]
	v_pk_fma_f32 v[4:5], v[168:169], s[38:39], v[116:117] op_sel_hi:[1,0,1]
	v_pk_mul_f32 v[92:93], v[92:93], v[60:61] op_sel_hi:[1,0]
	v_pk_mul_f32 v[90:91], v[90:91], v[60:61] op_sel_hi:[1,0]
	s_waitcnt lgkmcnt(0)
	v_pk_add_f32 v[42:43], v[42:43], 1.0 op_sel_hi:[1,0]
	s_waitcnt lgkmcnt(0)
	v_pk_fma_f32 v[42:43], v[42:43], v[96:97], v[80:81]
	v_mov_b32_e32 v80, 0
	v_cvt_pk_fp8_f32 v80, v42, v43
	v_pk_add_f32 v[44:45], v[44:45], 1.0 op_sel_hi:[1,0]
	v_lshl_add_u64 v[96:97], s[0:1], 0, v[36:37]
	v_pk_fma_f32 v[44:45], v[44:45], v[66:67], v[82:83]
	s_mov_b64 s[0:1], 0x8000
	v_cvt_pk_fp8_f32 v80, v44, v45 op_sel:[0,0,1]
	v_lshl_add_u64 v[82:83], v[38:39], 0, s[0:1]
	s_mov_b64 s[0:1], 0x6000
	global_store_dword v[96:97], v80, off
	ds_read_b128 v[134:137], v252 offset:9216
	ds_read_b128 v[138:141], v252 offset:1024
	v_lshl_add_u64 v[80:81], v[38:39], 0, s[0:1]
	v_pk_mul_f32 v[38:39], v[48:49], v[60:61] op_sel_hi:[1,0]
	s_lshl_b64 s[0:1], s[42:43], 12
	s_add_u32 s0, s3, s0
	s_addc_u32 s1, s39, s1
	s_waitcnt lgkmcnt(0)
	v_pk_fma_f32 v[38:39], v[134:135], v[38:39], v[138:139]
	v_pk_fma_f32 v[66:67], v[136:137], v[46:47], v[140:141]
	v_bfe_u32 v46, v38, 16, 1
	v_add3_u32 v46, v38, v46, s86
	v_bfe_u32 v47, v39, 16, 1
	v_lshrrev_b32_e32 v46, 16, v46
	v_add3_u32 v47, v39, v47, s86
	v_and_or_b32 v46, v47, s82, v46
	v_bfe_u32 v47, v66, 16, 1
	v_add3_u32 v47, v66, v47, s86
	v_bfe_u32 v48, v67, 16, 1
	v_lshrrev_b32_e32 v47, 16, v47
	v_add3_u32 v48, v67, v48, s86
	v_and_or_b32 v47, v48, s82, v47
	global_store_dwordx2 v[98:99], v[46:47], off offset:512
	ds_read_b128 v[46:49], v252 offset:17408
	s_nop 0
	ds_read_b128 v[134:137], v252 offset:25600
	v_mov_b32_e32 v138, 0
	s_waitcnt lgkmcnt(0)
	v_pk_add_f32 v[46:47], v[46:47], 1.0 op_sel_hi:[1,0]
	s_waitcnt lgkmcnt(0)
	v_pk_fma_f32 v[46:47], v[46:47], v[38:39], v[134:135]
	v_pk_add_f32 v[38:39], v[48:49], 1.0 op_sel_hi:[1,0]
	v_cvt_pk_fp8_f32 v138, v46, v47
	v_pk_fma_f32 v[48:49], v[38:39], v[66:67], v[136:137]
	v_pk_mul_f32 v[38:39], v[62:63], v[60:61] op_sel_hi:[1,0]
	v_cvt_pk_fp8_f32 v138, v48, v49 op_sel:[0,0,1]
	global_store_dword v[96:97], v138, off offset:256
	ds_read_b128 v[134:137], v252 offset:10240
	s_nop 0
	ds_read_b128 v[138:141], v252 offset:2048
	s_waitcnt lgkmcnt(0)
	v_pk_fma_f32 v[62:63], v[136:137], v[50:51], v[140:141]
	v_pk_fma_f32 v[38:39], v[134:135], v[38:39], v[138:139]
	v_bfe_u32 v66, v62, 16, 1
	v_bfe_u32 v50, v38, 16, 1
	v_bfe_u32 v51, v39, 16, 1
	v_bfe_u32 v67, v63, 16, 1
	v_add3_u32 v50, v38, v50, s86
	v_add3_u32 v66, v62, v66, s86
	v_add3_u32 v51, v39, v51, s86
	v_add3_u32 v67, v63, v67, s86
	v_lshrrev_b32_e32 v50, 16, v50
	v_lshrrev_b32_e32 v66, 16, v66
	v_and_or_b32 v50, v51, s82, v50
	v_and_or_b32 v51, v67, s82, v66
	global_store_dwordx2 v[98:99], v[50:51], off offset:1024
	ds_read_b128 v[134:137], v252 offset:18432
	ds_read_b128 v[138:141], v252 offset:26624
	v_mov_b32_e32 v66, 0
	s_waitcnt lgkmcnt(0)
	v_pk_add_f32 v[50:51], v[134:135], 1.0 op_sel_hi:[1,0]
	s_waitcnt lgkmcnt(0)
	v_pk_fma_f32 v[50:51], v[50:51], v[38:39], v[138:139]
	v_pk_add_f32 v[38:39], v[136:137], 1.0 op_sel_hi:[1,0]
	v_cvt_pk_fp8_f32 v66, v50, v51
	v_pk_fma_f32 v[62:63], v[38:39], v[62:63], v[140:141]
	v_pk_mul_f32 v[38:39], v[64:65], v[60:61] op_sel_hi:[1,0]
	v_cvt_pk_fp8_f32 v66, v62, v63 op_sel:[0,0,1]
	global_store_dword v[96:97], v66, off offset:512
	ds_read_b128 v[134:137], v252 offset:11264
	ds_read_b128 v[138:141], v252 offset:3072
	s_waitcnt lgkmcnt(0)
; #define GAS __attribute__((address_space(1)))
; #define LAS __attribute__((address_space(3)))
; __device__ __forceinline__ unsigned pk2(float lo, float hi) { return f2bf(lo) | (f2bf(hi) << 16); }
; __device__ __forceinline__ unsigned pk4_fp8(float a, float b, float c, float d) { int r = __builtin_amdgcn_cvt_pk_fp8_f32(a, b, 0, false); r = __builtin_amdgcn_cvt_pk_fp8_f32(c, d, r, true); return (unsigned)r; }
; template <int l>
; __device__ __forceinline__ void layer_phases(Frame& F, const XcdBarrier& bar, const int lo, const int hi) {
;     ...
;                     for (int j = 0; j < 8; ++j) { const int k = 4 * lq + 256 * j;
;                         const f32x4 xv = v[j] * rstd * *(const GAS f32x4*)(g1 + k) + *(const GAS f32x4*)(b1 + k);
;                         { v2u xo; xo.x = pk2(xv.x, xv.y); xo.y = pk2(xv.z, xv.w); *(GAS v2u*)(x1 + (size_t)m * D + k) = xo; }
;                         const f32x4 hv = xv * (*(const GAS f32x4*)(mrow + 8192 + k) + 1.0f) + *(const GAS f32x4*)(mrow + 6144 + k);
;                         v2u o; o.x = pk2(hv.x, hv.y); o.y = pk2(hv.z, hv.w);
;                         *(GAS unsigned*)(h2q + (size_t)m * D + k) = pk4_fp8(hv.x, hv.y, hv.z, hv.w);
;                         const int chunk = (lq >> 1) + 32 * j;
;                         *(LAS v2u*)(h2s + rloc * 4096 + ((chunk ^ (rloc & 15)) << 4) + (lq & 1) * 8) = o; }
	v_pk_fma_f32 v[136:137], v[40:41], v[136:137], v[140:141]
	v_pk_fma_f32 v[134:135], v[38:39], v[134:135], v[138:139]
	v_bfe_u32 v40, v136, 16, 1
	v_bfe_u32 v38, v134, 16, 1
	v_bfe_u32 v39, v135, 16, 1
	v_bfe_u32 v41, v137, 16, 1
	v_add3_u32 v38, v134, v38, s86
	v_add3_u32 v40, v136, v40, s86
	v_add3_u32 v39, v135, v39, s86
	v_add3_u32 v41, v137, v41, s86
	v_lshrrev_b32_e32 v38, 16, v38
	v_lshrrev_b32_e32 v40, 16, v40
	v_and_or_b32 v38, v39, s82, v38
	v_and_or_b32 v39, v41, s82, v40
	global_store_dwordx2 v[98:99], v[38:39], off offset:1536
	ds_read_b128 v[38:41], v252 offset:19456
	s_nop 0
	ds_read_b128 v[64:67], v252 offset:27648
	v_mov_b32_e32 v138, 0
	s_waitcnt lgkmcnt(0)
	v_pk_add_f32 v[38:39], v[38:39], 1.0 op_sel_hi:[1,0]
	s_waitcnt lgkmcnt(0)
	v_pk_fma_f32 v[64:65], v[134:135], v[38:39], v[64:65]
	v_pk_add_f32 v[40:41], v[40:41], 1.0 op_sel_hi:[1,0]
	v_cvt_pk_fp8_f32 v138, v64, v65
	v_pk_fma_f32 v[66:67], v[136:137], v[40:41], v[66:67]
	v_add_co_u32_e32 v38, vcc, s87, v72
	v_cvt_pk_fp8_f32 v138, v66, v67 op_sel:[0,0,1]
	s_nop 0
	v_addc_co_u32_e32 v39, vcc, 0, v73, vcc
	v_add_co_u32_e32 v40, vcc, s87, v74
	global_store_dword v[96:97], v138, off offset:768
	s_nop 0
	v_addc_co_u32_e32 v41, vcc, 0, v75, vcc
	ds_read_b128 v[134:137], v252 offset:12288
	ds_read_b128 v[138:141], v252 offset:4096
	s_waitcnt lgkmcnt(0)
	v_pk_fma_f32 v[140:141], v[68:69], v[136:137], v[140:141]
	v_pk_fma_f32 v[138:139], v[70:71], v[134:135], v[138:139]
	v_bfe_u32 v70, v140, 16, 1
	v_bfe_u32 v68, v138, 16, 1
	v_bfe_u32 v69, v139, 16, 1
	v_bfe_u32 v71, v141, 16, 1
	v_add3_u32 v68, v138, v68, s86
	v_add3_u32 v70, v140, v70, s86
	v_add3_u32 v69, v139, v69, s86
	v_add3_u32 v71, v141, v71, s86
	v_lshrrev_b32_e32 v68, 16, v68
	v_lshrrev_b32_e32 v70, 16, v70
	v_and_or_b32 v68, v69, s82, v68
	v_and_or_b32 v69, v71, s82, v70
	global_store_dwordx2 v[98:99], v[68:69], off offset:2048
	ds_read_b128 v[68:71], v252 offset:20480
	s_nop 0
	ds_read_b128 v[134:137], v252 offset:28672
	s_waitcnt lgkmcnt(0)
	v_pk_add_f32 v[68:69], v[68:69], 1.0 op_sel_hi:[1,0]
	s_waitcnt lgkmcnt(0)
	v_pk_fma_f32 v[68:69], v[138:139], v[68:69], v[134:135]
	v_pk_add_f32 v[70:71], v[70:71], 1.0 op_sel_hi:[1,0]
	v_cvt_pk_fp8_f32 v142, v68, v69
	v_pk_fma_f32 v[70:71], v[140:141], v[70:71], v[136:137]
	s_nop 0
	v_cvt_pk_fp8_f32 v142, v70, v71 op_sel:[0,0,1]
	global_store_dword v[96:97], v142, off offset:1024
	ds_read_b128 v[134:137], v252 offset:13312
	ds_read_b128 v[138:141], v252 offset:5120
	v_mov_b32_e32 v142, 0
	s_waitcnt lgkmcnt(0)
	v_pk_fma_f32 v[140:141], v[78:79], v[136:137], v[140:141]
	v_pk_fma_f32 v[138:139], v[76:77], v[134:135], v[138:139]
	v_bfe_u32 v78, v140, 16, 1
	v_bfe_u32 v76, v138, 16, 1
	v_bfe_u32 v77, v139, 16, 1
	v_bfe_u32 v79, v141, 16, 1
	v_add3_u32 v76, v138, v76, s86
	v_add3_u32 v78, v140, v78, s86
	v_add3_u32 v77, v139, v77, s86
	v_add3_u32 v79, v141, v79, s86
	v_lshrrev_b32_e32 v76, 16, v76
	v_lshrrev_b32_e32 v78, 16, v78
	v_and_or_b32 v76, v77, s82, v76
	v_and_or_b32 v77, v79, s82, v78
	global_store_dwordx2 v[98:99], v[76:77], off offset:2560
	ds_read_b128 v[76:79], v252 offset:21504
	s_nop 0
	ds_read_b128 v[134:137], v252 offset:29696
	s_waitcnt lgkmcnt(0)
	v_pk_add_f32 v[76:77], v[76:77], 1.0 op_sel_hi:[1,0]
	s_waitcnt lgkmcnt(0)
	v_pk_fma_f32 v[76:77], v[138:139], v[76:77], v[134:135]
	v_pk_add_f32 v[78:79], v[78:79], 1.0 op_sel_hi:[1,0]
	v_cvt_pk_fp8_f32 v142, v76, v77
	v_pk_fma_f32 v[78:79], v[140:141], v[78:79], v[136:137]
	s_nop 0
	v_cvt_pk_fp8_f32 v142, v78, v79 op_sel:[0,0,1]
	global_store_dword v[96:97], v142, off offset:1280
	ds_read_b128 v[134:137], v252 offset:14336
	ds_read_b128 v[138:141], v252 offset:6144
	v_lshlrev_b32_e32 v142, 16, v84
	v_pk_mul_f32 v[84:85], v[94:95], v[60:61] op_sel_hi:[1,0]
	v_pk_fma_f32 v[30:31], v[142:143], s[38:39], v[0:1] op_sel_hi:[1,0,1]
	s_waitcnt lgkmcnt(0)
	v_pk_fma_f32 v[94:95], v[86:87], v[136:137], v[140:141]
	v_pk_fma_f32 v[136:137], v[84:85], v[134:135], v[138:139]
	v_bfe_u32 v86, v94, 16, 1
	v_bfe_u32 v84, v136, 16, 1
	v_bfe_u32 v85, v137, 16, 1
	v_bfe_u32 v87, v95, 16, 1
	v_add3_u32 v84, v136, v84, s86
	v_add3_u32 v86, v94, v86, s86
	v_add3_u32 v85, v137, v85, s86
	v_add3_u32 v87, v95, v87, s86
	v_lshrrev_b32_e32 v84, 16, v84
	v_lshrrev_b32_e32 v86, 16, v86
	v_and_or_b32 v84, v85, s82, v84
	v_and_or_b32 v85, v87, s82, v86
	global_store_dwordx2 v[98:99], v[84:85], off offset:3072
	ds_read_b128 v[84:87], v252 offset:22528
	s_nop 0
	ds_read_b128 v[132:135], v252 offset:30720
	v_lshlrev_b32_e32 v138, 16, v130
	v_and_b32_e32 v139, 0xffff0000, v130
	v_lshlrev_b32_e32 v130, 16, v131
	v_and_b32_e32 v131, 0xffff0000, v131
	v_pk_mul_f32 v[12:13], v[12:13], v[138:139]
	v_pk_mul_f32 v[14:15], v[14:15], v[130:131]
	v_pk_mul_f32 v[130:131], v[24:25], v[102:103]
	v_pk_mul_f32 v[138:139], v[20:21], v[100:101]
	v_pk_fma_f32 v[26:27], v[150:151], s[38:39], v[12:13] op_sel_hi:[1,0,1]
	v_pk_fma_f32 v[12:13], v[104:105], s[38:39], v[106:107] op_sel_hi:[1,0,1]
	v_lshlrev_b32_e32 v140, 16, v118
	v_and_b32_e32 v141, 0xffff0000, v118
	v_lshlrev_b32_e32 v118, 16, v119
	v_and_b32_e32 v119, 0xffff0000, v119
	v_pk_fma_f32 v[24:25], v[124:125], s[38:39], v[14:15] op_sel_hi:[1,0,1]
	v_pk_fma_f32 v[20:21], v[118:119], s[38:39], v[10:11] op_sel_hi:[1,0,1]
	v_pk_fma_f32 v[22:23], v[140:141], s[38:39], v[8:9] op_sel_hi:[1,0,1]
	v_pk_fma_f32 v[10:11], v[110:111], s[38:39], v[120:121] op_sel_hi:[1,0,1]
	v_mov_b32_e32 v110, v28
	v_mov_b32_e32 v111, v24
	v_mov_b32_e32 v113, v25
	v_pk_fma_f32 v[14:15], v[158:159], s[38:39], v[114:115] op_sel_hi:[1,0,1]
	v_pk_mov_b32 v[114:115], v[22:23], v[20:21] op_sel:[1,0]
	v_mov_b32_e32 v116, v22
	v_mov_b32_e32 v117, v21
	v_pk_fma_f32 v[8:9], v[162:163], s[38:39], v[122:123] op_sel_hi:[1,0,1]
	v_add_f32_e32 v118, v18, v19
	v_add_f32_e32 v120, v16, v17
	v_mov_b32_e32 v123, v14
	v_mov_b32_e32 v119, v12
	v_mov_b32_e32 v121, v13
	v_pk_fma_f32 v[6:7], v[166:167], s[38:39], v[130:131] op_sel_hi:[1,0,1]
	v_pk_mov_b32 v[124:125], v[8:9], v[10:11] op_sel:[1,0]
	v_mov_b32_e32 v130, v8
	v_mov_b32_e32 v131, v11
	v_pk_fma_f32 v[2:3], v[170:171], s[38:39], v[138:139] op_sel_hi:[1,0,1]
	s_waitcnt lgkmcnt(0)
; #define GAS __attribute__((address_space(1)))
; #define LAS __attribute__((address_space(3)))
; __device__ __forceinline__ unsigned pk2(float lo, float hi) { return f2bf(lo) | (f2bf(hi) << 16); }
; __device__ __forceinline__ unsigned pk4_fp8(float a, float b, float c, float d) { int r = __builtin_amdgcn_cvt_pk_fp8_f32(a, b, 0, false); r = __builtin_amdgcn_cvt_pk_fp8_f32(c, d, r, true); return (unsigned)r; }
; template <int l>
; __device__ __forceinline__ void layer_phases(Frame& F, const XcdBarrier& bar, const int lo, const int hi) {
;     ...
;                 for (int rq = 0; rq < 2; ++rq) { const int rr = 2 * rp + rq, m = m0 + rr, rloc = 4 * F.wave + rr;
;                     f32x4 (&v)[8] = vv[rq]; float s = 0.f;
; #pragma unroll
;                     for (int j = 0; j < 8; ++j) s += (v[j].x + v[j].y) + (v[j].z + v[j].w);
;                     const float mean = wave_sum(s) * (1.f / D); float s2 = 0.f;
; #pragma unroll
;                     for (int j = 0; j < 8; ++j) { v[j] = v[j] - mean; s2 += (v[j].x * v[j].x + v[j].y * v[j].y) + (v[j].z * v[j].z + v[j].w * v[j].w); }
;                     const float rstd = 1.f / sqrtf(wave_sum(s2) * (1.f / D) + LN_EPS);
;     ...
;                     for (int j = 0; j < 8; ++j) { const int k = 4 * lq + 256 * j;
;                         const f32x4 xv = v[j] * rstd * *(const GAS f32x4*)(g1 + k) + *(const GAS f32x4*)(b1 + k);
;                         { v2u xo; xo.x = pk2(xv.x, xv.y); xo.y = pk2(xv.z, xv.w); *(GAS v2u*)(x1 + (size_t)m * D + k) = xo; }
;                         const f32x4 hv = xv * (*(const GAS f32x4*)(mrow + 8192 + k) + 1.0f) + *(const GAS f32x4*)(mrow + 6144 + k);
;                         v2u o; o.x = pk2(hv.x, hv.y); o.y = pk2(hv.z, hv.w);
;                         *(GAS unsigned*)(h2q + (size_t)m * D + k) = pk4_fp8(hv.x, hv.y, hv.z, hv.w);
;                         const int chunk = (lq >> 1) + 32 * j;
;                         *(LAS v2u*)(h2s + rloc * 4096 + ((chunk ^ (rloc & 15)) << 4) + (lq & 1) * 8) = o; }
	v_pk_add_f32 v[0:1], v[84:85], 1.0 op_sel_hi:[1,0]
	s_waitcnt lgkmcnt(0)
	v_pk_fma_f32 v[84:85], v[136:137], v[0:1], v[132:133]
	v_pk_add_f32 v[0:1], v[86:87], 1.0 op_sel_hi:[1,0]
	v_cvt_pk_fp8_f32 v174, v84, v85
	v_pk_fma_f32 v[86:87], v[94:95], v[0:1], v[134:135]
	v_pk_fma_f32 v[0:1], v[172:173], s[38:39], v[108:109] op_sel_hi:[1,0,1]
	v_mov_b32_e32 v94, v30
	v_cvt_pk_fp8_f32 v174, v86, v87 op_sel:[0,0,1]
	v_mov_b32_e32 v95, v26
	v_mov_b32_e32 v108, v31
	v_mov_b32_e32 v109, v27
	global_store_dword v[96:97], v174, off offset:1536
	ds_read_b128 v[100:103], v252 offset:15360
	ds_read_b128 v[104:107], v252 offset:7168
	v_pk_add_f32 v[94:95], v[94:95], v[108:109]
	v_pk_add_f32 v[108:109], v[110:111], v[112:113]
	v_pk_add_f32 v[110:111], v[114:115], v[116:117]
	v_pk_add_f32 v[94:95], v[94:95], v[108:109]
	v_pk_add_f32 v[108:109], v[110:111], v[110:111] op_sel:[0,1] op_sel_hi:[1,0]
	v_add_f32_e32 v94, 0, v94
	v_mov_b32_e32 v109, v15
	v_add_f32_e32 v122, v94, v95
	v_pk_add_f32 v[112:113], v[118:119], v[120:121]
	v_pk_add_f32 v[94:95], v[122:123], v[108:109]
	v_pk_add_f32 v[114:115], v[124:125], v[130:131]
	v_pk_add_f32 v[94:95], v[94:95], v[112:113]
	v_pk_add_f32 v[110:111], v[114:115], v[114:115] op_sel:[0,1] op_sel_hi:[1,0]
	v_pk_add_f32 v[94:95], v[94:95], v[94:95] op_sel:[0,1] op_sel_hi:[1,0]
	v_add_f32_e32 v132, v6, v7
	v_add_f32_e32 v134, v4, v5
	v_mov_b32_e32 v133, v0
	v_mov_b32_e32 v135, v1
	v_mov_b32_e32 v111, v3
	v_mov_b32_e32 v95, v2
	v_pk_add_f32 v[116:117], v[132:133], v[134:135]
	v_pk_add_f32 v[94:95], v[94:95], v[110:111]
	v_mov_b32_e32 v125, 0
	v_pk_add_f32 v[94:95], v[94:95], v[116:117]
	s_nop 0
	v_add_f32_e32 v94, v94, v95
	ds_bpermute_b32 v95, v53, v94
	s_waitcnt lgkmcnt(0)
	v_add_f32_e32 v94, v94, v95
	ds_bpermute_b32 v95, v194, v94
	s_waitcnt lgkmcnt(0)
	v_add_f32_e32 v94, v94, v95
	ds_bpermute_b32 v95, v195, v94
	s_waitcnt lgkmcnt(0)
	v_add_f32_e32 v94, v94, v95
	ds_bpermute_b32 v95, v196, v94
	s_waitcnt lgkmcnt(0)
	v_add_f32_e32 v94, v94, v95
	ds_bpermute_b32 v95, v197, v94
	s_waitcnt lgkmcnt(0)
	v_add_f32_e32 v108, v94, v95
	s_waitcnt lgkmcnt(0)
	v_pk_fma_f32 v[94:95], v[90:91], v[102:103], v[106:107]
	v_pk_fma_f32 v[102:103], v[92:93], v[100:101], v[104:105]
	v_bfe_u32 v91, v94, 16, 1
	v_bfe_u32 v60, v102, 16, 1
	v_bfe_u32 v90, v103, 16, 1
	v_bfe_u32 v92, v95, 16, 1
	v_add3_u32 v60, v102, v60, s86
	v_add3_u32 v91, v94, v91, s86
	v_add3_u32 v90, v103, v90, s86
	v_add3_u32 v92, v95, v92, s86
	v_lshrrev_b32_e32 v60, 16, v60
	v_lshrrev_b32_e32 v91, 16, v91
	v_and_or_b32 v90, v90, s82, v60
	v_and_or_b32 v91, v92, s82, v91
	global_store_dwordx2 v[98:99], v[90:91], off offset:3584
	ds_read_b128 v[90:93], v252 offset:23552
	s_nop 0
	ds_read_b128 v[98:101], v252 offset:31744
	ds_bpermute_b32 v60, v198, v108
	s_waitcnt lgkmcnt(0)
	v_add_f32_e32 v60, v108, v60
	v_fmamk_f32 v9, v60, 0xba000000, v9
	v_fmac_f32_e32 v8, 0xba000000, v60
	v_fmamk_f32 v11, v60, 0xba000000, v11
	v_fmac_f32_e32 v10, 0xba000000, v60
	v_fmac_f32_e32 v6, 0xba000000, v60
	v_fmac_f32_e32 v4, 0xba000000, v60
	v_fmamk_f32 v7, v60, 0xba000000, v7
	v_fmamk_f32 v5, v60, 0xba000000, v5
	v_pk_mul_f32 v[118:119], v[10:11], v[10:11]
	v_pk_mul_f32 v[120:121], v[8:9], v[8:9]
	v_mul_f32_e32 v122, v6, v6
	v_mul_f32_e32 v124, v4, v4
	v_pk_mov_b32 v[132:133], v[120:121], v[118:119] op_sel:[1,0]
	v_mov_b32_e32 v121, v119
	v_pk_fma_f32 v[118:119], v[6:7], v[6:7], v[122:123] op_sel_hi:[1,1,0]
	v_pk_fma_f32 v[122:123], v[4:5], v[4:5], v[124:125] op_sel_hi:[1,1,0]
	v_fmamk_f32 v29, v60, 0xba000000, v29
	v_fmamk_f32 v31, v60, 0xba000000, v31
	v_fmamk_f32 v25, v60, 0xba000000, v25
	v_fmamk_f32 v27, v60, 0xba000000, v27
	v_fmac_f32_e32 v28, 0xba000000, v60
	v_fmac_f32_e32 v30, 0xba000000, v60
	v_fmac_f32_e32 v24, 0xba000000, v60
	v_fmac_f32_e32 v26, 0xba000000, v60
	v_fmamk_f32 v23, v60, 0xba000000, v23
	v_fmac_f32_e32 v22, 0xba000000, v60
	v_fmamk_f32 v21, v60, 0xba000000, v21
	v_fmac_f32_e32 v20, 0xba000000, v60
	v_mov_b32_e32 v106, v31
	v_mov_b32_e32 v107, v27
	v_mov_b32_e32 v110, v29
	v_mov_b32_e32 v111, v25
	v_mov_b32_e32 v104, v30
	v_mov_b32_e32 v105, v26
	v_mov_b32_e32 v108, v28
	v_mov_b32_e32 v109, v24
	v_pk_mul_f32 v[112:113], v[20:21], v[20:21]
	v_pk_mul_f32 v[114:115], v[22:23], v[22:23]
	v_pk_mul_f32 v[106:107], v[106:107], v[106:107]
	v_pk_mul_f32 v[110:111], v[110:111], v[110:111]
	v_fmac_f32_e32 v18, 0xba000000, v60
	v_fmac_f32_e32 v16, 0xba000000, v60
	v_pk_mov_b32 v[130:131], v[114:115], v[112:113] op_sel:[1,0]
	v_mov_b32_e32 v115, v113
	v_pk_fma_f32 v[104:105], v[104:105], v[104:105], v[106:107]
	v_pk_fma_f32 v[106:107], v[108:109], v[108:109], v[110:111]
	v_fmamk_f32 v19, v60, 0xba000000, v19
	v_fmamk_f32 v17, v60, 0xba000000, v17
	v_fmamk_f32 v13, v60, 0xba000000, v13
	v_fmac_f32_e32 v12, 0xba000000, v60
	v_fmamk_f32 v15, v60, 0xba000000, v15
	v_fmac_f32_e32 v14, 0xba000000, v60
	v_fmamk_f32 v1, v60, 0xba000000, v1
	v_fmac_f32_e32 v0, 0xba000000, v60
	v_fmamk_f32 v3, v60, 0xba000000, v3
	v_fmac_f32_e32 v2, 0xba000000, v60
	v_mul_f32_e32 v60, v18, v18
	v_mul_f32_e32 v116, v16, v16
	v_pk_add_f32 v[108:109], v[130:131], v[114:115]
	v_pk_add_f32 v[104:105], v[104:105], v[106:107]
	v_pk_fma_f32 v[112:113], v[18:19], v[18:19], v[60:61] op_sel_hi:[1,1,0]
	v_pk_fma_f32 v[116:117], v[16:17], v[16:17], v[116:117] op_sel_hi:[1,1,0]
	v_pk_add_f32 v[106:107], v[108:109], v[108:109] op_sel_hi:[0,1]
	v_pk_add_f32 v[104:105], v[104:105], v[104:105] op_sel_hi:[0,1]
	v_mul_f32_e32 v112, v14, v14
	v_mul_f32_e32 v116, v15, v15
	v_mul_f32_e32 v106, v12, v12
	v_mul_f32_e32 v104, v13, v13
	v_pk_add_f32 v[108:109], v[112:113], v[116:117]
	v_pk_add_f32 v[110:111], v[132:133], v[120:121]
	v_mul_f32_e32 v118, v2, v2
	v_pk_add_f32 v[110:111], v[110:111], v[110:111] op_sel_hi:[0,1]
	s_waitcnt lgkmcnt(0)
; #define GAS __attribute__((address_space(1)))
; #define LAS __attribute__((address_space(3)))
; __device__ __forceinline__ unsigned pk2(float lo, float hi) { return f2bf(lo) | (f2bf(hi) << 16); }
; __device__ __forceinline__ unsigned pk4_fp8(float a, float b, float c, float d) { int r = __builtin_amdgcn_cvt_pk_fp8_f32(a, b, 0, false); r = __builtin_amdgcn_cvt_pk_fp8_f32(c, d, r, true); return (unsigned)r; }
; template <int l>
; __device__ __forceinline__ void layer_phases(Frame& F, const XcdBarrier& bar, const int lo, const int hi) {
;     ...
;                     const float rstd = 1.f / sqrtf(wave_sum(s2) * (1.f / D) + LN_EPS);
; #pragma unroll
;                     for (int j = 0; j < 8; ++j) { const int k = 4 * lq + 256 * j;
;                         const f32x4 xv = v[j] * rstd * *(const GAS f32x4*)(g1 + k) + *(const GAS f32x4*)(b1 + k);
;                         { v2u xo; xo.x = pk2(xv.x, xv.y); xo.y = pk2(xv.z, xv.w); *(GAS v2u*)(x1 + (size_t)m * D + k) = xo; }
;                         const f32x4 hv = xv * (*(const GAS f32x4*)(mrow + 8192 + k) + 1.0f) + *(const GAS f32x4*)(mrow + 6144 + k);
;                         v2u o; o.x = pk2(hv.x, hv.y); o.y = pk2(hv.z, hv.w);
;                         *(GAS unsigned*)(h2q + (size_t)m * D + k) = pk4_fp8(hv.x, hv.y, hv.z, hv.w);
;                         const int chunk = (lq >> 1) + 32 * j;
;                         *(LAS v2u*)(h2s + rloc * 4096 + ((chunk ^ (rloc & 15)) << 4) + (lq & 1) * 8) = o; }
	v_pk_add_f32 v[90:91], v[90:91], 1.0 op_sel_hi:[1,0]
	v_pk_add_f32 v[92:93], v[92:93], 1.0 op_sel_hi:[1,0]
	s_waitcnt lgkmcnt(0)
	v_pk_fma_f32 v[90:91], v[102:103], v[90:91], v[98:99]
	v_pk_fma_f32 v[92:93], v[94:95], v[92:93], v[100:101]
	v_cvt_pk_fp8_f32 v125, v90, v91
	v_pk_add_f32 v[102:103], v[106:107], v[104:105]
	v_mul_f32_e32 v122, v3, v3
	v_pk_add_f32 v[102:103], v[108:109], v[102:103]
	v_cvt_pk_fp8_f32 v125, v92, v93 op_sel:[0,0,1]
	v_pk_add_f32 v[102:103], v[102:103], v[102:103] op_sel_hi:[0,1]
	v_mul_f32_e32 v110, v0, v0
	v_mul_f32_e32 v102, v1, v1
	global_store_dword v[96:97], v125, off offset:1792
	ds_read_b128 v[94:97], v252 offset:8192
	s_nop 0
	ds_read_b128 v[98:101], v252 offset:0
	v_pk_add_f32 v[112:113], v[118:119], v[122:123]
	v_pk_add_f32 v[102:103], v[110:111], v[102:103]
	v_lshl_add_u64 v[122:123], s[0:1], 0, v[88:89]
	v_pk_add_f32 v[102:103], v[112:113], v[102:103]
	s_add_u32 s0, s48, s16
	v_add_f32_e32 v60, v102, v103
	ds_bpermute_b32 v102, v53, v60
	s_addc_u32 s1, s49, s17
	s_or_b32 s44, s40, 2
	s_ashr_i32 s45, s44, 31
	s_lshl_b64 s[18:19], s[44:45], 11
	s_waitcnt lgkmcnt(0)
	v_add_f32_e32 v60, v60, v102
	ds_bpermute_b32 v102, v194, v60
	s_or_b32 s46, s40, 3
	s_ashr_i32 s47, s46, 31
	s_lshl_b64 s[16:17], s[46:47], 11
	s_waitcnt lgkmcnt(0)
	v_add_f32_e32 v60, v60, v102
	ds_bpermute_b32 v102, v195, v60
	s_waitcnt lgkmcnt(0)
	v_add_f32_e32 v60, v60, v102
	ds_bpermute_b32 v102, v196, v60
	s_waitcnt lgkmcnt(0)
	v_add_f32_e32 v60, v60, v102
	ds_bpermute_b32 v102, v197, v60
	s_waitcnt lgkmcnt(0)
	v_add_f32_e32 v60, v60, v102
	ds_bpermute_b32 v102, v198, v60
	s_waitcnt lgkmcnt(0)
	v_add_f32_e32 v60, v60, v102
	v_fmamk_f32 v60, v60, 0x3a000000, v200
	v_mul_f32_e32 v102, 0x4f800000, v60
	v_cmp_gt_f32_e32 vcc, s85, v60
	s_nop 1
	v_cndmask_b32_e32 v60, v60, v102, vcc
	v_sqrt_f32_e32 v102, v60
	s_nop 0
	v_add_u32_e32 v103, -1, v102
	v_add_u32_e32 v104, 1, v102
	v_fma_f32 v105, -v103, v102, v60
	v_fma_f32 v106, -v104, v102, v60
	v_cmp_ge_f32_e64 s[14:15], 0, v105
	s_nop 1
	v_cndmask_b32_e64 v102, v102, v103, s[14:15]
	v_cmp_lt_f32_e64 s[14:15], 0, v106
	s_nop 1
	v_cndmask_b32_e64 v102, v102, v104, s[14:15]
	v_mul_f32_e32 v103, 0x37800000, v102
	v_cndmask_b32_e32 v102, v102, v103, vcc
	v_cmp_class_f32_e32 vcc, v60, v201
	s_nop 1
	v_cndmask_b32_e32 v60, v102, v60, vcc
	v_div_scale_f32 v102, s[14:15], v60, v60, 1.0
	v_rcp_f32_e32 v103, v102
	v_div_scale_f32 v104, vcc, 1.0, v60, 1.0
	v_fma_f32 v105, -v102, v103, 1.0
	v_fmac_f32_e32 v103, v105, v103
	v_mul_f32_e32 v105, v104, v103
	v_fma_f32 v106, -v102, v105, v104
	v_fmac_f32_e32 v105, v106, v103
	v_fma_f32 v102, -v102, v105, v104
	v_div_fmas_f32 v102, v102, v103, v105
	v_div_fixup_f32 v60, v102, v60, 1.0
	v_pk_mul_f32 v[30:31], v[30:31], v[60:61] op_sel_hi:[1,0]
	v_pk_mul_f32 v[28:29], v[28:29], v[60:61] op_sel_hi:[1,0]
	s_waitcnt lgkmcnt(0)
	v_pk_fma_f32 v[98:99], v[94:95], v[30:31], v[98:99]
	v_pk_fma_f32 v[100:101], v[96:97], v[28:29], v[100:101]
	v_bfe_u32 v28, v98, 16, 1
	v_bfe_u32 v30, v100, 16, 1
	v_bfe_u32 v29, v99, 16, 1
	v_bfe_u32 v31, v101, 16, 1
	v_add3_u32 v28, v98, v28, s86
	v_add3_u32 v30, v100, v30, s86
	v_add3_u32 v29, v99, v29, s86
	v_add3_u32 v31, v101, v31, s86
	v_lshrrev_b32_e32 v28, 16, v28
	v_lshrrev_b32_e32 v30, 16, v30
	v_and_or_b32 v28, v29, s82, v28
	v_and_or_b32 v29, v31, s82, v30
	global_store_dwordx2 v[122:123], v[28:29], off
	ds_read_b128 v[28:31], v252 offset:16384
	s_nop 0
	ds_read_b128 v[94:97], v252 offset:24576
	v_mov_b32_e32 v102, 0
	v_pk_mul_f32 v[26:27], v[26:27], v[60:61] op_sel_hi:[1,0]
	v_pk_mul_f32 v[24:25], v[24:25], v[60:61] op_sel_hi:[1,0]
	v_pk_mul_f32 v[22:23], v[22:23], v[60:61] op_sel_hi:[1,0]
	v_pk_mul_f32 v[20:21], v[20:21], v[60:61] op_sel_hi:[1,0]
	v_mov_b32_e32 v106, 0
	v_pk_mul_f32 v[18:19], v[18:19], v[60:61] op_sel_hi:[1,0]
	v_pk_mul_f32 v[16:17], v[16:17], v[60:61] op_sel_hi:[1,0]
	v_pk_mul_f32 v[14:15], v[14:15], v[60:61] op_sel_hi:[1,0]
	v_pk_mul_f32 v[12:13], v[12:13], v[60:61] op_sel_hi:[1,0]
	v_pk_mul_f32 v[8:9], v[8:9], v[60:61] op_sel_hi:[1,0]
	v_pk_mul_f32 v[10:11], v[10:11], v[60:61] op_sel_hi:[1,0]
	v_pk_mul_f32 v[6:7], v[6:7], v[60:61] op_sel_hi:[1,0]
	v_pk_mul_f32 v[4:5], v[4:5], v[60:61] op_sel_hi:[1,0]
	v_pk_mul_f32 v[2:3], v[2:3], v[60:61] op_sel_hi:[1,0]
	v_pk_mul_f32 v[0:1], v[0:1], v[60:61] op_sel_hi:[1,0]
	s_waitcnt lgkmcnt(0)
	v_pk_add_f32 v[28:29], v[28:29], 1.0 op_sel_hi:[1,0]
	s_waitcnt lgkmcnt(0)
	v_pk_fma_f32 v[94:95], v[28:29], v[98:99], v[94:95]
	v_pk_add_f32 v[28:29], v[30:31], 1.0 op_sel_hi:[1,0]
	v_cvt_pk_fp8_f32 v102, v94, v95
	v_pk_fma_f32 v[96:97], v[28:29], v[100:101], v[96:97]
	v_lshl_add_u64 v[28:29], s[0:1], 0, v[36:37]
	s_lshl_b64 s[0:1], s[44:45], 12
	v_cvt_pk_fp8_f32 v102, v96, v97 op_sel:[0,0,1]
	s_add_u32 s0, s3, s0
	s_addc_u32 s1, s39, s1
	global_store_dword v[28:29], v102, off
	ds_read_b128 v[98:101], v252 offset:9216
	s_nop 0
	ds_read_b128 v[102:105], v252 offset:1024
	s_waitcnt lgkmcnt(0)
	v_pk_fma_f32 v[30:31], v[100:101], v[24:25], v[104:105]
	v_pk_fma_f32 v[102:103], v[98:99], v[26:27], v[102:103]
	v_bfe_u32 v26, v30, 16, 1
	v_bfe_u32 v24, v102, 16, 1
	v_bfe_u32 v25, v103, 16, 1
	v_bfe_u32 v27, v31, 16, 1
	v_add3_u32 v24, v102, v24, s86
	v_add3_u32 v26, v30, v26, s86
	v_add3_u32 v25, v103, v25, s86
	v_add3_u32 v27, v31, v27, s86
	v_lshrrev_b32_e32 v24, 16, v24
	v_lshrrev_b32_e32 v26, 16, v26
	v_and_or_b32 v24, v25, s82, v24
	v_and_or_b32 v25, v27, s82, v26
	global_store_dwordx2 v[122:123], v[24:25], off offset:512
	ds_read_b128 v[24:27], v252 offset:17408
	s_nop 0
	ds_read_b128 v[98:101], v252 offset:25600
	v_mov_b32_e32 v104, 0
	s_waitcnt lgkmcnt(0)
; #define GAS __attribute__((address_space(1)))
; #define LAS __attribute__((address_space(3)))
; __device__ __forceinline__ unsigned pk2(float lo, float hi) { return f2bf(lo) | (f2bf(hi) << 16); }
; __device__ __forceinline__ unsigned pk4_fp8(float a, float b, float c, float d) { int r = __builtin_amdgcn_cvt_pk_fp8_f32(a, b, 0, false); r = __builtin_amdgcn_cvt_pk_fp8_f32(c, d, r, true); return (unsigned)r; }
; template <int l>
; __device__ __forceinline__ void layer_phases(Frame& F, const XcdBarrier& bar, const int lo, const int hi) {
;     ...
;                     for (int j = 0; j < 8; ++j) { const int k = 4 * lq + 256 * j;
;                         const f32x4 xv = v[j] * rstd * *(const GAS f32x4*)(g1 + k) + *(const GAS f32x4*)(b1 + k);
;                         { v2u xo; xo.x = pk2(xv.x, xv.y); xo.y = pk2(xv.z, xv.w); *(GAS v2u*)(x1 + (size_t)m * D + k) = xo; }
;                         const f32x4 hv = xv * (*(const GAS f32x4*)(mrow + 8192 + k) + 1.0f) + *(const GAS f32x4*)(mrow + 6144 + k);
;                         v2u o; o.x = pk2(hv.x, hv.y); o.y = pk2(hv.z, hv.w);
;                         *(GAS unsigned*)(h2q + (size_t)m * D + k) = pk4_fp8(hv.x, hv.y, hv.z, hv.w);
;                         const int chunk = (lq >> 1) + 32 * j;
;                         *(LAS v2u*)(h2s + rloc * 4096 + ((chunk ^ (rloc & 15)) << 4) + (lq & 1) * 8) = o; }
	v_pk_add_f32 v[24:25], v[24:25], 1.0 op_sel_hi:[1,0]
	s_waitcnt lgkmcnt(0)
	v_pk_fma_f32 v[98:99], v[24:25], v[102:103], v[98:99]
	v_pk_add_f32 v[24:25], v[26:27], 1.0 op_sel_hi:[1,0]
	v_cvt_pk_fp8_f32 v104, v98, v99
	v_pk_fma_f32 v[100:101], v[24:25], v[30:31], v[100:101]
	s_nop 0
	v_cvt_pk_fp8_f32 v104, v100, v101 op_sel:[0,0,1]
	global_store_dword v[28:29], v104, off offset:256
	ds_read_b128 v[24:27], v252 offset:10240
	s_nop 0
	ds_read_b128 v[102:105], v252 offset:2048
	s_waitcnt lgkmcnt(0)
	v_pk_fma_f32 v[30:31], v[26:27], v[20:21], v[104:105]
	v_pk_fma_f32 v[102:103], v[24:25], v[22:23], v[102:103]
	v_bfe_u32 v22, v30, 16, 1
	v_bfe_u32 v20, v102, 16, 1
	v_bfe_u32 v21, v103, 16, 1
	v_bfe_u32 v23, v31, 16, 1
	v_add3_u32 v20, v102, v20, s86
	v_add3_u32 v22, v30, v22, s86
	v_add3_u32 v21, v103, v21, s86
	v_add3_u32 v23, v31, v23, s86
	v_lshrrev_b32_e32 v20, 16, v20
	v_lshrrev_b32_e32 v22, 16, v22
	v_and_or_b32 v20, v21, s82, v20
	v_and_or_b32 v21, v23, s82, v22
	global_store_dwordx2 v[122:123], v[20:21], off offset:1024
	ds_read_b128 v[20:23], v252 offset:18432
	s_nop 0
	ds_read_b128 v[24:27], v252 offset:26624
	s_waitcnt lgkmcnt(0)
	v_pk_add_f32 v[20:21], v[20:21], 1.0 op_sel_hi:[1,0]
	s_waitcnt lgkmcnt(0)
	v_pk_fma_f32 v[102:103], v[20:21], v[102:103], v[24:25]
	v_pk_add_f32 v[20:21], v[22:23], 1.0 op_sel_hi:[1,0]
	v_cvt_pk_fp8_f32 v106, v102, v103
	v_pk_fma_f32 v[104:105], v[20:21], v[30:31], v[26:27]
	v_mov_b32_e32 v30, 0
	v_cvt_pk_fp8_f32 v106, v104, v105 op_sel:[0,0,1]
	global_store_dword v[28:29], v106, off offset:512
	ds_read_b128 v[20:23], v252 offset:11264
	ds_read_b128 v[24:27], v252 offset:3072
	s_waitcnt lgkmcnt(0)
	v_pk_fma_f32 v[26:27], v[16:17], v[22:23], v[26:27]
	v_pk_fma_f32 v[24:25], v[18:19], v[20:21], v[24:25]
	v_bfe_u32 v18, v26, 16, 1
	v_bfe_u32 v16, v24, 16, 1
	v_bfe_u32 v17, v25, 16, 1
	v_bfe_u32 v19, v27, 16, 1
	v_add3_u32 v16, v24, v16, s86
	v_add3_u32 v18, v26, v18, s86
	v_add3_u32 v17, v25, v17, s86
	v_add3_u32 v19, v27, v19, s86
	v_lshrrev_b32_e32 v16, 16, v16
	v_lshrrev_b32_e32 v18, 16, v18
	v_and_or_b32 v16, v17, s82, v16
	v_and_or_b32 v17, v19, s82, v18
	global_store_dwordx2 v[122:123], v[16:17], off offset:1536
	ds_read_b128 v[16:19], v252 offset:19456
	s_nop 0
	ds_read_b128 v[20:23], v252 offset:27648
	s_waitcnt lgkmcnt(0)
	v_pk_add_f32 v[16:17], v[16:17], 1.0 op_sel_hi:[1,0]
	s_waitcnt lgkmcnt(0)
	v_pk_fma_f32 v[106:107], v[24:25], v[16:17], v[20:21]
	v_pk_add_f32 v[16:17], v[18:19], 1.0 op_sel_hi:[1,0]
	v_cvt_pk_fp8_f32 v30, v106, v107
	v_pk_fma_f32 v[108:109], v[26:27], v[16:17], v[22:23]
	v_mov_b32_e32 v24, 0
	v_cvt_pk_fp8_f32 v30, v108, v109 op_sel:[0,0,1]
	global_store_dword v[28:29], v30, off offset:768
	ds_read_b128 v[16:19], v252 offset:12288
	ds_read_b128 v[20:23], v252 offset:4096
	s_waitcnt lgkmcnt(0)
	v_pk_fma_f32 v[22:23], v[12:13], v[18:19], v[22:23]
	v_pk_fma_f32 v[20:21], v[14:15], v[16:17], v[20:21]
	v_bfe_u32 v14, v22, 16, 1
	v_bfe_u32 v12, v20, 16, 1
	v_bfe_u32 v13, v21, 16, 1
	v_bfe_u32 v15, v23, 16, 1
	v_add3_u32 v12, v20, v12, s86
	v_add3_u32 v14, v22, v14, s86
	v_add3_u32 v13, v21, v13, s86
	v_add3_u32 v15, v23, v15, s86
	v_lshrrev_b32_e32 v12, 16, v12
	v_lshrrev_b32_e32 v14, 16, v14
	v_and_or_b32 v12, v13, s82, v12
	v_and_or_b32 v13, v15, s82, v14
	global_store_dwordx2 v[122:123], v[12:13], off offset:2048
	ds_read_b128 v[12:15], v252 offset:20480
	s_nop 0
	ds_read_b128 v[16:19], v252 offset:28672
	s_waitcnt lgkmcnt(0)
	v_pk_add_f32 v[12:13], v[12:13], 1.0 op_sel_hi:[1,0]
	s_waitcnt lgkmcnt(0)
	v_pk_fma_f32 v[110:111], v[20:21], v[12:13], v[16:17]
	v_pk_add_f32 v[12:13], v[14:15], 1.0 op_sel_hi:[1,0]
	v_cvt_pk_fp8_f32 v24, v110, v111
	v_pk_fma_f32 v[112:113], v[22:23], v[12:13], v[18:19]
	v_mov_b32_e32 v20, 0
	v_cvt_pk_fp8_f32 v24, v112, v113 op_sel:[0,0,1]
	global_store_dword v[28:29], v24, off offset:1024
	ds_read_b128 v[12:15], v252 offset:13312
	ds_read_b128 v[16:19], v252 offset:5120
	s_waitcnt lgkmcnt(0)
	v_pk_fma_f32 v[18:19], v[10:11], v[14:15], v[18:19]
	v_pk_fma_f32 v[16:17], v[8:9], v[12:13], v[16:17]
	v_bfe_u32 v10, v18, 16, 1
	v_bfe_u32 v8, v16, 16, 1
	v_bfe_u32 v9, v17, 16, 1
	v_bfe_u32 v11, v19, 16, 1
	v_add3_u32 v8, v16, v8, s86
	v_add3_u32 v10, v18, v10, s86
	v_add3_u32 v9, v17, v9, s86
	v_add3_u32 v11, v19, v11, s86
	v_lshrrev_b32_e32 v8, 16, v8
	v_lshrrev_b32_e32 v10, 16, v10
	v_and_or_b32 v8, v9, s82, v8
	v_and_or_b32 v9, v11, s82, v10
	global_store_dwordx2 v[122:123], v[8:9], off offset:2560
	ds_read_b128 v[8:11], v252 offset:21504
	s_nop 0
	ds_read_b128 v[12:15], v252 offset:29696
	s_waitcnt lgkmcnt(0)
	v_pk_add_f32 v[8:9], v[8:9], 1.0 op_sel_hi:[1,0]
	s_waitcnt lgkmcnt(0)
	v_pk_fma_f32 v[114:115], v[16:17], v[8:9], v[12:13]
	v_pk_add_f32 v[8:9], v[10:11], 1.0 op_sel_hi:[1,0]
	v_cvt_pk_fp8_f32 v20, v114, v115
	v_pk_fma_f32 v[116:117], v[18:19], v[8:9], v[14:15]
	v_mov_b32_e32 v16, 0
	v_cvt_pk_fp8_f32 v20, v116, v117 op_sel:[0,0,1]
	global_store_dword v[28:29], v20, off offset:1280
	ds_read_b128 v[8:11], v252 offset:14336
	ds_read_b128 v[12:15], v252 offset:6144
	s_waitcnt lgkmcnt(0)
	v_pk_fma_f32 v[14:15], v[4:5], v[10:11], v[14:15]
	v_pk_fma_f32 v[12:13], v[6:7], v[8:9], v[12:13]
	v_bfe_u32 v6, v14, 16, 1
	v_bfe_u32 v4, v12, 16, 1
	v_bfe_u32 v5, v13, 16, 1
	v_bfe_u32 v7, v15, 16, 1
	v_add3_u32 v4, v12, v4, s86
	v_add3_u32 v6, v14, v6, s86
	v_add3_u32 v5, v13, v5, s86
	v_add3_u32 v7, v15, v7, s86
	v_lshrrev_b32_e32 v4, 16, v4
	v_lshrrev_b32_e32 v6, 16, v6
	v_and_or_b32 v4, v5, s82, v4
	v_and_or_b32 v5, v7, s82, v6
	global_store_dwordx2 v[122:123], v[4:5], off offset:3072
	ds_read_b128 v[4:7], v252 offset:22528
	s_nop 0
	ds_read_b128 v[8:11], v252 offset:30720
	s_waitcnt lgkmcnt(0)
; #define GAS __attribute__((address_space(1)))
; #define LAS __attribute__((address_space(3)))
; __device__ __forceinline__ unsigned pk2(float lo, float hi) { return f2bf(lo) | (f2bf(hi) << 16); }
; __device__ __forceinline__ unsigned pk4_fp8(float a, float b, float c, float d) { int r = __builtin_amdgcn_cvt_pk_fp8_f32(a, b, 0, false); r = __builtin_amdgcn_cvt_pk_fp8_f32(c, d, r, true); return (unsigned)r; }
; __device__ __forceinline__ f32x4 bf4(unsigned a, unsigned b) { return (f32x4){bflo(a), bfhi(a), bflo(b), bfhi(b)}; }
; template <int l>
; __device__ __forceinline__ void layer_phases(Frame& F, const XcdBarrier& bar, const int lo, const int hi) {
;     ...
;                 for (int rp = 0; rp < 2; ++rp) {
;                 f32x4 vv[2][8];
; #pragma unroll
;                 for (int rr = 0; rr < 2; ++rr)
; #pragma unroll
;                     for (int j = 0; j < 8; ++j) { const size_t off = (size_t)(m0 + 2 * rp + rr) * D + 4 * lq + 256 * j;
;                         f32x4 xv; if (l == 0) xv = __builtin_nontemporal_load((const GAS f32x4*)(xin + off)); else { const v2u xw_ = __builtin_nontemporal_load((const GAS v2u*)(xinb + off)); xv = bf4(xw_.x, xw_.y); } const v2u mw = __builtin_nontemporal_load((const GAS v2u*)(mixb + off)); const f32x4 gv = *(const GAS f32x4*)(mrow + 4096 + 4 * lq + 256 * j);
;                         vv[rr][j] = xv * ALPHA + gv * (f32x4){bflo(mw.x), bfhi(mw.x), bflo(mw.y), bfhi(mw.y)}; }
;     ...
;                     for (int j = 0; j < 8; ++j) { const int k = 4 * lq + 256 * j;
;                         const f32x4 xv = v[j] * rstd * *(const GAS f32x4*)(g1 + k) + *(const GAS f32x4*)(b1 + k);
;                         { v2u xo; xo.x = pk2(xv.x, xv.y); xo.y = pk2(xv.z, xv.w); *(GAS v2u*)(x1 + (size_t)m * D + k) = xo; }
;                         const f32x4 hv = xv * (*(const GAS f32x4*)(mrow + 8192 + k) + 1.0f) + *(const GAS f32x4*)(mrow + 6144 + k);
;                         v2u o; o.x = pk2(hv.x, hv.y); o.y = pk2(hv.z, hv.w);
;                         *(GAS unsigned*)(h2q + (size_t)m * D + k) = pk4_fp8(hv.x, hv.y, hv.z, hv.w);
;                         const int chunk = (lq >> 1) + 32 * j;
;                         *(LAS v2u*)(h2s + rloc * 4096 + ((chunk ^ (rloc & 15)) << 4) + (lq & 1) * 8) = o; }
	v_pk_add_f32 v[4:5], v[4:5], 1.0 op_sel_hi:[1,0]
	s_waitcnt lgkmcnt(0)
	v_pk_fma_f32 v[118:119], v[12:13], v[4:5], v[8:9]
	v_pk_add_f32 v[4:5], v[6:7], 1.0 op_sel_hi:[1,0]
	v_cvt_pk_fp8_f32 v16, v118, v119
	v_pk_fma_f32 v[120:121], v[14:15], v[4:5], v[10:11]
	v_mov_b32_e32 v12, 0
	v_cvt_pk_fp8_f32 v16, v120, v121 op_sel:[0,0,1]
	global_store_dword v[28:29], v16, off offset:1536
	ds_read_b128 v[4:7], v252 offset:15360
	ds_read_b128 v[8:11], v252 offset:7168
	s_waitcnt lgkmcnt(0)
	v_pk_fma_f32 v[10:11], v[0:1], v[6:7], v[10:11]
	v_pk_fma_f32 v[8:9], v[2:3], v[4:5], v[8:9]
	v_bfe_u32 v2, v10, 16, 1
	v_bfe_u32 v0, v8, 16, 1
	v_bfe_u32 v1, v9, 16, 1
	v_bfe_u32 v3, v11, 16, 1
	v_add3_u32 v0, v8, v0, s86
	v_add3_u32 v2, v10, v2, s86
	v_add3_u32 v1, v9, v1, s86
	v_add3_u32 v3, v11, v3, s86
	v_lshrrev_b32_e32 v0, 16, v0
	v_lshrrev_b32_e32 v2, 16, v2
	v_and_or_b32 v0, v1, s82, v0
	v_and_or_b32 v1, v3, s82, v2
	global_store_dwordx2 v[122:123], v[0:1], off offset:3584
	ds_read_b128 v[0:3], v252 offset:23552
	s_nop 0
	ds_read_b128 v[4:7], v252 offset:31744
	s_waitcnt lgkmcnt(0)
	v_pk_add_f32 v[0:1], v[0:1], 1.0 op_sel_hi:[1,0]
	s_waitcnt lgkmcnt(0)
	v_pk_fma_f32 v[122:123], v[8:9], v[0:1], v[4:5]
	v_pk_add_f32 v[0:1], v[2:3], 1.0 op_sel_hi:[1,0]
	v_cvt_pk_fp8_f32 v12, v122, v123
	v_pk_fma_f32 v[124:125], v[10:11], v[0:1], v[6:7]
	v_lshl_add_u64 v[0:1], s[18:19], 0, v[36:37]
	v_lshlrev_b64 v[0:1], 1, v[0:1]
	v_cvt_pk_fp8_f32 v12, v124, v125 op_sel:[0,0,1]
	v_lshl_add_u64 v[2:3], s[22:23], 0, v[0:1]
	v_lshl_add_u64 v[0:1], s[20:21], 0, v[0:1]
	global_store_dword v[28:29], v12, off offset:1792
	global_load_dwordx2 v[130:131], v[2:3], off nt
	global_load_dwordx2 v[132:133], v[0:1], off nt
	global_load_dwordx2 v[134:135], v[2:3], off offset:512 nt
	global_load_dwordx2 v[136:137], v[0:1], off offset:512 nt
	global_load_dwordx2 v[138:139], v[2:3], off offset:1024 nt
	global_load_dwordx2 v[140:141], v[0:1], off offset:1024 nt
	global_load_dwordx2 v[142:143], v[2:3], off offset:1536 nt
	global_load_dwordx2 v[144:145], v[0:1], off offset:1536 nt
	global_load_dwordx2 v[146:147], v[2:3], off offset:2048 nt
	global_load_dwordx2 v[148:149], v[0:1], off offset:2048 nt
	global_load_dwordx2 v[150:151], v[2:3], off offset:2560 nt
	global_load_dwordx2 v[152:153], v[0:1], off offset:2560 nt
	global_load_dwordx2 v[154:155], v[2:3], off offset:3072 nt
	global_load_dwordx2 v[156:157], v[0:1], off offset:3072 nt
	global_load_dwordx2 v[158:159], v[2:3], off offset:3584 nt
	global_load_dwordx2 v[160:161], v[0:1], off offset:3584 nt
	global_load_dwordx4 v[28:31], v[126:127], off offset:-4096
	global_load_dwordx4 v[24:27], v[128:129], off offset:1024
	global_load_dwordx4 v[20:23], v[128:129], off offset:2048
	global_load_dwordx4 v[16:19], v[128:129], off offset:3072
	global_load_dwordx4 v[12:15], v[126:127], off
	global_load_dwordx4 v[8:11], v[126:127], off offset:1024
	global_load_dwordx4 v[4:7], v[126:127], off offset:2048
	global_load_dwordx4 v[0:3], v[126:127], off offset:3072
	ds_read_b128 v[206:209], v252 offset:8192
	ds_read_b128 v[210:213], v252 offset:0
	s_waitcnt vmcnt(21)
	s_waitcnt lgkmcnt(0)
	v_lshlrev_b32_e32 v162, 16, v134
	s_waitcnt vmcnt(20)
	s_waitcnt lgkmcnt(0)
	v_lshlrev_b32_e32 v164, 16, v136
	v_and_b32_e32 v165, 0xffff0000, v136
	v_lshlrev_b32_e32 v136, 16, v137
	v_and_b32_e32 v137, 0xffff0000, v137
	v_and_b32_e32 v163, 0xffff0000, v134
	v_lshlrev_b32_e32 v134, 16, v135
	v_and_b32_e32 v135, 0xffff0000, v135
	s_waitcnt vmcnt(18)
	s_waitcnt lgkmcnt(0)
	v_lshlrev_b32_e32 v168, 16, v140
	v_and_b32_e32 v169, 0xffff0000, v140
	v_lshlrev_b32_e32 v140, 16, v141
	v_and_b32_e32 v141, 0xffff0000, v141
	s_waitcnt vmcnt(16)
	s_waitcnt lgkmcnt(0)
	v_lshlrev_b32_e32 v172, 16, v144
	v_and_b32_e32 v173, 0xffff0000, v144
	v_lshlrev_b32_e32 v144, 16, v145
	v_and_b32_e32 v145, 0xffff0000, v145
	s_waitcnt vmcnt(14)
	s_waitcnt lgkmcnt(0)
	v_lshlrev_b32_e32 v176, 16, v148
	v_and_b32_e32 v177, 0xffff0000, v148
	v_lshlrev_b32_e32 v148, 16, v149
	v_and_b32_e32 v149, 0xffff0000, v149
	v_lshlrev_b32_e32 v128, 16, v130
	v_and_b32_e32 v129, 0xffff0000, v130
	v_lshlrev_b32_e32 v126, 16, v131
	v_and_b32_e32 v127, 0xffff0000, v131
	v_lshlrev_b32_e32 v130, 16, v132
	v_and_b32_e32 v131, 0xffff0000, v132
	v_lshlrev_b32_e32 v132, 16, v133
	v_and_b32_e32 v133, 0xffff0000, v133
	s_waitcnt vmcnt(12)
	s_waitcnt lgkmcnt(0)
	v_lshlrev_b32_e32 v180, 16, v152
	v_and_b32_e32 v181, 0xffff0000, v152
	v_lshlrev_b32_e32 v152, 16, v153
	v_and_b32_e32 v153, 0xffff0000, v153
	s_waitcnt vmcnt(8)
	s_waitcnt lgkmcnt(0)
	v_lshlrev_b32_e32 v188, 16, v160
	v_and_b32_e32 v189, 0xffff0000, v160
	v_lshlrev_b32_e32 v160, 16, v161
	v_and_b32_e32 v161, 0xffff0000, v161
	s_waitcnt vmcnt(7)
	s_waitcnt lgkmcnt(0)
	v_pk_mul_f32 v[130:131], v[28:29], v[130:131]
	v_pk_mul_f32 v[132:133], v[30:31], v[132:133]
	s_waitcnt vmcnt(6)
	s_waitcnt lgkmcnt(0)
	v_pk_mul_f32 v[136:137], v[26:27], v[136:137]
	v_pk_mul_f32 v[164:165], v[24:25], v[164:165]
	v_lshlrev_b32_e32 v166, 16, v138
	v_and_b32_e32 v167, 0xffff0000, v138
	v_lshlrev_b32_e32 v138, 16, v139
	v_and_b32_e32 v139, 0xffff0000, v139
	v_lshlrev_b32_e32 v170, 16, v142
	v_and_b32_e32 v171, 0xffff0000, v142
	v_lshlrev_b32_e32 v142, 16, v143
	v_and_b32_e32 v143, 0xffff0000, v143
	v_lshlrev_b32_e32 v174, 16, v146
	v_and_b32_e32 v175, 0xffff0000, v146
	v_lshlrev_b32_e32 v146, 16, v147
	v_and_b32_e32 v147, 0xffff0000, v147
	v_lshlrev_b32_e32 v178, 16, v150
	v_and_b32_e32 v179, 0xffff0000, v150
	v_lshlrev_b32_e32 v150, 16, v151
	v_and_b32_e32 v151, 0xffff0000, v151
	v_lshlrev_b32_e32 v186, 16, v158
	v_and_b32_e32 v187, 0xffff0000, v158
	v_lshlrev_b32_e32 v158, 16, v159
	v_and_b32_e32 v159, 0xffff0000, v159
	s_waitcnt vmcnt(5)
; #define GAS __attribute__((address_space(1)))
; __device__ __forceinline__ f32x4 bf4(unsigned a, unsigned b) { return (f32x4){bflo(a), bfhi(a), bflo(b), bfhi(b)}; }
; template <int l>
; __device__ __forceinline__ void layer_phases(Frame& F, const XcdBarrier& bar, const int lo, const int hi) {
;     ...
;                     for (int j = 0; j < 8; ++j) { const size_t off = (size_t)(m0 + 2 * rp + rr) * D + 4 * lq + 256 * j;
;                         f32x4 xv; if (l == 0) xv = __builtin_nontemporal_load((const GAS f32x4*)(xin + off)); else { const v2u xw_ = __builtin_nontemporal_load((const GAS v2u*)(xinb + off)); xv = bf4(xw_.x, xw_.y); } const v2u mw = __builtin_nontemporal_load((const GAS v2u*)(mixb + off)); const f32x4 gv = *(const GAS f32x4*)(mrow + 4096 + 4 * lq + 256 * j);
;                         vv[rr][j] = xv * ALPHA + gv * (f32x4){bflo(mw.x), bfhi(mw.x), bflo(mw.y), bfhi(mw.y)}; }
; #pragma unroll
;                 for (int rq = 0; rq < 2; ++rq) { const int rr = 2 * rp + rq, m = m0 + rr, rloc = 4 * F.wave + rr;
;                     f32x4 (&v)[8] = vv[rq]; float s = 0.f;
; #pragma unroll
;                     for (int j = 0; j < 8; ++j) s += (v[j].x + v[j].y) + (v[j].z + v[j].w);
;                     const float mean = wave_sum(s) * (1.f / D); float s2 = 0.f;
	s_waitcnt lgkmcnt(0)
	v_pk_mul_f32 v[140:141], v[22:23], v[140:141]
	v_pk_mul_f32 v[168:169], v[20:21], v[168:169]
	s_waitcnt vmcnt(4)
	s_waitcnt lgkmcnt(0)
	v_pk_mul_f32 v[144:145], v[18:19], v[144:145]
	s_waitcnt vmcnt(3)
	s_waitcnt lgkmcnt(0)
	v_pk_mul_f32 v[148:149], v[14:15], v[148:149]
	s_waitcnt vmcnt(2)
	s_waitcnt lgkmcnt(0)
	v_pk_mul_f32 v[152:153], v[10:11], v[152:153]
	s_waitcnt vmcnt(0)
	s_waitcnt lgkmcnt(0)
	v_pk_mul_f32 v[160:161], v[2:3], v[160:161]
	v_pk_fma_f32 v[126:127], v[126:127], s[38:39], v[132:133] op_sel_hi:[1,0,1]
	v_pk_fma_f32 v[128:129], v[128:129], s[38:39], v[130:131] op_sel_hi:[1,0,1]
	v_pk_fma_f32 v[130:131], v[134:135], s[38:39], v[136:137] op_sel_hi:[1,0,1]
	v_pk_fma_f32 v[132:133], v[162:163], s[38:39], v[164:165] op_sel_hi:[1,0,1]
	v_pk_fma_f32 v[134:135], v[138:139], s[38:39], v[140:141] op_sel_hi:[1,0,1]
	v_pk_fma_f32 v[136:137], v[166:167], s[38:39], v[168:169] op_sel_hi:[1,0,1]
	v_pk_fma_f32 v[138:139], v[142:143], s[38:39], v[144:145] op_sel_hi:[1,0,1]
	v_pk_fma_f32 v[142:143], v[146:147], s[38:39], v[148:149] op_sel_hi:[1,0,1]
	v_pk_fma_f32 v[146:147], v[150:151], s[38:39], v[152:153] op_sel_hi:[1,0,1]
	v_pk_fma_f32 v[150:151], v[158:159], s[38:39], v[160:161] op_sel_hi:[1,0,1]
	v_mov_b32_e32 v158, v128
	v_mov_b32_e32 v159, v132
	v_mov_b32_e32 v160, v129
	v_mov_b32_e32 v161, v133
	v_mov_b32_e32 v162, v126
	v_mov_b32_e32 v163, v130
	v_mov_b32_e32 v164, v127
	v_mov_b32_e32 v165, v131
	v_pk_mov_b32 v[166:167], v[136:137], v[134:135] op_sel:[1,0]
	v_mov_b32_e32 v168, v136
	v_mov_b32_e32 v169, v135
	v_pk_add_f32 v[158:159], v[158:159], v[160:161]
	v_pk_add_f32 v[160:161], v[162:163], v[164:165]
	v_pk_mul_f32 v[172:173], v[16:17], v[172:173]
	v_pk_mul_f32 v[176:177], v[12:13], v[176:177]
	v_pk_add_f32 v[162:163], v[166:167], v[168:169]
	v_pk_add_f32 v[158:159], v[158:159], v[160:161]
	v_pk_mul_f32 v[180:181], v[8:9], v[180:181]
	v_pk_fma_f32 v[140:141], v[170:171], s[38:39], v[172:173] op_sel_hi:[1,0,1]
	v_pk_fma_f32 v[144:145], v[174:175], s[38:39], v[176:177] op_sel_hi:[1,0,1]
	v_pk_add_f32 v[160:161], v[162:163], v[162:163] op_sel:[0,1] op_sel_hi:[1,0]
	v_add_f32_e32 v60, 0, v158
	v_pk_fma_f32 v[148:149], v[178:179], s[38:39], v[180:181] op_sel_hi:[1,0,1]
	v_add_f32_e32 v170, v140, v141
	v_add_f32_e32 v172, v138, v139
	v_mov_b32_e32 v175, v144
	v_mov_b32_e32 v171, v142
	v_mov_b32_e32 v173, v143
	v_mov_b32_e32 v161, v145
	v_add_f32_e32 v174, v60, v159
	v_lshlrev_b32_e32 v184, 16, v156
	v_and_b32_e32 v185, 0xffff0000, v156
	v_lshlrev_b32_e32 v156, 16, v157
	v_and_b32_e32 v157, 0xffff0000, v157
	v_pk_mov_b32 v[176:177], v[148:149], v[146:147] op_sel:[1,0]
	v_mov_b32_e32 v178, v148
	v_mov_b32_e32 v179, v147
	v_pk_add_f32 v[164:165], v[170:171], v[172:173]
	v_pk_add_f32 v[158:159], v[174:175], v[160:161]
	v_lshlrev_b32_e32 v182, 16, v154
	v_and_b32_e32 v183, 0xffff0000, v154
	v_lshlrev_b32_e32 v154, 16, v155
	v_and_b32_e32 v155, 0xffff0000, v155
	v_pk_mul_f32 v[184:185], v[4:5], v[184:185]
	v_pk_mul_f32 v[156:157], v[6:7], v[156:157]
	v_pk_mul_f32 v[188:189], v[0:1], v[188:189]
	v_pk_add_f32 v[166:167], v[176:177], v[178:179]
	v_pk_add_f32 v[158:159], v[158:159], v[164:165]
	v_pk_fma_f32 v[154:155], v[154:155], s[38:39], v[156:157] op_sel_hi:[1,0,1]
	v_pk_fma_f32 v[156:157], v[182:183], s[38:39], v[184:185] op_sel_hi:[1,0,1]
	v_pk_fma_f32 v[152:153], v[186:187], s[38:39], v[188:189] op_sel_hi:[1,0,1]
	v_pk_add_f32 v[162:163], v[166:167], v[166:167] op_sel:[0,1] op_sel_hi:[1,0]
	v_pk_add_f32 v[158:159], v[158:159], v[158:159] op_sel:[0,1] op_sel_hi:[1,0]
	v_add_f32_e32 v180, v156, v157
	v_add_f32_e32 v182, v154, v155
	v_mov_b32_e32 v181, v150
	v_mov_b32_e32 v183, v151
	v_mov_b32_e32 v163, v153
	v_mov_b32_e32 v159, v152
	v_pk_add_f32 v[168:169], v[180:181], v[182:183]
	v_pk_add_f32 v[158:159], v[158:159], v[162:163]
	s_nop 0
	v_pk_add_f32 v[158:159], v[158:159], v[168:169]
	s_nop 0
	v_add_f32_e32 v60, v158, v159
	ds_bpermute_b32 v158, v53, v60
	s_waitcnt lgkmcnt(0)
	v_add_f32_e32 v60, v60, v158
	ds_bpermute_b32 v158, v194, v60
	s_waitcnt lgkmcnt(0)
	v_add_f32_e32 v60, v60, v158
	ds_bpermute_b32 v158, v195, v60
	s_waitcnt lgkmcnt(0)
	v_add_f32_e32 v60, v60, v158
	ds_bpermute_b32 v158, v196, v60
	s_waitcnt lgkmcnt(0)
	v_add_f32_e32 v60, v60, v158
	ds_bpermute_b32 v158, v197, v60
	s_waitcnt lgkmcnt(0)
	v_add_f32_e32 v60, v60, v158
	ds_bpermute_b32 v158, v198, v60
	s_waitcnt lgkmcnt(0)
; #define GAS __attribute__((address_space(1)))
; __device__ __forceinline__ f32x4 bf4(unsigned a, unsigned b) { return (f32x4){bflo(a), bfhi(a), bflo(b), bfhi(b)}; }
; template <int l>
; __device__ __forceinline__ void layer_phases(Frame& F, const XcdBarrier& bar, const int lo, const int hi) {
;     ...
;                     for (int j = 0; j < 8; ++j) { const size_t off = (size_t)(m0 + 2 * rp + rr) * D + 4 * lq + 256 * j;
;                         f32x4 xv; if (l == 0) xv = __builtin_nontemporal_load((const GAS f32x4*)(xin + off)); else { const v2u xw_ = __builtin_nontemporal_load((const GAS v2u*)(xinb + off)); xv = bf4(xw_.x, xw_.y); } const v2u mw = __builtin_nontemporal_load((const GAS v2u*)(mixb + off)); const f32x4 gv = *(const GAS f32x4*)(mrow + 4096 + 4 * lq + 256 * j);
;                         vv[rr][j] = xv * ALPHA + gv * (f32x4){bflo(mw.x), bfhi(mw.x), bflo(mw.y), bfhi(mw.y)}; }
;     ...
;                     const float mean = wave_sum(s) * (1.f / D); float s2 = 0.f;
; #pragma unroll
;                     for (int j = 0; j < 8; ++j) { v[j] = v[j] - mean; s2 += (v[j].x * v[j].x + v[j].y * v[j].y) + (v[j].z * v[j].z + v[j].w * v[j].w); }
;                     const float rstd = 1.f / sqrtf(wave_sum(s2) * (1.f / D) + LN_EPS);
	v_add_f32_e32 v60, v60, v158
	v_fmamk_f32 v127, v60, 0xba000000, v127
	v_fmamk_f32 v129, v60, 0xba000000, v129
	v_fmamk_f32 v131, v60, 0xba000000, v131
	v_fmamk_f32 v133, v60, 0xba000000, v133
	v_fmac_f32_e32 v126, 0xba000000, v60
	v_fmac_f32_e32 v128, 0xba000000, v60
	v_fmac_f32_e32 v130, 0xba000000, v60
	v_fmac_f32_e32 v132, 0xba000000, v60
	v_fmamk_f32 v137, v60, 0xba000000, v137
	v_fmac_f32_e32 v136, 0xba000000, v60
	v_fmamk_f32 v135, v60, 0xba000000, v135
	v_fmac_f32_e32 v134, 0xba000000, v60
	v_mov_b32_e32 v160, v129
	v_mov_b32_e32 v161, v133
	v_mov_b32_e32 v164, v127
	v_mov_b32_e32 v165, v131
	v_mov_b32_e32 v158, v128
	v_mov_b32_e32 v159, v132
	v_mov_b32_e32 v162, v126
	v_mov_b32_e32 v163, v130
	v_pk_mul_f32 v[166:167], v[134:135], v[134:135]
	v_pk_mul_f32 v[168:169], v[136:137], v[136:137]
	v_pk_mul_f32 v[160:161], v[160:161], v[160:161]
	v_pk_mul_f32 v[164:165], v[164:165], v[164:165]
	v_fmac_f32_e32 v140, 0xba000000, v60
	v_fmac_f32_e32 v138, 0xba000000, v60
	v_pk_mov_b32 v[180:181], v[168:169], v[166:167] op_sel:[1,0]
	v_mov_b32_e32 v169, v167
	v_pk_fma_f32 v[158:159], v[158:159], v[158:159], v[160:161]
	v_pk_fma_f32 v[160:161], v[162:163], v[162:163], v[164:165]
	v_fmamk_f32 v141, v60, 0xba000000, v141
	v_fmamk_f32 v139, v60, 0xba000000, v139
	v_fmamk_f32 v143, v60, 0xba000000, v143
	v_fmac_f32_e32 v142, 0xba000000, v60
	v_fmamk_f32 v145, v60, 0xba000000, v145
	v_fmac_f32_e32 v144, 0xba000000, v60
	v_fmamk_f32 v149, v60, 0xba000000, v149
	v_fmac_f32_e32 v148, 0xba000000, v60
	v_fmamk_f32 v147, v60, 0xba000000, v147
	v_fmac_f32_e32 v146, 0xba000000, v60
	v_fmamk_f32 v157, v60, 0xba000000, v157
	v_fmac_f32_e32 v156, 0xba000000, v60
	v_fmamk_f32 v155, v60, 0xba000000, v155
	v_fmac_f32_e32 v154, 0xba000000, v60
	v_fmamk_f32 v151, v60, 0xba000000, v151
	v_fmac_f32_e32 v150, 0xba000000, v60
	v_fmamk_f32 v153, v60, 0xba000000, v153
	v_fmac_f32_e32 v152, 0xba000000, v60
	v_mul_f32_e32 v60, v140, v140
	v_mul_f32_e32 v170, v138, v138
	v_pk_add_f32 v[162:163], v[180:181], v[168:169]
	v_pk_add_f32 v[158:159], v[158:159], v[160:161]
	v_pk_fma_f32 v[166:167], v[140:141], v[140:141], v[60:61] op_sel_hi:[1,1,0]
	v_pk_fma_f32 v[170:171], v[138:139], v[138:139], v[170:171] op_sel_hi:[1,1,0]
	v_pk_add_f32 v[160:161], v[162:163], v[162:163] op_sel_hi:[0,1]
	v_pk_add_f32 v[158:159], v[158:159], v[158:159] op_sel_hi:[0,1]
	v_pk_mul_f32 v[172:173], v[146:147], v[146:147]
	v_pk_mul_f32 v[174:175], v[148:149], v[148:149]
	v_mul_f32_e32 v166, v144, v144
	v_mul_f32_e32 v170, v145, v145
	v_mul_f32_e32 v160, v142, v142
	v_mul_f32_e32 v158, v143, v143
	v_pk_mov_b32 v[182:183], v[174:175], v[172:173] op_sel:[1,0]
	v_mov_b32_e32 v175, v173
	v_pk_add_f32 v[162:163], v[166:167], v[170:171]
	v_pk_add_f32 v[158:159], v[160:161], v[158:159]
	v_mul_f32_e32 v176, v156, v156
	v_mul_f32_e32 v178, v154, v154
	v_pk_add_f32 v[164:165], v[182:183], v[174:175]
	v_pk_add_f32 v[158:159], v[162:163], v[158:159]
	v_pk_fma_f32 v[172:173], v[156:157], v[156:157], v[176:177] op_sel_hi:[1,1,0]
	v_pk_fma_f32 v[176:177], v[154:155], v[154:155], v[178:179] op_sel_hi:[1,1,0]
	v_pk_add_f32 v[164:165], v[164:165], v[164:165] op_sel_hi:[0,1]
	v_pk_add_f32 v[158:159], v[158:159], v[158:159] op_sel_hi:[0,1]
	v_mul_f32_e32 v172, v152, v152
	v_mul_f32_e32 v176, v153, v153
	v_mul_f32_e32 v164, v150, v150
	v_mul_f32_e32 v158, v151, v151
	v_pk_add_f32 v[166:167], v[172:173], v[176:177]
	v_pk_add_f32 v[158:159], v[164:165], v[158:159]
	s_nop 0
	v_pk_add_f32 v[158:159], v[166:167], v[158:159]
	s_nop 0
	v_add_f32_e32 v60, v158, v159
	ds_bpermute_b32 v158, v53, v60
	s_waitcnt lgkmcnt(0)
	v_add_f32_e32 v60, v60, v158
	ds_bpermute_b32 v158, v194, v60
	s_waitcnt lgkmcnt(0)
	v_add_f32_e32 v60, v60, v158
	ds_bpermute_b32 v160, v195, v60
	v_lshl_add_u64 v[158:159], s[16:17], 0, v[36:37]
	v_lshlrev_b64 v[158:159], 1, v[158:159]
	v_lshl_add_u64 v[162:163], s[22:23], 0, v[158:159]
	v_lshl_add_u64 v[158:159], s[20:21], 0, v[158:159]
	s_waitcnt lgkmcnt(0)
	v_add_f32_e32 v60, v60, v160
	ds_bpermute_b32 v164, v196, v60
	v_lshl_add_u64 v[160:161], s[0:1], 0, v[88:89]
	s_waitcnt lgkmcnt(0)
	v_add_f32_e32 v60, v60, v164
	ds_bpermute_b32 v166, v197, v60
	global_load_dwordx2 v[190:191], v[162:163], off nt
	global_load_dwordx2 v[176:177], v[162:163], off offset:512 nt
	global_load_dwordx2 v[170:171], v[162:163], off offset:1024 nt
	global_load_dwordx2 v[164:165], v[162:163], off offset:1536 nt
	global_load_dwordx2 v[192:193], v[158:159], off nt
	global_load_dwordx2 v[180:181], v[158:159], off offset:512 nt
	global_load_dwordx2 v[174:175], v[158:159], off offset:1024 nt
	global_load_dwordx2 v[168:169], v[158:159], off offset:1536 nt
	s_waitcnt lgkmcnt(0)
	v_add_f32_e32 v60, v60, v166
	ds_bpermute_b32 v166, v198, v60
	s_waitcnt lgkmcnt(0)
	v_add_f32_e32 v60, v60, v166
	v_fmamk_f32 v60, v60, 0x3a000000, v200
	v_mul_f32_e32 v166, 0x4f800000, v60
	v_cmp_gt_f32_e32 vcc, s85, v60
	s_waitcnt vmcnt(7)
	s_waitcnt lgkmcnt(0)
	v_lshlrev_b32_e32 v218, 16, v191
	v_cndmask_b32_e32 v60, v60, v166, vcc
	v_sqrt_f32_e32 v182, v60
	global_load_dwordx2 v[178:179], v[162:163], off offset:2048 nt
	global_load_dwordx2 v[172:173], v[162:163], off offset:2560 nt
	global_load_dwordx2 v[166:167], v[162:163], off offset:3072 nt
	s_nop 0
	global_load_dwordx2 v[162:163], v[162:163], off offset:3584 nt
	v_and_b32_e32 v219, 0xffff0000, v191
	s_waitcnt vmcnt(7)
	s_waitcnt lgkmcnt(0)
	v_lshlrev_b32_e32 v220, 16, v192
	v_add_u32_e32 v183, -1, v182
	v_add_u32_e32 v184, 1, v182
	v_fma_f32 v185, -v183, v182, v60
	v_fma_f32 v186, -v184, v182, v60
	v_cmp_ge_f32_e64 s[14:15], 0, v185
	v_and_b32_e32 v221, 0xffff0000, v192
	v_lshlrev_b32_e32 v222, 16, v193
	v_cndmask_b32_e64 v182, v182, v183, s[14:15]
	v_cmp_lt_f32_e64 s[14:15], 0, v186
	v_and_b32_e32 v223, 0xffff0000, v193
	s_waitcnt vmcnt(5)
; #define GAS __attribute__((address_space(1)))
; #define LAS __attribute__((address_space(3)))
; __device__ __forceinline__ unsigned pk2(float lo, float hi) { return f2bf(lo) | (f2bf(hi) << 16); }
; __device__ __forceinline__ unsigned pk4_fp8(float a, float b, float c, float d) { int r = __builtin_amdgcn_cvt_pk_fp8_f32(a, b, 0, false); r = __builtin_amdgcn_cvt_pk_fp8_f32(c, d, r, true); return (unsigned)r; }
; template <int l>
; __device__ __forceinline__ void layer_phases(Frame& F, const XcdBarrier& bar, const int lo, const int hi) {
;     ...
;                     const float rstd = 1.f / sqrtf(wave_sum(s2) * (1.f / D) + LN_EPS);
; #pragma unroll
;                     for (int j = 0; j < 8; ++j) { const int k = 4 * lq + 256 * j;
;                         const f32x4 xv = v[j] * rstd * *(const GAS f32x4*)(g1 + k) + *(const GAS f32x4*)(b1 + k);
;                         { v2u xo; xo.x = pk2(xv.x, xv.y); xo.y = pk2(xv.z, xv.w); *(GAS v2u*)(x1 + (size_t)m * D + k) = xo; }
;                         const f32x4 hv = xv * (*(const GAS f32x4*)(mrow + 8192 + k) + 1.0f) + *(const GAS f32x4*)(mrow + 6144 + k);
;                         v2u o; o.x = pk2(hv.x, hv.y); o.y = pk2(hv.z, hv.w);
;                         *(GAS unsigned*)(h2q + (size_t)m * D + k) = pk4_fp8(hv.x, hv.y, hv.z, hv.w);
;                         const int chunk = (lq >> 1) + 32 * j;
;                         *(LAS v2u*)(h2s + rloc * 4096 + ((chunk ^ (rloc & 15)) << 4) + (lq & 1) * 8) = o; }
	s_waitcnt lgkmcnt(0)
	v_lshlrev_b32_e32 v226, 16, v174
	v_cndmask_b32_e64 v182, v182, v184, s[14:15]
	v_mul_f32_e32 v183, 0x37800000, v182
	v_cndmask_b32_e32 v182, v182, v183, vcc
	v_cmp_class_f32_e32 vcc, v60, v201
	v_and_b32_e32 v227, 0xffff0000, v174
	v_lshlrev_b32_e32 v174, 16, v175
	v_cndmask_b32_e32 v60, v182, v60, vcc
	v_div_scale_f32 v205, s[0:1], v60, v60, 1.0
	v_rcp_f32_e32 v214, v205
	global_load_dwordx2 v[188:189], v[158:159], off offset:2048 nt
	global_load_dwordx2 v[186:187], v[158:159], off offset:2560 nt
	global_load_dwordx2 v[182:183], v[158:159], off offset:3072 nt
	global_load_dwordx2 v[184:185], v[158:159], off offset:3584 nt
	v_div_scale_f32 v158, vcc, 1.0, v60, 1.0
	v_fma_f32 v159, -v205, v214, 1.0
	v_fmac_f32_e32 v214, v159, v214
	v_mul_f32_e32 v159, v158, v214
	v_fma_f32 v215, -v205, v159, v158
	v_fmac_f32_e32 v159, v215, v214
	v_fma_f32 v158, -v205, v159, v158
	v_div_fmas_f32 v158, v158, v214, v159
	v_div_fixup_f32 v60, v158, v60, 1.0
	v_pk_mul_f32 v[128:129], v[128:129], v[60:61] op_sel_hi:[1,0]
	v_pk_mul_f32 v[126:127], v[126:127], v[60:61] op_sel_hi:[1,0]
	v_pk_fma_f32 v[210:211], v[206:207], v[128:129], v[210:211]
	v_pk_fma_f32 v[158:159], v[208:209], v[126:127], v[212:213]
	v_bfe_u32 v126, v210, 16, 1
	v_bfe_u32 v128, v158, 16, 1
	v_bfe_u32 v127, v211, 16, 1
	v_bfe_u32 v129, v159, 16, 1
	v_add3_u32 v126, v210, v126, s86
	v_add3_u32 v128, v158, v128, s86
	v_add3_u32 v127, v211, v127, s86
	v_add3_u32 v129, v159, v129, s86
	v_lshrrev_b32_e32 v126, 16, v126
	v_lshrrev_b32_e32 v128, 16, v128
	v_and_or_b32 v126, v127, s82, v126
	v_and_or_b32 v127, v129, s82, v128
	global_store_dwordx2 v[160:161], v[126:127], off
	ds_read_b128 v[126:129], v252 offset:16384
	s_nop 0
	ds_read_b128 v[206:209], v252 offset:24576
	v_mov_b32_e32 v205, 0
	s_add_u32 s0, s48, s18
	s_addc_u32 s1, s49, s19
	v_pk_mul_f32 v[132:133], v[132:133], v[60:61] op_sel_hi:[1,0]
	v_pk_mul_f32 v[130:131], v[130:131], v[60:61] op_sel_hi:[1,0]
	v_pk_mul_f32 v[136:137], v[136:137], v[60:61] op_sel_hi:[1,0]
	v_pk_mul_f32 v[134:135], v[134:135], v[60:61] op_sel_hi:[1,0]
	v_pk_mul_f32 v[140:141], v[140:141], v[60:61] op_sel_hi:[1,0]
	v_pk_mul_f32 v[138:139], v[138:139], v[60:61] op_sel_hi:[1,0]
	v_pk_mul_f32 v[144:145], v[144:145], v[60:61] op_sel_hi:[1,0]
	v_pk_mul_f32 v[142:143], v[142:143], v[60:61] op_sel_hi:[1,0]
	v_pk_mul_f32 v[148:149], v[148:149], v[60:61] op_sel_hi:[1,0]
	v_pk_mul_f32 v[146:147], v[146:147], v[60:61] op_sel_hi:[1,0]
	v_pk_mul_f32 v[156:157], v[156:157], v[60:61] op_sel_hi:[1,0]
	v_pk_mul_f32 v[154:155], v[154:155], v[60:61] op_sel_hi:[1,0]
	v_lshlrev_b32_e32 v214, 16, v190
	v_and_b32_e32 v215, 0xffff0000, v190
	v_and_b32_e32 v175, 0xffff0000, v175
	s_waitcnt vmcnt(9)
	s_waitcnt lgkmcnt(0)
	v_lshlrev_b32_e32 v230, 16, v168
	v_and_b32_e32 v231, 0xffff0000, v168
	v_lshlrev_b32_e32 v168, 16, v169
	v_and_b32_e32 v169, 0xffff0000, v169
	v_lshlrev_b32_e32 v228, 16, v164
	v_and_b32_e32 v229, 0xffff0000, v164
	v_lshlrev_b32_e32 v164, 16, v165
	v_and_b32_e32 v165, 0xffff0000, v165
	s_waitcnt vmcnt(6)
	s_waitcnt lgkmcnt(0)
	v_lshlrev_b32_e32 v240, 16, v166
	v_and_b32_e32 v241, 0xffff0000, v166
	v_lshlrev_b32_e32 v242, 16, v167
	v_and_b32_e32 v243, 0xffff0000, v167
	s_waitcnt vmcnt(5)
	s_waitcnt lgkmcnt(0)
	v_lshlrev_b32_e32 v244, 16, v162
	v_and_b32_e32 v245, 0xffff0000, v162
	v_lshlrev_b32_e32 v246, 16, v163
	v_and_b32_e32 v247, 0xffff0000, v163
	v_lshlrev_b32_e32 v232, 16, v178
	v_and_b32_e32 v233, 0xffff0000, v178
	v_lshlrev_b32_e32 v236, 16, v172
	v_and_b32_e32 v237, 0xffff0000, v172
	v_lshlrev_b32_e32 v172, 16, v173
	v_and_b32_e32 v173, 0xffff0000, v173
	v_pk_mul_f32 v[22:23], v[22:23], v[174:175]
	v_pk_mul_f32 v[18:19], v[18:19], v[168:169]
	v_pk_mul_f32 v[16:17], v[16:17], v[230:231]
	v_lshlrev_b32_e32 v224, 16, v176
	v_and_b32_e32 v225, 0xffff0000, v176
	v_lshlrev_b32_e32 v176, 16, v177
	v_and_b32_e32 v177, 0xffff0000, v177
	v_pk_mul_f32 v[28:29], v[28:29], v[220:221]
	s_waitcnt vmcnt(4)
	s_waitcnt lgkmcnt(0)
	v_lshlrev_b32_e32 v234, 16, v188
	v_and_b32_e32 v235, 0xffff0000, v188
	s_waitcnt vmcnt(2)
	s_waitcnt lgkmcnt(0)
	v_lshlrev_b32_e32 v166, 16, v182
	v_and_b32_e32 v167, 0xffff0000, v182
	v_lshlrev_b32_e32 v182, 16, v183
	v_and_b32_e32 v183, 0xffff0000, v183
	s_waitcnt vmcnt(1)
	s_waitcnt lgkmcnt(0)
	v_lshlrev_b32_e32 v162, 16, v184
	v_and_b32_e32 v163, 0xffff0000, v184
	v_pk_mul_f32 v[6:7], v[6:7], v[182:183]
	v_pk_mul_f32 v[182:183], v[0:1], v[162:163]
	v_lshlrev_b32_e32 v184, 16, v185
	v_and_b32_e32 v185, 0xffff0000, v185
	v_pk_mul_f32 v[184:185], v[2:3], v[184:185]
	v_lshlrev_b32_e32 v238, 16, v186
	v_and_b32_e32 v239, 0xffff0000, v186
	v_lshlrev_b32_e32 v186, 16, v187
	v_and_b32_e32 v187, 0xffff0000, v187
	v_pk_mul_f32 v[12:13], v[12:13], v[234:235]
	v_pk_mul_f32 v[10:11], v[10:11], v[186:187]
	v_pk_mul_f32 v[4:5], v[4:5], v[166:167]
	v_pk_fma_f32 v[162:163], v[164:165], s[38:39], v[18:19] op_sel_hi:[1,0,1]
	v_pk_fma_f32 v[164:165], v[228:229], s[38:39], v[16:17] op_sel_hi:[1,0,1]
	v_pk_mul_f32 v[30:31], v[30:31], v[222:223]
	v_lshlrev_b32_e32 v188, 16, v189
	v_and_b32_e32 v189, 0xffff0000, v189
	v_pk_mul_f32 v[174:175], v[20:21], v[226:227]
	v_pk_fma_f32 v[20:21], v[218:219], s[38:39], v[30:31] op_sel_hi:[1,0,1]
	v_lshlrev_b32_e32 v178, 16, v179
	v_and_b32_e32 v179, 0xffff0000, v179
	v_pk_mul_f32 v[14:15], v[14:15], v[188:189]
	s_waitcnt lgkmcnt(0)
	v_pk_add_f32 v[126:127], v[126:127], 1.0 op_sel_hi:[1,0]
	v_pk_add_f32 v[128:129], v[128:129], 1.0 op_sel_hi:[1,0]
	s_waitcnt lgkmcnt(0)
; #define GAS __attribute__((address_space(1)))
; #define LAS __attribute__((address_space(3)))
; __device__ __forceinline__ unsigned pk2(float lo, float hi) { return f2bf(lo) | (f2bf(hi) << 16); }
; __device__ __forceinline__ unsigned pk4_fp8(float a, float b, float c, float d) { int r = __builtin_amdgcn_cvt_pk_fp8_f32(a, b, 0, false); r = __builtin_amdgcn_cvt_pk_fp8_f32(c, d, r, true); return (unsigned)r; }
; template <int l>
; __device__ __forceinline__ void layer_phases(Frame& F, const XcdBarrier& bar, const int lo, const int hi) {
;     ...
;                     for (int j = 0; j < 8; ++j) { const int k = 4 * lq + 256 * j;
;                         const f32x4 xv = v[j] * rstd * *(const GAS f32x4*)(g1 + k) + *(const GAS f32x4*)(b1 + k);
;                         { v2u xo; xo.x = pk2(xv.x, xv.y); xo.y = pk2(xv.z, xv.w); *(GAS v2u*)(x1 + (size_t)m * D + k) = xo; }
;                         const f32x4 hv = xv * (*(const GAS f32x4*)(mrow + 8192 + k) + 1.0f) + *(const GAS f32x4*)(mrow + 6144 + k);
;                         v2u o; o.x = pk2(hv.x, hv.y); o.y = pk2(hv.z, hv.w);
;                         *(GAS unsigned*)(h2q + (size_t)m * D + k) = pk4_fp8(hv.x, hv.y, hv.z, hv.w);
;                         const int chunk = (lq >> 1) + 32 * j;
;                         *(LAS v2u*)(h2s + rloc * 4096 + ((chunk ^ (rloc & 15)) << 4) + (lq & 1) * 8) = o; }
	v_pk_fma_f32 v[126:127], v[126:127], v[210:211], v[206:207]
	v_pk_fma_f32 v[128:129], v[128:129], v[158:159], v[208:209]
	v_cvt_pk_fp8_f32 v205, v126, v127
	v_lshl_add_u64 v[158:159], s[0:1], 0, v[36:37]
	v_pk_mul_f32 v[8:9], v[8:9], v[238:239]
	s_lshl_b64 s[0:1], s[46:47], 12
	v_cvt_pk_fp8_f32 v205, v128, v129 op_sel:[0,0,1]
	s_add_u32 s0, s3, s0
	s_addc_u32 s1, s39, s1
	global_store_dword v[158:159], v205, off
	ds_read_b128 v[206:209], v252 offset:9216
	ds_read_b128 v[210:213], v252 offset:1024
	v_mov_b32_e32 v205, 0
	s_waitcnt lgkmcnt(0)
	v_pk_fma_f32 v[212:213], v[208:209], v[130:131], v[212:213]
	v_pk_fma_f32 v[210:211], v[206:207], v[132:133], v[210:211]
	v_bfe_u32 v132, v212, 16, 1
	v_bfe_u32 v130, v210, 16, 1
	v_bfe_u32 v131, v211, 16, 1
	v_bfe_u32 v133, v213, 16, 1
	v_add3_u32 v130, v210, v130, s86
	v_add3_u32 v132, v212, v132, s86
	v_add3_u32 v131, v211, v131, s86
	v_add3_u32 v133, v213, v133, s86
	v_lshrrev_b32_e32 v130, 16, v130
	v_lshrrev_b32_e32 v132, 16, v132
	v_and_or_b32 v130, v131, s82, v130
	v_and_or_b32 v131, v133, s82, v132
	global_store_dwordx2 v[160:161], v[130:131], off offset:512
	ds_read_b128 v[130:133], v252 offset:17408
	s_nop 0
	ds_read_b128 v[206:209], v252 offset:25600
	s_waitcnt lgkmcnt(0)
	v_pk_add_f32 v[130:131], v[130:131], 1.0 op_sel_hi:[1,0]
	s_waitcnt lgkmcnt(0)
	v_pk_fma_f32 v[130:131], v[130:131], v[210:211], v[206:207]
	v_pk_add_f32 v[132:133], v[132:133], 1.0 op_sel_hi:[1,0]
	v_cvt_pk_fp8_f32 v205, v130, v131
	v_pk_fma_f32 v[132:133], v[132:133], v[212:213], v[208:209]
	s_nop 0
	v_cvt_pk_fp8_f32 v205, v132, v133 op_sel:[0,0,1]
	global_store_dword v[158:159], v205, off offset:256
	ds_read_b128 v[206:209], v252 offset:10240
	ds_read_b128 v[210:213], v252 offset:2048
	v_mov_b32_e32 v205, 0
	s_waitcnt lgkmcnt(0)
	v_pk_fma_f32 v[212:213], v[208:209], v[134:135], v[212:213]
	v_pk_fma_f32 v[210:211], v[206:207], v[136:137], v[210:211]
	v_bfe_u32 v136, v212, 16, 1
	v_bfe_u32 v134, v210, 16, 1
	v_bfe_u32 v135, v211, 16, 1
	v_bfe_u32 v137, v213, 16, 1
	v_add3_u32 v134, v210, v134, s86
	v_add3_u32 v136, v212, v136, s86
	v_add3_u32 v135, v211, v135, s86
	v_add3_u32 v137, v213, v137, s86
	v_lshrrev_b32_e32 v134, 16, v134
	v_lshrrev_b32_e32 v136, 16, v136
	v_and_or_b32 v134, v135, s82, v134
	v_and_or_b32 v135, v137, s82, v136
	global_store_dwordx2 v[160:161], v[134:135], off offset:1024
	ds_read_b128 v[134:137], v252 offset:18432
	s_nop 0
	ds_read_b128 v[206:209], v252 offset:26624
	s_waitcnt lgkmcnt(0)
	v_pk_add_f32 v[134:135], v[134:135], 1.0 op_sel_hi:[1,0]
	s_waitcnt lgkmcnt(0)
	v_pk_fma_f32 v[134:135], v[134:135], v[210:211], v[206:207]
	v_pk_add_f32 v[136:137], v[136:137], 1.0 op_sel_hi:[1,0]
	v_cvt_pk_fp8_f32 v205, v134, v135
	v_pk_fma_f32 v[136:137], v[136:137], v[212:213], v[208:209]
	s_nop 0
	v_cvt_pk_fp8_f32 v205, v136, v137 op_sel:[0,0,1]
	global_store_dword v[158:159], v205, off offset:512
	ds_read_b128 v[206:209], v252 offset:11264
	ds_read_b128 v[210:213], v252 offset:3072
	v_mov_b32_e32 v205, 0
	s_waitcnt lgkmcnt(0)
	v_pk_fma_f32 v[212:213], v[138:139], v[208:209], v[212:213]
	v_pk_fma_f32 v[210:211], v[140:141], v[206:207], v[210:211]
	v_bfe_u32 v140, v212, 16, 1
	v_bfe_u32 v138, v210, 16, 1
	v_bfe_u32 v139, v211, 16, 1
	v_bfe_u32 v141, v213, 16, 1
	v_add3_u32 v138, v210, v138, s86
	v_add3_u32 v140, v212, v140, s86
	v_add3_u32 v139, v211, v139, s86
	v_add3_u32 v141, v213, v141, s86
	v_lshrrev_b32_e32 v138, 16, v138
	v_lshrrev_b32_e32 v140, 16, v140
	v_and_or_b32 v138, v139, s82, v138
	v_and_or_b32 v139, v141, s82, v140
	global_store_dwordx2 v[160:161], v[138:139], off offset:1536
	ds_read_b128 v[138:141], v252 offset:19456
	s_nop 0
	ds_read_b128 v[206:209], v252 offset:27648
	s_waitcnt lgkmcnt(0)
	v_pk_add_f32 v[138:139], v[138:139], 1.0 op_sel_hi:[1,0]
	s_waitcnt lgkmcnt(0)
	v_pk_fma_f32 v[138:139], v[210:211], v[138:139], v[206:207]
	v_pk_add_f32 v[140:141], v[140:141], 1.0 op_sel_hi:[1,0]
	v_cvt_pk_fp8_f32 v205, v138, v139
	v_pk_fma_f32 v[140:141], v[212:213], v[140:141], v[208:209]
	s_nop 0
	v_cvt_pk_fp8_f32 v205, v140, v141 op_sel:[0,0,1]
	global_store_dword v[158:159], v205, off offset:768
	ds_read_b128 v[206:209], v252 offset:12288
	ds_read_b128 v[210:213], v252 offset:4096
	v_mov_b32_e32 v205, 0
	s_waitcnt lgkmcnt(0)
	v_pk_fma_f32 v[212:213], v[142:143], v[208:209], v[212:213]
	v_pk_fma_f32 v[210:211], v[144:145], v[206:207], v[210:211]
	v_bfe_u32 v144, v212, 16, 1
	v_bfe_u32 v142, v210, 16, 1
	v_bfe_u32 v143, v211, 16, 1
	v_bfe_u32 v145, v213, 16, 1
	v_add3_u32 v142, v210, v142, s86
	v_add3_u32 v144, v212, v144, s86
	v_add3_u32 v143, v211, v143, s86
	v_add3_u32 v145, v213, v145, s86
	v_lshrrev_b32_e32 v142, 16, v142
	v_lshrrev_b32_e32 v144, 16, v144
	v_and_or_b32 v142, v143, s82, v142
	v_and_or_b32 v143, v145, s82, v144
	global_store_dwordx2 v[160:161], v[142:143], off offset:2048
	ds_read_b128 v[142:145], v252 offset:20480
	s_nop 0
	ds_read_b128 v[206:209], v252 offset:28672
	s_waitcnt lgkmcnt(0)
	v_pk_add_f32 v[142:143], v[142:143], 1.0 op_sel_hi:[1,0]
	s_waitcnt lgkmcnt(0)
	v_pk_fma_f32 v[142:143], v[210:211], v[142:143], v[206:207]
	v_pk_add_f32 v[144:145], v[144:145], 1.0 op_sel_hi:[1,0]
	v_cvt_pk_fp8_f32 v205, v142, v143
	v_pk_fma_f32 v[144:145], v[212:213], v[144:145], v[208:209]
	s_nop 0
	v_cvt_pk_fp8_f32 v205, v144, v145 op_sel:[0,0,1]
	global_store_dword v[158:159], v205, off offset:1024
	ds_read_b128 v[206:209], v252 offset:13312
	ds_read_b128 v[210:213], v252 offset:5120
	v_mov_b32_e32 v205, 0
	s_waitcnt lgkmcnt(0)
; #define GAS __attribute__((address_space(1)))
; #define LAS __attribute__((address_space(3)))
; __device__ __forceinline__ unsigned pk2(float lo, float hi) { return f2bf(lo) | (f2bf(hi) << 16); }
; __device__ __forceinline__ unsigned pk4_fp8(float a, float b, float c, float d) { int r = __builtin_amdgcn_cvt_pk_fp8_f32(a, b, 0, false); r = __builtin_amdgcn_cvt_pk_fp8_f32(c, d, r, true); return (unsigned)r; }
; template <int l>
; __device__ __forceinline__ void layer_phases(Frame& F, const XcdBarrier& bar, const int lo, const int hi) {
;     ...
;                     f32x4 (&v)[8] = vv[rq]; float s = 0.f;
; #pragma unroll
;                     for (int j = 0; j < 8; ++j) s += (v[j].x + v[j].y) + (v[j].z + v[j].w);
;                     const float mean = wave_sum(s) * (1.f / D); float s2 = 0.f;
;     ...
;                     for (int j = 0; j < 8; ++j) { const int k = 4 * lq + 256 * j;
;                         const f32x4 xv = v[j] * rstd * *(const GAS f32x4*)(g1 + k) + *(const GAS f32x4*)(b1 + k);
;                         { v2u xo; xo.x = pk2(xv.x, xv.y); xo.y = pk2(xv.z, xv.w); *(GAS v2u*)(x1 + (size_t)m * D + k) = xo; }
;                         const f32x4 hv = xv * (*(const GAS f32x4*)(mrow + 8192 + k) + 1.0f) + *(const GAS f32x4*)(mrow + 6144 + k);
;                         v2u o; o.x = pk2(hv.x, hv.y); o.y = pk2(hv.z, hv.w);
;                         *(GAS unsigned*)(h2q + (size_t)m * D + k) = pk4_fp8(hv.x, hv.y, hv.z, hv.w);
;                         const int chunk = (lq >> 1) + 32 * j;
;                         *(LAS v2u*)(h2s + rloc * 4096 + ((chunk ^ (rloc & 15)) << 4) + (lq & 1) * 8) = o; }
	v_pk_fma_f32 v[212:213], v[146:147], v[208:209], v[212:213]
	v_pk_fma_f32 v[210:211], v[148:149], v[206:207], v[210:211]
	v_bfe_u32 v148, v212, 16, 1
	v_bfe_u32 v146, v210, 16, 1
	v_bfe_u32 v147, v211, 16, 1
	v_bfe_u32 v149, v213, 16, 1
	v_add3_u32 v146, v210, v146, s86
	v_add3_u32 v148, v212, v148, s86
	v_add3_u32 v147, v211, v147, s86
	v_add3_u32 v149, v213, v149, s86
	v_lshrrev_b32_e32 v146, 16, v146
	v_lshrrev_b32_e32 v148, 16, v148
	v_and_or_b32 v146, v147, s82, v146
	v_and_or_b32 v147, v149, s82, v148
	global_store_dwordx2 v[160:161], v[146:147], off offset:2560
	ds_read_b128 v[146:149], v252 offset:21504
	s_nop 0
	ds_read_b128 v[206:209], v252 offset:29696
	s_waitcnt lgkmcnt(0)
	v_pk_add_f32 v[146:147], v[146:147], 1.0 op_sel_hi:[1,0]
	s_waitcnt lgkmcnt(0)
	v_pk_fma_f32 v[146:147], v[210:211], v[146:147], v[206:207]
	v_pk_add_f32 v[148:149], v[148:149], 1.0 op_sel_hi:[1,0]
	v_cvt_pk_fp8_f32 v205, v146, v147
	v_pk_fma_f32 v[148:149], v[212:213], v[148:149], v[208:209]
	s_nop 0
	v_cvt_pk_fp8_f32 v205, v148, v149 op_sel:[0,0,1]
	global_store_dword v[158:159], v205, off offset:1280
	ds_read_b128 v[206:209], v252 offset:14336
	ds_read_b128 v[210:213], v252 offset:6144
	v_mov_b32_e32 v205, 0
	s_waitcnt lgkmcnt(0)
	v_pk_fma_f32 v[208:209], v[154:155], v[208:209], v[212:213]
	v_pk_fma_f32 v[206:207], v[156:157], v[206:207], v[210:211]
	v_bfe_u32 v156, v208, 16, 1
	v_bfe_u32 v154, v206, 16, 1
	v_bfe_u32 v155, v207, 16, 1
	v_bfe_u32 v157, v209, 16, 1
	v_add3_u32 v154, v206, v154, s86
	v_add3_u32 v156, v208, v156, s86
	v_add3_u32 v155, v207, v155, s86
	v_add3_u32 v157, v209, v157, s86
	v_lshrrev_b32_e32 v154, 16, v154
	v_lshrrev_b32_e32 v156, 16, v156
	v_and_or_b32 v154, v155, s82, v154
	v_and_or_b32 v155, v157, s82, v156
	global_store_dwordx2 v[160:161], v[154:155], off offset:3072
	ds_read_b128 v[154:157], v252 offset:22528
	s_nop 0
	ds_read_b128 v[190:193], v252 offset:30720
	v_lshlrev_b32_e32 v212, 16, v170
	v_and_b32_e32 v213, 0xffff0000, v170
	v_lshlrev_b32_e32 v170, 16, v171
	v_and_b32_e32 v171, 0xffff0000, v171
	v_pk_fma_f32 v[166:167], v[170:171], s[38:39], v[22:23] op_sel_hi:[1,0,1]
	v_lshlrev_b32_e32 v210, 16, v180
	v_and_b32_e32 v211, 0xffff0000, v180
	v_lshlrev_b32_e32 v180, 16, v181
	v_and_b32_e32 v181, 0xffff0000, v181
	v_pk_mul_f32 v[26:27], v[26:27], v[180:181]
	v_pk_mul_f32 v[180:181], v[24:25], v[210:211]
	v_pk_fma_f32 v[24:25], v[214:215], s[38:39], v[28:29] op_sel_hi:[1,0,1]
	v_pk_fma_f32 v[28:29], v[176:177], s[38:39], v[26:27] op_sel_hi:[1,0,1]
	v_pk_fma_f32 v[30:31], v[224:225], s[38:39], v[180:181] op_sel_hi:[1,0,1]
	v_pk_fma_f32 v[168:169], v[212:213], s[38:39], v[174:175] op_sel_hi:[1,0,1]
	v_mov_b32_e32 v22, v24
	v_mov_b32_e32 v23, v30
	v_mov_b32_e32 v26, v25
	v_mov_b32_e32 v27, v31
	v_mov_b32_e32 v174, v20
	v_mov_b32_e32 v175, v28
	v_mov_b32_e32 v176, v21
	v_mov_b32_e32 v177, v29
	v_mov_b32_e32 v180, v168
	v_mov_b32_e32 v181, v167
	v_pk_add_f32 v[22:23], v[22:23], v[26:27]
	v_pk_add_f32 v[26:27], v[174:175], v[176:177]
	s_waitcnt lgkmcnt(0)
	v_pk_add_f32 v[0:1], v[154:155], 1.0 op_sel_hi:[1,0]
	s_waitcnt lgkmcnt(0)
	v_pk_fma_f32 v[0:1], v[206:207], v[0:1], v[190:191]
	v_pk_add_f32 v[2:3], v[156:157], 1.0 op_sel_hi:[1,0]
	v_cvt_pk_fp8_f32 v205, v0, v1
	v_pk_fma_f32 v[2:3], v[208:209], v[2:3], v[192:193]
	v_pk_fma_f32 v[156:157], v[232:233], s[38:39], v[12:13] op_sel_hi:[1,0,1]
	v_pk_fma_f32 v[12:13], v[172:173], s[38:39], v[10:11] op_sel_hi:[1,0,1]
	v_cvt_pk_fp8_f32 v205, v2, v3 op_sel:[0,0,1]
	v_pk_fma_f32 v[154:155], v[178:179], s[38:39], v[14:15] op_sel_hi:[1,0,1]
	v_pk_mov_b32 v[178:179], v[168:169], v[166:167] op_sel:[1,0]
	v_pk_add_f32 v[22:23], v[22:23], v[26:27]
	global_store_dword v[158:159], v205, off offset:1536
	ds_read_b128 v[16:19], v252 offset:15360
	ds_read_b128 v[170:173], v252 offset:7168
	v_pk_add_f32 v[174:175], v[178:179], v[180:181]
	v_add_f32_e32 v22, 0, v22
	v_pk_add_f32 v[26:27], v[174:175], v[174:175] op_sel:[0,1] op_sel_hi:[1,0]
	v_pk_fma_f32 v[14:15], v[236:237], s[38:39], v[8:9] op_sel_hi:[1,0,1]
	v_pk_fma_f32 v[8:9], v[242:243], s[38:39], v[6:7] op_sel_hi:[1,0,1]
	v_pk_fma_f32 v[10:11], v[240:241], s[38:39], v[4:5] op_sel_hi:[1,0,1]
	v_pk_fma_f32 v[4:5], v[246:247], s[38:39], v[184:185] op_sel_hi:[1,0,1]
	v_pk_fma_f32 v[6:7], v[244:245], s[38:39], v[182:183] op_sel_hi:[1,0,1]
	v_add_f32_e32 v182, v164, v165
	v_add_f32_e32 v184, v162, v163
	v_mov_b32_e32 v187, v156
	v_mov_b32_e32 v183, v154
	v_mov_b32_e32 v185, v155
	v_mov_b32_e32 v27, v157
	v_add_f32_e32 v186, v22, v23
	v_pk_mov_b32 v[188:189], v[14:15], v[12:13] op_sel:[1,0]
	v_mov_b32_e32 v190, v14
	v_mov_b32_e32 v191, v13
	v_pk_add_f32 v[176:177], v[182:183], v[184:185]
	v_pk_add_f32 v[22:23], v[186:187], v[26:27]
	v_pk_add_f32 v[178:179], v[188:189], v[190:191]
	v_pk_add_f32 v[22:23], v[22:23], v[176:177]
	v_pk_add_f32 v[174:175], v[178:179], v[178:179] op_sel:[0,1] op_sel_hi:[1,0]
	v_pk_add_f32 v[22:23], v[22:23], v[22:23] op_sel:[0,1] op_sel_hi:[1,0]
	v_add_f32_e32 v192, v10, v11
	v_add_f32_e32 v206, v8, v9
	v_mov_b32_e32 v193, v4
	v_mov_b32_e32 v207, v5
	v_mov_b32_e32 v175, v7
	v_mov_b32_e32 v23, v6
	v_pk_add_f32 v[180:181], v[192:193], v[206:207]
	v_pk_add_f32 v[22:23], v[22:23], v[174:175]
	v_pk_mul_f32 v[26:27], v[150:151], v[60:61] op_sel_hi:[1,0]
	v_pk_add_f32 v[22:23], v[22:23], v[180:181]
	v_mov_b32_e32 v189, 0
	v_add_f32_e32 v22, v22, v23
	ds_bpermute_b32 v23, v53, v22
	s_waitcnt lgkmcnt(0)
	v_add_f32_e32 v22, v22, v23
	ds_bpermute_b32 v23, v194, v22
	s_waitcnt lgkmcnt(0)
	v_add_f32_e32 v22, v22, v23
	ds_bpermute_b32 v23, v195, v22
	s_waitcnt lgkmcnt(0)
	v_add_f32_e32 v22, v22, v23
	ds_bpermute_b32 v23, v196, v22
	s_waitcnt lgkmcnt(0)
; #define GAS __attribute__((address_space(1)))
; #define LAS __attribute__((address_space(3)))
; __device__ __forceinline__ unsigned pk2(float lo, float hi) { return f2bf(lo) | (f2bf(hi) << 16); }
; __device__ __forceinline__ unsigned pk4_fp8(float a, float b, float c, float d) { int r = __builtin_amdgcn_cvt_pk_fp8_f32(a, b, 0, false); r = __builtin_amdgcn_cvt_pk_fp8_f32(c, d, r, true); return (unsigned)r; }
; template <int l>
; __device__ __forceinline__ void layer_phases(Frame& F, const XcdBarrier& bar, const int lo, const int hi) {
;     ...
;                     const float mean = wave_sum(s) * (1.f / D); float s2 = 0.f;
; #pragma unroll
;                     for (int j = 0; j < 8; ++j) { v[j] = v[j] - mean; s2 += (v[j].x * v[j].x + v[j].y * v[j].y) + (v[j].z * v[j].z + v[j].w * v[j].w); }
;                     const float rstd = 1.f / sqrtf(wave_sum(s2) * (1.f / D) + LN_EPS);
; #pragma unroll
;                     for (int j = 0; j < 8; ++j) { const int k = 4 * lq + 256 * j;
;                         const f32x4 xv = v[j] * rstd * *(const GAS f32x4*)(g1 + k) + *(const GAS f32x4*)(b1 + k);
;                         { v2u xo; xo.x = pk2(xv.x, xv.y); xo.y = pk2(xv.z, xv.w); *(GAS v2u*)(x1 + (size_t)m * D + k) = xo; }
;                         const f32x4 hv = xv * (*(const GAS f32x4*)(mrow + 8192 + k) + 1.0f) + *(const GAS f32x4*)(mrow + 6144 + k);
;                         v2u o; o.x = pk2(hv.x, hv.y); o.y = pk2(hv.z, hv.w);
;                         *(GAS unsigned*)(h2q + (size_t)m * D + k) = pk4_fp8(hv.x, hv.y, hv.z, hv.w);
;                         const int chunk = (lq >> 1) + 32 * j;
;                         *(LAS v2u*)(h2s + rloc * 4096 + ((chunk ^ (rloc & 15)) << 4) + (lq & 1) * 8) = o; }
	v_add_f32_e32 v22, v22, v23
	ds_bpermute_b32 v23, v197, v22
	s_waitcnt lgkmcnt(0)
	v_add_f32_e32 v174, v22, v23
	v_pk_mul_f32 v[22:23], v[152:153], v[60:61] op_sel_hi:[1,0]
	ds_bpermute_b32 v60, v198, v174
	s_waitcnt lgkmcnt(0)
	v_add_f32_e32 v60, v174, v60
	v_fmamk_f32 v15, v60, 0xba000000, v15
	v_fmac_f32_e32 v14, 0xba000000, v60
	v_fmamk_f32 v13, v60, 0xba000000, v13
	v_fmac_f32_e32 v12, 0xba000000, v60
	v_fmac_f32_e32 v10, 0xba000000, v60
	v_fmac_f32_e32 v8, 0xba000000, v60
	s_waitcnt lgkmcnt(0)
	v_pk_fma_f32 v[26:27], v[26:27], v[18:19], v[172:173]
	v_pk_fma_f32 v[22:23], v[22:23], v[16:17], v[170:171]
	v_bfe_u32 v18, v26, 16, 1
	v_bfe_u32 v16, v22, 16, 1
	v_bfe_u32 v17, v23, 16, 1
	v_bfe_u32 v19, v27, 16, 1
	v_add3_u32 v16, v22, v16, s86
	v_add3_u32 v18, v26, v18, s86
	v_add3_u32 v17, v23, v17, s86
	v_add3_u32 v19, v27, v19, s86
	v_lshrrev_b32_e32 v16, 16, v16
	v_lshrrev_b32_e32 v18, 16, v18
	v_and_or_b32 v16, v17, s82, v16
	v_and_or_b32 v17, v19, s82, v18
	global_store_dwordx2 v[160:161], v[16:17], off offset:3584
	ds_read_b128 v[16:19], v252 offset:23552
	s_nop 0
	ds_read_b128 v[150:153], v252 offset:31744
	v_fmamk_f32 v11, v60, 0xba000000, v11
	v_fmamk_f32 v9, v60, 0xba000000, v9
	v_pk_mul_f32 v[182:183], v[12:13], v[12:13]
	v_pk_mul_f32 v[184:185], v[14:15], v[14:15]
	v_mul_f32_e32 v186, v10, v10
	v_mul_f32_e32 v188, v8, v8
	v_pk_mov_b32 v[192:193], v[184:185], v[182:183] op_sel:[1,0]
	v_mov_b32_e32 v185, v183
	v_pk_fma_f32 v[182:183], v[10:11], v[10:11], v[186:187] op_sel_hi:[1,1,0]
	v_pk_fma_f32 v[186:187], v[8:9], v[8:9], v[188:189] op_sel_hi:[1,1,0]
	v_fmamk_f32 v21, v60, 0xba000000, v21
	v_fmamk_f32 v25, v60, 0xba000000, v25
	v_fmamk_f32 v29, v60, 0xba000000, v29
	v_fmamk_f32 v31, v60, 0xba000000, v31
	v_fmac_f32_e32 v20, 0xba000000, v60
	v_fmac_f32_e32 v24, 0xba000000, v60
	v_fmac_f32_e32 v28, 0xba000000, v60
	v_fmac_f32_e32 v30, 0xba000000, v60
	v_fmamk_f32 v169, v60, 0xba000000, v169
	v_fmac_f32_e32 v168, 0xba000000, v60
	v_fmamk_f32 v167, v60, 0xba000000, v167
	v_fmac_f32_e32 v166, 0xba000000, v60
	v_mov_b32_e32 v170, v25
	v_mov_b32_e32 v171, v31
	v_mov_b32_e32 v174, v21
	v_mov_b32_e32 v175, v29
	v_mov_b32_e32 v160, v24
	v_mov_b32_e32 v161, v30
	v_mov_b32_e32 v172, v20
	v_mov_b32_e32 v173, v28
	v_pk_mul_f32 v[176:177], v[166:167], v[166:167]
	v_pk_mul_f32 v[178:179], v[168:169], v[168:169]
	v_pk_mul_f32 v[170:171], v[170:171], v[170:171]
	v_pk_mul_f32 v[174:175], v[174:175], v[174:175]
	v_pk_mov_b32 v[190:191], v[178:179], v[176:177] op_sel:[1,0]
	v_mov_b32_e32 v179, v177
	v_pk_fma_f32 v[160:161], v[160:161], v[160:161], v[170:171]
	v_pk_fma_f32 v[170:171], v[172:173], v[172:173], v[174:175]
	v_pk_add_f32 v[172:173], v[190:191], v[178:179]
	v_pk_add_f32 v[160:161], v[160:161], v[170:171]
	v_fmamk_f32 v155, v60, 0xba000000, v155
	v_fmac_f32_e32 v154, 0xba000000, v60
	v_pk_add_f32 v[170:171], v[172:173], v[172:173] op_sel_hi:[0,1]
	v_pk_add_f32 v[160:161], v[160:161], v[160:161] op_sel_hi:[0,1]
	v_mul_f32_e32 v170, v154, v154
	v_mul_f32_e32 v160, v155, v155
	v_fmac_f32_e32 v164, 0xba000000, v60
	v_fmac_f32_e32 v162, 0xba000000, v60
	v_fmamk_f32 v165, v60, 0xba000000, v165
	v_fmamk_f32 v163, v60, 0xba000000, v163
	v_fmamk_f32 v157, v60, 0xba000000, v157
	v_fmac_f32_e32 v156, 0xba000000, v60
	v_fmamk_f32 v5, v60, 0xba000000, v5
	v_fmac_f32_e32 v4, 0xba000000, v60
	v_fmamk_f32 v7, v60, 0xba000000, v7
	v_fmac_f32_e32 v6, 0xba000000, v60
	v_mul_f32_e32 v60, v164, v164
	v_mul_f32_e32 v180, v162, v162
	v_pk_fma_f32 v[176:177], v[164:165], v[164:165], v[60:61] op_sel_hi:[1,1,0]
	v_pk_fma_f32 v[180:181], v[162:163], v[162:163], v[180:181] op_sel_hi:[1,1,0]
	v_mul_f32_e32 v176, v156, v156
	v_mul_f32_e32 v180, v157, v157
	v_pk_add_f32 v[172:173], v[176:177], v[180:181]
	v_pk_add_f32 v[174:175], v[192:193], v[184:185]
	v_mul_f32_e32 v182, v6, v6
	v_pk_add_f32 v[174:175], v[174:175], v[174:175] op_sel_hi:[0,1]
	v_mul_f32_e32 v186, v7, v7
	v_mul_f32_e32 v174, v4, v4
	v_pk_add_f32 v[176:177], v[182:183], v[186:187]
	s_waitcnt lgkmcnt(0)
	v_pk_add_f32 v[16:17], v[16:17], 1.0 op_sel_hi:[1,0]
	s_waitcnt lgkmcnt(0)
	v_pk_fma_f32 v[16:17], v[22:23], v[16:17], v[150:151]
	v_pk_add_f32 v[18:19], v[18:19], 1.0 op_sel_hi:[1,0]
	v_cvt_pk_fp8_f32 v189, v16, v17
	v_pk_fma_f32 v[18:19], v[26:27], v[18:19], v[152:153]
	v_pk_add_f32 v[22:23], v[170:171], v[160:161]
	v_cvt_pk_fp8_f32 v189, v18, v19 op_sel:[0,0,1]
	v_pk_add_f32 v[22:23], v[172:173], v[22:23]
	global_store_dword v[158:159], v189, off offset:1792
	ds_read_b128 v[150:153], v252 offset:8192
	s_nop 0
	ds_read_b128 v[158:161], v252 offset:0
	v_pk_add_f32 v[22:23], v[22:23], v[22:23] op_sel_hi:[0,1]
	v_mul_f32_e32 v22, v5, v5
	v_pk_add_f32 v[22:23], v[174:175], v[22:23]
	s_nop 0
	v_pk_add_f32 v[22:23], v[176:177], v[22:23]
	s_nop 0
	v_add_f32_e32 v22, v22, v23
	ds_bpermute_b32 v23, v53, v22
	s_waitcnt lgkmcnt(0)
	v_add_f32_e32 v22, v22, v23
	ds_bpermute_b32 v23, v194, v22
	s_waitcnt lgkmcnt(0)
	v_add_f32_e32 v22, v22, v23
	ds_bpermute_b32 v23, v195, v22
	s_waitcnt lgkmcnt(0)
	v_add_f32_e32 v22, v22, v23
	ds_bpermute_b32 v23, v196, v22
	s_waitcnt lgkmcnt(0)
	v_add_f32_e32 v22, v22, v23
	ds_bpermute_b32 v23, v197, v22
	s_waitcnt lgkmcnt(0)
	v_add_f32_e32 v22, v22, v23
	ds_bpermute_b32 v23, v198, v22
	s_waitcnt lgkmcnt(0)
; #define GAS __attribute__((address_space(1)))
; #define LAS __attribute__((address_space(3)))
; __device__ __forceinline__ unsigned pk2(float lo, float hi) { return f2bf(lo) | (f2bf(hi) << 16); }
; __device__ __forceinline__ unsigned pk4_fp8(float a, float b, float c, float d) { int r = __builtin_amdgcn_cvt_pk_fp8_f32(a, b, 0, false); r = __builtin_amdgcn_cvt_pk_fp8_f32(c, d, r, true); return (unsigned)r; }
; template <int l>
; __device__ __forceinline__ void layer_phases(Frame& F, const XcdBarrier& bar, const int lo, const int hi) {
;     ...
;                     const float rstd = 1.f / sqrtf(wave_sum(s2) * (1.f / D) + LN_EPS);
; #pragma unroll
;                     for (int j = 0; j < 8; ++j) { const int k = 4 * lq + 256 * j;
;                         const f32x4 xv = v[j] * rstd * *(const GAS f32x4*)(g1 + k) + *(const GAS f32x4*)(b1 + k);
;                         { v2u xo; xo.x = pk2(xv.x, xv.y); xo.y = pk2(xv.z, xv.w); *(GAS v2u*)(x1 + (size_t)m * D + k) = xo; }
;                         const f32x4 hv = xv * (*(const GAS f32x4*)(mrow + 8192 + k) + 1.0f) + *(const GAS f32x4*)(mrow + 6144 + k);
;                         v2u o; o.x = pk2(hv.x, hv.y); o.y = pk2(hv.z, hv.w);
;                         *(GAS unsigned*)(h2q + (size_t)m * D + k) = pk4_fp8(hv.x, hv.y, hv.z, hv.w);
;                         const int chunk = (lq >> 1) + 32 * j;
;                         *(LAS v2u*)(h2s + rloc * 4096 + ((chunk ^ (rloc & 15)) << 4) + (lq & 1) * 8) = o; }
	v_add_f32_e32 v22, v22, v23
	v_fmamk_f32 v22, v22, 0x3a000000, v200
	v_mul_f32_e32 v23, 0x4f800000, v22
	v_cmp_gt_f32_e32 vcc, s85, v22
	s_nop 1
	v_cndmask_b32_e32 v22, v22, v23, vcc
	v_sqrt_f32_e32 v23, v22
	s_nop 0
	v_add_u32_e32 v26, -1, v23
	v_add_u32_e32 v27, 1, v23
	v_fma_f32 v60, -v26, v23, v22
	v_fma_f32 v170, -v27, v23, v22
	v_cmp_ge_f32_e64 s[14:15], 0, v60
	s_nop 1
	v_cndmask_b32_e64 v23, v23, v26, s[14:15]
	v_cmp_lt_f32_e64 s[14:15], 0, v170
	s_nop 1
	v_cndmask_b32_e64 v23, v23, v27, s[14:15]
	v_mul_f32_e32 v26, 0x37800000, v23
	v_cndmask_b32_e32 v23, v23, v26, vcc
	v_cmp_class_f32_e32 vcc, v22, v201
	s_nop 1
	v_cndmask_b32_e32 v26, v23, v22, vcc
	v_div_scale_f32 v27, s[14:15], v26, v26, 1.0
	v_rcp_f32_e32 v60, v27
	v_lshl_add_u64 v[22:23], s[0:1], 0, v[88:89]
	v_div_scale_f32 v88, vcc, 1.0, v26, 1.0
	v_fma_f32 v89, -v27, v60, 1.0
	v_fmac_f32_e32 v60, v89, v60
	v_mul_f32_e32 v89, v88, v60
	v_fma_f32 v170, -v27, v89, v88
	v_fmac_f32_e32 v89, v170, v60
	v_fma_f32 v27, -v27, v89, v88
	v_div_fmas_f32 v27, v27, v60, v89
	v_div_fixup_f32 v88, v27, v26, 1.0
	v_pk_mul_f32 v[24:25], v[24:25], v[88:89] op_sel_hi:[1,0]
	v_pk_mul_f32 v[20:21], v[20:21], v[88:89] op_sel_hi:[1,0]
	s_waitcnt lgkmcnt(0)
	v_pk_fma_f32 v[158:159], v[150:151], v[24:25], v[158:159]
	v_pk_fma_f32 v[20:21], v[152:153], v[20:21], v[160:161]
	v_bfe_u32 v24, v158, 16, 1
	v_bfe_u32 v26, v20, 16, 1
	v_bfe_u32 v25, v159, 16, 1
	v_bfe_u32 v27, v21, 16, 1
	v_add3_u32 v24, v158, v24, s86
	v_add3_u32 v26, v20, v26, s86
	v_add3_u32 v25, v159, v25, s86
	v_add3_u32 v27, v21, v27, s86
	v_lshrrev_b32_e32 v24, 16, v24
	v_lshrrev_b32_e32 v26, 16, v26
	v_and_or_b32 v24, v25, s82, v24
	v_and_or_b32 v25, v27, s82, v26
	global_store_dwordx2 v[22:23], v[24:25], off
	ds_read_b128 v[24:27], v252 offset:16384
	s_nop 0
	ds_read_b128 v[150:153], v252 offset:24576
	v_mov_b32_e32 v60, 0
	s_add_u32 s0, s48, s16
	s_addc_u32 s1, s49, s17
	v_pk_mul_f32 v[30:31], v[30:31], v[88:89] op_sel_hi:[1,0]
	v_pk_mul_f32 v[28:29], v[28:29], v[88:89] op_sel_hi:[1,0]
	v_pk_mul_f32 v[166:167], v[166:167], v[88:89] op_sel_hi:[1,0]
	s_mov_b32 s14, 0x8000
	s_waitcnt lgkmcnt(0)
	v_pk_add_f32 v[24:25], v[24:25], 1.0 op_sel_hi:[1,0]
	s_waitcnt lgkmcnt(0)
	v_pk_fma_f32 v[24:25], v[24:25], v[158:159], v[150:151]
	v_pk_add_f32 v[26:27], v[26:27], 1.0 op_sel_hi:[1,0]
	v_cvt_pk_fp8_f32 v60, v24, v25
	v_pk_fma_f32 v[26:27], v[26:27], v[20:21], v[152:153]
	v_lshl_add_u64 v[20:21], s[0:1], 0, v[36:37]
	v_readlane_b32 s0, v248, 24
	v_cvt_pk_fp8_f32 v60, v26, v27 op_sel:[0,0,1]
	global_store_dword v[20:21], v60, off
	ds_read_b128 v[150:153], v252 offset:9216
	ds_read_b128 v[158:161], v252 offset:1024
	v_mov_b32_e32 v60, 0
	s_waitcnt lgkmcnt(0)
	v_pk_fma_f32 v[36:37], v[152:153], v[28:29], v[160:161]
	v_pk_fma_f32 v[158:159], v[150:151], v[30:31], v[158:159]
	v_bfe_u32 v30, v36, 16, 1
	v_bfe_u32 v28, v158, 16, 1
	v_bfe_u32 v29, v159, 16, 1
	v_bfe_u32 v31, v37, 16, 1
	v_add3_u32 v28, v158, v28, s86
	v_add3_u32 v30, v36, v30, s86
	v_add3_u32 v29, v159, v29, s86
	v_add3_u32 v31, v37, v31, s86
	v_lshrrev_b32_e32 v28, 16, v28
	v_lshrrev_b32_e32 v30, 16, v30
	v_and_or_b32 v28, v29, s82, v28
	v_and_or_b32 v29, v31, s82, v30
	global_store_dwordx2 v[22:23], v[28:29], off offset:512
	ds_read_b128 v[28:31], v252 offset:17408
	s_nop 0
	ds_read_b128 v[150:153], v252 offset:25600
	s_waitcnt lgkmcnt(0)
	v_pk_add_f32 v[28:29], v[28:29], 1.0 op_sel_hi:[1,0]
	s_waitcnt lgkmcnt(0)
	v_pk_fma_f32 v[28:29], v[28:29], v[158:159], v[150:151]
	v_pk_add_f32 v[30:31], v[30:31], 1.0 op_sel_hi:[1,0]
	v_cvt_pk_fp8_f32 v60, v28, v29
	v_pk_fma_f32 v[30:31], v[30:31], v[36:37], v[152:153]
	v_pk_mul_f32 v[36:37], v[168:169], v[88:89] op_sel_hi:[1,0]
	v_cvt_pk_fp8_f32 v60, v30, v31 op_sel:[0,0,1]
	global_store_dword v[20:21], v60, off offset:256
	ds_read_b128 v[150:153], v252 offset:10240
	ds_read_b128 v[158:161], v252 offset:2048
	s_waitcnt lgkmcnt(0)
	v_pk_fma_f32 v[166:167], v[152:153], v[166:167], v[160:161]
	v_pk_fma_f32 v[36:37], v[150:151], v[36:37], v[158:159]
	v_bfe_u32 v150, v166, 16, 1
	v_bfe_u32 v60, v36, 16, 1
	v_bfe_u32 v89, v37, 16, 1
	v_bfe_u32 v151, v167, 16, 1
	v_add3_u32 v60, v36, v60, s86
	v_add3_u32 v150, v166, v150, s86
	v_add3_u32 v89, v37, v89, s86
	v_add3_u32 v151, v167, v151, s86
	v_lshrrev_b32_e32 v60, 16, v60
	v_lshrrev_b32_e32 v152, 16, v150
	v_and_or_b32 v150, v89, s82, v60
	v_and_or_b32 v151, v151, s82, v152
	global_store_dwordx2 v[22:23], v[150:151], off offset:1024
	ds_read_b128 v[150:153], v252 offset:18432
	s_nop 0
	ds_read_b128 v[158:161], v252 offset:26624
	v_mov_b32_e32 v60, 0
	v_pk_mul_f32 v[162:163], v[162:163], v[88:89] op_sel_hi:[1,0]
	s_waitcnt lgkmcnt(0)
	v_pk_add_f32 v[150:151], v[150:151], 1.0 op_sel_hi:[1,0]
	s_waitcnt lgkmcnt(0)
	v_pk_fma_f32 v[36:37], v[150:151], v[36:37], v[158:159]
	v_pk_add_f32 v[150:151], v[152:153], 1.0 op_sel_hi:[1,0]
	v_cvt_pk_fp8_f32 v60, v36, v37
	v_pk_fma_f32 v[150:151], v[150:151], v[166:167], v[160:161]
	v_pk_mul_f32 v[152:153], v[164:165], v[88:89] op_sel_hi:[1,0]
	v_lshrrev_b32_e32 v167, 1, v204
	v_cvt_pk_fp8_f32 v60, v150, v151 op_sel:[0,0,1]
	v_add_u32_e32 v170, 32, v167
	v_add_u32_e32 v171, 64, v167
	v_add_u32_e32 v172, 0x60, v167
	global_store_dword v[20:21], v60, off offset:512
	ds_read_b128 v[158:161], v252 offset:11264
	s_nop 0
	ds_read_b128 v[72:75], v252 offset:3072
	v_add_u32_e32 v173, 0x80, v167
	v_add_u32_e32 v174, 0xa0, v167
	v_add_u32_e32 v175, 0xc0, v167
	v_xor_b32_e32 v169, s54, v167
	v_xor_b32_e32 v176, s64, v167
	v_xor_b32_e32 v177, s66, v167
	v_xor_b32_e32 v178, s54, v170
	v_xor_b32_e32 v179, s54, v171
	v_xor_b32_e32 v180, s54, v172
	v_xor_b32_e32 v181, s54, v173
	v_xor_b32_e32 v182, s54, v174
	v_xor_b32_e32 v183, s54, v175
	v_xor_b32_e32 v185, s64, v170
	v_xor_b32_e32 v186, s64, v171
	v_xor_b32_e32 v187, s64, v172
	v_xor_b32_e32 v188, s64, v173
	v_xor_b32_e32 v189, s64, v174
	v_xor_b32_e32 v190, s64, v175
	v_xor_b32_e32 v192, s66, v170
	v_xor_b32_e32 v193, s66, v171
	v_xor_b32_e32 v205, s66, v172
	v_xor_b32_e32 v206, s66, v173
	v_xor_b32_e32 v207, s66, v174
	v_xor_b32_e32 v208, s66, v175
	v_xor_b32_e32 v170, s68, v170
	v_xor_b32_e32 v171, s68, v171
	v_xor_b32_e32 v172, s68, v172
	v_xor_b32_e32 v173, s68, v173
	v_xor_b32_e32 v174, s68, v174
	v_xor_b32_e32 v175, s68, v175
	v_mov_b32_e32 v166, 0
	s_waitcnt lgkmcnt(0)
; #define GAS __attribute__((address_space(1)))
; #define LAS __attribute__((address_space(3)))
; __device__ __forceinline__ unsigned pk2(float lo, float hi) { return f2bf(lo) | (f2bf(hi) << 16); }
; __device__ __forceinline__ unsigned pk4_fp8(float a, float b, float c, float d) { int r = __builtin_amdgcn_cvt_pk_fp8_f32(a, b, 0, false); r = __builtin_amdgcn_cvt_pk_fp8_f32(c, d, r, true); return (unsigned)r; }
; template <int l>
; __device__ __forceinline__ void layer_phases(Frame& F, const XcdBarrier& bar, const int lo, const int hi) {
;     ...
;                     for (int j = 0; j < 8; ++j) { const int k = 4 * lq + 256 * j;
;                         const f32x4 xv = v[j] * rstd * *(const GAS f32x4*)(g1 + k) + *(const GAS f32x4*)(b1 + k);
;                         { v2u xo; xo.x = pk2(xv.x, xv.y); xo.y = pk2(xv.z, xv.w); *(GAS v2u*)(x1 + (size_t)m * D + k) = xo; }
;                         const f32x4 hv = xv * (*(const GAS f32x4*)(mrow + 8192 + k) + 1.0f) + *(const GAS f32x4*)(mrow + 6144 + k);
;                         v2u o; o.x = pk2(hv.x, hv.y); o.y = pk2(hv.z, hv.w);
;                         *(GAS unsigned*)(h2q + (size_t)m * D + k) = pk4_fp8(hv.x, hv.y, hv.z, hv.w);
;                         const int chunk = (lq >> 1) + 32 * j;
;                         *(LAS v2u*)(h2s + rloc * 4096 + ((chunk ^ (rloc & 15)) << 4) + (lq & 1) * 8) = o; }
	v_pk_fma_f32 v[162:163], v[162:163], v[160:161], v[74:75]
	v_pk_fma_f32 v[72:73], v[152:153], v[158:159], v[72:73]
	v_bfe_u32 v75, v162, 16, 1
	v_bfe_u32 v60, v72, 16, 1
	v_bfe_u32 v74, v73, 16, 1
	v_bfe_u32 v89, v163, 16, 1
	v_add3_u32 v60, v72, v60, s86
	v_add3_u32 v75, v162, v75, s86
	v_add3_u32 v74, v73, v74, s86
	v_add3_u32 v89, v163, v89, s86
	v_lshrrev_b32_e32 v60, 16, v60
	v_lshrrev_b32_e32 v75, 16, v75
	v_and_or_b32 v74, v74, s82, v60
	v_and_or_b32 v75, v89, s82, v75
	global_store_dwordx2 v[22:23], v[74:75], off offset:1536
	ds_read_b128 v[158:161], v252 offset:19456
	s_nop 0
	ds_read_b128 v[80:83], v252 offset:27648
	v_mov_b32_e32 v60, 0
	s_waitcnt lgkmcnt(0)
	v_pk_add_f32 v[74:75], v[158:159], 1.0 op_sel_hi:[1,0]
	s_waitcnt lgkmcnt(0)
	v_pk_fma_f32 v[74:75], v[72:73], v[74:75], v[80:81]
	v_pk_add_f32 v[72:73], v[160:161], 1.0 op_sel_hi:[1,0]
	v_cvt_pk_fp8_f32 v60, v74, v75
	v_pk_fma_f32 v[80:81], v[162:163], v[72:73], v[82:83]
	v_pk_mul_f32 v[72:73], v[156:157], v[88:89] op_sel_hi:[1,0]
	v_pk_mul_f32 v[82:83], v[154:155], v[88:89] op_sel_hi:[1,0]
	v_cvt_pk_fp8_f32 v60, v80, v81 op_sel:[0,0,1]
	v_mov_b32_e32 v155, 0
	v_ashrrev_i32_e32 v154, 5, v204
	global_store_dword v[20:21], v60, off offset:768
	ds_read_b128 v[158:161], v252 offset:12288
	ds_read_b128 v[162:165], v252 offset:4096
	s_waitcnt lgkmcnt(0)
	v_pk_fma_f32 v[152:153], v[82:83], v[160:161], v[164:165]
	v_pk_fma_f32 v[72:73], v[72:73], v[158:159], v[162:163]
	v_bfe_u32 v83, v152, 16, 1
	v_bfe_u32 v60, v72, 16, 1
	v_bfe_u32 v82, v73, 16, 1
	v_bfe_u32 v89, v153, 16, 1
	v_add3_u32 v60, v72, v60, s86
	v_add3_u32 v83, v152, v83, s86
	v_add3_u32 v82, v73, v82, s86
	v_add3_u32 v89, v153, v89, s86
	v_lshrrev_b32_e32 v60, 16, v60
	v_lshrrev_b32_e32 v83, 16, v83
	v_and_or_b32 v82, v82, s82, v60
	v_and_or_b32 v83, v89, s82, v83
	global_store_dwordx2 v[22:23], v[82:83], off offset:2048
	ds_read_b128 v[156:159], v252 offset:20480
	ds_read_b128 v[160:163], v252 offset:28672
	v_lshlrev_b32_e32 v82, 3, v204
	v_and_b32_e32 v168, 8, v82
	v_mov_b32_e32 v164, 0
	v_add_u32_e32 v168, 0, v168
	v_add_u32_e32 v210, s0, v168
	v_readlane_b32 s0, v248, 25
	v_and_b32_e32 v89, 31, v204
	v_lshl_add_u32 v169, v169, 4, v210
	v_add_u32_e32 v211, s0, v168
	v_readlane_b32 s0, v248, 26
	v_lshl_add_u32 v178, v178, 4, v210
	v_lshl_add_u32 v179, v179, 4, v210
	v_add_u32_e32 v212, s0, v168
	v_readlane_b32 s0, v248, 27
	v_lshl_add_u32 v180, v180, 4, v210
	v_lshl_add_u32 v181, v181, 4, v210
	v_add_u32_e32 v168, s0, v168
	v_lshl_add_u32 v182, v182, 4, v210
	v_lshl_add_u32 v183, v183, 4, v210
	v_lshl_add_u32 v176, v176, 4, v211
	v_lshl_add_u32 v185, v185, 4, v211
	v_lshl_add_u32 v186, v186, 4, v211
	v_lshl_add_u32 v187, v187, 4, v211
	v_lshl_add_u32 v188, v188, 4, v211
	v_lshl_add_u32 v189, v189, 4, v211
	v_lshl_add_u32 v190, v190, 4, v211
	v_lshl_add_u32 v170, v170, 4, v168
	v_lshl_add_u32 v171, v171, 4, v168
	v_lshl_add_u32 v172, v172, 4, v168
	v_lshl_add_u32 v173, v173, 4, v168
	v_lshl_add_u32 v174, v174, 4, v168
	v_lshl_add_u32 v175, v175, 4, v168
	v_pk_mul_f32 v[14:15], v[14:15], v[88:89] op_sel_hi:[1,0]
	v_pk_mul_f32 v[12:13], v[12:13], v[88:89] op_sel_hi:[1,0]
	v_lshl_add_u32 v177, v177, 4, v212
	v_lshl_add_u32 v192, v192, 4, v212
	v_lshl_add_u32 v193, v193, 4, v212
	v_lshl_add_u32 v205, v205, 4, v212
	v_lshl_add_u32 v206, v206, 4, v212
	v_lshl_add_u32 v207, v207, 4, v212
	v_lshl_add_u32 v208, v208, 4, v212
	v_mov_b32_e32 v165, 0
	v_pk_mul_f32 v[10:11], v[10:11], v[88:89] op_sel_hi:[1,0]
	v_pk_mul_f32 v[8:9], v[8:9], v[88:89] op_sel_hi:[1,0]
	v_lshlrev_b32_e32 v60, 4, v204
	s_movk_i32 s0, 0x2000
	s_waitcnt lgkmcnt(0)
	v_pk_add_f32 v[82:83], v[156:157], 1.0 op_sel_hi:[1,0]
	s_waitcnt lgkmcnt(0)
	v_pk_fma_f32 v[82:83], v[72:73], v[82:83], v[160:161]
	v_pk_add_f32 v[72:73], v[158:159], 1.0 op_sel_hi:[1,0]
	v_cvt_pk_fp8_f32 v164, v82, v83
	v_pk_fma_f32 v[152:153], v[152:153], v[72:73], v[162:163]
	v_lshl_add_u64 v[72:73], s[36:37], 0, v[60:61]
	v_cvt_pk_fp8_f32 v164, v152, v153 op_sel:[0,0,1]
	global_store_dword v[20:21], v164, off offset:1024
	ds_read_b128 v[156:159], v252 offset:13312
	ds_read_b128 v[160:163], v252 offset:5120
	v_add_u32_e32 v164, 0xe0, v167
	v_xor_b32_e32 v167, s68, v167
	v_xor_b32_e32 v184, s54, v164
	v_xor_b32_e32 v191, s64, v164
	v_xor_b32_e32 v209, s66, v164
	v_xor_b32_e32 v164, s68, v164
	v_lshl_add_u32 v184, v184, 4, v210
	v_lshl_add_u32 v191, v191, 4, v211
	v_lshl_add_u32 v167, v167, 4, v168
	v_lshl_add_u32 v164, v164, 4, v168
	v_and_b32_sdwa v168, v44, v203 dst_sel:DWORD dst_unused:UNUSED_PAD src0_sel:WORD_1 src1_sel:DWORD
	v_and_b32_sdwa v210, v42, v203 dst_sel:DWORD dst_unused:UNUSED_PAD src0_sel:WORD_1 src1_sel:DWORD
	v_and_b32_sdwa v211, v45, v203 dst_sel:DWORD dst_unused:UNUSED_PAD src0_sel:WORD_1 src1_sel:DWORD
	v_add3_u32 v42, v42, v210, s86
	v_add3_u32 v168, v44, v168, s86
	v_add3_u32 v210, v45, v211, s86
	v_lshl_add_u32 v209, v209, 4, v212
	v_and_b32_sdwa v212, v43, v203 dst_sel:DWORD dst_unused:UNUSED_PAD src0_sel:WORD_1 src1_sel:DWORD
	v_add3_u32 v43, v43, v212, s86
	s_waitcnt lgkmcnt(0)
; #define GAS __attribute__((address_space(1)))
; #define LAS __attribute__((address_space(3)))
; __device__ __forceinline__ unsigned pk2(float lo, float hi) { return f2bf(lo) | (f2bf(hi) << 16); }
; __device__ __forceinline__ unsigned pk4_fp8(float a, float b, float c, float d) { int r = __builtin_amdgcn_cvt_pk_fp8_f32(a, b, 0, false); r = __builtin_amdgcn_cvt_pk_fp8_f32(c, d, r, true); return (unsigned)r; }
; template <int l>
; __device__ __forceinline__ void layer_phases(Frame& F, const XcdBarrier& bar, const int lo, const int hi) {
;     ...
;                     for (int j = 0; j < 8; ++j) { const int k = 4 * lq + 256 * j;
;                         const f32x4 xv = v[j] * rstd * *(const GAS f32x4*)(g1 + k) + *(const GAS f32x4*)(b1 + k);
;                         { v2u xo; xo.x = pk2(xv.x, xv.y); xo.y = pk2(xv.z, xv.w); *(GAS v2u*)(x1 + (size_t)m * D + k) = xo; }
;                         const f32x4 hv = xv * (*(const GAS f32x4*)(mrow + 8192 + k) + 1.0f) + *(const GAS f32x4*)(mrow + 6144 + k);
;                         v2u o; o.x = pk2(hv.x, hv.y); o.y = pk2(hv.z, hv.w);
;                         *(GAS unsigned*)(h2q + (size_t)m * D + k) = pk4_fp8(hv.x, hv.y, hv.z, hv.w);
;                         const int chunk = (lq >> 1) + 32 * j;
;                         *(LAS v2u*)(h2s + rloc * 4096 + ((chunk ^ (rloc & 15)) << 4) + (lq & 1) * 8) = o; }
	v_pk_fma_f32 v[44:45], v[12:13], v[158:159], v[162:163]
	v_pk_fma_f32 v[160:161], v[14:15], v[156:157], v[160:161]
	v_bfe_u32 v14, v44, 16, 1
	v_bfe_u32 v12, v160, 16, 1
	v_bfe_u32 v13, v161, 16, 1
	v_bfe_u32 v15, v45, 16, 1
	v_add3_u32 v12, v160, v12, s86
	v_add3_u32 v14, v44, v14, s86
	v_add3_u32 v13, v161, v13, s86
	v_add3_u32 v15, v45, v15, s86
	v_lshrrev_b32_e32 v12, 16, v12
	v_lshrrev_b32_e32 v14, 16, v14
	v_and_or_b32 v12, v13, s82, v12
	v_and_or_b32 v13, v15, s82, v14
	global_store_dwordx2 v[22:23], v[12:13], off offset:2560
	ds_read_b128 v[12:15], v252 offset:21504
	s_nop 0
	ds_read_b128 v[156:159], v252 offset:29696
	v_and_b32_e32 v162, 0xffff0000, v210
	v_and_b32_e32 v163, 0xffff0000, v43
	v_or_b32_sdwa v43, v162, v168 dst_sel:DWORD dst_unused:UNUSED_PAD src0_sel:DWORD src1_sel:WORD_1
	v_or_b32_sdwa v42, v163, v42 dst_sel:DWORD dst_unused:UNUSED_PAD src0_sel:DWORD src1_sel:WORD_1
	ds_write_b64 v169, v[42:43]
	v_and_b32_sdwa v43, v46, v203 dst_sel:DWORD dst_unused:UNUSED_PAD src0_sel:WORD_1 src1_sel:DWORD
	v_and_b32_sdwa v162, v49, v203 dst_sel:DWORD dst_unused:UNUSED_PAD src0_sel:WORD_1 src1_sel:DWORD
	v_and_b32_sdwa v163, v47, v203 dst_sel:DWORD dst_unused:UNUSED_PAD src0_sel:WORD_1 src1_sel:DWORD
	v_and_b32_sdwa v42, v48, v203 dst_sel:DWORD dst_unused:UNUSED_PAD src0_sel:WORD_1 src1_sel:DWORD
	v_add3_u32 v46, v46, v43, s86
	v_add3_u32 v43, v49, v162, s86
	v_add3_u32 v47, v47, v163, s86
	v_add3_u32 v42, v48, v42, s86
	v_and_b32_e32 v43, 0xffff0000, v43
	v_and_b32_e32 v47, 0xffff0000, v47
	v_or_b32_sdwa v43, v43, v42 dst_sel:DWORD dst_unused:UNUSED_PAD src0_sel:DWORD src1_sel:WORD_1
	v_or_b32_sdwa v42, v47, v46 dst_sel:DWORD dst_unused:UNUSED_PAD src0_sel:DWORD src1_sel:WORD_1
	ds_write_b64 v178, v[42:43]
	v_and_b32_sdwa v43, v50, v203 dst_sel:DWORD dst_unused:UNUSED_PAD src0_sel:WORD_1 src1_sel:DWORD
	v_and_b32_sdwa v46, v63, v203 dst_sel:DWORD dst_unused:UNUSED_PAD src0_sel:WORD_1 src1_sel:DWORD
	v_and_b32_sdwa v47, v51, v203 dst_sel:DWORD dst_unused:UNUSED_PAD src0_sel:WORD_1 src1_sel:DWORD
	v_and_b32_sdwa v42, v62, v203 dst_sel:DWORD dst_unused:UNUSED_PAD src0_sel:WORD_1 src1_sel:DWORD
	v_add3_u32 v48, v50, v43, s86
	v_add3_u32 v43, v63, v46, s86
	v_add3_u32 v46, v51, v47, s86
	v_add3_u32 v42, v62, v42, s86
	v_and_b32_e32 v43, 0xffff0000, v43
	v_and_b32_e32 v46, 0xffff0000, v46
	v_or_b32_sdwa v43, v43, v42 dst_sel:DWORD dst_unused:UNUSED_PAD src0_sel:DWORD src1_sel:WORD_1
	v_or_b32_sdwa v42, v46, v48 dst_sel:DWORD dst_unused:UNUSED_PAD src0_sel:DWORD src1_sel:WORD_1
	ds_write_b64 v179, v[42:43]
	v_and_b32_sdwa v43, v64, v203 dst_sel:DWORD dst_unused:UNUSED_PAD src0_sel:WORD_1 src1_sel:DWORD
	v_and_b32_sdwa v46, v67, v203 dst_sel:DWORD dst_unused:UNUSED_PAD src0_sel:WORD_1 src1_sel:DWORD
	v_and_b32_sdwa v47, v65, v203 dst_sel:DWORD dst_unused:UNUSED_PAD src0_sel:WORD_1 src1_sel:DWORD
	v_and_b32_sdwa v42, v66, v203 dst_sel:DWORD dst_unused:UNUSED_PAD src0_sel:WORD_1 src1_sel:DWORD
	v_add3_u32 v48, v64, v43, s86
	v_add3_u32 v43, v67, v46, s86
	v_add3_u32 v46, v65, v47, s86
	v_add3_u32 v42, v66, v42, s86
	v_and_b32_e32 v43, 0xffff0000, v43
	v_and_b32_e32 v46, 0xffff0000, v46
	v_or_b32_sdwa v43, v43, v42 dst_sel:DWORD dst_unused:UNUSED_PAD src0_sel:DWORD src1_sel:WORD_1
	v_or_b32_sdwa v42, v46, v48 dst_sel:DWORD dst_unused:UNUSED_PAD src0_sel:DWORD src1_sel:WORD_1
	ds_write_b64 v180, v[42:43]
	v_and_b32_sdwa v43, v68, v203 dst_sel:DWORD dst_unused:UNUSED_PAD src0_sel:WORD_1 src1_sel:DWORD
	v_and_b32_sdwa v46, v71, v203 dst_sel:DWORD dst_unused:UNUSED_PAD src0_sel:WORD_1 src1_sel:DWORD
	v_and_b32_sdwa v47, v69, v203 dst_sel:DWORD dst_unused:UNUSED_PAD src0_sel:WORD_1 src1_sel:DWORD
	v_and_b32_sdwa v42, v70, v203 dst_sel:DWORD dst_unused:UNUSED_PAD src0_sel:WORD_1 src1_sel:DWORD
	v_add3_u32 v48, v68, v43, s86
	v_add3_u32 v43, v71, v46, s86
	v_add3_u32 v46, v69, v47, s86
	v_add3_u32 v42, v70, v42, s86
	v_and_b32_e32 v43, 0xffff0000, v43
	v_and_b32_e32 v46, 0xffff0000, v46
	v_or_b32_sdwa v43, v43, v42 dst_sel:DWORD dst_unused:UNUSED_PAD src0_sel:DWORD src1_sel:WORD_1
	v_or_b32_sdwa v42, v46, v48 dst_sel:DWORD dst_unused:UNUSED_PAD src0_sel:DWORD src1_sel:WORD_1
	ds_write_b64 v181, v[42:43]
	v_and_b32_sdwa v43, v76, v203 dst_sel:DWORD dst_unused:UNUSED_PAD src0_sel:WORD_1 src1_sel:DWORD
	v_and_b32_sdwa v46, v79, v203 dst_sel:DWORD dst_unused:UNUSED_PAD src0_sel:WORD_1 src1_sel:DWORD
	v_and_b32_sdwa v47, v77, v203 dst_sel:DWORD dst_unused:UNUSED_PAD src0_sel:WORD_1 src1_sel:DWORD
	v_and_b32_sdwa v42, v78, v203 dst_sel:DWORD dst_unused:UNUSED_PAD src0_sel:WORD_1 src1_sel:DWORD
	v_add3_u32 v48, v76, v43, s86
	v_add3_u32 v43, v79, v46, s86
	v_add3_u32 v46, v77, v47, s86
	v_add3_u32 v42, v78, v42, s86
	v_and_b32_e32 v43, 0xffff0000, v43
	v_and_b32_e32 v46, 0xffff0000, v46
	v_or_b32_sdwa v43, v43, v42 dst_sel:DWORD dst_unused:UNUSED_PAD src0_sel:DWORD src1_sel:WORD_1
	v_or_b32_sdwa v42, v46, v48 dst_sel:DWORD dst_unused:UNUSED_PAD src0_sel:DWORD src1_sel:WORD_1
	ds_write_b64 v182, v[42:43]
	v_and_b32_sdwa v43, v84, v203 dst_sel:DWORD dst_unused:UNUSED_PAD src0_sel:WORD_1 src1_sel:DWORD
	v_and_b32_sdwa v46, v87, v203 dst_sel:DWORD dst_unused:UNUSED_PAD src0_sel:WORD_1 src1_sel:DWORD
	v_and_b32_sdwa v42, v86, v203 dst_sel:DWORD dst_unused:UNUSED_PAD src0_sel:WORD_1 src1_sel:DWORD
	v_and_b32_sdwa v47, v85, v203 dst_sel:DWORD dst_unused:UNUSED_PAD src0_sel:WORD_1 src1_sel:DWORD
	v_add3_u32 v50, v84, v43, s86
	v_add3_u32 v43, v87, v46, s86
	v_add3_u32 v42, v86, v42, s86
	v_add3_u32 v46, v85, v47, s86
	s_waitcnt lgkmcnt(0)
	v_pk_add_f32 v[12:13], v[12:13], 1.0 op_sel_hi:[1,0]
	v_pk_add_f32 v[14:15], v[14:15], 1.0 op_sel_hi:[1,0]
	s_waitcnt lgkmcnt(0)
; #define GAS __attribute__((address_space(1)))
; #define LAS __attribute__((address_space(3)))
; __device__ __forceinline__ unsigned pk2(float lo, float hi) { return f2bf(lo) | (f2bf(hi) << 16); }
; __device__ __forceinline__ unsigned pk4_fp8(float a, float b, float c, float d) { int r = __builtin_amdgcn_cvt_pk_fp8_f32(a, b, 0, false); r = __builtin_amdgcn_cvt_pk_fp8_f32(c, d, r, true); return (unsigned)r; }
; template <int l>
; __device__ __forceinline__ void layer_phases(Frame& F, const XcdBarrier& bar, const int lo, const int hi) {
;     ...
;                     for (int j = 0; j < 8; ++j) { const int k = 4 * lq + 256 * j;
;                         const f32x4 xv = v[j] * rstd * *(const GAS f32x4*)(g1 + k) + *(const GAS f32x4*)(b1 + k);
;                         { v2u xo; xo.x = pk2(xv.x, xv.y); xo.y = pk2(xv.z, xv.w); *(GAS v2u*)(x1 + (size_t)m * D + k) = xo; }
;                         const f32x4 hv = xv * (*(const GAS f32x4*)(mrow + 8192 + k) + 1.0f) + *(const GAS f32x4*)(mrow + 6144 + k);
;                         v2u o; o.x = pk2(hv.x, hv.y); o.y = pk2(hv.z, hv.w);
;                         *(GAS unsigned*)(h2q + (size_t)m * D + k) = pk4_fp8(hv.x, hv.y, hv.z, hv.w);
;                         const int chunk = (lq >> 1) + 32 * j;
;                         *(LAS v2u*)(h2s + rloc * 4096 + ((chunk ^ (rloc & 15)) << 4) + (lq & 1) * 8) = o; }
	v_pk_fma_f32 v[12:13], v[160:161], v[12:13], v[156:157]
	v_pk_fma_f32 v[14:15], v[44:45], v[14:15], v[158:159]
	v_cvt_pk_fp8_f32 v165, v12, v13
	v_and_b32_e32 v43, 0xffff0000, v43
	v_and_b32_e32 v62, 0xffff0000, v46
	v_or_b32_sdwa v51, v43, v42 dst_sel:DWORD dst_unused:UNUSED_PAD src0_sel:DWORD src1_sel:WORD_1
	v_cvt_pk_fp8_f32 v165, v14, v15 op_sel:[0,0,1]
	v_or_b32_sdwa v50, v62, v50 dst_sel:DWORD dst_unused:UNUSED_PAD src0_sel:DWORD src1_sel:WORD_1
	v_and_b32_sdwa v62, v93, v203 dst_sel:DWORD dst_unused:UNUSED_PAD src0_sel:WORD_1 src1_sel:DWORD
	v_and_b32_sdwa v63, v91, v203 dst_sel:DWORD dst_unused:UNUSED_PAD src0_sel:WORD_1 src1_sel:DWORD
	global_store_dword v[20:21], v165, off offset:1280
	ds_read_b128 v[42:45], v252 offset:14336
	ds_read_b128 v[46:49], v252 offset:6144
	ds_write_b64 v183, v[50:51]
	v_and_b32_sdwa v51, v90, v203 dst_sel:DWORD dst_unused:UNUSED_PAD src0_sel:WORD_1 src1_sel:DWORD
	v_and_b32_sdwa v50, v92, v203 dst_sel:DWORD dst_unused:UNUSED_PAD src0_sel:WORD_1 src1_sel:DWORD
	v_add3_u32 v64, v90, v51, s86
	v_add3_u32 v51, v93, v62, s86
	v_add3_u32 v62, v91, v63, s86
	v_add3_u32 v50, v92, v50, s86
	v_and_b32_e32 v51, 0xffff0000, v51
	v_and_b32_e32 v62, 0xffff0000, v62
	v_or_b32_sdwa v51, v51, v50 dst_sel:DWORD dst_unused:UNUSED_PAD src0_sel:DWORD src1_sel:WORD_1
	v_or_b32_sdwa v50, v62, v64 dst_sel:DWORD dst_unused:UNUSED_PAD src0_sel:DWORD src1_sel:WORD_1
	ds_write_b64 v184, v[50:51]
	v_and_b32_sdwa v51, v94, v203 dst_sel:DWORD dst_unused:UNUSED_PAD src0_sel:WORD_1 src1_sel:DWORD
	v_and_b32_sdwa v62, v97, v203 dst_sel:DWORD dst_unused:UNUSED_PAD src0_sel:WORD_1 src1_sel:DWORD
	v_and_b32_sdwa v63, v95, v203 dst_sel:DWORD dst_unused:UNUSED_PAD src0_sel:WORD_1 src1_sel:DWORD
	v_and_b32_sdwa v50, v96, v203 dst_sel:DWORD dst_unused:UNUSED_PAD src0_sel:WORD_1 src1_sel:DWORD
	v_add3_u32 v64, v94, v51, s86
	v_add3_u32 v51, v97, v62, s86
	v_add3_u32 v62, v95, v63, s86
	v_add3_u32 v50, v96, v50, s86
	v_and_b32_e32 v51, 0xffff0000, v51
	v_and_b32_e32 v62, 0xffff0000, v62
	v_or_b32_sdwa v51, v51, v50 dst_sel:DWORD dst_unused:UNUSED_PAD src0_sel:DWORD src1_sel:WORD_1
	v_or_b32_sdwa v50, v62, v64 dst_sel:DWORD dst_unused:UNUSED_PAD src0_sel:DWORD src1_sel:WORD_1
	ds_write_b64 v176, v[50:51]
	v_and_b32_sdwa v51, v98, v203 dst_sel:DWORD dst_unused:UNUSED_PAD src0_sel:WORD_1 src1_sel:DWORD
	v_and_b32_sdwa v62, v101, v203 dst_sel:DWORD dst_unused:UNUSED_PAD src0_sel:WORD_1 src1_sel:DWORD
	v_and_b32_sdwa v63, v99, v203 dst_sel:DWORD dst_unused:UNUSED_PAD src0_sel:WORD_1 src1_sel:DWORD
	v_and_b32_sdwa v50, v100, v203 dst_sel:DWORD dst_unused:UNUSED_PAD src0_sel:WORD_1 src1_sel:DWORD
	v_add3_u32 v64, v98, v51, s86
	v_add3_u32 v51, v101, v62, s86
	v_add3_u32 v62, v99, v63, s86
	v_add3_u32 v50, v100, v50, s86
	v_and_b32_e32 v51, 0xffff0000, v51
	v_and_b32_e32 v62, 0xffff0000, v62
	v_or_b32_sdwa v51, v51, v50 dst_sel:DWORD dst_unused:UNUSED_PAD src0_sel:DWORD src1_sel:WORD_1
	v_or_b32_sdwa v50, v62, v64 dst_sel:DWORD dst_unused:UNUSED_PAD src0_sel:DWORD src1_sel:WORD_1
	ds_write_b64 v185, v[50:51]
	v_and_b32_sdwa v51, v102, v203 dst_sel:DWORD dst_unused:UNUSED_PAD src0_sel:WORD_1 src1_sel:DWORD
	v_and_b32_sdwa v62, v105, v203 dst_sel:DWORD dst_unused:UNUSED_PAD src0_sel:WORD_1 src1_sel:DWORD
	v_and_b32_sdwa v63, v103, v203 dst_sel:DWORD dst_unused:UNUSED_PAD src0_sel:WORD_1 src1_sel:DWORD
	v_and_b32_sdwa v50, v104, v203 dst_sel:DWORD dst_unused:UNUSED_PAD src0_sel:WORD_1 src1_sel:DWORD
	v_add3_u32 v64, v102, v51, s86
	v_add3_u32 v51, v105, v62, s86
	v_add3_u32 v62, v103, v63, s86
	v_add3_u32 v50, v104, v50, s86
	v_and_b32_e32 v51, 0xffff0000, v51
	v_and_b32_e32 v62, 0xffff0000, v62
	v_or_b32_sdwa v51, v51, v50 dst_sel:DWORD dst_unused:UNUSED_PAD src0_sel:DWORD src1_sel:WORD_1
	v_or_b32_sdwa v50, v62, v64 dst_sel:DWORD dst_unused:UNUSED_PAD src0_sel:DWORD src1_sel:WORD_1
	ds_write_b64 v186, v[50:51]
	v_and_b32_sdwa v51, v106, v203 dst_sel:DWORD dst_unused:UNUSED_PAD src0_sel:WORD_1 src1_sel:DWORD
	v_and_b32_sdwa v62, v109, v203 dst_sel:DWORD dst_unused:UNUSED_PAD src0_sel:WORD_1 src1_sel:DWORD
	v_and_b32_sdwa v63, v107, v203 dst_sel:DWORD dst_unused:UNUSED_PAD src0_sel:WORD_1 src1_sel:DWORD
	v_and_b32_sdwa v50, v108, v203 dst_sel:DWORD dst_unused:UNUSED_PAD src0_sel:WORD_1 src1_sel:DWORD
	v_add3_u32 v64, v106, v51, s86
	v_add3_u32 v51, v109, v62, s86
	v_add3_u32 v62, v107, v63, s86
	v_add3_u32 v50, v108, v50, s86
	v_and_b32_e32 v51, 0xffff0000, v51
	v_and_b32_e32 v62, 0xffff0000, v62
	v_or_b32_sdwa v51, v51, v50 dst_sel:DWORD dst_unused:UNUSED_PAD src0_sel:DWORD src1_sel:WORD_1
	v_or_b32_sdwa v50, v62, v64 dst_sel:DWORD dst_unused:UNUSED_PAD src0_sel:DWORD src1_sel:WORD_1
	ds_write_b64 v187, v[50:51]
	v_and_b32_sdwa v51, v110, v203 dst_sel:DWORD dst_unused:UNUSED_PAD src0_sel:WORD_1 src1_sel:DWORD
	v_and_b32_sdwa v62, v113, v203 dst_sel:DWORD dst_unused:UNUSED_PAD src0_sel:WORD_1 src1_sel:DWORD
	v_and_b32_sdwa v63, v111, v203 dst_sel:DWORD dst_unused:UNUSED_PAD src0_sel:WORD_1 src1_sel:DWORD
	v_and_b32_sdwa v50, v112, v203 dst_sel:DWORD dst_unused:UNUSED_PAD src0_sel:WORD_1 src1_sel:DWORD
	v_add3_u32 v64, v110, v51, s86
	v_add3_u32 v51, v113, v62, s86
	v_add3_u32 v62, v111, v63, s86
	v_add3_u32 v50, v112, v50, s86
	v_and_b32_e32 v51, 0xffff0000, v51
	v_and_b32_e32 v62, 0xffff0000, v62
	v_or_b32_sdwa v51, v51, v50 dst_sel:DWORD dst_unused:UNUSED_PAD src0_sel:DWORD src1_sel:WORD_1
	v_or_b32_sdwa v50, v62, v64 dst_sel:DWORD dst_unused:UNUSED_PAD src0_sel:DWORD src1_sel:WORD_1
	v_and_b32_sdwa v62, v117, v203 dst_sel:DWORD dst_unused:UNUSED_PAD src0_sel:WORD_1 src1_sel:DWORD
	v_and_b32_sdwa v63, v115, v203 dst_sel:DWORD dst_unused:UNUSED_PAD src0_sel:WORD_1 src1_sel:DWORD
	s_waitcnt lgkmcnt(0)
; #define GAS __attribute__((address_space(1)))
; #define LAS __attribute__((address_space(3)))
; __device__ __forceinline__ unsigned pk2(float lo, float hi) { return f2bf(lo) | (f2bf(hi) << 16); }
; __device__ __forceinline__ unsigned pk4_fp8(float a, float b, float c, float d) { int r = __builtin_amdgcn_cvt_pk_fp8_f32(a, b, 0, false); r = __builtin_amdgcn_cvt_pk_fp8_f32(c, d, r, true); return (unsigned)r; }
; template <int l>
; __device__ __forceinline__ void layer_phases(Frame& F, const XcdBarrier& bar, const int lo, const int hi) {
;     ...
;                     for (int j = 0; j < 8; ++j) { const int k = 4 * lq + 256 * j;
;                         const f32x4 xv = v[j] * rstd * *(const GAS f32x4*)(g1 + k) + *(const GAS f32x4*)(b1 + k);
;                         { v2u xo; xo.x = pk2(xv.x, xv.y); xo.y = pk2(xv.z, xv.w); *(GAS v2u*)(x1 + (size_t)m * D + k) = xo; }
;                         const f32x4 hv = xv * (*(const GAS f32x4*)(mrow + 8192 + k) + 1.0f) + *(const GAS f32x4*)(mrow + 6144 + k);
;                         v2u o; o.x = pk2(hv.x, hv.y); o.y = pk2(hv.z, hv.w);
;                         *(GAS unsigned*)(h2q + (size_t)m * D + k) = pk4_fp8(hv.x, hv.y, hv.z, hv.w);
;                         const int chunk = (lq >> 1) + 32 * j;
;                         *(LAS v2u*)(h2s + rloc * 4096 + ((chunk ^ (rloc & 15)) << 4) + (lq & 1) * 8) = o; }
	v_pk_fma_f32 v[48:49], v[8:9], v[44:45], v[48:49]
	v_pk_fma_f32 v[46:47], v[10:11], v[42:43], v[46:47]
	v_bfe_u32 v10, v48, 16, 1
	v_bfe_u32 v8, v46, 16, 1
	v_bfe_u32 v9, v47, 16, 1
	v_bfe_u32 v11, v49, 16, 1
	v_add3_u32 v8, v46, v8, s86
	v_add3_u32 v10, v48, v10, s86
	v_add3_u32 v9, v47, v9, s86
	v_add3_u32 v11, v49, v11, s86
	v_lshrrev_b32_e32 v8, 16, v8
	v_lshrrev_b32_e32 v10, 16, v10
	v_and_or_b32 v8, v9, s82, v8
	v_and_or_b32 v9, v11, s82, v10
	global_store_dwordx2 v[22:23], v[8:9], off offset:3072
	ds_read_b128 v[8:11], v252 offset:22528
	s_nop 0
	ds_read_b128 v[42:45], v252 offset:30720
	ds_write_b64 v188, v[50:51]
	v_and_b32_sdwa v51, v114, v203 dst_sel:DWORD dst_unused:UNUSED_PAD src0_sel:WORD_1 src1_sel:DWORD
	v_and_b32_sdwa v50, v116, v203 dst_sel:DWORD dst_unused:UNUSED_PAD src0_sel:WORD_1 src1_sel:DWORD
	v_add3_u32 v64, v114, v51, s86
	v_add3_u32 v51, v117, v62, s86
	v_add3_u32 v62, v115, v63, s86
	v_add3_u32 v50, v116, v50, s86
	v_and_b32_e32 v51, 0xffff0000, v51
	v_and_b32_e32 v62, 0xffff0000, v62
	v_or_b32_sdwa v51, v51, v50 dst_sel:DWORD dst_unused:UNUSED_PAD src0_sel:DWORD src1_sel:WORD_1
	v_or_b32_sdwa v50, v62, v64 dst_sel:DWORD dst_unused:UNUSED_PAD src0_sel:DWORD src1_sel:WORD_1
	ds_write_b64 v189, v[50:51]
	v_and_b32_sdwa v51, v118, v203 dst_sel:DWORD dst_unused:UNUSED_PAD src0_sel:WORD_1 src1_sel:DWORD
	v_and_b32_sdwa v62, v121, v203 dst_sel:DWORD dst_unused:UNUSED_PAD src0_sel:WORD_1 src1_sel:DWORD
	v_and_b32_sdwa v63, v119, v203 dst_sel:DWORD dst_unused:UNUSED_PAD src0_sel:WORD_1 src1_sel:DWORD
	v_and_b32_sdwa v50, v120, v203 dst_sel:DWORD dst_unused:UNUSED_PAD src0_sel:WORD_1 src1_sel:DWORD
	v_add3_u32 v64, v118, v51, s86
	v_add3_u32 v51, v121, v62, s86
	v_add3_u32 v62, v119, v63, s86
	v_add3_u32 v50, v120, v50, s86
	v_and_b32_e32 v51, 0xffff0000, v51
	v_and_b32_e32 v62, 0xffff0000, v62
	v_or_b32_sdwa v51, v51, v50 dst_sel:DWORD dst_unused:UNUSED_PAD src0_sel:DWORD src1_sel:WORD_1
	v_or_b32_sdwa v50, v62, v64 dst_sel:DWORD dst_unused:UNUSED_PAD src0_sel:DWORD src1_sel:WORD_1
	ds_write_b64 v190, v[50:51]
	v_and_b32_sdwa v51, v122, v203 dst_sel:DWORD dst_unused:UNUSED_PAD src0_sel:WORD_1 src1_sel:DWORD
	v_and_b32_sdwa v62, v125, v203 dst_sel:DWORD dst_unused:UNUSED_PAD src0_sel:WORD_1 src1_sel:DWORD
	v_and_b32_sdwa v63, v123, v203 dst_sel:DWORD dst_unused:UNUSED_PAD src0_sel:WORD_1 src1_sel:DWORD
	v_and_b32_sdwa v50, v124, v203 dst_sel:DWORD dst_unused:UNUSED_PAD src0_sel:WORD_1 src1_sel:DWORD
	v_add3_u32 v64, v122, v51, s86
	v_add3_u32 v51, v125, v62, s86
	v_add3_u32 v62, v123, v63, s86
	v_add3_u32 v50, v124, v50, s86
	v_and_b32_e32 v51, 0xffff0000, v51
	v_and_b32_e32 v62, 0xffff0000, v62
	v_or_b32_sdwa v51, v51, v50 dst_sel:DWORD dst_unused:UNUSED_PAD src0_sel:DWORD src1_sel:WORD_1
	v_or_b32_sdwa v50, v62, v64 dst_sel:DWORD dst_unused:UNUSED_PAD src0_sel:DWORD src1_sel:WORD_1
	ds_write_b64 v191, v[50:51]
	v_pk_mul_f32 v[50:51], v[6:7], v[88:89] op_sel_hi:[1,0]
	v_pk_mul_f32 v[62:63], v[4:5], v[88:89] op_sel_hi:[1,0]
	v_and_b32_sdwa v5, v126, v203 dst_sel:DWORD dst_unused:UNUSED_PAD src0_sel:WORD_1 src1_sel:DWORD
	v_and_b32_sdwa v6, v129, v203 dst_sel:DWORD dst_unused:UNUSED_PAD src0_sel:WORD_1 src1_sel:DWORD
	v_and_b32_sdwa v7, v127, v203 dst_sel:DWORD dst_unused:UNUSED_PAD src0_sel:WORD_1 src1_sel:DWORD
	v_and_b32_sdwa v4, v128, v203 dst_sel:DWORD dst_unused:UNUSED_PAD src0_sel:WORD_1 src1_sel:DWORD
	v_add3_u32 v64, v126, v5, s86
	v_add3_u32 v5, v129, v6, s86
	v_add3_u32 v6, v127, v7, s86
	v_add3_u32 v4, v128, v4, s86
	v_and_b32_e32 v5, 0xffff0000, v5
	v_and_b32_e32 v6, 0xffff0000, v6
	v_or_b32_sdwa v5, v5, v4 dst_sel:DWORD dst_unused:UNUSED_PAD src0_sel:DWORD src1_sel:WORD_1
	v_or_b32_sdwa v4, v6, v64 dst_sel:DWORD dst_unused:UNUSED_PAD src0_sel:DWORD src1_sel:WORD_1
	ds_write_b64 v177, v[4:5]
	v_and_b32_sdwa v5, v130, v203 dst_sel:DWORD dst_unused:UNUSED_PAD src0_sel:WORD_1 src1_sel:DWORD
	v_and_b32_sdwa v6, v133, v203 dst_sel:DWORD dst_unused:UNUSED_PAD src0_sel:WORD_1 src1_sel:DWORD
	v_and_b32_sdwa v7, v131, v203 dst_sel:DWORD dst_unused:UNUSED_PAD src0_sel:WORD_1 src1_sel:DWORD
	v_and_b32_sdwa v4, v132, v203 dst_sel:DWORD dst_unused:UNUSED_PAD src0_sel:WORD_1 src1_sel:DWORD
	v_add3_u32 v64, v130, v5, s86
	v_add3_u32 v5, v133, v6, s86
	v_add3_u32 v6, v131, v7, s86
	v_add3_u32 v4, v132, v4, s86
	v_and_b32_e32 v5, 0xffff0000, v5
	v_and_b32_e32 v6, 0xffff0000, v6
	v_or_b32_sdwa v5, v5, v4 dst_sel:DWORD dst_unused:UNUSED_PAD src0_sel:DWORD src1_sel:WORD_1
	v_or_b32_sdwa v4, v6, v64 dst_sel:DWORD dst_unused:UNUSED_PAD src0_sel:DWORD src1_sel:WORD_1
	ds_write_b64 v192, v[4:5]
	v_and_b32_sdwa v4, v136, v203 dst_sel:DWORD dst_unused:UNUSED_PAD src0_sel:WORD_1 src1_sel:DWORD
	v_and_b32_sdwa v5, v134, v203 dst_sel:DWORD dst_unused:UNUSED_PAD src0_sel:WORD_1 src1_sel:DWORD
	v_add3_u32 v64, v134, v5, s86
	v_add3_u32 v65, v136, v4, s86
	v_and_b32_sdwa v6, v137, v203 dst_sel:DWORD dst_unused:UNUSED_PAD src0_sel:WORD_1 src1_sel:DWORD
	v_and_b32_sdwa v7, v135, v203 dst_sel:DWORD dst_unused:UNUSED_PAD src0_sel:WORD_1 src1_sel:DWORD
	v_add3_u32 v6, v137, v6, s86
	v_add3_u32 v7, v135, v7, s86
	v_and_b32_e32 v6, 0xffff0000, v6
	s_waitcnt lgkmcnt(0)
	v_pk_add_f32 v[4:5], v[8:9], 1.0 op_sel_hi:[1,0]
	s_waitcnt lgkmcnt(0)
; #define GAS __attribute__((address_space(1)))
; #define LAS __attribute__((address_space(3)))
; __device__ __forceinline__ unsigned pk2(float lo, float hi) { return f2bf(lo) | (f2bf(hi) << 16); }
; __device__ __forceinline__ unsigned pk4_fp8(float a, float b, float c, float d) { int r = __builtin_amdgcn_cvt_pk_fp8_f32(a, b, 0, false); r = __builtin_amdgcn_cvt_pk_fp8_f32(c, d, r, true); return (unsigned)r; }
; template <int l>
; __device__ __forceinline__ void layer_phases(Frame& F, const XcdBarrier& bar, const int lo, const int hi) {
;     ...
;                     for (int j = 0; j < 8; ++j) { const int k = 4 * lq + 256 * j;
;                         const f32x4 xv = v[j] * rstd * *(const GAS f32x4*)(g1 + k) + *(const GAS f32x4*)(b1 + k);
;                         { v2u xo; xo.x = pk2(xv.x, xv.y); xo.y = pk2(xv.z, xv.w); *(GAS v2u*)(x1 + (size_t)m * D + k) = xo; }
;                         const f32x4 hv = xv * (*(const GAS f32x4*)(mrow + 8192 + k) + 1.0f) + *(const GAS f32x4*)(mrow + 6144 + k);
;                         v2u o; o.x = pk2(hv.x, hv.y); o.y = pk2(hv.z, hv.w);
;                         *(GAS unsigned*)(h2q + (size_t)m * D + k) = pk4_fp8(hv.x, hv.y, hv.z, hv.w);
;                         const int chunk = (lq >> 1) + 32 * j;
;                         *(LAS v2u*)(h2s + rloc * 4096 + ((chunk ^ (rloc & 15)) << 4) + (lq & 1) * 8) = o; }
	v_pk_fma_f32 v[42:43], v[46:47], v[4:5], v[42:43]
	v_pk_add_f32 v[4:5], v[10:11], 1.0 op_sel_hi:[1,0]
	v_cvt_pk_fp8_f32 v166, v42, v43
	v_pk_fma_f32 v[44:45], v[48:49], v[4:5], v[44:45]
	v_and_b32_e32 v4, 0xffff0000, v7
	v_or_b32_sdwa v47, v6, v65 dst_sel:DWORD dst_unused:UNUSED_PAD src0_sel:DWORD src1_sel:WORD_1
	v_cvt_pk_fp8_f32 v166, v44, v45 op_sel:[0,0,1]
	v_or_b32_sdwa v46, v4, v64 dst_sel:DWORD dst_unused:UNUSED_PAD src0_sel:DWORD src1_sel:WORD_1
	global_store_dword v[20:21], v166, off offset:1536
	ds_read_b128 v[4:7], v252 offset:15360
	ds_read_b128 v[8:11], v252 offset:7168
	v_and_b32_sdwa v39, v138, v203 dst_sel:DWORD dst_unused:UNUSED_PAD src0_sel:WORD_1 src1_sel:DWORD
	v_and_b32_sdwa v40, v141, v203 dst_sel:DWORD dst_unused:UNUSED_PAD src0_sel:WORD_1 src1_sel:DWORD
	v_and_b32_sdwa v41, v139, v203 dst_sel:DWORD dst_unused:UNUSED_PAD src0_sel:WORD_1 src1_sel:DWORD
	ds_write_b64 v193, v[46:47]
	v_and_b32_sdwa v38, v140, v203 dst_sel:DWORD dst_unused:UNUSED_PAD src0_sel:WORD_1 src1_sel:DWORD
	v_add3_u32 v46, v138, v39, s86
	v_add3_u32 v39, v141, v40, s86
	v_add3_u32 v40, v139, v41, s86
	v_add3_u32 v38, v140, v38, s86
	v_and_b32_e32 v39, 0xffff0000, v39
	v_and_b32_e32 v40, 0xffff0000, v40
	v_or_b32_sdwa v39, v39, v38 dst_sel:DWORD dst_unused:UNUSED_PAD src0_sel:DWORD src1_sel:WORD_1
	v_or_b32_sdwa v38, v40, v46 dst_sel:DWORD dst_unused:UNUSED_PAD src0_sel:DWORD src1_sel:WORD_1
	ds_write_b64 v205, v[38:39]
	v_and_b32_sdwa v39, v142, v203 dst_sel:DWORD dst_unused:UNUSED_PAD src0_sel:WORD_1 src1_sel:DWORD
	v_and_b32_sdwa v40, v145, v203 dst_sel:DWORD dst_unused:UNUSED_PAD src0_sel:WORD_1 src1_sel:DWORD
	v_and_b32_sdwa v41, v143, v203 dst_sel:DWORD dst_unused:UNUSED_PAD src0_sel:WORD_1 src1_sel:DWORD
	v_and_b32_sdwa v38, v144, v203 dst_sel:DWORD dst_unused:UNUSED_PAD src0_sel:WORD_1 src1_sel:DWORD
	v_add3_u32 v46, v142, v39, s86
	v_add3_u32 v39, v145, v40, s86
	v_add3_u32 v40, v143, v41, s86
	v_add3_u32 v38, v144, v38, s86
	v_and_b32_e32 v39, 0xffff0000, v39
	v_and_b32_e32 v40, 0xffff0000, v40
	v_or_b32_sdwa v39, v39, v38 dst_sel:DWORD dst_unused:UNUSED_PAD src0_sel:DWORD src1_sel:WORD_1
	v_or_b32_sdwa v38, v40, v46 dst_sel:DWORD dst_unused:UNUSED_PAD src0_sel:DWORD src1_sel:WORD_1
	ds_write_b64 v206, v[38:39]
	v_and_b32_sdwa v39, v146, v203 dst_sel:DWORD dst_unused:UNUSED_PAD src0_sel:WORD_1 src1_sel:DWORD
	v_and_b32_sdwa v40, v149, v203 dst_sel:DWORD dst_unused:UNUSED_PAD src0_sel:WORD_1 src1_sel:DWORD
	v_and_b32_sdwa v41, v147, v203 dst_sel:DWORD dst_unused:UNUSED_PAD src0_sel:WORD_1 src1_sel:DWORD
	v_and_b32_sdwa v38, v148, v203 dst_sel:DWORD dst_unused:UNUSED_PAD src0_sel:WORD_1 src1_sel:DWORD
	v_add3_u32 v46, v146, v39, s86
	v_add3_u32 v39, v149, v40, s86
	v_add3_u32 v40, v147, v41, s86
	v_add3_u32 v38, v148, v38, s86
	v_and_b32_e32 v39, 0xffff0000, v39
	v_and_b32_e32 v40, 0xffff0000, v40
	v_or_b32_sdwa v39, v39, v38 dst_sel:DWORD dst_unused:UNUSED_PAD src0_sel:DWORD src1_sel:WORD_1
	v_or_b32_sdwa v38, v40, v46 dst_sel:DWORD dst_unused:UNUSED_PAD src0_sel:DWORD src1_sel:WORD_1
	v_and_b32_sdwa v40, v3, v203 dst_sel:DWORD dst_unused:UNUSED_PAD src0_sel:WORD_1 src1_sel:DWORD
	v_and_b32_sdwa v41, v1, v203 dst_sel:DWORD dst_unused:UNUSED_PAD src0_sel:WORD_1 src1_sel:DWORD
	ds_write_b64 v207, v[38:39]
	v_and_b32_sdwa v38, v2, v203 dst_sel:DWORD dst_unused:UNUSED_PAD src0_sel:WORD_1 src1_sel:DWORD
	v_and_b32_sdwa v39, v0, v203 dst_sel:DWORD dst_unused:UNUSED_PAD src0_sel:WORD_1 src1_sel:DWORD
	v_add3_u32 v3, v3, v40, s86
	v_add3_u32 v1, v1, v41, s86
	v_add3_u32 v0, v0, v39, s86
	v_add3_u32 v2, v2, v38, s86
	v_and_b32_e32 v3, 0xffff0000, v3
	v_and_b32_e32 v38, 0xffff0000, v1
	v_or_b32_sdwa v1, v3, v2 dst_sel:DWORD dst_unused:UNUSED_PAD src0_sel:DWORD src1_sel:WORD_1
	v_or_b32_sdwa v0, v38, v0 dst_sel:DWORD dst_unused:UNUSED_PAD src0_sel:DWORD src1_sel:WORD_1
	ds_write_b64 v208, v[0:1]
	v_and_b32_sdwa v1, v16, v203 dst_sel:DWORD dst_unused:UNUSED_PAD src0_sel:WORD_1 src1_sel:DWORD
	v_and_b32_sdwa v2, v19, v203 dst_sel:DWORD dst_unused:UNUSED_PAD src0_sel:WORD_1 src1_sel:DWORD
	v_and_b32_sdwa v3, v17, v203 dst_sel:DWORD dst_unused:UNUSED_PAD src0_sel:WORD_1 src1_sel:DWORD
	v_and_b32_sdwa v0, v18, v203 dst_sel:DWORD dst_unused:UNUSED_PAD src0_sel:WORD_1 src1_sel:DWORD
	v_add3_u32 v16, v16, v1, s86
	v_add3_u32 v1, v19, v2, s86
	v_add3_u32 v2, v17, v3, s86
	v_add3_u32 v0, v18, v0, s86
	v_and_b32_e32 v1, 0xffff0000, v1
	v_and_b32_e32 v2, 0xffff0000, v2
	v_or_b32_sdwa v1, v1, v0 dst_sel:DWORD dst_unused:UNUSED_PAD src0_sel:DWORD src1_sel:WORD_1
	v_or_b32_sdwa v0, v2, v16 dst_sel:DWORD dst_unused:UNUSED_PAD src0_sel:DWORD src1_sel:WORD_1
	ds_write_b64 v209, v[0:1]
	v_and_b32_sdwa v1, v24, v203 dst_sel:DWORD dst_unused:UNUSED_PAD src0_sel:WORD_1 src1_sel:DWORD
	v_and_b32_sdwa v2, v27, v203 dst_sel:DWORD dst_unused:UNUSED_PAD src0_sel:WORD_1 src1_sel:DWORD
	v_and_b32_sdwa v3, v25, v203 dst_sel:DWORD dst_unused:UNUSED_PAD src0_sel:WORD_1 src1_sel:DWORD
	v_and_b32_sdwa v0, v26, v203 dst_sel:DWORD dst_unused:UNUSED_PAD src0_sel:WORD_1 src1_sel:DWORD
	v_add3_u32 v16, v24, v1, s86
	v_add3_u32 v1, v27, v2, s86
	v_add3_u32 v2, v25, v3, s86
	v_add3_u32 v0, v26, v0, s86
	v_and_b32_e32 v1, 0xffff0000, v1
	v_and_b32_e32 v2, 0xffff0000, v2
	v_or_b32_sdwa v1, v1, v0 dst_sel:DWORD dst_unused:UNUSED_PAD src0_sel:DWORD src1_sel:WORD_1
	v_or_b32_sdwa v0, v2, v16 dst_sel:DWORD dst_unused:UNUSED_PAD src0_sel:DWORD src1_sel:WORD_1
	ds_write_b64 v167, v[0:1]
	s_waitcnt lgkmcnt(0)
; #define GAS __attribute__((address_space(1)))
; #define LAS __attribute__((address_space(3)))
; __device__ __forceinline__ unsigned pk2(float lo, float hi) { return f2bf(lo) | (f2bf(hi) << 16); }
; __device__ __forceinline__ unsigned pk4_fp8(float a, float b, float c, float d) { int r = __builtin_amdgcn_cvt_pk_fp8_f32(a, b, 0, false); r = __builtin_amdgcn_cvt_pk_fp8_f32(c, d, r, true); return (unsigned)r; }
; template <int l>
; __device__ __forceinline__ void layer_phases(Frame& F, const XcdBarrier& bar, const int lo, const int hi) {
;     ...
;                     for (int j = 0; j < 8; ++j) { const int k = 4 * lq + 256 * j;
;                         const f32x4 xv = v[j] * rstd * *(const GAS f32x4*)(g1 + k) + *(const GAS f32x4*)(b1 + k);
;                         { v2u xo; xo.x = pk2(xv.x, xv.y); xo.y = pk2(xv.z, xv.w); *(GAS v2u*)(x1 + (size_t)m * D + k) = xo; }
;                         const f32x4 hv = xv * (*(const GAS f32x4*)(mrow + 8192 + k) + 1.0f) + *(const GAS f32x4*)(mrow + 6144 + k);
;                         v2u o; o.x = pk2(hv.x, hv.y); o.y = pk2(hv.z, hv.w);
;                         *(GAS unsigned*)(h2q + (size_t)m * D + k) = pk4_fp8(hv.x, hv.y, hv.z, hv.w);
;                         const int chunk = (lq >> 1) + 32 * j;
;                         *(LAS v2u*)(h2s + rloc * 4096 + ((chunk ^ (rloc & 15)) << 4) + (lq & 1) * 8) = o; }
	v_pk_fma_f32 v[10:11], v[62:63], v[6:7], v[10:11]
	v_pk_fma_f32 v[8:9], v[50:51], v[4:5], v[8:9]
	v_bfe_u32 v2, v10, 16, 1
	v_bfe_u32 v0, v8, 16, 1
	v_bfe_u32 v1, v9, 16, 1
	v_bfe_u32 v3, v11, 16, 1
	v_add3_u32 v0, v8, v0, s86
	v_add3_u32 v2, v10, v2, s86
	v_add3_u32 v1, v9, v1, s86
	v_add3_u32 v3, v11, v3, s86
	v_lshrrev_b32_e32 v0, 16, v0
	v_lshrrev_b32_e32 v2, 16, v2
	v_and_or_b32 v0, v1, s82, v0
	v_and_or_b32 v1, v3, s82, v2
	global_store_dwordx2 v[22:23], v[0:1], off offset:3584
	ds_read_b128 v[0:3], v252 offset:23552
	v_and_b32_sdwa v17, v28, v203 dst_sel:DWORD dst_unused:UNUSED_PAD src0_sel:WORD_1 src1_sel:DWORD
	ds_read_b128 v[4:7], v252 offset:31744
	v_and_b32_sdwa v18, v31, v203 dst_sel:DWORD dst_unused:UNUSED_PAD src0_sel:WORD_1 src1_sel:DWORD
	v_and_b32_sdwa v19, v29, v203 dst_sel:DWORD dst_unused:UNUSED_PAD src0_sel:WORD_1 src1_sel:DWORD
	v_and_b32_sdwa v16, v30, v203 dst_sel:DWORD dst_unused:UNUSED_PAD src0_sel:WORD_1 src1_sel:DWORD
	v_add3_u32 v22, v28, v17, s86
	v_add3_u32 v17, v31, v18, s86
	v_add3_u32 v18, v29, v19, s86
	v_add3_u32 v16, v30, v16, s86
	v_and_b32_e32 v17, 0xffff0000, v17
	v_and_b32_e32 v18, 0xffff0000, v18
	v_or_b32_sdwa v17, v17, v16 dst_sel:DWORD dst_unused:UNUSED_PAD src0_sel:DWORD src1_sel:WORD_1
	v_or_b32_sdwa v16, v18, v22 dst_sel:DWORD dst_unused:UNUSED_PAD src0_sel:DWORD src1_sel:WORD_1
	ds_write_b64 v170, v[16:17]
	v_and_b32_sdwa v17, v36, v203 dst_sel:DWORD dst_unused:UNUSED_PAD src0_sel:WORD_1 src1_sel:DWORD
	v_and_b32_sdwa v18, v151, v203 dst_sel:DWORD dst_unused:UNUSED_PAD src0_sel:WORD_1 src1_sel:DWORD
	v_and_b32_sdwa v19, v37, v203 dst_sel:DWORD dst_unused:UNUSED_PAD src0_sel:WORD_1 src1_sel:DWORD
	v_and_b32_sdwa v16, v150, v203 dst_sel:DWORD dst_unused:UNUSED_PAD src0_sel:WORD_1 src1_sel:DWORD
	v_add3_u32 v22, v36, v17, s86
	v_add3_u32 v17, v151, v18, s86
	v_add3_u32 v18, v37, v19, s86
	v_add3_u32 v16, v150, v16, s86
	v_and_b32_e32 v17, 0xffff0000, v17
	v_and_b32_e32 v18, 0xffff0000, v18
	v_or_b32_sdwa v17, v17, v16 dst_sel:DWORD dst_unused:UNUSED_PAD src0_sel:DWORD src1_sel:WORD_1
	v_or_b32_sdwa v16, v18, v22 dst_sel:DWORD dst_unused:UNUSED_PAD src0_sel:DWORD src1_sel:WORD_1
	ds_write_b64 v171, v[16:17]
	v_and_b32_sdwa v17, v74, v203 dst_sel:DWORD dst_unused:UNUSED_PAD src0_sel:WORD_1 src1_sel:DWORD
	v_and_b32_sdwa v18, v81, v203 dst_sel:DWORD dst_unused:UNUSED_PAD src0_sel:WORD_1 src1_sel:DWORD
	v_and_b32_sdwa v19, v75, v203 dst_sel:DWORD dst_unused:UNUSED_PAD src0_sel:WORD_1 src1_sel:DWORD
	v_and_b32_sdwa v16, v80, v203 dst_sel:DWORD dst_unused:UNUSED_PAD src0_sel:WORD_1 src1_sel:DWORD
	v_add3_u32 v22, v74, v17, s86
	v_add3_u32 v17, v81, v18, s86
	v_add3_u32 v18, v75, v19, s86
	v_add3_u32 v16, v80, v16, s86
	v_and_b32_e32 v17, 0xffff0000, v17
	v_and_b32_e32 v18, 0xffff0000, v18
	v_or_b32_sdwa v17, v17, v16 dst_sel:DWORD dst_unused:UNUSED_PAD src0_sel:DWORD src1_sel:WORD_1
	v_or_b32_sdwa v16, v18, v22 dst_sel:DWORD dst_unused:UNUSED_PAD src0_sel:DWORD src1_sel:WORD_1
	ds_write_b64 v172, v[16:17]
	v_and_b32_sdwa v17, v82, v203 dst_sel:DWORD dst_unused:UNUSED_PAD src0_sel:WORD_1 src1_sel:DWORD
	v_and_b32_sdwa v18, v153, v203 dst_sel:DWORD dst_unused:UNUSED_PAD src0_sel:WORD_1 src1_sel:DWORD
	v_and_b32_sdwa v19, v83, v203 dst_sel:DWORD dst_unused:UNUSED_PAD src0_sel:WORD_1 src1_sel:DWORD
	v_and_b32_sdwa v16, v152, v203 dst_sel:DWORD dst_unused:UNUSED_PAD src0_sel:WORD_1 src1_sel:DWORD
	v_add3_u32 v22, v82, v17, s86
	v_add3_u32 v17, v153, v18, s86
	v_add3_u32 v18, v83, v19, s86
	v_add3_u32 v16, v152, v16, s86
	v_and_b32_e32 v17, 0xffff0000, v17
	v_and_b32_e32 v18, 0xffff0000, v18
	v_or_b32_sdwa v17, v17, v16 dst_sel:DWORD dst_unused:UNUSED_PAD src0_sel:DWORD src1_sel:WORD_1
	v_or_b32_sdwa v16, v18, v22 dst_sel:DWORD dst_unused:UNUSED_PAD src0_sel:DWORD src1_sel:WORD_1
	v_and_b32_sdwa v18, v15, v203 dst_sel:DWORD dst_unused:UNUSED_PAD src0_sel:WORD_1 src1_sel:DWORD
	v_and_b32_sdwa v19, v13, v203 dst_sel:DWORD dst_unused:UNUSED_PAD src0_sel:WORD_1 src1_sel:DWORD
	ds_write_b64 v173, v[16:17]
	v_and_b32_sdwa v16, v14, v203 dst_sel:DWORD dst_unused:UNUSED_PAD src0_sel:WORD_1 src1_sel:DWORD
	v_and_b32_sdwa v17, v12, v203 dst_sel:DWORD dst_unused:UNUSED_PAD src0_sel:WORD_1 src1_sel:DWORD
	v_add3_u32 v15, v15, v18, s86
	v_add3_u32 v13, v13, v19, s86
	v_add3_u32 v12, v12, v17, s86
	v_add3_u32 v14, v14, v16, s86
	v_and_b32_e32 v15, 0xffff0000, v15
	v_and_b32_e32 v16, 0xffff0000, v13
	v_or_b32_sdwa v13, v15, v14 dst_sel:DWORD dst_unused:UNUSED_PAD src0_sel:DWORD src1_sel:WORD_1
	v_or_b32_sdwa v12, v16, v12 dst_sel:DWORD dst_unused:UNUSED_PAD src0_sel:DWORD src1_sel:WORD_1
	ds_write_b64 v174, v[12:13]
	v_and_b32_sdwa v13, v42, v203 dst_sel:DWORD dst_unused:UNUSED_PAD src0_sel:WORD_1 src1_sel:DWORD
	v_and_b32_sdwa v14, v45, v203 dst_sel:DWORD dst_unused:UNUSED_PAD src0_sel:WORD_1 src1_sel:DWORD
	v_and_b32_sdwa v15, v43, v203 dst_sel:DWORD dst_unused:UNUSED_PAD src0_sel:WORD_1 src1_sel:DWORD
	v_and_b32_sdwa v12, v44, v203 dst_sel:DWORD dst_unused:UNUSED_PAD src0_sel:WORD_1 src1_sel:DWORD
	v_add3_u32 v16, v42, v13, s86
	v_add3_u32 v13, v45, v14, s86
	v_add3_u32 v14, v43, v15, s86
	v_add3_u32 v12, v44, v12, s86
	v_and_b32_e32 v13, 0xffff0000, v13
	v_and_b32_e32 v14, 0xffff0000, v14
	v_or_b32_sdwa v13, v13, v12 dst_sel:DWORD dst_unused:UNUSED_PAD src0_sel:DWORD src1_sel:WORD_1
	v_or_b32_sdwa v12, v14, v16 dst_sel:DWORD dst_unused:UNUSED_PAD src0_sel:DWORD src1_sel:WORD_1
	ds_write_b64 v175, v[12:13]
	s_waitcnt lgkmcnt(0)
	v_pk_add_f32 v[0:1], v[0:1], 1.0 op_sel_hi:[1,0]
	v_pk_add_f32 v[2:3], v[2:3], 1.0 op_sel_hi:[1,0]
	s_waitcnt lgkmcnt(0)
; #define GAS __attribute__((address_space(1)))
; #define LAS __attribute__((address_space(3)))
; __device__ __forceinline__ unsigned pk2(float lo, float hi) { return f2bf(lo) | (f2bf(hi) << 16); }
; __device__ __forceinline__ unsigned pk4_fp8(float a, float b, float c, float d) { int r = __builtin_amdgcn_cvt_pk_fp8_f32(a, b, 0, false); r = __builtin_amdgcn_cvt_pk_fp8_f32(c, d, r, true); return (unsigned)r; }
; #define P5_LDB(dst, q0) do { _Pragma("unroll") for (int q_ = 0; q_ < 4; ++q_) _Pragma("unroll") for (int c_ = 0; c_ < 4; ++c_) dst[q_][c_] = *(const GAS bf16x8*)(wbase + (size_t)((q0) + q_) * 4096 + c_ * 1024); } while (0)
; template <int l>
; __device__ __forceinline__ void layer_phases(Frame& F, const XcdBarrier& bar, const int lo, const int hi) {
;     ...
;                     for (int j = 0; j < 8; ++j) { const int k = 4 * lq + 256 * j;
;                         const f32x4 xv = v[j] * rstd * *(const GAS f32x4*)(g1 + k) + *(const GAS f32x4*)(b1 + k);
;                         { v2u xo; xo.x = pk2(xv.x, xv.y); xo.y = pk2(xv.z, xv.w); *(GAS v2u*)(x1 + (size_t)m * D + k) = xo; }
;                         const f32x4 hv = xv * (*(const GAS f32x4*)(mrow + 8192 + k) + 1.0f) + *(const GAS f32x4*)(mrow + 6144 + k);
;                         v2u o; o.x = pk2(hv.x, hv.y); o.y = pk2(hv.z, hv.w);
;                         *(GAS unsigned*)(h2q + (size_t)m * D + k) = pk4_fp8(hv.x, hv.y, hv.z, hv.w);
;                         const int chunk = (lq >> 1) + 32 * j;
;                         *(LAS v2u*)(h2s + rloc * 4096 + ((chunk ^ (rloc & 15)) << 4) + (lq & 1) * 8) = o; }
;     ...
;                 bf16x8 bqa[4][4], bqb[4][4];
;                 const unsigned lo_ = lq * 16;
;                 const unsigned char* wbase = wrf + (size_t)(16 * F.wave) * 4096 + lo_;
;     ...
;                 asm volatile("" ::: "memory");
;                 P5_LDB(bqa, 0); P5_LDB(bqb, 4);
;                 __syncthreads();
;                 att::f32x16 acc0 = att::f32x16{}, acc1 = att::f32x16{};
;                 P5_MMA(bqa, 0); asm volatile("" ::: "memory"); P5_LDB(bqa, 8);
;                 P5_MMA(bqb, 4); asm volatile("" ::: "memory"); P5_LDB(bqb, 12);
;                 P5_MMA(bqa, 8); P5_MMA(bqb, 12);
	v_pk_fma_f32 v[0:1], v[8:9], v[0:1], v[4:5]
	v_pk_fma_f32 v[2:3], v[10:11], v[2:3], v[6:7]
	v_cvt_pk_fp8_f32 v155, v0, v1
	v_and_b32_sdwa v5, v0, v203 dst_sel:DWORD dst_unused:UNUSED_PAD src0_sel:WORD_1 src1_sel:DWORD
	v_and_b32_sdwa v6, v3, v203 dst_sel:DWORD dst_unused:UNUSED_PAD src0_sel:WORD_1 src1_sel:DWORD
	v_and_b32_sdwa v7, v1, v203 dst_sel:DWORD dst_unused:UNUSED_PAD src0_sel:WORD_1 src1_sel:DWORD
	v_cvt_pk_fp8_f32 v155, v2, v3 op_sel:[0,0,1]
	v_and_b32_sdwa v4, v2, v203 dst_sel:DWORD dst_unused:UNUSED_PAD src0_sel:WORD_1 src1_sel:DWORD
	v_add3_u32 v0, v0, v5, s86
	v_add3_u32 v5, v3, v6, s86
	v_add3_u32 v1, v1, v7, s86
	v_add3_u32 v4, v2, v4, s86
	v_and_b32_e32 v5, 0xffff0000, v5
	v_and_b32_e32 v6, 0xffff0000, v1
	v_or_b32_sdwa v1, v5, v4 dst_sel:DWORD dst_unused:UNUSED_PAD src0_sel:DWORD src1_sel:WORD_1
	v_or_b32_sdwa v0, v6, v0 dst_sel:DWORD dst_unused:UNUSED_PAD src0_sel:DWORD src1_sel:WORD_1
	ds_write_b64 v164, v[0:1]
	global_store_dword v[20:21], v155, off offset:1792
	global_load_dwordx4 v[0:3], v60, s[36:37]
	global_load_dwordx4 v[36:39], v60, s[36:37] offset:1024
	global_load_dwordx4 v[16:19], v60, s[36:37] offset:2048
	global_load_dwordx4 v[32:35], v60, s[36:37] offset:3072
	v_add_co_u32_e32 v4, vcc, s87, v72
	v_add_u32_e32 v63, s69, v154
	s_nop 0
	v_addc_co_u32_e32 v5, vcc, 0, v73, vcc
	v_add_co_u32_e32 v8, vcc, s0, v72
	s_movk_i32 s0, 0x3000
	s_nop 0
	v_addc_co_u32_e32 v9, vcc, 0, v73, vcc
	global_load_dwordx4 v[40:43], v[8:9], off offset:-4096
	global_load_dwordx4 v[64:67], v[4:5], off offset:1024
	global_load_dwordx4 v[68:71], v[4:5], off offset:2048
	v_add_co_u32_e32 v12, vcc, s0, v72
	s_movk_i32 s0, 0x6000
	s_nop 0
	v_addc_co_u32_e32 v13, vcc, 0, v73, vcc
	v_add_co_u32_e32 v10, vcc, s83, v72
	v_lshl_add_u32 v62, v89, 12, 0
	s_nop 0
	v_addc_co_u32_e32 v11, vcc, 0, v73, vcc
	v_add_co_u32_e32 v6, vcc, s24, v72
	v_bitop3_b32 v22, v63, v204, 15 bitop3:0x78
	s_nop 0
	v_addc_co_u32_e32 v7, vcc, 0, v73, vcc
	v_add_co_u32_e32 v20, vcc, s0, v72
	v_lshl_add_u32 v22, v22, 4, v62
	s_nop 0
	v_addc_co_u32_e32 v21, vcc, 0, v73, vcc
	v_add_co_u32_e32 v14, vcc, s26, v72
	v_readlane_b32 s0, v248, 30
	s_nop 0
	v_addc_co_u32_e32 v15, vcc, 0, v73, vcc
	v_add_co_u32_e32 v86, vcc, s14, v72
	s_nop 1
	v_addc_co_u32_e32 v87, vcc, 0, v73, vcc
	global_load_dwordx4 v[74:77], v[8:9], off
	global_load_dwordx4 v[78:81], v[8:9], off offset:1024
	global_load_dwordx4 v[82:85], v[8:9], off offset:2048
	global_load_dwordx4 v[90:93], v[8:9], off offset:3072
	global_load_dwordx4 v[94:97], v[10:11], off offset:-4096
	global_load_dwordx4 v[98:101], v[4:5], off offset:3072
	global_load_dwordx4 v[102:105], v[12:13], off offset:1024
	global_load_dwordx4 v[106:109], v[12:13], off offset:2048
	global_load_dwordx4 v[110:113], v[12:13], off offset:3072
	global_load_dwordx4 v[114:117], v[10:11], off
	global_load_dwordx4 v[118:121], v[10:11], off offset:1024
	global_load_dwordx4 v[122:125], v[10:11], off offset:2048
	global_load_dwordx4 v[126:129], v[10:11], off offset:3072
	global_load_dwordx4 v[130:133], v[6:7], off offset:1024
	global_load_dwordx4 v[134:137], v[6:7], off offset:2048
	global_load_dwordx4 v[138:141], v[20:21], off offset:-4096
	global_load_dwordx4 v[142:145], v[20:21], off
	global_load_dwordx4 v[146:149], v[20:21], off offset:1024
	global_load_dwordx4 v[150:153], v[20:21], off offset:2048
	global_load_dwordx4 v[156:159], v[20:21], off offset:3072
	global_load_dwordx4 v[160:163], v[86:87], off offset:-4096
	global_load_dwordx4 v[164:167], v[6:7], off offset:3072
	global_load_dwordx4 v[48:51], v[14:15], off offset:1024
	global_load_dwordx4 v[168:171], v[14:15], off offset:2048
	global_load_dwordx4 v[44:47], v[14:15], off offset:3072
	s_waitcnt lgkmcnt(0)
	s_barrier
	ds_read_b128 v[172:175], v22
	v_add_u32_e32 v4, 2, v63
	v_bitop3_b32 v4, v4, v204, 15 bitop3:0x78
	v_lshl_add_u32 v4, v4, 4, v62
	ds_read_b128 v[176:179], v4
	s_waitcnt vmcnt(31)
	s_waitcnt lgkmcnt(0)
	v_mfma_f32_32x32x16_bf16 v[0:15], v[172:175], v[0:3], 0
	s_waitcnt vmcnt(29)
	s_waitcnt lgkmcnt(0)
	v_mfma_f32_32x32x16_bf16 v[16:31], v[172:175], v[16:19], 0
	v_mfma_f32_32x32x16_bf16 v[0:15], v[172:175], v[36:39], v[0:15]
	v_add_u32_e32 v36, 6, v63
	v_bitop3_b32 v36, v36, v204, 15 bitop3:0x78
	v_lshl_add_u32 v36, v36, 4, v62
	ds_read_b128 v[36:39], v36
	s_waitcnt vmcnt(28)
	s_waitcnt lgkmcnt(0)
	v_mfma_f32_32x32x16_bf16 v[16:31], v[172:175], v[32:35], v[16:31]
	v_add_u32_e32 v32, 4, v63
	v_bitop3_b32 v32, v32, v204, 15 bitop3:0x78
	v_lshl_add_u32 v32, v32, 4, v62
	ds_read_b128 v[32:35], v32
	s_waitcnt vmcnt(27)
	s_waitcnt lgkmcnt(0)
	v_mfma_f32_32x32x16_bf16 v[0:15], v[176:179], v[40:43], v[0:15]
	v_add_u32_e32 v40, s0, v154
	s_mov_b32 s0, 0xa000
	s_waitcnt vmcnt(25)
	s_waitcnt lgkmcnt(0)
	v_mfma_f32_32x32x16_bf16 v[16:31], v[176:179], v[68:71], v[16:31]
	v_mfma_f32_32x32x16_bf16 v[0:15], v[176:179], v[64:67], v[0:15]
	global_load_dwordx4 v[64:67], v[86:87], off offset:2048
	s_waitcnt vmcnt(20)
	s_waitcnt lgkmcnt(0)
	v_mfma_f32_32x32x16_bf16 v[16:31], v[176:179], v[98:101], v[16:31]
	s_waitcnt lgkmcnt(0)
	v_mfma_f32_32x32x16_bf16 v[0:15], v[32:35], v[74:77], v[0:15]
	v_mfma_f32_32x32x16_bf16 v[16:31], v[32:35], v[82:85], v[16:31]
	v_mfma_f32_32x32x16_bf16 v[0:15], v[32:35], v[78:81], v[0:15]
	v_mfma_f32_32x32x16_bf16 v[16:31], v[32:35], v[90:93], v[16:31]
	v_bitop3_b32 v32, v40, v204, 15 bitop3:0x78
	v_lshl_add_u32 v32, v32, 4, v62
	ds_read_b128 v[32:35], v32
	v_mfma_f32_32x32x16_bf16 v[0:15], v[36:39], v[94:97], v[0:15]
	s_waitcnt vmcnt(18)
	s_waitcnt lgkmcnt(0)
	v_mfma_f32_32x32x16_bf16 v[16:31], v[36:39], v[106:109], v[16:31]
	v_mfma_f32_32x32x16_bf16 v[0:15], v[36:39], v[102:105], v[0:15]
	s_waitcnt vmcnt(17)
; #define P5_LDB(dst, q0) do { _Pragma("unroll") for (int q_ = 0; q_ < 4; ++q_) _Pragma("unroll") for (int c_ = 0; c_ < 4; ++c_) dst[q_][c_] = *(const GAS bf16x8*)(wbase + (size_t)((q0) + q_) * 4096 + c_ * 1024); } while (0)
; template <int l>
; __device__ __forceinline__ void layer_phases(Frame& F, const XcdBarrier& bar, const int lo, const int hi) {
;     ...
;                 asm volatile("" ::: "memory");
;                 P5_LDB(bqa, 0); P5_LDB(bqb, 4);
;                 __syncthreads();
;                 att::f32x16 acc0 = att::f32x16{}, acc1 = att::f32x16{};
;                 P5_MMA(bqa, 0); asm volatile("" ::: "memory"); P5_LDB(bqa, 8);
;                 P5_MMA(bqb, 4); asm volatile("" ::: "memory"); P5_LDB(bqb, 12);
;                 P5_MMA(bqa, 8); P5_MMA(bqb, 12);
	s_waitcnt lgkmcnt(0)
	v_mfma_f32_32x32x16_bf16 v[16:31], v[36:39], v[110:113], v[16:31]
	v_add_u32_e32 v36, 2, v40
	v_bitop3_b32 v36, v36, v204, 15 bitop3:0x78
	v_lshl_add_u32 v36, v36, 4, v62
	ds_read_b128 v[36:39], v36
	s_waitcnt vmcnt(16)
	s_waitcnt lgkmcnt(0)
	v_mfma_f32_32x32x16_bf16 v[0:15], v[32:35], v[114:117], v[0:15]
	s_waitcnt vmcnt(14)
	s_waitcnt lgkmcnt(0)
	v_mfma_f32_32x32x16_bf16 v[16:31], v[32:35], v[122:125], v[16:31]
	v_mfma_f32_32x32x16_bf16 v[0:15], v[32:35], v[118:121], v[0:15]
	s_waitcnt vmcnt(13)
	s_waitcnt lgkmcnt(0)
	v_mfma_f32_32x32x16_bf16 v[16:31], v[32:35], v[126:129], v[16:31]
	v_add_u32_e32 v32, 4, v40
	v_bitop3_b32 v32, v32, v204, 15 bitop3:0x78
	v_lshl_add_u32 v32, v32, 4, v62
	ds_read_b128 v[32:35], v32
	v_add_u32_e32 v40, 6, v40
	v_bitop3_b32 v40, v40, v204, 15 bitop3:0x78
	v_lshl_add_u32 v40, v40, 4, v62
	s_waitcnt vmcnt(10)
	s_waitcnt lgkmcnt(0)
	v_mfma_f32_32x32x16_bf16 v[0:15], v[36:39], v[138:141], v[0:15]
	ds_read_b128 v[40:43], v40
	v_mfma_f32_32x32x16_bf16 v[16:31], v[36:39], v[134:137], v[16:31]
	v_mfma_f32_32x32x16_bf16 v[0:15], v[36:39], v[130:133], v[0:15]
	s_waitcnt vmcnt(4)
	s_waitcnt lgkmcnt(0)
	v_mfma_f32_32x32x16_bf16 v[16:31], v[36:39], v[164:167], v[16:31]
	global_load_dwordx4 v[36:39], v[86:87], off
	global_load_dwordx4 v[68:71], v[86:87], off offset:1024
	global_load_dwordx4 v[74:77], v[86:87], off offset:3072
	v_add_co_u32_e32 v86, vcc, s0, v72
	v_readlane_b32 s0, v248, 28
	s_nop 0
	v_addc_co_u32_e32 v87, vcc, 0, v73, vcc
	s_waitcnt lgkmcnt(1)
	v_mfma_f32_32x32x16_bf16 v[0:15], v[32:35], v[142:145], v[0:15]
	v_add_co_u32_e32 v90, vcc, s25, v72
	global_load_dwordx4 v[78:81], v[86:87], off offset:-4096
	global_load_dwordx4 v[94:97], v[86:87], off
	v_addc_co_u32_e32 v91, vcc, 0, v73, vcc
	global_load_dwordx4 v[82:85], v[90:91], off offset:1024
	v_mfma_f32_32x32x16_bf16 v[16:31], v[32:35], v[150:153], v[16:31]
	v_add_u32_e32 v60, s0, v154
	s_mov_b32 s0, 0xb000
	v_add_co_u32_e32 v118, vcc, s0, v72
	s_mov_b32 s0, 0xc000
	s_nop 0
	v_addc_co_u32_e32 v119, vcc, 0, v73, vcc
	v_mfma_f32_32x32x16_bf16 v[0:15], v[32:35], v[146:149], v[0:15]
	v_add_co_u32_e32 v122, vcc, s0, v72
	v_bitop3_b32 v63, v60, v204, 15 bitop3:0x78
	s_nop 0
	v_addc_co_u32_e32 v123, vcc, 0, v73, vcc
	v_lshl_add_u32 v63, v63, 4, v62
	v_readlane_b32 s0, v248, 29
	v_mfma_f32_32x32x16_bf16 v[16:31], v[32:35], v[156:159], v[16:31]
	global_load_dwordx4 v[32:35], v[90:91], off offset:2048
	s_nop 0
	global_load_dwordx4 v[90:93], v[90:91], off offset:3072
	s_waitcnt lgkmcnt(0)
	v_mfma_f32_32x32x16_bf16 v[0:15], v[40:43], v[160:163], v[0:15]
	s_waitcnt vmcnt(11)
	s_waitcnt lgkmcnt(0)
	v_mfma_f32_32x32x16_bf16 v[0:15], v[40:43], v[48:51], v[0:15]
	global_load_dwordx4 v[48:51], v[86:87], off offset:1024
	global_load_dwordx4 v[98:101], v[86:87], off offset:2048
	global_load_dwordx4 v[102:105], v[86:87], off offset:3072
	global_load_dwordx4 v[106:109], v[122:123], off offset:-4096
	global_load_dwordx4 v[110:113], v[118:119], off offset:1024
	global_load_dwordx4 v[114:117], v[118:119], off offset:2048
	s_nop 0
	global_load_dwordx4 v[118:121], v[118:119], off offset:3072
	s_waitcnt vmcnt(17)
	s_waitcnt lgkmcnt(0)
	v_mfma_f32_32x32x16_bf16 v[16:31], v[40:43], v[168:171], v[16:31]
	s_waitcnt vmcnt(16)
	s_waitcnt lgkmcnt(0)
	v_mfma_f32_32x32x16_bf16 v[16:31], v[40:43], v[44:47], v[16:31]
	ds_read_b128 v[40:43], v63
	v_add_u32_e32 v44, 2, v60
	v_bitop3_b32 v44, v44, v204, 15 bitop3:0x78
	v_lshl_add_u32 v44, v44, 4, v62
	ds_read_b128 v[44:47], v44
	s_waitcnt vmcnt(14)
	s_waitcnt lgkmcnt(0)
	v_mfma_f32_32x32x16_bf16 v[0:15], v[40:43], v[36:39], v[0:15]
	v_add_u32_e32 v36, 6, v60
	v_bitop3_b32 v36, v36, v204, 15 bitop3:0x78
	v_lshl_add_u32 v36, v36, 4, v62
	ds_read_b128 v[36:39], v36
	v_mfma_f32_32x32x16_bf16 v[16:31], v[40:43], v[64:67], v[16:31]
	s_waitcnt vmcnt(13)
	s_waitcnt lgkmcnt(0)
	v_mfma_f32_32x32x16_bf16 v[0:15], v[40:43], v[68:71], v[0:15]
	s_waitcnt vmcnt(12)
	s_waitcnt lgkmcnt(0)
	v_mfma_f32_32x32x16_bf16 v[16:31], v[40:43], v[74:77], v[16:31]
	global_load_dwordx4 v[40:43], v[122:123], off offset:2048
	s_waitcnt vmcnt(12)
	s_waitcnt lgkmcnt(0)
	v_mfma_f32_32x32x16_bf16 v[0:15], v[44:47], v[78:81], v[0:15]
	s_waitcnt vmcnt(9)
	s_waitcnt lgkmcnt(0)
	v_mfma_f32_32x32x16_bf16 v[16:31], v[44:47], v[32:35], v[16:31]
	v_add_u32_e32 v32, 4, v60
	v_bitop3_b32 v32, v32, v204, 15 bitop3:0x78
	v_lshl_add_u32 v32, v32, 4, v62
	ds_read_b128 v[32:35], v32
	v_add_u32_e32 v60, s0, v154
	s_mov_b32 s0, 0xe000
	v_add_co_u32_e32 v64, vcc, s0, v72
	v_mfma_f32_32x32x16_bf16 v[0:15], v[44:47], v[82:85], v[0:15]
	s_nop 0
	v_addc_co_u32_e32 v65, vcc, 0, v73, vcc
	s_mov_b32 s0, 0xd000
	v_add_co_u32_e32 v66, vcc, s0, v72
	s_mov_b32 s0, 0xf000
	s_nop 0
	v_addc_co_u32_e32 v67, vcc, 0, v73, vcc
	s_waitcnt vmcnt(8)
	s_waitcnt lgkmcnt(0)
	v_mfma_f32_32x32x16_bf16 v[16:31], v[44:47], v[90:93], v[16:31]
	v_bitop3_b32 v44, v60, v204, 15 bitop3:0x78
	v_lshl_add_u32 v44, v44, 4, v62
	ds_read_b128 v[44:47], v44
	s_waitcnt lgkmcnt(1)
	v_mfma_f32_32x32x16_bf16 v[0:15], v[32:35], v[94:97], v[0:15]
	s_waitcnt vmcnt(6)
	s_waitcnt lgkmcnt(0)
	v_mfma_f32_32x32x16_bf16 v[16:31], v[32:35], v[98:101], v[16:31]
	v_mfma_f32_32x32x16_bf16 v[0:15], v[32:35], v[48:51], v[0:15]
	v_add_u32_e32 v48, 2, v60
	v_bitop3_b32 v48, v48, v204, 15 bitop3:0x78
	v_lshl_add_u32 v48, v48, 4, v62
	ds_read_b128 v[48:51], v48
	s_waitcnt vmcnt(5)
	s_waitcnt lgkmcnt(0)
	v_mfma_f32_32x32x16_bf16 v[16:31], v[32:35], v[102:105], v[16:31]
	global_load_dwordx4 v[32:35], v[122:123], off
	s_waitcnt vmcnt(5)
	s_waitcnt lgkmcnt(0)
	v_mfma_f32_32x32x16_bf16 v[0:15], v[36:39], v[106:109], v[0:15]
	s_waitcnt vmcnt(3)
; __device__ __forceinline__ int crow(int r, int hi) { return (r & 3) + 8 * (r >> 2) + 4 * hi; }
; #define P5_LDB(dst, q0) do { _Pragma("unroll") for (int q_ = 0; q_ < 4; ++q_) _Pragma("unroll") for (int c_ = 0; c_ < 4; ++c_) dst[q_][c_] = *(const GAS bf16x8*)(wbase + (size_t)((q0) + q_) * 4096 + c_ * 1024); } while (0)
; template <int l>
; __device__ __forceinline__ void layer_phases(Frame& F, const XcdBarrier& bar, const int lo, const int hi) {
;     ...
;                 P5_MMA(bqa, 0); asm volatile("" ::: "memory"); P5_LDB(bqa, 8);
;                 P5_MMA(bqb, 4); asm volatile("" ::: "memory"); P5_LDB(bqb, 12);
;                 P5_MMA(bqa, 8); P5_MMA(bqb, 12);
;     ...
;                 __syncthreads();
; #pragma unroll
;                 for (int r = 0; r < 16; ++r) { const int row = att::crow(r, hi5); part[(F.wave * 32 + row) * 64 + r32] = acc0[r]; part[(F.wave * 32 + row) * 64 + 32 + r32] = acc1[r]; }
;                 __syncthreads();
;                 float score[4]; unsigned key[4]; int ek[4][6]; float sk[4][6];
; #pragma unroll
;                 for (int rr = 0; rr < 4; ++rr) { const int rloc = 4 * F.wave + rr; float lg = 0.f;
; #pragma unroll
;                     for (int w = 0; w < 8; ++w) lg += part[(w * 32 + rloc) * 64 + F.lane];
	s_waitcnt lgkmcnt(0)
	v_mfma_f32_32x32x16_bf16 v[16:31], v[36:39], v[114:117], v[16:31]
	v_mfma_f32_32x32x16_bf16 v[0:15], v[36:39], v[110:113], v[0:15]
	s_waitcnt vmcnt(2)
	s_waitcnt lgkmcnt(0)
	v_mfma_f32_32x32x16_bf16 v[16:31], v[36:39], v[118:121], v[16:31]
	global_load_dwordx4 v[36:39], v[122:123], off offset:1024
	s_waitcnt vmcnt(1)
	s_waitcnt lgkmcnt(0)
	v_mfma_f32_32x32x16_bf16 v[0:15], v[44:47], v[32:35], v[0:15]
	global_load_dwordx4 v[32:35], v[122:123], off offset:3072
	s_waitcnt vmcnt(1)
	s_waitcnt lgkmcnt(0)
	v_mfma_f32_32x32x16_bf16 v[0:15], v[44:47], v[36:39], v[0:15]
	global_load_dwordx4 v[36:39], v[64:65], off offset:-4096
	v_mfma_f32_32x32x16_bf16 v[16:31], v[44:47], v[40:43], v[16:31]
	s_waitcnt vmcnt(1)
	s_waitcnt lgkmcnt(0)
	v_mfma_f32_32x32x16_bf16 v[16:31], v[44:47], v[32:35], v[16:31]
	global_load_dwordx4 v[32:35], v[66:67], off offset:2048
	global_load_dwordx4 v[40:43], v[64:65], off
	s_waitcnt vmcnt(2)
	s_waitcnt lgkmcnt(0)
	v_mfma_f32_32x32x16_bf16 v[0:15], v[48:51], v[36:39], v[0:15]
	global_load_dwordx4 v[36:39], v[66:67], off offset:1024
	s_waitcnt vmcnt(2)
	s_waitcnt lgkmcnt(0)
	v_mfma_f32_32x32x16_bf16 v[16:31], v[48:51], v[32:35], v[16:31]
	global_load_dwordx4 v[32:35], v[66:67], off offset:3072
	v_add_co_u32_e32 v66, vcc, s0, v72
	v_readlane_b32 s0, v248, 31
	s_nop 0
	v_addc_co_u32_e32 v67, vcc, 0, v73, vcc
	s_waitcnt vmcnt(0)
	s_waitcnt lgkmcnt(0)
	v_mfma_f32_32x32x16_bf16 v[16:31], v[48:51], v[32:35], v[16:31]
	global_load_dwordx4 v[32:35], v[64:65], off offset:2048
	v_mfma_f32_32x32x16_bf16 v[0:15], v[48:51], v[36:39], v[0:15]
	v_add_u32_e32 v36, 4, v60
	v_bitop3_b32 v36, v36, v204, 15 bitop3:0x78
	v_lshl_add_u32 v44, v36, 4, v62
	ds_read_b128 v[44:47], v44
	v_add_u32_e32 v48, 6, v60
	v_bitop3_b32 v48, v48, v204, 15 bitop3:0x78
	v_lshl_add_u32 v48, v48, 4, v62
	global_load_dwordx4 v[36:39], v[66:67], off
	ds_read_b128 v[48:51], v48
	s_waitcnt lgkmcnt(1)
	v_mfma_f32_32x32x16_bf16 v[0:15], v[44:47], v[40:43], v[0:15]
	global_load_dwordx4 v[40:43], v[64:65], off offset:1024
	s_waitcnt vmcnt(2)
	s_waitcnt lgkmcnt(0)
	v_mfma_f32_32x32x16_bf16 v[16:31], v[44:47], v[32:35], v[16:31]
	global_load_dwordx4 v[32:35], v[64:65], off offset:3072
	s_waitcnt vmcnt(0)
	s_waitcnt lgkmcnt(0)
	v_mfma_f32_32x32x16_bf16 v[16:31], v[44:47], v[32:35], v[16:31]
	global_load_dwordx4 v[32:35], v[66:67], off offset:2048
	v_mfma_f32_32x32x16_bf16 v[0:15], v[44:47], v[40:43], v[0:15]
	v_lshlrev_b32_e32 v40, 10, v154
	v_lshlrev_b32_e32 v41, 2, v89
	s_waitcnt lgkmcnt(0)
	v_mfma_f32_32x32x16_bf16 v[0:15], v[48:51], v[36:39], v[0:15]
	global_load_dwordx4 v[36:39], v[66:67], off offset:1024
	s_waitcnt vmcnt(1)
	s_waitcnt lgkmcnt(0)
	v_mfma_f32_32x32x16_bf16 v[16:31], v[48:51], v[32:35], v[16:31]
	global_load_dwordx4 v[32:35], v[66:67], off offset:3072
	s_barrier
	s_waitcnt vmcnt(1)
	s_waitcnt lgkmcnt(0)
	v_mfma_f32_32x32x16_bf16 v[0:15], v[48:51], v[36:39], v[0:15]
	v_add3_u32 v36, s0, v40, v41
	v_add_u32_e32 v37, 0x800, v36
	v_add_u32_e32 v38, 0x1000, v36
	v_add_u32_e32 v39, 0x1800, v36
	s_waitcnt vmcnt(0)
	s_waitcnt lgkmcnt(0)
	v_mfma_f32_32x32x16_bf16 v[16:31], v[48:51], v[32:35], v[16:31]
	s_nop 11
	ds_write2_b32 v36, v0, v16 offset1:32
	ds_write2_b32 v36, v1, v17 offset0:64 offset1:96
	ds_write2_b32 v36, v2, v18 offset0:128 offset1:160
	ds_write2_b32 v36, v3, v19 offset0:192 offset1:224
	ds_write2_b32 v37, v4, v20 offset1:32
	ds_write2_b32 v37, v5, v21 offset0:64 offset1:96
	ds_write2_b32 v37, v6, v22 offset0:128 offset1:160
	ds_write2_b32 v37, v7, v23 offset0:192 offset1:224
	ds_write2_b32 v38, v8, v24 offset1:32
	ds_write2_b32 v38, v9, v25 offset0:64 offset1:96
	ds_write2_b32 v38, v10, v26 offset0:128 offset1:160
	ds_write2_b32 v38, v11, v27 offset0:192 offset1:224
	ds_write2_b32 v39, v12, v28 offset1:32
	ds_write2_b32 v39, v13, v29 offset0:64 offset1:96
	ds_write2_b32 v39, v14, v30 offset0:128 offset1:160
	ds_write2_b32 v39, v15, v31 offset0:192 offset1:224
	s_waitcnt lgkmcnt(0)
	s_barrier
	ds_read2st64_b32 v[0:1], v202 offset1:1
	ds_read2st64_b32 v[2:3], v202 offset0:32 offset1:33
	ds_read2st64_b32 v[4:5], v202 offset0:34 offset1:35
	ds_read2st64_b32 v[6:7], v202 offset0:2 offset1:3
	ds_read2st64_b32 v[8:9], v202 offset0:64 offset1:65
	ds_read2st64_b32 v[10:11], v202 offset0:96 offset1:97
	ds_read2st64_b32 v[12:13], v202 offset0:98 offset1:99
	ds_read2st64_b32 v[14:15], v202 offset0:66 offset1:67
	ds_read2st64_b32 v[16:17], v202 offset0:128 offset1:129
	ds_read2st64_b32 v[18:19], v202 offset0:160 offset1:161
	ds_read2st64_b32 v[20:21], v202 offset0:162 offset1:163
	ds_read2st64_b32 v[22:23], v202 offset0:130 offset1:131
	ds_read2st64_b32 v[24:25], v202 offset0:192 offset1:193
	ds_read2st64_b32 v[26:27], v202 offset0:224 offset1:225
	ds_read2st64_b32 v[28:29], v202 offset0:226 offset1:227
	ds_read2st64_b32 v[30:31], v202 offset0:194 offset1:195
	s_waitcnt lgkmcnt(14)
	v_add_f32_e32 v0, 0, v0
	v_add_f32_e32 v1, 0, v1
	v_add_f32_e32 v0, v0, v2
	v_add_f32_e32 v1, v1, v3
	s_waitcnt lgkmcnt(12)
	v_add_f32_e32 v6, 0, v6
	v_add_f32_e32 v7, 0, v7
	s_waitcnt lgkmcnt(11)
	v_add_f32_e32 v0, v0, v8
	v_add_f32_e32 v1, v1, v9
	v_add_f32_e32 v2, v6, v4
	v_add_f32_e32 v3, v7, v5
	s_waitcnt lgkmcnt(10)
	v_add_f32_e32 v0, v0, v10
	v_add_f32_e32 v1, v1, v11
	s_waitcnt lgkmcnt(8)
	v_add_f32_e32 v2, v2, v14
	v_add_f32_e32 v3, v3, v15
	s_waitcnt lgkmcnt(7)
	v_add_f32_e32 v0, v0, v16
	v_add_f32_e32 v1, v1, v17
	v_add_f32_e32 v2, v2, v12
	v_add_f32_e32 v3, v3, v13
	s_waitcnt lgkmcnt(6)
	v_add_f32_e32 v0, v0, v18
	v_add_f32_e32 v1, v1, v19
	s_waitcnt lgkmcnt(4)
	v_add_f32_e32 v2, v2, v22
	v_add_f32_e32 v3, v3, v23
	s_waitcnt lgkmcnt(3)
; template <int l>
; __device__ __forceinline__ void layer_phases(Frame& F, const XcdBarrier& bar, const int lo, const int hi) {
;     ...
;                 for (int rr = 0; rr < 4; ++rr) { const int rloc = 4 * F.wave + rr; float lg = 0.f;
; #pragma unroll
;                     for (int w = 0; w < 8; ++w) lg += part[(w * 32 + rloc) * 64 + F.lane];
;                     score[rr] = 1.0f / (1.0f + __expf(-lg)); const float sel = score[rr] + rb;
;                     unsigned ob = __float_as_uint(sel); ob = (ob & 0x80000000u) ? ~ob : (ob | 0x80000000u);
;                     key[rr] = (ob & ~63u) | (unsigned)(63 - F.lane); }
; #pragma unroll
;                 for (int k = 0; k < 6; ++k) {
;                     unsigned mx[4];
; #pragma unroll
;                     for (int rr = 0; rr < 4; ++rr) mx[rr] = key[rr];
; #pragma unroll
;                     for (int o = 1; o < 64; o <<= 1) {
; #pragma unroll
;                         for (int rr = 0; rr < 4; ++rr) { const unsigned t = __shfl_xor(mx[rr], o); mx[rr] = t > mx[rr] ? t : mx[rr]; } }
; #pragma unroll
;                     for (int rr = 0; rr < 4; ++rr) { const int win = 63 - (int)(__builtin_amdgcn_readfirstlane((int)mx[rr]) & 63);
;                         ek[rr][k] = win; sk[rr][k] = __uint_as_float((unsigned)__builtin_amdgcn_readlane((int)__float_as_uint(score[rr]), win)); if (F.lane == win) key[rr] = 0u; }
	v_add_f32_e32 v0, v0, v24
	v_add_f32_e32 v1, v1, v25
	v_add_f32_e32 v2, v2, v20
	v_add_f32_e32 v3, v3, v21
	s_waitcnt lgkmcnt(2)
	v_add_f32_e32 v0, v0, v26
	v_add_f32_e32 v1, v1, v27
	s_waitcnt lgkmcnt(0)
	v_add_f32_e32 v2, v2, v30
	v_add_f32_e32 v3, v3, v31
	v_mul_f32_e32 v0, 0xbfb8aa3b, v0
	v_mul_f32_e32 v4, 0xbfb8aa3b, v1
	v_add_f32_e32 v2, v2, v28
	v_add_f32_e32 v3, v3, v29
	v_exp_f32_e32 v1, v0
	v_exp_f32_e32 v0, v4
	v_mul_f32_e32 v2, 0xbfb8aa3b, v2
	v_mul_f32_e32 v5, 0xbfb8aa3b, v3
	v_exp_f32_e32 v3, v2
	v_exp_f32_e32 v2, v5
	v_pk_add_f32 v[0:1], v[0:1], 1.0 op_sel_hi:[1,0]
	v_pk_add_f32 v[2:3], v[2:3], 1.0 op_sel_hi:[1,0]
	v_div_scale_f32 v4, s[0:1], v1, v1, 1.0
	v_div_scale_f32 v6, s[0:1], v0, v0, 1.0
	v_rcp_f32_e32 v12, v4
	v_div_scale_f32 v8, s[0:1], v3, v3, 1.0
	v_rcp_f32_e32 v13, v6
	v_div_scale_f32 v10, s[0:1], v2, v2, 1.0
	v_rcp_f32_e32 v14, v8
	v_rcp_f32_e32 v15, v10
	v_fma_f32 v16, -v4, v12, 1.0
	v_div_scale_f32 v5, vcc, 1.0, v1, 1.0
	v_fma_f32 v17, -v6, v13, 1.0
	v_fmac_f32_e32 v12, v16, v12
	v_div_scale_f32 v7, s[14:15], 1.0, v0, 1.0
	v_fma_f32 v18, -v8, v14, 1.0
	v_fmac_f32_e32 v13, v17, v13
	v_mul_f32_e32 v16, v5, v12
	v_div_scale_f32 v9, s[16:17], 1.0, v3, 1.0
	v_fma_f32 v19, -v10, v15, 1.0
	v_fmac_f32_e32 v14, v18, v14
	v_mul_f32_e32 v17, v7, v13
	v_fma_f32 v20, -v4, v16, v5
	v_div_scale_f32 v11, s[18:19], 1.0, v2, 1.0
	v_fmac_f32_e32 v15, v19, v15
	v_mul_f32_e32 v18, v9, v14
	v_fma_f32 v21, -v6, v17, v7
	v_fmac_f32_e32 v16, v20, v12
	v_mul_f32_e32 v19, v11, v15
	v_fma_f32 v22, -v8, v18, v9
	v_fmac_f32_e32 v17, v21, v13
	v_fma_f32 v4, -v4, v16, v5
	v_fma_f32 v23, -v10, v19, v11
	v_fmac_f32_e32 v18, v22, v14
	v_fma_f32 v5, -v6, v17, v7
	v_div_fmas_f32 v4, v4, v12, v16
	s_mov_b64 vcc, s[14:15]
	v_fmac_f32_e32 v19, v23, v15
	v_fma_f32 v6, -v8, v18, v9
	v_div_fixup_f32 v1, v4, v1, 1.0
	v_div_fmas_f32 v4, v5, v13, v17
	s_mov_b64 vcc, s[16:17]
	v_fma_f32 v7, -v10, v19, v11
	v_div_fixup_f32 v0, v4, v0, 1.0
	v_div_fmas_f32 v6, v6, v14, v18
	s_mov_b64 vcc, s[18:19]
	v_pk_add_f32 v[4:5], v[54:55], v[0:1]
	v_div_fixup_f32 v3, v6, v3, 1.0
	v_div_fmas_f32 v6, v7, v15, v19
	v_not_b32_e32 v7, v5
	v_or_b32_e32 v8, 0x80000000, v5
	v_div_fixup_f32 v2, v6, v2, 1.0
	v_cmp_gt_i32_e32 vcc, 0, v5
	v_not_b32_e32 v9, v4
	v_or_b32_e32 v10, 0x80000000, v4
	v_cndmask_b32_e32 v6, v8, v7, vcc
	v_cmp_gt_i32_e32 vcc, 0, v4
	v_pk_add_f32 v[4:5], v[54:55], v[2:3]
	v_and_or_b32 v6, v6, s90, v199
	v_cndmask_b32_e32 v7, v10, v9, vcc
	v_not_b32_e32 v8, v5
	v_or_b32_e32 v9, 0x80000000, v5
	v_cmp_gt_i32_e32 vcc, 0, v5
	v_and_or_b32 v7, v7, s90, v199
	v_not_b32_e32 v10, v4
	v_or_b32_e32 v11, 0x80000000, v4
	v_cndmask_b32_e32 v5, v9, v8, vcc
	v_cmp_gt_i32_e32 vcc, 0, v4
	ds_bpermute_b32 v8, v53, v6
	ds_bpermute_b32 v9, v53, v7
	v_cndmask_b32_e32 v4, v11, v10, vcc
	v_and_or_b32 v5, v5, s90, v199
	v_and_or_b32 v4, v4, s90, v199
	ds_bpermute_b32 v10, v53, v5
	ds_bpermute_b32 v11, v53, v4
	s_waitcnt lgkmcnt(3)
	v_max_u32_e32 v8, v8, v6
	s_waitcnt lgkmcnt(2)
	v_max_u32_e32 v9, v9, v7
	ds_bpermute_b32 v12, v194, v8
	ds_bpermute_b32 v13, v194, v9
	s_waitcnt lgkmcnt(3)
	v_max_u32_e32 v10, v10, v5
	s_waitcnt lgkmcnt(2)
	v_max_u32_e32 v11, v11, v4
	ds_bpermute_b32 v14, v194, v10
	ds_bpermute_b32 v15, v194, v11
	s_waitcnt lgkmcnt(3)
	v_max_u32_e32 v8, v12, v8
	s_waitcnt lgkmcnt(2)
	v_max_u32_e32 v9, v13, v9
	ds_bpermute_b32 v12, v195, v8
	ds_bpermute_b32 v13, v195, v9
	s_waitcnt lgkmcnt(3)
	v_max_u32_e32 v10, v14, v10
	s_waitcnt lgkmcnt(2)
	v_max_u32_e32 v11, v15, v11
	ds_bpermute_b32 v14, v195, v10
	ds_bpermute_b32 v15, v195, v11
	s_waitcnt lgkmcnt(3)
	v_max_u32_e32 v8, v12, v8
	s_waitcnt lgkmcnt(2)
	v_max_u32_e32 v9, v13, v9
	ds_bpermute_b32 v12, v196, v8
	ds_bpermute_b32 v13, v196, v9
	s_waitcnt lgkmcnt(3)
	v_max_u32_e32 v10, v14, v10
	s_waitcnt lgkmcnt(2)
	v_max_u32_e32 v11, v15, v11
	ds_bpermute_b32 v14, v196, v10
	ds_bpermute_b32 v15, v196, v11
	s_waitcnt lgkmcnt(3)
	v_max_u32_e32 v8, v12, v8
	s_waitcnt lgkmcnt(2)
	v_max_u32_e32 v9, v13, v9
	ds_bpermute_b32 v12, v197, v8
	ds_bpermute_b32 v13, v197, v9
	s_waitcnt lgkmcnt(3)
	v_max_u32_e32 v10, v14, v10
	s_waitcnt lgkmcnt(2)
	v_max_u32_e32 v11, v15, v11
	ds_bpermute_b32 v14, v197, v10
	ds_bpermute_b32 v15, v197, v11
	s_waitcnt lgkmcnt(3)
	v_max_u32_e32 v8, v12, v8
	s_waitcnt lgkmcnt(2)
	v_max_u32_e32 v9, v13, v9
	ds_bpermute_b32 v12, v198, v8
	ds_bpermute_b32 v13, v198, v9
	s_waitcnt lgkmcnt(3)
	v_max_u32_e32 v10, v14, v10
	s_waitcnt lgkmcnt(2)
	v_max_u32_e32 v11, v15, v11
	ds_bpermute_b32 v14, v198, v10
	ds_bpermute_b32 v15, v198, v11
	s_waitcnt lgkmcnt(3)
	v_max_u32_e32 v8, v12, v8
	s_waitcnt lgkmcnt(2)
	v_max_u32_e32 v9, v13, v9
	v_readfirstlane_b32 s0, v8
	v_readfirstlane_b32 s1, v9
	s_waitcnt lgkmcnt(1)
	v_max_u32_e32 v8, v14, v10
	s_andn2_b32 s16, 63, s0
	s_waitcnt lgkmcnt(0)
	v_max_u32_e32 v9, v15, v11
	s_andn2_b32 s92, 63, s1
	v_cmp_ne_u32_e32 vcc, s16, v52
	v_readfirstlane_b32 s0, v8
	v_readfirstlane_b32 s1, v9
	v_cndmask_b32_e32 v6, 0, v6, vcc
	v_cmp_ne_u32_e32 vcc, s92, v52
	s_andn2_b32 s43, 63, s0
	s_andn2_b32 s19, 63, s1
	v_cndmask_b32_e32 v7, 0, v7, vcc
	ds_bpermute_b32 v8, v53, v6
	v_cmp_ne_u32_e32 vcc, s43, v52
	ds_bpermute_b32 v9, v53, v7
	v_readlane_b32 s93, v1, s16
	v_cndmask_b32_e32 v5, 0, v5, vcc
	v_cmp_ne_u32_e32 vcc, s19, v52
	ds_bpermute_b32 v10, v53, v5
	s_waitcnt lgkmcnt(2)
	v_max_u32_e32 v8, v8, v6
	v_cndmask_b32_e32 v4, 0, v4, vcc
	ds_bpermute_b32 v11, v53, v4
	s_waitcnt lgkmcnt(2)
	v_max_u32_e32 v9, v9, v7
	ds_bpermute_b32 v12, v194, v8
	ds_bpermute_b32 v13, v194, v9
	s_waitcnt lgkmcnt(3)
	v_max_u32_e32 v10, v10, v5
	s_waitcnt lgkmcnt(2)
; template <int l>
; __device__ __forceinline__ void layer_phases(Frame& F, const XcdBarrier& bar, const int lo, const int hi) {
;     ...
;                 for (int k = 0; k < 6; ++k) {
;                     unsigned mx[4];
; #pragma unroll
;                     for (int rr = 0; rr < 4; ++rr) mx[rr] = key[rr];
; #pragma unroll
;                     for (int o = 1; o < 64; o <<= 1) {
; #pragma unroll
;                         for (int rr = 0; rr < 4; ++rr) { const unsigned t = __shfl_xor(mx[rr], o); mx[rr] = t > mx[rr] ? t : mx[rr]; } }
; #pragma unroll
;                     for (int rr = 0; rr < 4; ++rr) { const int win = 63 - (int)(__builtin_amdgcn_readfirstlane((int)mx[rr]) & 63);
;                         ek[rr][k] = win; sk[rr][k] = __uint_as_float((unsigned)__builtin_amdgcn_readlane((int)__float_as_uint(score[rr]), win)); if (F.lane == win) key[rr] = 0u; }
	v_max_u32_e32 v11, v11, v4
	ds_bpermute_b32 v14, v194, v10
	ds_bpermute_b32 v15, v194, v11
	s_waitcnt lgkmcnt(3)
	v_max_u32_e32 v8, v12, v8
	s_waitcnt lgkmcnt(2)
	v_max_u32_e32 v9, v13, v9
	ds_bpermute_b32 v12, v195, v8
	ds_bpermute_b32 v13, v195, v9
	s_waitcnt lgkmcnt(3)
	v_max_u32_e32 v10, v14, v10
	s_waitcnt lgkmcnt(2)
	v_max_u32_e32 v11, v15, v11
	ds_bpermute_b32 v14, v195, v10
	ds_bpermute_b32 v15, v195, v11
	s_waitcnt lgkmcnt(3)
	v_max_u32_e32 v8, v12, v8
	s_waitcnt lgkmcnt(2)
	v_max_u32_e32 v9, v13, v9
	ds_bpermute_b32 v12, v196, v8
	ds_bpermute_b32 v13, v196, v9
	s_waitcnt lgkmcnt(3)
	v_max_u32_e32 v10, v14, v10
	s_waitcnt lgkmcnt(2)
	v_max_u32_e32 v11, v15, v11
	ds_bpermute_b32 v14, v196, v10
	ds_bpermute_b32 v15, v196, v11
	s_waitcnt lgkmcnt(3)
	v_max_u32_e32 v8, v12, v8
	s_waitcnt lgkmcnt(2)
	v_max_u32_e32 v9, v13, v9
	ds_bpermute_b32 v12, v197, v8
	ds_bpermute_b32 v13, v197, v9
	s_waitcnt lgkmcnt(3)
	v_max_u32_e32 v10, v14, v10
	s_waitcnt lgkmcnt(2)
	v_max_u32_e32 v11, v15, v11
	ds_bpermute_b32 v14, v197, v10
	ds_bpermute_b32 v15, v197, v11
	s_waitcnt lgkmcnt(3)
	v_max_u32_e32 v8, v12, v8
	s_waitcnt lgkmcnt(2)
	v_max_u32_e32 v9, v13, v9
	ds_bpermute_b32 v12, v198, v8
	ds_bpermute_b32 v13, v198, v9
	s_waitcnt lgkmcnt(3)
	v_max_u32_e32 v10, v14, v10
	s_waitcnt lgkmcnt(2)
	v_max_u32_e32 v11, v15, v11
	ds_bpermute_b32 v14, v198, v10
	ds_bpermute_b32 v15, v198, v11
	s_waitcnt lgkmcnt(3)
	v_max_u32_e32 v8, v12, v8
	s_waitcnt lgkmcnt(2)
	v_max_u32_e32 v9, v13, v9
	v_readfirstlane_b32 s0, v8
	v_readfirstlane_b32 s1, v9
	s_waitcnt lgkmcnt(1)
	v_max_u32_e32 v8, v14, v10
	s_andn2_b32 s17, 63, s0
	s_waitcnt lgkmcnt(0)
	v_max_u32_e32 v9, v15, v11
	s_andn2_b32 s63, 63, s1
	v_cmp_ne_u32_e32 vcc, s17, v52
	v_readfirstlane_b32 s0, v8
	v_readfirstlane_b32 s1, v9
	v_cndmask_b32_e32 v6, 0, v6, vcc
	v_cmp_ne_u32_e32 vcc, s63, v52
	s_andn2_b32 s95, 63, s0
	s_andn2_b32 s47, 63, s1
	v_cndmask_b32_e32 v7, 0, v7, vcc
	ds_bpermute_b32 v8, v53, v6
	v_cmp_ne_u32_e32 vcc, s95, v52
	ds_bpermute_b32 v9, v53, v7
	v_readlane_b32 s45, v0, s92
	v_cndmask_b32_e32 v5, 0, v5, vcc
	v_cmp_ne_u32_e32 vcc, s47, v52
	ds_bpermute_b32 v10, v53, v5
	s_waitcnt lgkmcnt(2)
	v_max_u32_e32 v8, v8, v6
	v_cndmask_b32_e32 v4, 0, v4, vcc
	ds_bpermute_b32 v11, v53, v4
	s_waitcnt lgkmcnt(2)
	v_max_u32_e32 v9, v9, v7
	ds_bpermute_b32 v12, v194, v8
	ds_bpermute_b32 v13, v194, v9
	s_waitcnt lgkmcnt(3)
	v_max_u32_e32 v10, v10, v5
	s_waitcnt lgkmcnt(2)
	v_max_u32_e32 v11, v11, v4
	ds_bpermute_b32 v14, v194, v10
	ds_bpermute_b32 v15, v194, v11
	s_waitcnt lgkmcnt(3)
	v_max_u32_e32 v8, v12, v8
	s_waitcnt lgkmcnt(2)
	v_max_u32_e32 v9, v13, v9
	ds_bpermute_b32 v12, v195, v8
	ds_bpermute_b32 v13, v195, v9
	s_waitcnt lgkmcnt(3)
	v_max_u32_e32 v10, v14, v10
	s_waitcnt lgkmcnt(2)
	v_max_u32_e32 v11, v15, v11
	ds_bpermute_b32 v14, v195, v10
	ds_bpermute_b32 v15, v195, v11
	s_waitcnt lgkmcnt(3)
	v_max_u32_e32 v8, v12, v8
	s_waitcnt lgkmcnt(2)
	v_max_u32_e32 v9, v13, v9
	ds_bpermute_b32 v12, v196, v8
	ds_bpermute_b32 v13, v196, v9
	s_waitcnt lgkmcnt(3)
	v_max_u32_e32 v10, v14, v10
	s_waitcnt lgkmcnt(2)
	v_max_u32_e32 v11, v15, v11
	ds_bpermute_b32 v14, v196, v10
	ds_bpermute_b32 v15, v196, v11
	s_waitcnt lgkmcnt(3)
	v_max_u32_e32 v8, v12, v8
	s_waitcnt lgkmcnt(2)
	v_max_u32_e32 v9, v13, v9
	ds_bpermute_b32 v12, v197, v8
	ds_bpermute_b32 v13, v197, v9
	s_waitcnt lgkmcnt(3)
	v_max_u32_e32 v10, v14, v10
	s_waitcnt lgkmcnt(2)
	v_max_u32_e32 v11, v15, v11
	ds_bpermute_b32 v14, v197, v10
	ds_bpermute_b32 v15, v197, v11
	s_waitcnt lgkmcnt(3)
	v_max_u32_e32 v8, v12, v8
	s_waitcnt lgkmcnt(2)
	v_max_u32_e32 v9, v13, v9
	ds_bpermute_b32 v12, v198, v8
	ds_bpermute_b32 v13, v198, v9
	s_waitcnt lgkmcnt(3)
	v_max_u32_e32 v10, v14, v10
	s_waitcnt lgkmcnt(2)
	v_max_u32_e32 v11, v15, v11
	ds_bpermute_b32 v14, v198, v10
	ds_bpermute_b32 v15, v198, v11
	s_waitcnt lgkmcnt(3)
	v_max_u32_e32 v8, v12, v8
	s_waitcnt lgkmcnt(2)
	v_max_u32_e32 v9, v13, v9
	v_readfirstlane_b32 s0, v8
	v_readfirstlane_b32 s1, v9
	s_waitcnt lgkmcnt(1)
	v_max_u32_e32 v8, v14, v10
	s_andn2_b32 s77, 63, s0
	s_waitcnt lgkmcnt(0)
	v_max_u32_e32 v9, v15, v11
	s_andn2_b32 s79, 63, s1
	v_cmp_ne_u32_e32 vcc, s77, v52
	v_readfirstlane_b32 s0, v8
	v_readfirstlane_b32 s1, v9
	v_cndmask_b32_e32 v6, 0, v6, vcc
	v_cmp_ne_u32_e32 vcc, s79, v52
	s_andn2_b32 s97, 63, s0
	s_andn2_b32 s94, 63, s1
	v_cndmask_b32_e32 v7, 0, v7, vcc
	ds_bpermute_b32 v8, v53, v6
	v_cmp_ne_u32_e32 vcc, s97, v52
	ds_bpermute_b32 v9, v53, v7
	v_readlane_b32 s41, v3, s43
	v_cndmask_b32_e32 v5, 0, v5, vcc
	v_cmp_ne_u32_e32 vcc, s94, v52
	ds_bpermute_b32 v10, v53, v5
	s_waitcnt lgkmcnt(2)
	v_max_u32_e32 v8, v8, v6
	v_cndmask_b32_e32 v4, 0, v4, vcc
	ds_bpermute_b32 v11, v53, v4
	s_waitcnt lgkmcnt(2)
	v_max_u32_e32 v9, v9, v7
	ds_bpermute_b32 v12, v194, v8
	ds_bpermute_b32 v13, v194, v9
	s_waitcnt lgkmcnt(3)
	v_max_u32_e32 v10, v10, v5
	s_waitcnt lgkmcnt(2)
	v_max_u32_e32 v11, v11, v4
	ds_bpermute_b32 v14, v194, v10
	ds_bpermute_b32 v15, v194, v11
	s_waitcnt lgkmcnt(3)
	v_max_u32_e32 v8, v12, v8
	s_waitcnt lgkmcnt(2)
	v_max_u32_e32 v9, v13, v9
	ds_bpermute_b32 v12, v195, v8
	ds_bpermute_b32 v13, v195, v9
	s_waitcnt lgkmcnt(3)
	v_max_u32_e32 v10, v14, v10
	s_waitcnt lgkmcnt(2)
	v_max_u32_e32 v11, v15, v11
	ds_bpermute_b32 v14, v195, v10
	ds_bpermute_b32 v15, v195, v11
	s_waitcnt lgkmcnt(3)
	v_max_u32_e32 v8, v12, v8
	s_waitcnt lgkmcnt(2)
	v_max_u32_e32 v9, v13, v9
	ds_bpermute_b32 v12, v196, v8
	ds_bpermute_b32 v13, v196, v9
	s_waitcnt lgkmcnt(3)
	v_max_u32_e32 v10, v14, v10
	s_waitcnt lgkmcnt(2)
	v_max_u32_e32 v11, v15, v11
	ds_bpermute_b32 v14, v196, v10
	ds_bpermute_b32 v15, v196, v11
	s_waitcnt lgkmcnt(3)
; template <int l>
; __device__ __forceinline__ void layer_phases(Frame& F, const XcdBarrier& bar, const int lo, const int hi) {
;     ...
;                 for (int k = 0; k < 6; ++k) {
;                     unsigned mx[4];
; #pragma unroll
;                     for (int rr = 0; rr < 4; ++rr) mx[rr] = key[rr];
; #pragma unroll
;                     for (int o = 1; o < 64; o <<= 1) {
; #pragma unroll
;                         for (int rr = 0; rr < 4; ++rr) { const unsigned t = __shfl_xor(mx[rr], o); mx[rr] = t > mx[rr] ? t : mx[rr]; } }
; #pragma unroll
;                     for (int rr = 0; rr < 4; ++rr) { const int win = 63 - (int)(__builtin_amdgcn_readfirstlane((int)mx[rr]) & 63);
;                         ek[rr][k] = win; sk[rr][k] = __uint_as_float((unsigned)__builtin_amdgcn_readlane((int)__float_as_uint(score[rr]), win)); if (F.lane == win) key[rr] = 0u; }
;                 }
	v_max_u32_e32 v8, v12, v8
	s_waitcnt lgkmcnt(2)
	v_max_u32_e32 v9, v13, v9
	ds_bpermute_b32 v12, v197, v8
	ds_bpermute_b32 v13, v197, v9
	s_waitcnt lgkmcnt(3)
	v_max_u32_e32 v10, v14, v10
	s_waitcnt lgkmcnt(2)
	v_max_u32_e32 v11, v15, v11
	ds_bpermute_b32 v14, v197, v10
	ds_bpermute_b32 v15, v197, v11
	s_waitcnt lgkmcnt(3)
	v_max_u32_e32 v8, v12, v8
	s_waitcnt lgkmcnt(2)
	v_max_u32_e32 v9, v13, v9
	ds_bpermute_b32 v12, v198, v8
	ds_bpermute_b32 v13, v198, v9
	s_waitcnt lgkmcnt(3)
	v_max_u32_e32 v10, v14, v10
	s_waitcnt lgkmcnt(2)
	v_max_u32_e32 v11, v15, v11
	ds_bpermute_b32 v14, v198, v10
	ds_bpermute_b32 v15, v198, v11
	s_waitcnt lgkmcnt(3)
	v_max_u32_e32 v8, v12, v8
	s_waitcnt lgkmcnt(2)
	v_max_u32_e32 v9, v13, v9
	v_readfirstlane_b32 s0, v8
	v_readfirstlane_b32 s1, v9
	s_waitcnt lgkmcnt(1)
	v_max_u32_e32 v8, v14, v10
	s_andn2_b32 s84, 63, s0
	s_waitcnt lgkmcnt(0)
	v_max_u32_e32 v9, v15, v11
	s_andn2_b32 s59, 63, s1
	v_cmp_ne_u32_e32 vcc, s84, v52
	v_readfirstlane_b32 s0, v8
	v_readfirstlane_b32 s1, v9
	v_cndmask_b32_e32 v6, 0, v6, vcc
	v_cmp_ne_u32_e32 vcc, s59, v52
	s_andn2_b32 s78, 63, s0
	s_andn2_b32 s62, 63, s1
	v_cndmask_b32_e32 v7, 0, v7, vcc
	ds_bpermute_b32 v8, v53, v6
	v_cmp_ne_u32_e32 vcc, s78, v52
	ds_bpermute_b32 v9, v53, v7
	v_readlane_b32 s18, v2, s19
	v_cndmask_b32_e32 v5, 0, v5, vcc
	v_cmp_ne_u32_e32 vcc, s62, v52
	ds_bpermute_b32 v10, v53, v5
	s_waitcnt lgkmcnt(2)
	v_max_u32_e32 v8, v8, v6
	v_cndmask_b32_e32 v4, 0, v4, vcc
	ds_bpermute_b32 v11, v53, v4
	s_waitcnt lgkmcnt(2)
	v_max_u32_e32 v9, v9, v7
	ds_bpermute_b32 v12, v194, v8
	ds_bpermute_b32 v13, v194, v9
	s_waitcnt lgkmcnt(3)
	v_max_u32_e32 v10, v10, v5
	s_waitcnt lgkmcnt(2)
	v_max_u32_e32 v11, v11, v4
	ds_bpermute_b32 v14, v194, v10
	ds_bpermute_b32 v15, v194, v11
	s_waitcnt lgkmcnt(3)
	v_max_u32_e32 v8, v12, v8
	s_waitcnt lgkmcnt(2)
	v_max_u32_e32 v9, v13, v9
	ds_bpermute_b32 v12, v195, v8
	ds_bpermute_b32 v13, v195, v9
	s_waitcnt lgkmcnt(3)
	v_max_u32_e32 v10, v14, v10
	s_waitcnt lgkmcnt(2)
	v_max_u32_e32 v11, v15, v11
	ds_bpermute_b32 v14, v195, v10
	ds_bpermute_b32 v15, v195, v11
	s_waitcnt lgkmcnt(3)
	v_max_u32_e32 v8, v12, v8
	s_waitcnt lgkmcnt(2)
	v_max_u32_e32 v9, v13, v9
	ds_bpermute_b32 v12, v196, v8
	ds_bpermute_b32 v13, v196, v9
	s_waitcnt lgkmcnt(3)
	v_max_u32_e32 v10, v14, v10
	s_waitcnt lgkmcnt(2)
	v_max_u32_e32 v11, v15, v11
	ds_bpermute_b32 v14, v196, v10
	ds_bpermute_b32 v15, v196, v11
	s_waitcnt lgkmcnt(3)
	v_max_u32_e32 v8, v12, v8
	s_waitcnt lgkmcnt(2)
	v_max_u32_e32 v9, v13, v9
	ds_bpermute_b32 v12, v197, v8
	ds_bpermute_b32 v13, v197, v9
	s_waitcnt lgkmcnt(3)
	v_max_u32_e32 v10, v14, v10
	s_waitcnt lgkmcnt(2)
	v_max_u32_e32 v11, v15, v11
	ds_bpermute_b32 v14, v197, v10
	ds_bpermute_b32 v15, v197, v11
	s_waitcnt lgkmcnt(3)
	v_max_u32_e32 v8, v12, v8
	s_waitcnt lgkmcnt(2)
	v_max_u32_e32 v9, v13, v9
	ds_bpermute_b32 v12, v198, v8
	ds_bpermute_b32 v13, v198, v9
	s_waitcnt lgkmcnt(3)
	v_max_u32_e32 v10, v14, v10
	s_waitcnt lgkmcnt(2)
	v_max_u32_e32 v11, v15, v11
	ds_bpermute_b32 v14, v198, v10
	ds_bpermute_b32 v15, v198, v11
	s_waitcnt lgkmcnt(3)
	v_max_u32_e32 v8, v12, v8
	s_waitcnt lgkmcnt(2)
	v_max_u32_e32 v9, v13, v9
	v_readfirstlane_b32 s0, v8
	v_readfirstlane_b32 s1, v9
	s_waitcnt lgkmcnt(1)
	v_max_u32_e32 v8, v14, v10
	s_andn2_b32 s89, 63, s0
	s_waitcnt lgkmcnt(0)
	v_max_u32_e32 v9, v15, v11
	s_andn2_b32 s81, 63, s1
	v_cmp_ne_u32_e32 vcc, s89, v52
	v_readfirstlane_b32 s0, v8
	v_readfirstlane_b32 s1, v9
	v_cndmask_b32_e32 v6, 0, v6, vcc
	v_cmp_ne_u32_e32 vcc, s81, v52
	s_andn2_b32 s58, 63, s0
	s_andn2_b32 s61, 63, s1
	v_cndmask_b32_e32 v7, 0, v7, vcc
	v_cmp_ne_u32_e32 vcc, s58, v52
	ds_bpermute_b32 v8, v53, v6
	ds_bpermute_b32 v9, v53, v7
	v_cndmask_b32_e32 v5, 0, v5, vcc
	v_cmp_ne_u32_e32 vcc, s61, v52
	ds_bpermute_b32 v10, v53, v5
	s_waitcnt lgkmcnt(2)
	v_max_u32_e32 v6, v8, v6
	v_cndmask_b32_e32 v4, 0, v4, vcc
	ds_bpermute_b32 v11, v53, v4
	s_waitcnt lgkmcnt(2)
	v_max_u32_e32 v7, v9, v7
	ds_bpermute_b32 v8, v194, v6
	ds_bpermute_b32 v9, v194, v7
	s_waitcnt lgkmcnt(3)
	v_max_u32_e32 v5, v10, v5
	s_waitcnt lgkmcnt(2)
	v_max_u32_e32 v4, v11, v4
	ds_bpermute_b32 v10, v194, v5
	ds_bpermute_b32 v11, v194, v4
	s_waitcnt lgkmcnt(3)
	v_max_u32_e32 v6, v8, v6
	s_waitcnt lgkmcnt(2)
	v_max_u32_e32 v7, v9, v7
	ds_bpermute_b32 v8, v195, v6
	ds_bpermute_b32 v9, v195, v7
	s_waitcnt lgkmcnt(3)
	v_max_u32_e32 v5, v10, v5
	s_waitcnt lgkmcnt(2)
	v_max_u32_e32 v4, v11, v4
	ds_bpermute_b32 v10, v195, v5
	ds_bpermute_b32 v11, v195, v4
	s_waitcnt lgkmcnt(3)
	v_max_u32_e32 v6, v8, v6
	s_waitcnt lgkmcnt(2)
	v_max_u32_e32 v7, v9, v7
	ds_bpermute_b32 v8, v196, v6
	ds_bpermute_b32 v9, v196, v7
	s_waitcnt lgkmcnt(3)
	v_max_u32_e32 v5, v10, v5
	s_waitcnt lgkmcnt(2)
	v_max_u32_e32 v4, v11, v4
	ds_bpermute_b32 v10, v196, v5
	ds_bpermute_b32 v11, v196, v4
	s_waitcnt lgkmcnt(3)
	v_max_u32_e32 v6, v8, v6
	s_waitcnt lgkmcnt(2)
	v_max_u32_e32 v7, v9, v7
	ds_bpermute_b32 v8, v197, v6
	ds_bpermute_b32 v9, v197, v7
	s_waitcnt lgkmcnt(3)
	v_max_u32_e32 v5, v10, v5
	s_waitcnt lgkmcnt(2)
	v_max_u32_e32 v4, v11, v4
	ds_bpermute_b32 v10, v197, v5
	ds_bpermute_b32 v11, v197, v4
	s_waitcnt lgkmcnt(3)
	v_max_u32_e32 v6, v8, v6
	s_waitcnt lgkmcnt(2)
	v_max_u32_e32 v7, v9, v7
	ds_bpermute_b32 v8, v198, v6
	ds_bpermute_b32 v9, v198, v7
	s_waitcnt lgkmcnt(3)
	v_max_u32_e32 v5, v10, v5
	s_waitcnt lgkmcnt(2)
	v_max_u32_e32 v4, v11, v4
	ds_bpermute_b32 v10, v198, v5
	ds_bpermute_b32 v11, v198, v4
	s_waitcnt lgkmcnt(3)
	v_max_u32_e32 v6, v8, v6
	s_waitcnt lgkmcnt(2)
	v_max_u32_e32 v7, v9, v7
	v_readfirstlane_b32 s0, v6
	v_readfirstlane_b32 s1, v7
	s_waitcnt lgkmcnt(1)
	v_max_u32_e32 v5, v10, v5
	s_waitcnt lgkmcnt(0)
	v_max_u32_e32 v4, v11, v4
	s_andn2_b32 vcc_lo, 63, s0
	s_andn2_b32 s88, 63, s1
	v_readfirstlane_b32 s0, v5
	v_readfirstlane_b32 s1, v4
	s_andn2_b32 s80, 63, s0
	s_andn2_b32 s33, 63, s1
	v_readlane_b32 s60, v1, s17
	v_readlane_b32 s96, v0, s63
	v_readlane_b32 s34, v3, s95
	v_readlane_b32 s50, v2, s47
	v_readlane_b32 s73, v1, s77
	v_readlane_b32 s65, v0, s79
	v_readlane_b32 s53, v3, s97
	v_readlane_b32 s51, v2, s94
	v_readlane_b32 s75, v1, s84
	v_readlane_b32 s72, v0, s59
	v_readlane_b32 s67, v3, s78
	v_readlane_b32 s35, v2, s62
	v_readlane_b32 s25, v1, s89
	v_readlane_b32 s1, v0, s81
	v_readlane_b32 s71, v3, s58
	v_readlane_b32 s55, v2, s61
	v_readlane_b32 s26, v1, vcc_lo
	v_readlane_b32 s24, v0, s88
	v_readlane_b32 s0, v3, s80
	v_readlane_b32 s70, v2, s33
	s_mov_b64 s[14:15], exec
	v_readlane_b32 s28, v248, 32
	v_readlane_b32 s29, v248, 33
	s_and_b64 s[28:29], s[14:15], s[28:29]
	s_mov_b64 exec, s[28:29]
	s_cbranch_execz .LBB0_1519
; template <int l>
; __device__ __forceinline__ void layer_phases(Frame& F, const XcdBarrier& bar, const int lo, const int hi) {
;     ...
; #pragma unroll
;                 for (int rr = 0; rr < 4; ++rr) { const int m = m0 + rr;
;                     const float ssum = ((sk[rr][0] + sk[rr][1]) + (sk[rr][2] + sk[rr][3])) + (sk[rr][4] + sk[rr][5]);
;                     if (F.lane < 6 && rep == 0) { int e = ek[rr][0]; float sc = sk[rr][0];
; #pragma unroll
;                         for (int k = 1; k < 6; ++k) if (F.lane == k) { e = ek[rr][k]; sc = sk[rr][k]; }
;                         const unsigned pos = __hip_atomic_fetch_add(F.ctl + CW_CURSOR + (l * 64 + e) * 16, 1u, RLX_AGENT);
;                         if (pos < (unsigned)LISTCAP) { list[(size_t)e * LISTCAP + pos] = m; list2[(size_t)e * LISTCAP + pos] = m * 7 + F.lane; }
;                         tinfo[(size_t)m * 6 + F.lane] = e | (int)(pos << 8); gates[(size_t)m * 6 + F.lane] = sc / ssum * ROUTED_SCALE; }
	v_mov_b32_e32 v40, s16
	v_mov_b32_e32 v48, s17
	v_cndmask_b32_e64 v40, v40, v48, s[4:5]
	v_mov_b32_e32 v48, s77
	v_cndmask_b32_e64 v40, v40, v48, s[6:7]
	v_mov_b32_e32 v48, s84
	v_cndmask_b32_e64 v40, v40, v48, s[8:9]
	v_mov_b32_e32 v48, s89
	v_cndmask_b32_e64 v40, v40, v48, s[10:11]
	v_mov_b32_e32 v48, vcc_lo
	v_cndmask_b32_e64 v40, v40, v48, s[12:13]
	v_lshlrev_b32_e32 v34, 6, v40
	v_add_u32_e32 v34, 0x9000, v34
	global_atomic_add v44, v34, v203, s[56:57] sc0
	v_mov_b32_e32 v41, s92
	v_mov_b32_e32 v48, s63
	v_cndmask_b32_e64 v41, v41, v48, s[4:5]
	v_mov_b32_e32 v48, s79
	v_cndmask_b32_e64 v41, v41, v48, s[6:7]
	v_mov_b32_e32 v48, s59
	v_cndmask_b32_e64 v41, v41, v48, s[8:9]
	v_mov_b32_e32 v48, s81
	v_cndmask_b32_e64 v41, v41, v48, s[10:11]
	v_mov_b32_e32 v48, s88
	v_cndmask_b32_e64 v41, v41, v48, s[12:13]
	v_lshlrev_b32_e32 v34, 6, v41
	v_add_u32_e32 v34, 0x9000, v34
	global_atomic_add v45, v34, v203, s[56:57] sc0
	v_mov_b32_e32 v42, s43
	v_mov_b32_e32 v48, s95
	v_cndmask_b32_e64 v42, v42, v48, s[4:5]
	v_mov_b32_e32 v48, s97
	v_cndmask_b32_e64 v42, v42, v48, s[6:7]
	v_mov_b32_e32 v48, s78
	v_cndmask_b32_e64 v42, v42, v48, s[8:9]
	v_mov_b32_e32 v48, s58
	v_cndmask_b32_e64 v42, v42, v48, s[10:11]
	v_mov_b32_e32 v48, s80
	v_cndmask_b32_e64 v42, v42, v48, s[12:13]
	v_lshlrev_b32_e32 v34, 6, v42
	v_add_u32_e32 v34, 0x9000, v34
	global_atomic_add v46, v34, v203, s[56:57] sc0
	v_mov_b32_e32 v43, s19
	v_mov_b32_e32 v48, s47
	v_cndmask_b32_e64 v43, v43, v48, s[4:5]
	v_mov_b32_e32 v48, s94
	v_cndmask_b32_e64 v43, v43, v48, s[6:7]
	v_mov_b32_e32 v48, s62
	v_cndmask_b32_e64 v43, v43, v48, s[8:9]
	v_mov_b32_e32 v48, s61
	v_cndmask_b32_e64 v43, v43, v48, s[10:11]
	v_mov_b32_e32 v48, s33
	v_cndmask_b32_e64 v43, v43, v48, s[12:13]
	v_lshlrev_b32_e32 v34, 6, v43
	v_add_u32_e32 v34, 0x9000, v34
	global_atomic_add v47, v34, v203, s[56:57] sc0
	s_waitcnt vmcnt(0)
	v_mov_b32_e32 v0, v40
	v_mov_b32_e32 v60, v44
	v_cmp_gt_u32_e32 vcc, s83, v60
	s_and_saveexec_b64 s[16:17], vcc
	s_cbranch_execz .LBB0_1525
	v_lshlrev_b64 v[2:3], 2, v[60:61]
	v_readlane_b32 s28, v248, 13
	v_lshl_or_b32 v2, v0, 16, v2
	v_readlane_b32 s29, v248, 14
	v_mov_b32_e32 v1, s40
	s_nop 0
	v_lshl_add_u64 v[4:5], s[28:29], 0, v[2:3]
	global_store_dword v[4:5], v1, off
	v_mad_u64_u32 v[4:5], s[28:29], s40, 7, v[52:53]
	v_readlane_b32 s28, v248, 15
	v_readlane_b32 s29, v248, 16
	s_nop 1
	v_lshl_add_u64 v[2:3], s[28:29], 0, v[2:3]
	global_store_dword v[2:3], v4, off

; #define GRID_BAR() xcd_barrier(bar, F.tid == 0)
; #define GRID_BAR() do { } while (0)
; #define BOTH(k) (IN(k) && IN((k) + 1))
; __device__ __forceinline__ void xcd_barrier(const XcdBarrier& b, bool leader  ) {
;     asm volatile("s_waitcnt vmcnt(0)" ::: "memory");
;     __syncthreads();
;     if (leader) {
;         unsigned* bar = b.bar;
;         __builtin_amdgcn_s_waitcnt(0);
;         unsigned nloc = b.st[0], nx = b.st[1];
;         if (nloc == 0u) { xcd_barrier_complete(bar, b.x, nloc, nx); b.st[0] = nloc; b.st[1] = nx; }
; template <int l>
; __device__ __forceinline__ void layer_phases(Frame& F, const XcdBarrier& bar, const int lo, const int hi) {
;     ...
;                 __syncthreads();
;             }
;             __syncthreads();
;             if (BOTH(pb + 3)) GRID_BAR();
.LBB0_1531:
	s_waitcnt lgkmcnt(0)
	s_barrier
	v_lshlrev_b32_e32 v252, 3, v216
	v_add_u32_e32 v252, 0x21400, v252
	ds_write_b64 v252, v[254:255]
	s_waitcnt lgkmcnt(0)
	s_barrier
	s_cmp_gt_u32 s93, 14
	v_readlane_b32 s78, v248, 10
	v_readlane_b32 s79, v248, 11
	v_readlane_b32 s90, v248, 6
	s_barrier
	s_cbranch_scc0 .LBB0_1585
	s_waitcnt vmcnt(0)
	v_sub_u32_e32 v0, 0, v52
	v_readlane_b32 s0, v248, 0
	s_barrier
	s_nop 0
	v_cmp_eq_u32_e32 vcc, s0, v0
	s_and_saveexec_b64 s[0:1], vcc
	s_cbranch_execz .LBB0_1584
	s_add_i32 s3, 0, 0x21520
	v_mov_b32_e32 v0, s3
	s_waitcnt vmcnt(0) expcnt(0) lgkmcnt(0)
	ds_read_b32 v2, v0
	s_add_i32 s3, 0, 0x21524
	v_mov_b32_e32 v0, s3
	ds_read_b32 v0, v0
	s_waitcnt lgkmcnt(1)
	v_cmp_ne_u32_e32 vcc, 0, v2
	s_cbranch_vccnz .LBB0_1548
	v_readlane_b32 s4, v248, 1
	v_readlane_b32 s5, v248, 2
	s_load_dwordx2 s[8:9], s[4:5], 0x4
	s_add_u32 s4, s56, 0x4200
	s_addc_u32 s5, s57, 0
	s_add_u32 s6, s56, 0x4400
	s_addc_u32 s7, s57, 0
	s_waitcnt lgkmcnt(0)
	s_mul_i32 s3, s8, s76
	s_add_u32 s8, s56, 0x4500
	s_mul_i32 s3, s3, s9
	s_addc_u32 s9, s57, 0
	s_add_u32 s10, s56, 0x4600
	s_addc_u32 s11, s57, 0
	s_add_u32 s12, s56, 0x4700
	s_addc_u32 s13, s57, 0
	s_add_u32 s14, s56, 0x4800
	s_addc_u32 s15, s57, 0
	s_add_u32 s16, s56, 0x4900
	s_addc_u32 s17, s57, 0
	s_add_u32 s18, s56, 0x4a00
	s_addc_u32 s19, s57, 0
	s_add_u32 s20, s56, 0x4b00
	s_addc_u32 s21, s57, 0
	s_add_u32 s22, s56, 0x4c00
	s_addc_u32 s23, s57, 0
	s_add_u32 s24, s56, 0x4d00
	s_addc_u32 s25, s57, 0
	s_add_u32 s26, s56, 0x4e00
	s_addc_u32 s27, s57, 0
	s_add_u32 s28, s56, 0x4f00
	s_addc_u32 s29, s57, 0
	s_add_u32 s30, s56, 0x5000
	s_addc_u32 s31, s57, 0
	s_add_u32 s34, s56, 0x5100
	s_addc_u32 s35, s57, 0
	s_add_u32 s36, s56, 0x5200
	s_addc_u32 s37, s57, 0
	s_add_u32 s38, s56, 0x5300
	s_addc_u32 s39, s57, 0
	s_mov_b32 s33, 1
	v_mov_b32_e32 v16, 0
	s_branch .LBB0_1536

; __global__ void __launch_bounds__(NWAVES * 64, 2) fwd_kernel(Args args) {
;     extern __shared__ __attribute__((aligned(16))) unsigned char lds[];
	.amdhsa_kernel _Z10fwd_kernel4Args
		.amdhsa_group_segment_fixed_size 16384
		.amdhsa_private_segment_fixed_size 0
		.amdhsa_kernarg_size 448
		.amdhsa_user_sgpr_count 2
		.amdhsa_user_sgpr_dispatch_ptr 0
		.amdhsa_user_sgpr_queue_ptr 0
		.amdhsa_user_sgpr_kernarg_segment_ptr 1
		.amdhsa_user_sgpr_dispatch_id 0
		.amdhsa_user_sgpr_kernarg_preload_length 0
		.amdhsa_user_sgpr_kernarg_preload_offset 0
		.amdhsa_user_sgpr_private_segment_size 0
		.amdhsa_uses_dynamic_stack 0
		.amdhsa_enable_private_segment 0
		.amdhsa_system_sgpr_workgroup_id_x 1
		.amdhsa_system_sgpr_workgroup_id_y 0
		.amdhsa_system_sgpr_workgroup_id_z 0
		.amdhsa_system_sgpr_workgroup_info 0
		.amdhsa_system_vgpr_workitem_id 0
		.amdhsa_next_free_vgpr 256
		.amdhsa_next_free_sgpr 102
		.amdhsa_accum_offset 256
		.amdhsa_reserve_vcc 1
		.amdhsa_float_round_mode_32 0
		.amdhsa_float_round_mode_16_64 0
		.amdhsa_float_denorm_mode_32 3
		.amdhsa_float_denorm_mode_16_64 3
		.amdhsa_dx10_clamp 1
		.amdhsa_ieee_mode 1
		.amdhsa_fp16_overflow 0
		.amdhsa_tg_split 0
		.amdhsa_exception_fp_ieee_invalid_op 0
		.amdhsa_exception_fp_denorm_src 0
		.amdhsa_exception_fp_ieee_div_zero 0
		.amdhsa_exception_fp_ieee_overflow 0
		.amdhsa_exception_fp_ieee_underflow 0
		.amdhsa_exception_fp_ieee_inexact 0
		.amdhsa_exception_int_div_zero 0
	.end_amdhsa_kernel

; __global__ void __launch_bounds__(NWAVES * 64, 2) fwd_kernel(Args args) {
;     extern __shared__ __attribute__((aligned(16))) unsigned char lds[];
amdhsa.kernels:
  - .agpr_count:     0
    .args:
      - .offset:         0
        .size:           192
        .value_kind:     by_value
      - .offset:         192
        .size:           4
        .value_kind:     hidden_block_count_x
      - .offset:         196
        .size:           4
        .value_kind:     hidden_block_count_y
      - .offset:         200
        .size:           4
        .value_kind:     hidden_block_count_z
      - .offset:         204
        .size:           2
        .value_kind:     hidden_group_size_x
      - .offset:         206
        .size:           2
        .value_kind:     hidden_group_size_y
      - .offset:         208
        .size:           2
        .value_kind:     hidden_group_size_z
      - .offset:         210
        .size:           2
        .value_kind:     hidden_remainder_x
      - .offset:         212
        .size:           2
        .value_kind:     hidden_remainder_y
      - .offset:         214
        .size:           2
        .value_kind:     hidden_remainder_z
      - .offset:         232
        .size:           8
        .value_kind:     hidden_global_offset_x
      - .offset:         240
        .size:           8
        .value_kind:     hidden_global_offset_y
      - .offset:         248
        .size:           8
        .value_kind:     hidden_global_offset_z
      - .offset:         256
        .size:           2
        .value_kind:     hidden_grid_dims
      - .offset:         312
        .size:           4
        .value_kind:     hidden_dynamic_lds_size
    .group_segment_fixed_size: 16384
    .kernarg_segment_align: 8
    .kernarg_segment_size: 448
    .language:       OpenCL C
    .language_version:
      - 2
      - 0
    .max_flat_workgroup_size: 512
    .name:           _Z10fwd_kernel4Args
    .private_segment_fixed_size: 0
    .sgpr_count:     108
    .sgpr_spill_count: 56
    .symbol:         _Z10fwd_kernel4Args.kd
    .uniform_work_group_size: 1
    .uses_dynamic_stack: false
    .vgpr_count:     256
    .vgpr_spill_count: 0
    .wavefront_size: 64
